# all-in combination on v11: wide8 QK/PV read pipelining, attention VALU trims, barrier-ladder shortening, epilogue store-block trims, bpermute butterflies as DPP/permlane swaps, hand-written final RMSN
# speedup vs baseline: 1.0117x; 1.0117x over previous
; #define SBAR() __builtin_amdgcn_sched_barrier(0)
; __device__ __forceinline__ int crow(int r, int hi) { return (r & 3) + 8 * (r >> 2) + 4 * hi; }
; #define FIN(PY0_, PY1_, alY_) do { if constexpr (F8) finishSM8(PY0_, PY1_, alY_, l_reg, pa8); else finishSM(PY0_, PY1_, alY_, l_reg, pa0, pa1, pa2, pa3); } while (0)
; #define PVT(VB_) do { if constexpr (F8) PV8(VB_); else pv_tile<VB_, false>(o, vb0, pa0, pa1, pa2, pa3, true); } while (0)
; #define PSM(P0_, P1_, mn_, al_) partialSM<F8 ? 8 : 0, F8 ? 2 : 8, F8 ? 5 : 0>(P0_, P1_, m_reg, mn_, al_, dead_)
; __device__ __forceinline__ void finishSM8(f32x16& p0, f32x16& p1, float alpha, float& l_reg, i32x8& pa) {
;     for (int r = 0; r < 16; ++r) p1[r] = __builtin_amdgcn_exp2f(p1[r]);
;     float ps;
;     { float s0 = p0[0] + p0[1], s1 = p0[2] + p0[3], s2 = p1[0] + p1[1], s3 = p1[2] + p1[3];
; #pragma unroll
;       for (int r = 4; r < 16; r += 4) { s0 += p0[r]; s0 += p0[r + 1]; s1 += p0[r + 2]; s1 += p0[r + 3]; s2 += p1[r]; s2 += p1[r + 1]; s3 += p1[r + 2]; s3 += p1[r + 3]; }
;       ps = (s0 + s1) + (s2 + s3); }
;     { auto rr = __builtin_amdgcn_permlane32_swap(__float_as_uint(ps), __float_as_uint(ps), false, false);
;       ps = __uint_as_float(rr[0]) + __uint_as_float(rr[1]); }
;     l_reg = l_reg * alpha + ps;
; #pragma unroll
;     for (int d = 0; d < 4; ++d) { int w0 = 0, w1 = 0;
;         w0 = __builtin_amdgcn_cvt_pk_fp8_f32(p0[4 * d], p0[4 * d + 1], w0, false); w0 = __builtin_amdgcn_cvt_pk_fp8_f32(p0[4 * d + 2], p0[4 * d + 3], w0, true);
;         w1 = __builtin_amdgcn_cvt_pk_fp8_f32(p1[4 * d], p1[4 * d + 1], w1, false); w1 = __builtin_amdgcn_cvt_pk_fp8_f32(p1[4 * d + 2], p1[4 * d + 3], w1, true);
;         pa[d] = w0; pa[4 + d] = w1; }
; template <class Epi, bool F8 = false>
; __device__ __forceinline__ void block(const BlockRef& cur, int skv, char* lds, Seam& S, bool moba, unsigned selmask, const Epi& E) {
;     ...
;     if (even) { MASKT(pB0, pB1, NT - 1); PSM(pB0, pB1, mnB, alB); __syncthreads(); RESC(alB);
;         FIN(pB0, pB1, alB); SBAR(); PVT(1); }
;     SBAR();
;     if (hi == 0) li_l[r32] = l_reg; asm volatile("s_waitcnt lgkmcnt(0)" ::: "memory");
;     float rli[16];
; #pragma unroll
;     for (int r = 0; r < 16; ++r) rli[r] = __builtin_amdgcn_rcpf(li_l[crow(r, hi)]) * (F8 ? 1.0f / 16.0f : 1.0f);
.LBB0_1068:
	v_cndmask_b32_e64 v7, v7, v163, s[8:9]
	v_fmamk_f32 v7, v7, 0xba0293ee, v1
	v_cndmask_b32_e64 v7, v7, v210, s[6:7]
	v_fmamk_f32 v8, v98, 0x3a0293ee, v7
	v_fmamk_f32 v9, v99, 0x3a0293ee, v7
	v_fmamk_f32 v10, v100, 0x3a0293ee, v7
	v_fmamk_f32 v11, v101, 0x3a0293ee, v7
	v_fmamk_f32 v98, v82, 0x3a0293ee, v7
	v_fmamk_f32 v99, v83, 0x3a0293ee, v7
	v_fmamk_f32 v100, v84, 0x3a0293ee, v7
	v_fmamk_f32 v101, v85, 0x3a0293ee, v7
	v_fmamk_f32 v12, v102, 0x3a0293ee, v7
	v_fmamk_f32 v13, v103, 0x3a0293ee, v7
	v_fmamk_f32 v15, v104, 0x3a0293ee, v7
	v_fmamk_f32 v17, v105, 0x3a0293ee, v7
	v_fmamk_f32 v104, v106, 0x3a0293ee, v7
	v_fmamk_f32 v105, v107, 0x3a0293ee, v7
	v_fmamk_f32 v106, v108, 0x3a0293ee, v7
	v_fmamk_f32 v107, v109, 0x3a0293ee, v7
	v_fmamk_f32 v108, v110, 0x3a0293ee, v7
	v_fmamk_f32 v109, v111, 0x3a0293ee, v7
	v_fmamk_f32 v110, v112, 0x3a0293ee, v7
	v_fmamk_f32 v111, v113, 0x3a0293ee, v7
	v_fmamk_f32 v102, v86, 0x3a0293ee, v7
	v_fmamk_f32 v103, v87, 0x3a0293ee, v7
	v_fmamk_f32 v88, v88, 0x3a0293ee, v7
	v_fmamk_f32 v89, v89, 0x3a0293ee, v7
	v_fmamk_f32 v90, v90, 0x3a0293ee, v7
	v_fmamk_f32 v91, v91, 0x3a0293ee, v7
	v_fmamk_f32 v92, v92, 0x3a0293ee, v7
	v_fmamk_f32 v93, v93, 0x3a0293ee, v7
	v_fmamk_f32 v94, v94, 0x3a0293ee, v7
	v_exp_f32_e32 v86, v8
	v_exp_f32_e32 v87, v9
	v_exp_f32_e32 v14, v10
	v_exp_f32_e32 v16, v11
	v_fmamk_f32 v95, v95, 0x3a0293ee, v7
	v_fmamk_f32 v96, v96, 0x3a0293ee, v7
	v_fmac_f32_e32 v7, 0x3a0293ee, v97
	v_exp_f32_e32 v97, v98
	v_exp_f32_e32 v98, v99
	v_exp_f32_e32 v99, v100
	v_exp_f32_e32 v100, v101
	v_exp_f32_e32 v84, v12
	v_exp_f32_e32 v82, v15
	v_exp_f32_e32 v101, v102
	v_exp_f32_e32 v102, v103
	v_exp_f32_e32 v103, v88
	v_exp_f32_e32 v85, v13
	v_exp_f32_e32 v83, v17
	v_exp_f32_e32 v15, v104
	v_exp_f32_e32 v104, v89
	v_exp_f32_e32 v17, v105
	v_exp_f32_e32 v8, v106
	v_exp_f32_e32 v105, v90
	v_exp_f32_e32 v106, v92
	v_exp_f32_e32 v9, v107
	v_exp_f32_e32 v10, v110
	v_exp_f32_e32 v91, v91
	v_exp_f32_e32 v107, v93
	v_exp_f32_e32 v110, v7
	v_add_f32_e32 v7, v86, v87
	v_add_f32_e32 v88, v14, v16
	v_add_f32_e32 v89, v97, v98
	v_add_f32_e32 v90, v99, v100
	v_exp_f32_e32 v12, v108
	v_exp_f32_e32 v108, v94
	v_exp_f32_e32 v96, v96
	v_add_f32_e32 v7, v84, v7
	v_add_f32_e32 v88, v82, v88
	v_add_f32_e32 v89, v101, v89
	v_add_f32_e32 v90, v103, v90
	v_exp_f32_e32 v13, v109
	v_exp_f32_e32 v11, v111
	v_exp_f32_e32 v109, v95
	v_add_f32_e32 v7, v85, v7
	v_add_f32_e32 v88, v83, v88
	v_add_f32_e32 v89, v102, v89
	v_add_f32_e32 v90, v104, v90
	v_add_f32_e32 v7, v15, v7
	v_add_f32_e32 v88, v8, v88
	v_add_f32_e32 v89, v105, v89
	v_add_f32_e32 v90, v106, v90
	v_add_f32_e32 v7, v17, v7
	v_add_f32_e32 v88, v9, v88
	v_add_f32_e32 v89, v91, v89
	v_add_f32_e32 v90, v107, v90
	v_add_f32_e32 v7, v12, v7
	v_add_f32_e32 v88, v10, v88
	v_add_f32_e32 v89, v108, v89
	v_add_f32_e32 v90, v96, v90
	v_add_f32_e32 v7, v13, v7
	v_add_f32_e32 v88, v11, v88
	v_add_f32_e32 v89, v109, v89
	v_add_f32_e32 v90, v110, v90
	v_add_f32_e32 v7, v88, v7
	v_add_f32_e32 v88, v89, v90
	v_mov_b32_e32 v90, v3
	v_cvt_pk_fp8_f32 v90, v15, v17
	v_mov_b32_e32 v94, v3
	v_add_f32_e32 v7, v88, v7
	v_mov_b32_e32 v88, v3
	v_mov_b32_e32 v92, v3
	v_mov_b32_e32 v89, v3
	v_mov_b32_e32 v93, v3
	v_cvt_pk_fp8_f32 v94, v105, v91
	v_mov_b32_e32 v91, v3
	v_mov_b32_e32 v95, v3
	v_cvt_pk_fp8_f32 v88, v86, v87
	v_cvt_pk_fp8_f32 v92, v97, v98
	v_cvt_pk_fp8_f32 v89, v84, v85
	v_cvt_pk_fp8_f32 v93, v101, v102
	v_cvt_pk_fp8_f32 v91, v12, v13
	v_cvt_pk_fp8_f32 v95, v108, v109
	v_cvt_pk_fp8_f32 v90, v8, v9 op_sel:[0,0,1]
	v_mov_b32_e32 v8, v7
	s_nop 1
	v_permlane32_swap_b32_e32 v7, v8
	v_cvt_pk_fp8_f32 v88, v14, v16 op_sel:[0,0,1]
	v_cvt_pk_fp8_f32 v92, v99, v100 op_sel:[0,0,1]
	v_cvt_pk_fp8_f32 v89, v82, v83 op_sel:[0,0,1]
	v_cvt_pk_fp8_f32 v93, v103, v104 op_sel:[0,0,1]
	v_cvt_pk_fp8_f32 v94, v106, v107 op_sel:[0,0,1]
	v_cvt_pk_fp8_f32 v91, v10, v11 op_sel:[0,0,1]
	v_cvt_pk_fp8_f32 v95, v96, v110 op_sel:[0,0,1]
	ds_read_b128 v[10:13], v157 offset:16384
	ds_read_b128 v[96:99], v157 offset:18432
	ds_read_b128 v[14:17], v158 offset:16384
	ds_read_b128 v[100:103], v158 offset:18432
	s_waitcnt lgkmcnt(1)
	v_mfma_f32_32x32x64_f8f6f4 v[34:49], v[88:95], v[10:17], v[34:49]
	ds_read_b128 v[10:13], v157 offset:20480
	ds_read_b128 v[14:17], v158 offset:20480
	s_waitcnt lgkmcnt(2)
	v_mfma_f32_32x32x64_f8f6f4 v[50:65], v[88:95], v[96:103], v[50:65]
	ds_read_b128 v[96:99], v157 offset:22528
	ds_read_b128 v[100:103], v158 offset:22528
	s_waitcnt lgkmcnt(2)
	v_mfma_f32_32x32x64_f8f6f4 v[18:33], v[88:95], v[10:17], v[18:33]
	s_waitcnt lgkmcnt(0)
	v_mfma_f32_32x32x64_f8f6f4 v[66:81], v[88:95], v[96:103], v[66:81]
	s_nop 15
	s_nop 15
	s_and_saveexec_b64 s[6:7], s[4:5]
	v_add_f32_e32 v2, v2, v5
	v_fmac_f32_e32 v2, v156, v4
	v_add_f32_e32 v4, v7, v8
	v_fmac_f32_e32 v4, v2, v6
	ds_write_b32 v155, v4
	s_or_b64 exec, exec, s[6:7]
	s_waitcnt lgkmcnt(0)
	v_add_u32_e32 v2, s73, v154
	ds_read_b128 v[4:7], v2
	ds_read_b128 v[8:11], v2 offset:32
	s_brev_b32 s10, 60
	s_mov_b32 s53, 0x800000
	s_lshl_b32 s4, s29, 8
	s_waitcnt lgkmcnt(1)
	v_rcp_f32_e32 v4, v4
	s_and_b32 s4, s4, 0x3000
	s_or_b32 s4, s72, s4
	s_lshl_b32 s4, s4, 12
	v_mul_f32_e32 v88, 0x3d800000, v4
	v_rcp_f32_e32 v4, v5
	v_readlane_b32 s6, v252, 34
	v_readlane_b32 s7, v252, 35
	s_add_u32 s4, s6, s4
	v_mul_f32_e32 v92, 0x3d800000, v4
	v_rcp_f32_e32 v4, v6
	s_addc_u32 s5, s7, 0
	s_lshl_b32 s6, s29, 7
	s_and_b32 s6, s6, 0x780
	v_mul_f32_e32 v86, 0x3d800000, v4
	v_rcp_f32_e32 v4, v7
	v_readlane_b32 s12, v253, 30
	s_add_u32 s8, s4, s6
	v_readlane_b32 s13, v253, 31
	v_mul_f32_e32 v84, 0x3d800000, v4
	s_waitcnt lgkmcnt(0)
; __device__ __forceinline__ float half_sum(float s) {
;     s += swz_xor<1>(s); s += swz_xor<2>(s); s += swz_xor<4>(s); s += swz_xor<8>(s); s += swz_xor<16>(s); return s;
; }
;     __device__ __forceinline__ void operator()(f32x16 (&o)[4], const float (&rli)[16], int wid, int lane, int r32, int hi) const {
;     ...
;         if (mode == 0) {
;             float rn[16];
; #pragma unroll
;             for (int r = 0; r < 16; ++r) { float s = 0.f;
; #pragma unroll
;                 for (int d0 = 0; d0 < 4; ++d0) { const float v = o[d0][r] * rli[r]; o[d0][r] = v; s += v * v; }
;                 s = half_sum(s); rn[r] = rsqrtf(s * (1.0f / 128.0f) + 1e-5f); }
	v_rcp_f32_e32 v4, v8
	v_readlane_b32 s20, v253, 38
	v_readlane_b32 s21, v253, 39
	s_addc_u32 s9, s5, 0
	v_mul_f32_e32 v82, 0x3d800000, v4
	v_rcp_f32_e32 v4, v9
	s_lshl_b32 s4, s6, 2
	s_mov_b64 s[12:13], s[20:21]
	s_add_u32 s6, s12, s4
	v_mul_f32_e32 v106, 0x3d800000, v4
	v_rcp_f32_e32 v4, v10
	ds_read_b128 v[96:99], v2 offset:96
	s_addc_u32 s7, s13, 0
	s_ashr_i32 s89, s88, 31
	v_mul_f32_e32 v94, 0x3d800000, v4
	v_rcp_f32_e32 v4, v11
	s_lshl_b64 s[4:5], s[88:89], 12
	s_add_u32 s8, s8, s4
	s_addc_u32 s9, s9, s5
	v_mul_f32_e32 v90, 0x3d800000, v4
	ds_read_b128 v[4:7], v2 offset:64
	s_waitcnt lgkmcnt(1)
	v_rcp_f32_e32 v2, v96
	v_mov_b32_e32 v96, v34
	v_readlane_b32 s14, v253, 32
	s_waitcnt lgkmcnt(0)
	v_rcp_f32_e32 v4, v4
	v_mul_f32_e32 v8, 0x3d800000, v2
	v_rcp_f32_e32 v2, v97
	v_mov_b32_e32 v97, v50
	v_mul_f32_e32 v16, 0x3d800000, v4
	v_rcp_f32_e32 v4, v5
	v_mov_b32_e32 v50, v35
	v_pk_mul_f32 v[110:111], v[96:97], v[88:89] op_sel_hi:[1,0]
	v_mov_b32_e32 v96, v66
	v_mul_f32_e32 v14, 0x3d800000, v4
	v_rcp_f32_e32 v4, v6
	v_mul_f32_e32 v6, 0x3d800000, v2
	v_rcp_f32_e32 v2, v98
	v_mov_b32_e32 v97, v18
	v_mul_f32_e32 v12, 0x3d800000, v4
	v_rcp_f32_e32 v4, v7
	v_mov_b32_e32 v18, v67
	v_pk_mul_f32 v[100:101], v[110:111], v[110:111]
	v_pk_mul_f32 v[104:105], v[96:97], v[88:89] op_sel_hi:[1,0]
	v_mul_f32_e32 v10, 0x3d800000, v4
	v_mul_f32_e32 v4, 0x3d800000, v2
	v_rcp_f32_e32 v2, v99
	v_pk_mul_f32 v[98:99], v[50:51], v[92:93] op_sel_hi:[1,0]
	v_pk_mul_f32 v[96:97], v[18:19], v[92:93] op_sel_hi:[1,0]
	v_pk_mul_f32 v[34:35], v[98:99], v[98:99]
	v_pk_mul_f32 v[88:89], v[104:105], v[104:105]
	v_pk_mul_f32 v[18:19], v[96:97], v[96:97]
	v_mov_b32_e32 v50, v34
	v_mov_b32_e32 v51, v100
	v_mov_b32_e32 v100, v35
	v_pk_add_f32 v[34:35], v[50:51], v[100:101]
	v_mov_b32_e32 v50, v19
	v_mov_b32_e32 v51, v89
	v_pk_add_f32 v[34:35], v[50:51], v[34:35]
	v_mov_b32_e32 v19, v88
	v_pk_add_f32 v[18:19], v[18:19], v[34:35]
	s_nop 1
	v_mov_b32_dpp v35, v19 quad_perm:[1,0,3,2] row_mask:0xf bank_mask:0xf
	s_nop 1
	v_mov_b32_dpp v34, v18 quad_perm:[1,0,3,2] row_mask:0xf bank_mask:0xf
	v_mul_f32_e32 v2, 0x3d800000, v2
	v_ashrrev_i32_e32 v131, 31, v130
	v_readlane_b32 s15, v253, 33
	v_readlane_b32 s16, v253, 34
	v_pk_add_f32 v[18:19], v[18:19], v[34:35]
	s_nop 1
	v_mov_b32_dpp v35, v19 quad_perm:[2,3,0,1] row_mask:0xf bank_mask:0xf
	s_nop 1
	v_mov_b32_dpp v34, v18 quad_perm:[2,3,0,1] row_mask:0xf bank_mask:0xf
	v_readlane_b32 s17, v253, 35
	v_readlane_b32 s18, v253, 36
	v_readlane_b32 s19, v253, 37
	v_readlane_b32 s22, v253, 40
	v_pk_add_f32 v[18:19], v[18:19], v[34:35]
	ds_swizzle_b32 v35, v19 offset:swizzle(SWAP,4)
	ds_swizzle_b32 v34, v18 offset:swizzle(SWAP,4)
	v_readlane_b32 s23, v253, 41
	v_readlane_b32 s24, v253, 42
	v_readlane_b32 s25, v253, 43
	v_readlane_b32 s26, v253, 44
	s_waitcnt lgkmcnt(0)
	v_pk_add_f32 v[18:19], v[18:19], v[34:35]
	ds_swizzle_b32 v35, v19 offset:swizzle(SWAP,8)
	ds_swizzle_b32 v34, v18 offset:swizzle(SWAP,8)
	v_readlane_b32 s27, v253, 45
	s_waitcnt lgkmcnt(0)
	v_pk_add_f32 v[18:19], v[18:19], v[34:35]
	ds_swizzle_b32 v35, v19 offset:swizzle(SWAP,16)
	ds_swizzle_b32 v34, v18 offset:swizzle(SWAP,16)
	s_waitcnt lgkmcnt(0)
	v_pk_add_f32 v[18:19], v[18:19], v[34:35]
	s_nop 0
	v_pk_fma_f32 v[116:117], v[18:19], s[10:11], v[198:199] op_sel_hi:[1,0,0]
	v_mov_b32_e32 v18, v36
	v_mov_b32_e32 v19, v52
	v_mov_b32_e32 v52, v37
	v_pk_mul_f32 v[102:103], v[18:19], v[86:87] op_sel_hi:[1,0]
	v_mov_b32_e32 v34, v68
	v_mov_b32_e32 v35, v20
	v_pk_mul_f32 v[92:93], v[52:53], v[84:85] op_sel_hi:[1,0]
	v_mov_b32_e32 v20, v69
	v_pk_mul_f32 v[18:19], v[102:103], v[102:103]
	v_pk_mul_f32 v[100:101], v[34:35], v[86:87] op_sel_hi:[1,0]
	v_pk_mul_f32 v[36:37], v[92:93], v[92:93]
	v_pk_mul_f32 v[86:87], v[20:21], v[84:85] op_sel_hi:[1,0]
	v_pk_mul_f32 v[34:35], v[100:101], v[100:101]
	v_pk_mul_f32 v[20:21], v[86:87], v[86:87]
	v_mov_b32_e32 v50, v36
	v_mov_b32_e32 v51, v18
	v_mov_b32_e32 v18, v37
	v_pk_add_f32 v[18:19], v[50:51], v[18:19]
	v_mov_b32_e32 v36, v21
	v_mov_b32_e32 v37, v35
	v_pk_add_f32 v[18:19], v[36:37], v[18:19]
	v_mov_b32_e32 v21, v34
	v_pk_add_f32 v[18:19], v[20:21], v[18:19]
	s_nop 1
	v_mov_b32_dpp v21, v19 quad_perm:[1,0,3,2] row_mask:0xf bank_mask:0xf
	s_nop 1
	v_mov_b32_dpp v20, v18 quad_perm:[1,0,3,2] row_mask:0xf bank_mask:0xf
	v_mul_f32_e32 v5, 0x4b800000, v117
	v_cmp_gt_f32_e32 vcc, s53, v117
	v_cmp_gt_f32_e64 s[4:5], s53, v116
	v_pk_add_f32 v[18:19], v[18:19], v[20:21]
	s_nop 1
	v_mov_b32_dpp v21, v19 quad_perm:[2,3,0,1] row_mask:0xf bank_mask:0xf
	s_nop 1
	v_mov_b32_dpp v20, v18 quad_perm:[2,3,0,1] row_mask:0xf bank_mask:0xf
	v_cndmask_b32_e32 v5, v117, v5, vcc
	v_rsq_f32_e32 v5, v5
	v_pk_add_f32 v[18:19], v[18:19], v[20:21]
	ds_swizzle_b32 v21, v19 offset:swizzle(SWAP,4)
	ds_swizzle_b32 v20, v18 offset:swizzle(SWAP,4)
	v_mul_f32_e32 v7, 0x45800000, v5
	v_cndmask_b32_e32 v117, v5, v7, vcc
	s_waitcnt lgkmcnt(0)
	v_pk_add_f32 v[18:19], v[18:19], v[20:21]
	ds_swizzle_b32 v21, v19 offset:swizzle(SWAP,8)
	ds_swizzle_b32 v20, v18 offset:swizzle(SWAP,8)
	s_waitcnt lgkmcnt(0)
	v_pk_add_f32 v[112:113], v[18:19], v[20:21]
	v_mov_b32_e32 v18, v38
	v_mov_b32_e32 v19, v54
	v_mov_b32_e32 v20, v70
	v_mov_b32_e32 v21, v22
	v_mov_b32_e32 v54, v39
	v_pk_mul_f32 v[88:89], v[18:19], v[82:83] op_sel_hi:[1,0]
	v_pk_mul_f32 v[84:85], v[20:21], v[82:83] op_sel_hi:[1,0]
	v_pk_mul_f32 v[82:83], v[54:55], v[106:107] op_sel_hi:[1,0]
	v_mov_b32_e32 v22, v71
	v_pk_mul_f32 v[18:19], v[88:89], v[88:89]
	v_pk_mul_f32 v[34:35], v[82:83], v[82:83]
	v_pk_mul_f32 v[66:67], v[22:23], v[106:107] op_sel_hi:[1,0]
	v_pk_mul_f32 v[20:21], v[84:85], v[84:85]
	v_pk_mul_f32 v[22:23], v[66:67], v[66:67]
	v_mov_b32_e32 v36, v34
	v_mov_b32_e32 v37, v18
	v_mov_b32_e32 v18, v35
	v_pk_add_f32 v[18:19], v[36:37], v[18:19]
	v_mov_b32_e32 v34, v23
	v_mov_b32_e32 v35, v21
	v_pk_add_f32 v[18:19], v[34:35], v[18:19]
	v_mov_b32_e32 v23, v20
	v_pk_add_f32 v[18:19], v[22:23], v[18:19]
	s_nop 1
	v_mov_b32_dpp v21, v19 quad_perm:[1,0,3,2] row_mask:0xf bank_mask:0xf
	s_nop 1
	v_mov_b32_dpp v20, v18 quad_perm:[1,0,3,2] row_mask:0xf bank_mask:0xf
	ds_swizzle_b32 v115, v113 offset:swizzle(SWAP,16)
	ds_swizzle_b32 v114, v112 offset:swizzle(SWAP,16)
	s_waitcnt lgkmcnt(0)
; __device__ __forceinline__ float half_sum(float s) {
;     s += swz_xor<1>(s); s += swz_xor<2>(s); s += swz_xor<4>(s); s += swz_xor<8>(s); s += swz_xor<16>(s); return s;
; }
;     __device__ __forceinline__ void operator()(f32x16 (&o)[4], const float (&rli)[16], int wid, int lane, int r32, int hi) const {
;     ...
;         if (mode == 0) {
;             float rn[16];
; #pragma unroll
;             for (int r = 0; r < 16; ++r) { float s = 0.f;
; #pragma unroll
;                 for (int d0 = 0; d0 < 4; ++d0) { const float v = o[d0][r] * rli[r]; o[d0][r] = v; s += v * v; }
;                 s = half_sum(s); rn[r] = rsqrtf(s * (1.0f / 128.0f) + 1e-5f); }
	v_pk_add_f32 v[18:19], v[18:19], v[20:21]
	s_nop 1
	v_mov_b32_dpp v21, v19 quad_perm:[2,3,0,1] row_mask:0xf bank_mask:0xf
	s_nop 1
	v_mov_b32_dpp v20, v18 quad_perm:[2,3,0,1] row_mask:0xf bank_mask:0xf
	v_pk_add_f32 v[18:19], v[18:19], v[20:21]
	ds_swizzle_b32 v21, v19 offset:swizzle(SWAP,4)
	ds_swizzle_b32 v20, v18 offset:swizzle(SWAP,4)
	s_waitcnt lgkmcnt(0)
	v_pk_add_f32 v[18:19], v[18:19], v[20:21]
	ds_swizzle_b32 v21, v19 offset:swizzle(SWAP,8)
	ds_swizzle_b32 v20, v18 offset:swizzle(SWAP,8)
	s_waitcnt lgkmcnt(0)
	v_pk_add_f32 v[106:107], v[18:19], v[20:21]
	v_mov_b32_e32 v18, v40
	v_mov_b32_e32 v19, v56
	v_mov_b32_e32 v56, v41
	v_pk_mul_f32 v[70:71], v[18:19], v[94:95] op_sel_hi:[1,0]
	v_mov_b32_e32 v20, v72
	v_mov_b32_e32 v21, v24
	v_pk_mul_f32 v[54:55], v[56:57], v[90:91] op_sel_hi:[1,0]
	v_mov_b32_e32 v24, v73
	v_pk_mul_f32 v[18:19], v[70:71], v[70:71]
	v_pk_mul_f32 v[68:69], v[20:21], v[94:95] op_sel_hi:[1,0]
	v_pk_mul_f32 v[22:23], v[54:55], v[54:55]
	v_pk_mul_f32 v[50:51], v[24:25], v[90:91] op_sel_hi:[1,0]
	v_pk_mul_f32 v[20:21], v[68:69], v[68:69]
	v_pk_mul_f32 v[24:25], v[50:51], v[50:51]
	v_mov_b32_e32 v34, v22
	v_mov_b32_e32 v35, v18
	v_mov_b32_e32 v18, v23
	v_pk_add_f32 v[18:19], v[34:35], v[18:19]
	v_mov_b32_e32 v22, v25
	v_mov_b32_e32 v23, v21
	v_pk_add_f32 v[18:19], v[22:23], v[18:19]
	v_mov_b32_e32 v25, v20
	v_pk_add_f32 v[18:19], v[24:25], v[18:19]
	s_nop 1
	v_mov_b32_dpp v21, v19 quad_perm:[1,0,3,2] row_mask:0xf bank_mask:0xf
	s_nop 1
	v_mov_b32_dpp v20, v18 quad_perm:[1,0,3,2] row_mask:0xf bank_mask:0xf
	ds_swizzle_b32 v109, v107 offset:swizzle(SWAP,16)
	ds_swizzle_b32 v108, v106 offset:swizzle(SWAP,16)
	s_waitcnt lgkmcnt(0)
	v_pk_add_f32 v[18:19], v[18:19], v[20:21]
	s_nop 1
	v_mov_b32_dpp v21, v19 quad_perm:[2,3,0,1] row_mask:0xf bank_mask:0xf
	s_nop 1
	v_mov_b32_dpp v20, v18 quad_perm:[2,3,0,1] row_mask:0xf bank_mask:0xf
	v_pk_add_f32 v[18:19], v[18:19], v[20:21]
	ds_swizzle_b32 v21, v19 offset:swizzle(SWAP,4)
	ds_swizzle_b32 v20, v18 offset:swizzle(SWAP,4)
	s_waitcnt lgkmcnt(0)
	v_pk_add_f32 v[18:19], v[18:19], v[20:21]
	ds_swizzle_b32 v21, v19 offset:swizzle(SWAP,8)
	ds_swizzle_b32 v20, v18 offset:swizzle(SWAP,8)
	s_waitcnt lgkmcnt(0)
	v_pk_add_f32 v[90:91], v[18:19], v[20:21]
	v_mov_b32_e32 v18, v42
	v_mov_b32_e32 v19, v58
	v_mov_b32_e32 v58, v43
	v_pk_mul_f32 v[56:57], v[18:19], v[16:17] op_sel_hi:[1,0]
	v_mov_b32_e32 v20, v74
	v_mov_b32_e32 v21, v26
	v_pk_mul_f32 v[38:39], v[58:59], v[14:15] op_sel_hi:[1,0]
	v_mov_b32_e32 v26, v75
	v_pk_mul_f32 v[18:19], v[56:57], v[56:57]
	v_pk_mul_f32 v[52:53], v[20:21], v[16:17] op_sel_hi:[1,0]
	v_pk_mul_f32 v[20:21], v[38:39], v[38:39]
	v_pk_mul_f32 v[34:35], v[26:27], v[14:15] op_sel_hi:[1,0]
	v_pk_mul_f32 v[16:17], v[52:53], v[52:53]
	v_pk_mul_f32 v[14:15], v[34:35], v[34:35]
	v_mov_b32_e32 v22, v20
	v_mov_b32_e32 v23, v18
	v_mov_b32_e32 v18, v21
	v_pk_add_f32 v[18:19], v[22:23], v[18:19]
	v_mov_b32_e32 v20, v15
	v_mov_b32_e32 v21, v17
	v_pk_add_f32 v[18:19], v[20:21], v[18:19]
	v_mov_b32_e32 v15, v16
	v_pk_add_f32 v[14:15], v[14:15], v[18:19]
	s_nop 1
	v_mov_b32_dpp v17, v15 quad_perm:[1,0,3,2] row_mask:0xf bank_mask:0xf
	s_nop 1
	v_mov_b32_dpp v16, v14 quad_perm:[1,0,3,2] row_mask:0xf bank_mask:0xf
	ds_swizzle_b32 v95, v91 offset:swizzle(SWAP,16)
	ds_swizzle_b32 v94, v90 offset:swizzle(SWAP,16)
	s_waitcnt lgkmcnt(0)
	v_pk_add_f32 v[14:15], v[14:15], v[16:17]
	s_nop 1
	v_mov_b32_dpp v17, v15 quad_perm:[2,3,0,1] row_mask:0xf bank_mask:0xf
	s_nop 1
	v_mov_b32_dpp v16, v14 quad_perm:[2,3,0,1] row_mask:0xf bank_mask:0xf
	v_pk_add_f32 v[14:15], v[14:15], v[16:17]
	ds_swizzle_b32 v17, v15 offset:swizzle(SWAP,4)
	ds_swizzle_b32 v16, v14 offset:swizzle(SWAP,4)
	s_waitcnt lgkmcnt(0)
	v_pk_add_f32 v[14:15], v[14:15], v[16:17]
	ds_swizzle_b32 v17, v15 offset:swizzle(SWAP,8)
	ds_swizzle_b32 v16, v14 offset:swizzle(SWAP,8)
	s_waitcnt lgkmcnt(0)
	v_pk_add_f32 v[72:73], v[14:15], v[16:17]
	v_mov_b32_e32 v14, v44
	v_mov_b32_e32 v15, v60
	v_mov_b32_e32 v60, v45
	v_pk_mul_f32 v[40:41], v[14:15], v[12:13] op_sel_hi:[1,0]
	v_mov_b32_e32 v16, v76
	v_mov_b32_e32 v17, v28
	v_pk_mul_f32 v[24:25], v[60:61], v[10:11] op_sel_hi:[1,0]
	v_mov_b32_e32 v28, v77
	v_pk_mul_f32 v[14:15], v[40:41], v[40:41]
	v_pk_mul_f32 v[36:37], v[16:17], v[12:13] op_sel_hi:[1,0]
	v_pk_mul_f32 v[16:17], v[24:25], v[24:25]
	v_pk_mul_f32 v[20:21], v[28:29], v[10:11] op_sel_hi:[1,0]
	v_pk_mul_f32 v[12:13], v[36:37], v[36:37]
	v_pk_mul_f32 v[10:11], v[20:21], v[20:21]
	v_mov_b32_e32 v18, v16
	v_mov_b32_e32 v19, v14
	v_mov_b32_e32 v14, v17
	v_pk_add_f32 v[14:15], v[18:19], v[14:15]
	v_mov_b32_e32 v16, v11
	v_mov_b32_e32 v17, v13
	v_pk_add_f32 v[14:15], v[16:17], v[14:15]
	v_mov_b32_e32 v11, v12
	v_pk_add_f32 v[10:11], v[10:11], v[14:15]
	s_nop 1
	v_mov_b32_dpp v13, v11 quad_perm:[1,0,3,2] row_mask:0xf bank_mask:0xf
	s_nop 1
	v_mov_b32_dpp v12, v10 quad_perm:[1,0,3,2] row_mask:0xf bank_mask:0xf
	ds_swizzle_b32 v75, v73 offset:swizzle(SWAP,16)
	ds_swizzle_b32 v74, v72 offset:swizzle(SWAP,16)
	s_waitcnt lgkmcnt(0)
	v_pk_add_f32 v[10:11], v[10:11], v[12:13]
	s_nop 1
	v_mov_b32_dpp v13, v11 quad_perm:[2,3,0,1] row_mask:0xf bank_mask:0xf
	s_nop 1
	v_mov_b32_dpp v12, v10 quad_perm:[2,3,0,1] row_mask:0xf bank_mask:0xf
	v_pk_add_f32 v[10:11], v[10:11], v[12:13]
	ds_swizzle_b32 v13, v11 offset:swizzle(SWAP,4)
	ds_swizzle_b32 v12, v10 offset:swizzle(SWAP,4)
	s_waitcnt lgkmcnt(0)
	v_pk_add_f32 v[10:11], v[10:11], v[12:13]
	ds_swizzle_b32 v13, v11 offset:swizzle(SWAP,8)
	ds_swizzle_b32 v12, v10 offset:swizzle(SWAP,8)
	s_waitcnt lgkmcnt(0)
; __device__ __forceinline__ int crow(int r, int hi) { return (r & 3) + 8 * (r >> 2) + 4 * hi; }
; __device__ __forceinline__ void store_quad8(unsigned char* p, float v, int r32) {
;     v = fminf(fmaxf(v, -448.f), 448.f);
;     const float v1 = swz_xor<1>(v);
;     const int w = __builtin_amdgcn_cvt_pk_fp8_f32(v, v1, 0, false);
;     const int w2 = __builtin_amdgcn_ds_swizzle(w, (2 << 10) | 0x1f);
;     if ((r32 & 3) == 0) *(unsigned*)p = ((unsigned)w & 0xffffu) | ((unsigned)w2 << 16);
; }
;     __device__ __forceinline__ void operator()(f32x16 (&o)[4], const float (&rli)[16], int wid, int lane, int r32, int hi) const {
;     ...
;         if (mode == 0) {
;             float rn[16];
; #pragma unroll
;             for (int r = 0; r < 16; ++r) { float s = 0.f;
; #pragma unroll
;                 for (int d0 = 0; d0 < 4; ++d0) { const float v = o[d0][r] * rli[r]; o[d0][r] = v; s += v * v; }
;                 s = half_sum(s); rn[r] = rsqrtf(s * (1.0f / 128.0f) + 1e-5f); }
;             float g[4];
; #pragma unroll
;             for (int d0 = 0; d0 < 4; ++d0) g[d0] = gain[d0 * 32 + r32];
; #pragma unroll
;             for (int r = 0; r < 16; ++r)
; #pragma unroll
;                 for (int d0 = 0; d0 < 4; ++d0) store_quad8(base + (size_t)crow(r, hi) * 4096 + d0 * 32 + r32, o[d0][r] * rn[r] * g[d0], r32);
	v_pk_add_f32 v[44:45], v[10:11], v[12:13]
	v_mov_b32_e32 v10, v46
	v_mov_b32_e32 v11, v62
	v_mov_b32_e32 v62, v47
	v_pk_mul_f32 v[26:27], v[10:11], v[8:9] op_sel_hi:[1,0]
	v_mov_b32_e32 v12, v78
	v_mov_b32_e32 v13, v30
	v_pk_mul_f32 v[14:15], v[62:63], v[6:7] op_sel_hi:[1,0]
	v_mov_b32_e32 v30, v79
	v_pk_mul_f32 v[10:11], v[26:27], v[26:27]
	v_pk_mul_f32 v[22:23], v[12:13], v[8:9] op_sel_hi:[1,0]
	v_pk_mul_f32 v[16:17], v[14:15], v[14:15]
	v_pk_mul_f32 v[12:13], v[30:31], v[6:7] op_sel_hi:[1,0]
	v_pk_mul_f32 v[8:9], v[22:23], v[22:23]
	v_pk_mul_f32 v[6:7], v[12:13], v[12:13]
	v_mov_b32_e32 v18, v16
	v_mov_b32_e32 v19, v10
	v_mov_b32_e32 v10, v17
	v_pk_add_f32 v[10:11], v[18:19], v[10:11]
	v_mov_b32_e32 v16, v7
	v_mov_b32_e32 v17, v9
	v_pk_add_f32 v[10:11], v[16:17], v[10:11]
	v_mov_b32_e32 v7, v8
	v_pk_add_f32 v[6:7], v[6:7], v[10:11]
	s_nop 1
	v_mov_b32_dpp v9, v7 quad_perm:[1,0,3,2] row_mask:0xf bank_mask:0xf
	s_nop 1
	v_mov_b32_dpp v8, v6 quad_perm:[1,0,3,2] row_mask:0xf bank_mask:0xf
	ds_swizzle_b32 v59, v45 offset:swizzle(SWAP,16)
	ds_swizzle_b32 v58, v44 offset:swizzle(SWAP,16)
	s_waitcnt lgkmcnt(0)
	v_pk_add_f32 v[6:7], v[6:7], v[8:9]
	s_nop 1
	v_mov_b32_dpp v9, v7 quad_perm:[2,3,0,1] row_mask:0xf bank_mask:0xf
	s_nop 1
	v_mov_b32_dpp v8, v6 quad_perm:[2,3,0,1] row_mask:0xf bank_mask:0xf
	v_pk_add_f32 v[6:7], v[6:7], v[8:9]
	ds_swizzle_b32 v9, v7 offset:swizzle(SWAP,4)
	ds_swizzle_b32 v8, v6 offset:swizzle(SWAP,4)
	s_waitcnt lgkmcnt(0)
	v_pk_add_f32 v[6:7], v[6:7], v[8:9]
	ds_swizzle_b32 v9, v7 offset:swizzle(SWAP,8)
	ds_swizzle_b32 v8, v6 offset:swizzle(SWAP,8)
	s_waitcnt lgkmcnt(0)
	v_pk_add_f32 v[28:29], v[6:7], v[8:9]
	v_mov_b32_e32 v6, v48
	v_mov_b32_e32 v7, v64
	v_pk_mul_f32 v[10:11], v[6:7], v[4:5] op_sel_hi:[1,0]
	v_mov_b32_e32 v6, v80
	v_mov_b32_e32 v7, v32
	v_mov_b32_e32 v64, v49
	v_pk_mul_f32 v[8:9], v[6:7], v[4:5] op_sel_hi:[1,0]
	v_pk_mul_f32 v[6:7], v[64:65], v[2:3] op_sel_hi:[1,0]
	v_mov_b32_e32 v32, v81
	v_pk_mul_f32 v[16:17], v[10:11], v[10:11]
	v_pk_mul_f32 v[42:43], v[6:7], v[6:7]
	v_pk_mul_f32 v[4:5], v[32:33], v[2:3] op_sel_hi:[1,0]
	v_pk_mul_f32 v[18:19], v[8:9], v[8:9]
	v_pk_mul_f32 v[32:33], v[4:5], v[4:5]
	v_mov_b32_e32 v46, v42
	v_mov_b32_e32 v47, v16
	v_mov_b32_e32 v16, v43
	v_pk_add_f32 v[16:17], v[46:47], v[16:17]
	v_mov_b32_e32 v42, v33
	v_mov_b32_e32 v43, v19
	v_pk_add_f32 v[16:17], v[42:43], v[16:17]
	v_mov_b32_e32 v33, v18
	v_pk_add_f32 v[16:17], v[32:33], v[16:17]
	v_lshl_add_u64 v[32:33], v[130:131], 2, s[6:7]
	global_load_dword v60, v[32:33], off
	global_load_dword v62, v[32:33], off offset:128
	global_load_dword v61, v[32:33], off offset:256
	global_load_dword v2, v[32:33], off offset:384
	s_nop 1
	v_mov_b32_dpp v19, v17 quad_perm:[1,0,3,2] row_mask:0xf bank_mask:0xf
	s_nop 1
	v_mov_b32_dpp v18, v16 quad_perm:[1,0,3,2] row_mask:0xf bank_mask:0xf
	v_lshlrev_b32_e32 v42, 2, v152
	v_ashrrev_i32_e32 v43, 31, v42
	v_lshlrev_b64 v[46:47], 12, v[42:43]
	v_mul_f32_e32 v43, v110, v117
	v_pk_add_f32 v[16:17], v[16:17], v[18:19]
	s_nop 1
	v_mov_b32_dpp v19, v17 quad_perm:[2,3,0,1] row_mask:0xf bank_mask:0xf
	s_nop 1
	v_mov_b32_dpp v18, v16 quad_perm:[2,3,0,1] row_mask:0xf bank_mask:0xf
	ds_swizzle_b32 v31, v29 offset:swizzle(SWAP,16)
	ds_swizzle_b32 v30, v28 offset:swizzle(SWAP,16)
	v_and_b32_e32 v32, 3, v130
	v_cmp_eq_u32_e32 vcc, 0, v32
	s_waitcnt lgkmcnt(0)
	v_pk_add_f32 v[16:17], v[16:17], v[18:19]
	ds_swizzle_b32 v19, v17 offset:swizzle(SWAP,4)
	ds_swizzle_b32 v18, v16 offset:swizzle(SWAP,4)
	v_lshl_add_u64 v[32:33], s[8:9], 0, v[130:131]
	v_lshl_add_u64 v[46:47], v[32:33], 0, v[46:47]
	s_waitcnt lgkmcnt(0)
	v_pk_add_f32 v[16:17], v[16:17], v[18:19]
	ds_swizzle_b32 v19, v17 offset:swizzle(SWAP,8)
	ds_swizzle_b32 v18, v16 offset:swizzle(SWAP,8)
	s_waitcnt lgkmcnt(0)
	v_pk_add_f32 v[16:17], v[16:17], v[18:19]
	ds_swizzle_b32 v19, v17 offset:swizzle(SWAP,16)
	ds_swizzle_b32 v18, v16 offset:swizzle(SWAP,16)
	s_waitcnt vmcnt(3)
	v_mul_f32_e32 v43, v43, v60
	v_max_f32_e32 v43, 0xc3e00000, v43
	v_min_f32_e32 v48, 0x43e00000, v43
	s_nop 1
	v_mov_b32_dpp v49, v48 quad_perm:[1,0,3,2] row_mask:0xf bank_mask:0xf
	s_waitcnt lgkmcnt(0)
	v_cvt_pk_fp8_f32 v43, v48, v49
	s_nop 1
	v_mov_b32_dpp v48, v43 quad_perm:[2,3,0,1] row_mask:0xf bank_mask:0xf
	s_and_saveexec_b64 s[6:7], vcc
	v_and_b32_e32 v43, 0xffff, v43
	v_lshl_or_b32 v43, v48, 16, v43
	global_store_dword v[46:47], v43, off
.LBB0_1072:
	s_or_b64 exec, exec, s[6:7]
	v_mul_f32_e32 v43, v111, v117
	s_waitcnt vmcnt(2)
	v_mul_f32_e32 v43, v43, v62
	v_max_f32_e32 v43, 0xc3e00000, v43
	v_min_f32_e32 v48, 0x43e00000, v43
	s_nop 1
	v_mov_b32_dpp v49, v48 quad_perm:[1,0,3,2] row_mask:0xf bank_mask:0xf
	v_cvt_pk_fp8_f32 v43, v48, v49
	s_nop 1
	v_mov_b32_dpp v48, v43 quad_perm:[2,3,0,1] row_mask:0xf bank_mask:0xf
	s_and_saveexec_b64 s[6:7], vcc
	v_and_b32_e32 v43, 0xffff, v43
	v_lshl_or_b32 v43, v48, 16, v43
	global_store_dword v[46:47], v43, off offset:32
.LBB0_1074:
	s_or_b64 exec, exec, s[6:7]
	v_mul_f32_e32 v43, v105, v117
	s_waitcnt vmcnt(1)
	v_mul_f32_e32 v43, v43, v61
	v_max_f32_e32 v43, 0xc3e00000, v43
	v_min_f32_e32 v48, 0x43e00000, v43
	s_nop 1
	v_mov_b32_dpp v49, v48 quad_perm:[1,0,3,2] row_mask:0xf bank_mask:0xf
	v_cvt_pk_fp8_f32 v43, v48, v49
	s_nop 1
	v_mov_b32_dpp v48, v43 quad_perm:[2,3,0,1] row_mask:0xf bank_mask:0xf
	s_and_saveexec_b64 s[6:7], vcc
	v_readlane_b32 s88, v252, 34
	v_readlane_b32 s89, v252, 35
	s_cbranch_execz .LBB0_1076
	v_and_b32_e32 v43, 0xffff, v43
	s_waitcnt lgkmcnt(0)
	v_lshl_or_b32 v43, v48, 16, v43
	global_store_dword v[46:47], v43, off offset:64
; __device__ __forceinline__ int crow(int r, int hi) { return (r & 3) + 8 * (r >> 2) + 4 * hi; }
; __device__ __forceinline__ void store_quad8(unsigned char* p, float v, int r32) {
;     v = fminf(fmaxf(v, -448.f), 448.f);
;     const float v1 = swz_xor<1>(v);
;     const int w = __builtin_amdgcn_cvt_pk_fp8_f32(v, v1, 0, false);
;     const int w2 = __builtin_amdgcn_ds_swizzle(w, (2 << 10) | 0x1f);
;     if ((r32 & 3) == 0) *(unsigned*)p = ((unsigned)w & 0xffffu) | ((unsigned)w2 << 16);
; }
;     __device__ __forceinline__ void operator()(f32x16 (&o)[4], const float (&rli)[16], int wid, int lane, int r32, int hi) const {
;     ...
;             for (int r = 0; r < 16; ++r)
; #pragma unroll
;                 for (int d0 = 0; d0 < 4; ++d0) store_quad8(base + (size_t)crow(r, hi) * 4096 + d0 * 32 + r32, o[d0][r] * rn[r] * g[d0], r32);
.LBB0_1076:
	s_or_b64 exec, exec, s[6:7]
	v_mul_f32_e32 v43, v104, v117
	s_waitcnt vmcnt(0)
	v_mul_f32_e32 v43, v43, v2
	v_max_f32_e32 v43, 0xc3e00000, v43
	s_waitcnt lgkmcnt(0)
	v_min_f32_e32 v48, 0x43e00000, v43
	s_nop 1
	v_mov_b32_dpp v49, v48 quad_perm:[1,0,3,2] row_mask:0xf bank_mask:0xf
	v_cvt_pk_fp8_f32 v43, v48, v49
	s_nop 1
	v_mov_b32_dpp v48, v43 quad_perm:[2,3,0,1] row_mask:0xf bank_mask:0xf
	s_and_saveexec_b64 s[6:7], vcc
	v_and_b32_e32 v43, 0xffff, v43
	v_lshl_or_b32 v43, v48, 16, v43
	global_store_dword v[46:47], v43, off offset:96
.LBB0_1078:
	s_or_b64 exec, exec, s[6:7]
	v_mul_f32_e32 v43, 0x4b800000, v116
	v_cndmask_b32_e64 v43, v116, v43, s[4:5]
	v_rsq_f32_e32 v43, v43
	s_nop 0
	v_mul_f32_e32 v46, 0x45800000, v43
	v_cndmask_b32_e64 v43, v43, v46, s[4:5]
	v_mul_f32_e32 v48, v98, v43
	v_mul_f32_e32 v48, v48, v60
	v_max_f32_e32 v48, 0xc3e00000, v48
	v_min_f32_e32 v49, 0x43e00000, v48
	s_nop 1
	v_mov_b32_dpp v63, v49 quad_perm:[1,0,3,2] row_mask:0xf bank_mask:0xf
	v_or_b32_e32 v46, 1, v42
	v_ashrrev_i32_e32 v47, 31, v46
	v_lshlrev_b64 v[46:47], 12, v[46:47]
	v_cvt_pk_fp8_f32 v48, v49, v63
	v_lshl_add_u64 v[46:47], v[32:33], 0, v[46:47]
	s_nop 1
	v_mov_b32_dpp v49, v48 quad_perm:[2,3,0,1] row_mask:0xf bank_mask:0xf
	s_and_saveexec_b64 s[4:5], vcc
	v_and_b32_e32 v48, 0xffff, v48
	v_lshl_or_b32 v48, v49, 16, v48
	global_store_dword v[46:47], v48, off
.LBB0_1080:
	s_or_b64 exec, exec, s[4:5]
	v_mul_f32_e32 v48, v99, v43
	v_mul_f32_e32 v48, v48, v62
	v_max_f32_e32 v48, 0xc3e00000, v48
	v_min_f32_e32 v49, 0x43e00000, v48
	s_nop 1
	v_mov_b32_dpp v63, v49 quad_perm:[1,0,3,2] row_mask:0xf bank_mask:0xf
	v_cvt_pk_fp8_f32 v48, v49, v63
	s_nop 1
	v_mov_b32_dpp v49, v48 quad_perm:[2,3,0,1] row_mask:0xf bank_mask:0xf
	s_and_saveexec_b64 s[4:5], vcc
	v_and_b32_e32 v48, 0xffff, v48
	v_lshl_or_b32 v48, v49, 16, v48
	global_store_dword v[46:47], v48, off offset:32
.LBB0_1082:
	s_or_b64 exec, exec, s[4:5]
	v_mul_f32_e32 v48, v97, v43
	v_mul_f32_e32 v48, v48, v61
	v_max_f32_e32 v48, 0xc3e00000, v48
	v_min_f32_e32 v49, 0x43e00000, v48
	s_nop 1
	v_mov_b32_dpp v63, v49 quad_perm:[1,0,3,2] row_mask:0xf bank_mask:0xf
	v_cvt_pk_fp8_f32 v48, v49, v63
	s_nop 1
	v_mov_b32_dpp v49, v48 quad_perm:[2,3,0,1] row_mask:0xf bank_mask:0xf
	s_and_saveexec_b64 s[4:5], vcc
	v_and_b32_e32 v48, 0xffff, v48
	v_lshl_or_b32 v48, v49, 16, v48
	global_store_dword v[46:47], v48, off offset:64
.LBB0_1084:
	s_or_b64 exec, exec, s[4:5]
	v_mul_f32_e32 v43, v96, v43
	v_mul_f32_e32 v43, v43, v2
	v_max_f32_e32 v43, 0xc3e00000, v43
	v_min_f32_e32 v48, 0x43e00000, v43
	s_nop 1
	v_mov_b32_dpp v49, v48 quad_perm:[1,0,3,2] row_mask:0xf bank_mask:0xf
	v_cvt_pk_fp8_f32 v43, v48, v49
	s_nop 1
	v_mov_b32_dpp v48, v43 quad_perm:[2,3,0,1] row_mask:0xf bank_mask:0xf
	s_and_saveexec_b64 s[4:5], vcc
	v_and_b32_e32 v43, 0xffff, v43
	v_lshl_or_b32 v43, v48, 16, v43
	global_store_dword v[46:47], v43, off offset:96
.LBB0_1086:
	s_or_b64 exec, exec, s[4:5]
	v_pk_add_f32 v[46:47], v[112:113], v[114:115]
	s_nop 0
	v_pk_fma_f32 v[46:47], v[46:47], s[10:11], v[198:199] op_sel_hi:[1,0,0]
	s_nop 0
	v_mul_f32_e32 v43, 0x4b800000, v47
	v_cmp_gt_f32_e64 s[4:5], s53, v47
	s_nop 1
	v_cndmask_b32_e64 v43, v47, v43, s[4:5]
	v_rsq_f32_e32 v43, v43
	s_nop 0
	v_mul_f32_e32 v47, 0x45800000, v43
	v_cndmask_b32_e64 v43, v43, v47, s[4:5]
	v_mul_f32_e32 v47, v102, v43
	v_mul_f32_e32 v47, v47, v60
	v_max_f32_e32 v47, 0xc3e00000, v47
	v_min_f32_e32 v48, 0x43e00000, v47
	s_nop 1
	v_mov_b32_dpp v49, v48 quad_perm:[1,0,3,2] row_mask:0xf bank_mask:0xf
	v_cmp_gt_f32_e64 s[4:5], s53, v46
	v_cvt_pk_fp8_f32 v47, v48, v49
	v_or_b32_e32 v48, 2, v42
	v_ashrrev_i32_e32 v49, 31, v48
	v_lshlrev_b64 v[48:49], 12, v[48:49]
	s_nop 1
	v_mov_b32_dpp v63, v47 quad_perm:[2,3,0,1] row_mask:0xf bank_mask:0xf
	v_lshl_add_u64 v[48:49], v[32:33], 0, v[48:49]
	s_and_saveexec_b64 s[6:7], vcc
	v_and_b32_e32 v47, 0xffff, v47
	v_lshl_or_b32 v47, v63, 16, v47
	global_store_dword v[48:49], v47, off
.LBB0_1088:
	s_or_b64 exec, exec, s[6:7]
	v_mul_f32_e32 v47, v103, v43
	v_mul_f32_e32 v47, v47, v62
	v_max_f32_e32 v47, 0xc3e00000, v47
	v_min_f32_e32 v63, 0x43e00000, v47
	s_nop 1
	v_mov_b32_dpp v64, v63 quad_perm:[1,0,3,2] row_mask:0xf bank_mask:0xf
	v_cvt_pk_fp8_f32 v47, v63, v64
	s_nop 1
	v_mov_b32_dpp v63, v47 quad_perm:[2,3,0,1] row_mask:0xf bank_mask:0xf
	s_and_saveexec_b64 s[6:7], vcc
	v_and_b32_e32 v47, 0xffff, v47
	v_lshl_or_b32 v47, v63, 16, v47
	global_store_dword v[48:49], v47, off offset:32
.LBB0_1090:
	s_or_b64 exec, exec, s[6:7]
	v_mul_f32_e32 v47, v101, v43
	v_mul_f32_e32 v47, v47, v61
	v_max_f32_e32 v47, 0xc3e00000, v47
	v_min_f32_e32 v63, 0x43e00000, v47
	s_nop 1
	v_mov_b32_dpp v64, v63 quad_perm:[1,0,3,2] row_mask:0xf bank_mask:0xf
	v_cvt_pk_fp8_f32 v47, v63, v64
	s_nop 1
	v_mov_b32_dpp v63, v47 quad_perm:[2,3,0,1] row_mask:0xf bank_mask:0xf
	s_and_saveexec_b64 s[6:7], vcc
	v_and_b32_e32 v47, 0xffff, v47
	v_lshl_or_b32 v47, v63, 16, v47
	global_store_dword v[48:49], v47, off offset:64
.LBB0_1092:
	s_or_b64 exec, exec, s[6:7]
	v_mul_f32_e32 v43, v100, v43
	v_mul_f32_e32 v43, v43, v2
	v_max_f32_e32 v43, 0xc3e00000, v43
	v_min_f32_e32 v47, 0x43e00000, v43
	s_nop 1
	v_mov_b32_dpp v63, v47 quad_perm:[1,0,3,2] row_mask:0xf bank_mask:0xf
	v_cvt_pk_fp8_f32 v43, v47, v63
	s_nop 1
	v_mov_b32_dpp v47, v43 quad_perm:[2,3,0,1] row_mask:0xf bank_mask:0xf
	s_and_saveexec_b64 s[6:7], vcc
	v_and_b32_e32 v43, 0xffff, v43
	v_lshl_or_b32 v43, v47, 16, v43
	global_store_dword v[48:49], v43, off offset:96
; __device__ __forceinline__ int crow(int r, int hi) { return (r & 3) + 8 * (r >> 2) + 4 * hi; }
; __device__ __forceinline__ void store_quad8(unsigned char* p, float v, int r32) {
;     v = fminf(fmaxf(v, -448.f), 448.f);
;     const float v1 = swz_xor<1>(v);
;     const int w = __builtin_amdgcn_cvt_pk_fp8_f32(v, v1, 0, false);
;     const int w2 = __builtin_amdgcn_ds_swizzle(w, (2 << 10) | 0x1f);
;     if ((r32 & 3) == 0) *(unsigned*)p = ((unsigned)w & 0xffffu) | ((unsigned)w2 << 16);
; }
;     __device__ __forceinline__ void operator()(f32x16 (&o)[4], const float (&rli)[16], int wid, int lane, int r32, int hi) const {
;     ...
;             for (int r = 0; r < 16; ++r) { float s = 0.f;
; #pragma unroll
;                 for (int d0 = 0; d0 < 4; ++d0) { const float v = o[d0][r] * rli[r]; o[d0][r] = v; s += v * v; }
;                 s = half_sum(s); rn[r] = rsqrtf(s * (1.0f / 128.0f) + 1e-5f); }
;             float g[4];
; #pragma unroll
;             for (int d0 = 0; d0 < 4; ++d0) g[d0] = gain[d0 * 32 + r32];
; #pragma unroll
;             for (int r = 0; r < 16; ++r)
; #pragma unroll
;                 for (int d0 = 0; d0 < 4; ++d0) store_quad8(base + (size_t)crow(r, hi) * 4096 + d0 * 32 + r32, o[d0][r] * rn[r] * g[d0], r32);
.LBB0_1094:
	s_or_b64 exec, exec, s[6:7]
	v_mul_f32_e32 v43, 0x4b800000, v46
	v_cndmask_b32_e64 v43, v46, v43, s[4:5]
	v_rsq_f32_e32 v43, v43
	s_nop 0
	v_mul_f32_e32 v46, 0x45800000, v43
	v_cndmask_b32_e64 v43, v43, v46, s[4:5]
	v_mul_f32_e32 v48, v92, v43
	v_mul_f32_e32 v48, v48, v60
	v_max_f32_e32 v48, 0xc3e00000, v48
	v_min_f32_e32 v49, 0x43e00000, v48
	s_nop 1
	v_mov_b32_dpp v63, v49 quad_perm:[1,0,3,2] row_mask:0xf bank_mask:0xf
	v_or_b32_e32 v46, 3, v42
	v_ashrrev_i32_e32 v47, 31, v46
	v_lshlrev_b64 v[46:47], 12, v[46:47]
	v_cvt_pk_fp8_f32 v48, v49, v63
	v_lshl_add_u64 v[46:47], v[32:33], 0, v[46:47]
	s_nop 1
	v_mov_b32_dpp v49, v48 quad_perm:[2,3,0,1] row_mask:0xf bank_mask:0xf
	s_and_saveexec_b64 s[4:5], vcc
	v_and_b32_e32 v48, 0xffff, v48
	v_lshl_or_b32 v48, v49, 16, v48
	global_store_dword v[46:47], v48, off
.LBB0_1096:
	s_or_b64 exec, exec, s[4:5]
	v_mul_f32_e32 v48, v93, v43
	v_mul_f32_e32 v48, v48, v62
	v_max_f32_e32 v48, 0xc3e00000, v48
	v_min_f32_e32 v49, 0x43e00000, v48
	s_nop 1
	v_mov_b32_dpp v63, v49 quad_perm:[1,0,3,2] row_mask:0xf bank_mask:0xf
	v_cvt_pk_fp8_f32 v48, v49, v63
	s_nop 1
	v_mov_b32_dpp v49, v48 quad_perm:[2,3,0,1] row_mask:0xf bank_mask:0xf
	s_and_saveexec_b64 s[4:5], vcc
	v_and_b32_e32 v48, 0xffff, v48
	v_lshl_or_b32 v48, v49, 16, v48
	global_store_dword v[46:47], v48, off offset:32
.LBB0_1098:
	s_or_b64 exec, exec, s[4:5]
	v_mul_f32_e32 v48, v87, v43
	v_mul_f32_e32 v48, v48, v61
	v_max_f32_e32 v48, 0xc3e00000, v48
	v_min_f32_e32 v49, 0x43e00000, v48
	s_nop 1
	v_mov_b32_dpp v63, v49 quad_perm:[1,0,3,2] row_mask:0xf bank_mask:0xf
	v_cvt_pk_fp8_f32 v48, v49, v63
	s_nop 1
	v_mov_b32_dpp v49, v48 quad_perm:[2,3,0,1] row_mask:0xf bank_mask:0xf
	s_and_saveexec_b64 s[4:5], vcc
	v_and_b32_e32 v48, 0xffff, v48
	v_lshl_or_b32 v48, v49, 16, v48
	global_store_dword v[46:47], v48, off offset:64
.LBB0_1100:
	s_or_b64 exec, exec, s[4:5]
	v_mul_f32_e32 v43, v86, v43
	v_mul_f32_e32 v43, v43, v2
	v_max_f32_e32 v43, 0xc3e00000, v43
	v_min_f32_e32 v48, 0x43e00000, v43
	s_nop 1
	v_mov_b32_dpp v49, v48 quad_perm:[1,0,3,2] row_mask:0xf bank_mask:0xf
	v_cvt_pk_fp8_f32 v43, v48, v49
	s_nop 1
	v_mov_b32_dpp v48, v43 quad_perm:[2,3,0,1] row_mask:0xf bank_mask:0xf
	s_and_saveexec_b64 s[4:5], vcc
	v_and_b32_e32 v43, 0xffff, v43
	v_lshl_or_b32 v43, v48, 16, v43
	global_store_dword v[46:47], v43, off offset:96
.LBB0_1102:
	s_or_b64 exec, exec, s[4:5]
	v_pk_add_f32 v[46:47], v[106:107], v[108:109]
	s_nop 0
	v_pk_fma_f32 v[46:47], v[46:47], s[10:11], v[198:199] op_sel_hi:[1,0,0]
	s_nop 0
	v_mul_f32_e32 v43, 0x4b800000, v47
	v_cmp_gt_f32_e64 s[4:5], s53, v47
	s_nop 1
	v_cndmask_b32_e64 v43, v47, v43, s[4:5]
	v_rsq_f32_e32 v43, v43
	s_nop 0
	v_mul_f32_e32 v47, 0x45800000, v43
	v_cndmask_b32_e64 v43, v43, v47, s[4:5]
	v_mul_f32_e32 v47, v88, v43
	v_mul_f32_e32 v47, v47, v60
	v_max_f32_e32 v47, 0xc3e00000, v47
	v_min_f32_e32 v48, 0x43e00000, v47
	s_nop 1
	v_mov_b32_dpp v49, v48 quad_perm:[1,0,3,2] row_mask:0xf bank_mask:0xf
	v_cmp_gt_f32_e64 s[4:5], s53, v46
	v_cvt_pk_fp8_f32 v47, v48, v49
	v_add_u32_e32 v48, 8, v42
	v_ashrrev_i32_e32 v49, 31, v48
	v_lshlrev_b64 v[48:49], 12, v[48:49]
	s_nop 1
	v_mov_b32_dpp v63, v47 quad_perm:[2,3,0,1] row_mask:0xf bank_mask:0xf
	v_lshl_add_u64 v[48:49], v[32:33], 0, v[48:49]
	s_and_saveexec_b64 s[6:7], vcc
	v_and_b32_e32 v47, 0xffff, v47
	v_lshl_or_b32 v47, v63, 16, v47
	global_store_dword v[48:49], v47, off
.LBB0_1104:
	s_or_b64 exec, exec, s[6:7]
	v_mul_f32_e32 v47, v89, v43
	v_mul_f32_e32 v47, v47, v62
	v_max_f32_e32 v47, 0xc3e00000, v47
	v_min_f32_e32 v63, 0x43e00000, v47
	s_nop 1
	v_mov_b32_dpp v64, v63 quad_perm:[1,0,3,2] row_mask:0xf bank_mask:0xf
	v_cvt_pk_fp8_f32 v47, v63, v64
	s_nop 1
	v_mov_b32_dpp v63, v47 quad_perm:[2,3,0,1] row_mask:0xf bank_mask:0xf
	s_and_saveexec_b64 s[6:7], vcc
	v_and_b32_e32 v47, 0xffff, v47
	v_lshl_or_b32 v47, v63, 16, v47
	global_store_dword v[48:49], v47, off offset:32
.LBB0_1106:
	s_or_b64 exec, exec, s[6:7]
	v_mul_f32_e32 v47, v85, v43
	v_mul_f32_e32 v47, v47, v61
	v_max_f32_e32 v47, 0xc3e00000, v47
	v_min_f32_e32 v63, 0x43e00000, v47
	s_nop 1
	v_mov_b32_dpp v64, v63 quad_perm:[1,0,3,2] row_mask:0xf bank_mask:0xf
	v_cvt_pk_fp8_f32 v47, v63, v64
	s_nop 1
	v_mov_b32_dpp v63, v47 quad_perm:[2,3,0,1] row_mask:0xf bank_mask:0xf
	s_and_saveexec_b64 s[6:7], vcc
	v_and_b32_e32 v47, 0xffff, v47
	v_lshl_or_b32 v47, v63, 16, v47
	global_store_dword v[48:49], v47, off offset:64
.LBB0_1108:
	s_or_b64 exec, exec, s[6:7]
	v_mul_f32_e32 v43, v84, v43
	v_mul_f32_e32 v43, v43, v2
	v_max_f32_e32 v43, 0xc3e00000, v43
	v_min_f32_e32 v47, 0x43e00000, v43
	s_nop 1
	v_mov_b32_dpp v63, v47 quad_perm:[1,0,3,2] row_mask:0xf bank_mask:0xf
	v_cvt_pk_fp8_f32 v43, v47, v63
	s_nop 1
	v_mov_b32_dpp v47, v43 quad_perm:[2,3,0,1] row_mask:0xf bank_mask:0xf
	s_and_saveexec_b64 s[6:7], vcc
	v_and_b32_e32 v43, 0xffff, v43
	v_lshl_or_b32 v43, v47, 16, v43
	global_store_dword v[48:49], v43, off offset:96
.LBB0_1110:
	s_or_b64 exec, exec, s[6:7]
	v_mul_f32_e32 v43, 0x4b800000, v46
	v_cndmask_b32_e64 v43, v46, v43, s[4:5]
	v_rsq_f32_e32 v43, v43
	s_nop 0
	v_mul_f32_e32 v46, 0x45800000, v43
	v_cndmask_b32_e64 v43, v43, v46, s[4:5]
	v_mul_f32_e32 v48, v82, v43
	v_mul_f32_e32 v48, v48, v60
	v_max_f32_e32 v48, 0xc3e00000, v48
	v_min_f32_e32 v49, 0x43e00000, v48
	s_nop 1
	v_mov_b32_dpp v63, v49 quad_perm:[1,0,3,2] row_mask:0xf bank_mask:0xf
	v_add_u32_e32 v46, 9, v42
	v_ashrrev_i32_e32 v47, 31, v46
	v_lshlrev_b64 v[46:47], 12, v[46:47]
	v_cvt_pk_fp8_f32 v48, v49, v63
	v_lshl_add_u64 v[46:47], v[32:33], 0, v[46:47]
	s_nop 1
	v_mov_b32_dpp v49, v48 quad_perm:[2,3,0,1] row_mask:0xf bank_mask:0xf
	s_and_saveexec_b64 s[4:5], vcc
	v_and_b32_e32 v48, 0xffff, v48
	v_lshl_or_b32 v48, v49, 16, v48
	global_store_dword v[46:47], v48, off
; __device__ __forceinline__ int crow(int r, int hi) { return (r & 3) + 8 * (r >> 2) + 4 * hi; }
; __device__ __forceinline__ void store_quad8(unsigned char* p, float v, int r32) {
;     v = fminf(fmaxf(v, -448.f), 448.f);
;     const float v1 = swz_xor<1>(v);
;     const int w = __builtin_amdgcn_cvt_pk_fp8_f32(v, v1, 0, false);
;     const int w2 = __builtin_amdgcn_ds_swizzle(w, (2 << 10) | 0x1f);
;     if ((r32 & 3) == 0) *(unsigned*)p = ((unsigned)w & 0xffffu) | ((unsigned)w2 << 16);
; }
;     __device__ __forceinline__ void operator()(f32x16 (&o)[4], const float (&rli)[16], int wid, int lane, int r32, int hi) const {
;     ...
;             for (int r = 0; r < 16; ++r) { float s = 0.f;
; #pragma unroll
;                 for (int d0 = 0; d0 < 4; ++d0) { const float v = o[d0][r] * rli[r]; o[d0][r] = v; s += v * v; }
;                 s = half_sum(s); rn[r] = rsqrtf(s * (1.0f / 128.0f) + 1e-5f); }
;             float g[4];
; #pragma unroll
;             for (int d0 = 0; d0 < 4; ++d0) g[d0] = gain[d0 * 32 + r32];
; #pragma unroll
;             for (int r = 0; r < 16; ++r)
; #pragma unroll
;                 for (int d0 = 0; d0 < 4; ++d0) store_quad8(base + (size_t)crow(r, hi) * 4096 + d0 * 32 + r32, o[d0][r] * rn[r] * g[d0], r32);
.LBB0_1112:
	s_or_b64 exec, exec, s[4:5]
	v_mul_f32_e32 v48, v83, v43
	v_mul_f32_e32 v48, v48, v62
	v_max_f32_e32 v48, 0xc3e00000, v48
	v_min_f32_e32 v49, 0x43e00000, v48
	s_nop 1
	v_mov_b32_dpp v63, v49 quad_perm:[1,0,3,2] row_mask:0xf bank_mask:0xf
	v_cvt_pk_fp8_f32 v48, v49, v63
	s_nop 1
	v_mov_b32_dpp v49, v48 quad_perm:[2,3,0,1] row_mask:0xf bank_mask:0xf
	s_and_saveexec_b64 s[4:5], vcc
	v_and_b32_e32 v48, 0xffff, v48
	v_lshl_or_b32 v48, v49, 16, v48
	global_store_dword v[46:47], v48, off offset:32
.LBB0_1114:
	s_or_b64 exec, exec, s[4:5]
	v_mul_f32_e32 v48, v67, v43
	v_mul_f32_e32 v48, v48, v61
	v_max_f32_e32 v48, 0xc3e00000, v48
	v_min_f32_e32 v49, 0x43e00000, v48
	s_nop 1
	v_mov_b32_dpp v63, v49 quad_perm:[1,0,3,2] row_mask:0xf bank_mask:0xf
	v_cvt_pk_fp8_f32 v48, v49, v63
	s_nop 1
	v_mov_b32_dpp v49, v48 quad_perm:[2,3,0,1] row_mask:0xf bank_mask:0xf
	s_and_saveexec_b64 s[4:5], vcc
	v_and_b32_e32 v48, 0xffff, v48
	v_lshl_or_b32 v48, v49, 16, v48
	global_store_dword v[46:47], v48, off offset:64
.LBB0_1116:
	s_or_b64 exec, exec, s[4:5]
	v_mul_f32_e32 v43, v66, v43
	v_mul_f32_e32 v43, v43, v2
	v_max_f32_e32 v43, 0xc3e00000, v43
	v_min_f32_e32 v48, 0x43e00000, v43
	s_nop 1
	v_mov_b32_dpp v49, v48 quad_perm:[1,0,3,2] row_mask:0xf bank_mask:0xf
	v_cvt_pk_fp8_f32 v43, v48, v49
	s_nop 1
	v_mov_b32_dpp v48, v43 quad_perm:[2,3,0,1] row_mask:0xf bank_mask:0xf
	s_and_saveexec_b64 s[4:5], vcc
	v_and_b32_e32 v43, 0xffff, v43
	v_lshl_or_b32 v43, v48, 16, v43
	global_store_dword v[46:47], v43, off offset:96
.LBB0_1118:
	s_or_b64 exec, exec, s[4:5]
	v_pk_add_f32 v[46:47], v[90:91], v[94:95]
	s_nop 0
	v_pk_fma_f32 v[46:47], v[46:47], s[10:11], v[198:199] op_sel_hi:[1,0,0]
	s_nop 0
	v_mul_f32_e32 v43, 0x4b800000, v47
	v_cmp_gt_f32_e64 s[4:5], s53, v47
	s_nop 1
	v_cndmask_b32_e64 v43, v47, v43, s[4:5]
	v_rsq_f32_e32 v43, v43
	s_nop 0
	v_mul_f32_e32 v47, 0x45800000, v43
	v_cndmask_b32_e64 v43, v43, v47, s[4:5]
	v_mul_f32_e32 v47, v70, v43
	v_mul_f32_e32 v47, v47, v60
	v_max_f32_e32 v47, 0xc3e00000, v47
	v_min_f32_e32 v48, 0x43e00000, v47
	s_nop 1
	v_mov_b32_dpp v49, v48 quad_perm:[1,0,3,2] row_mask:0xf bank_mask:0xf
	v_cmp_gt_f32_e64 s[4:5], s53, v46
	v_cvt_pk_fp8_f32 v47, v48, v49
	v_add_u32_e32 v48, 10, v42
	v_ashrrev_i32_e32 v49, 31, v48
	v_lshlrev_b64 v[48:49], 12, v[48:49]
	s_nop 1
	v_mov_b32_dpp v63, v47 quad_perm:[2,3,0,1] row_mask:0xf bank_mask:0xf
	v_lshl_add_u64 v[48:49], v[32:33], 0, v[48:49]
	s_and_saveexec_b64 s[6:7], vcc
	v_and_b32_e32 v47, 0xffff, v47
	v_lshl_or_b32 v47, v63, 16, v47
	global_store_dword v[48:49], v47, off
.LBB0_1120:
	s_or_b64 exec, exec, s[6:7]
	v_mul_f32_e32 v47, v71, v43
	v_mul_f32_e32 v47, v47, v62
	v_max_f32_e32 v47, 0xc3e00000, v47
	v_min_f32_e32 v63, 0x43e00000, v47
	s_nop 1
	v_mov_b32_dpp v64, v63 quad_perm:[1,0,3,2] row_mask:0xf bank_mask:0xf
	v_cvt_pk_fp8_f32 v47, v63, v64
	s_nop 1
	v_mov_b32_dpp v63, v47 quad_perm:[2,3,0,1] row_mask:0xf bank_mask:0xf
	s_and_saveexec_b64 s[6:7], vcc
	v_and_b32_e32 v47, 0xffff, v47
	v_lshl_or_b32 v47, v63, 16, v47
	global_store_dword v[48:49], v47, off offset:32
.LBB0_1122:
	s_or_b64 exec, exec, s[6:7]
	v_mul_f32_e32 v47, v69, v43
	v_mul_f32_e32 v47, v47, v61
	v_max_f32_e32 v47, 0xc3e00000, v47
	v_min_f32_e32 v63, 0x43e00000, v47
	s_nop 1
	v_mov_b32_dpp v64, v63 quad_perm:[1,0,3,2] row_mask:0xf bank_mask:0xf
	v_cvt_pk_fp8_f32 v47, v63, v64
	s_nop 1
	v_mov_b32_dpp v63, v47 quad_perm:[2,3,0,1] row_mask:0xf bank_mask:0xf
	s_and_saveexec_b64 s[6:7], vcc
	v_and_b32_e32 v47, 0xffff, v47
	v_lshl_or_b32 v47, v63, 16, v47
	global_store_dword v[48:49], v47, off offset:64
.LBB0_1124:
	s_or_b64 exec, exec, s[6:7]
	v_mul_f32_e32 v43, v68, v43
	v_mul_f32_e32 v43, v43, v2
	v_max_f32_e32 v43, 0xc3e00000, v43
	v_min_f32_e32 v47, 0x43e00000, v43
	s_nop 1
	v_mov_b32_dpp v63, v47 quad_perm:[1,0,3,2] row_mask:0xf bank_mask:0xf
	v_cvt_pk_fp8_f32 v43, v47, v63
	s_nop 1
	v_mov_b32_dpp v47, v43 quad_perm:[2,3,0,1] row_mask:0xf bank_mask:0xf
	s_and_saveexec_b64 s[6:7], vcc
	v_and_b32_e32 v43, 0xffff, v43
	v_lshl_or_b32 v43, v47, 16, v43
	global_store_dword v[48:49], v43, off offset:96
.LBB0_1126:
	s_or_b64 exec, exec, s[6:7]
	v_mul_f32_e32 v43, 0x4b800000, v46
	v_cndmask_b32_e64 v43, v46, v43, s[4:5]
	v_rsq_f32_e32 v43, v43
	s_nop 0
	v_mul_f32_e32 v46, 0x45800000, v43
	v_cndmask_b32_e64 v43, v43, v46, s[4:5]
	v_mul_f32_e32 v48, v54, v43
	v_mul_f32_e32 v48, v48, v60
	v_max_f32_e32 v48, 0xc3e00000, v48
	v_min_f32_e32 v49, 0x43e00000, v48
	s_nop 1
	v_mov_b32_dpp v54, v49 quad_perm:[1,0,3,2] row_mask:0xf bank_mask:0xf
	v_add_u32_e32 v46, 11, v42
	v_ashrrev_i32_e32 v47, 31, v46
	v_lshlrev_b64 v[46:47], 12, v[46:47]
	v_cvt_pk_fp8_f32 v48, v49, v54
	v_lshl_add_u64 v[46:47], v[32:33], 0, v[46:47]
	s_nop 1
	v_mov_b32_dpp v49, v48 quad_perm:[2,3,0,1] row_mask:0xf bank_mask:0xf
	s_and_saveexec_b64 s[4:5], vcc
	v_and_b32_e32 v48, 0xffff, v48
	v_lshl_or_b32 v48, v49, 16, v48
	global_store_dword v[46:47], v48, off
.LBB0_1128:
	s_or_b64 exec, exec, s[4:5]
	v_mul_f32_e32 v48, v55, v43
	v_mul_f32_e32 v48, v48, v62
	v_max_f32_e32 v48, 0xc3e00000, v48
	v_min_f32_e32 v49, 0x43e00000, v48
	s_nop 1
	v_mov_b32_dpp v54, v49 quad_perm:[1,0,3,2] row_mask:0xf bank_mask:0xf
	v_cvt_pk_fp8_f32 v48, v49, v54
	s_nop 1
	v_mov_b32_dpp v49, v48 quad_perm:[2,3,0,1] row_mask:0xf bank_mask:0xf
	s_and_saveexec_b64 s[4:5], vcc
	v_and_b32_e32 v48, 0xffff, v48
	v_lshl_or_b32 v48, v49, 16, v48
	global_store_dword v[46:47], v48, off offset:32
; __device__ __forceinline__ int crow(int r, int hi) { return (r & 3) + 8 * (r >> 2) + 4 * hi; }
; __device__ __forceinline__ void store_quad8(unsigned char* p, float v, int r32) {
;     v = fminf(fmaxf(v, -448.f), 448.f);
;     const float v1 = swz_xor<1>(v);
;     const int w = __builtin_amdgcn_cvt_pk_fp8_f32(v, v1, 0, false);
;     const int w2 = __builtin_amdgcn_ds_swizzle(w, (2 << 10) | 0x1f);
;     if ((r32 & 3) == 0) *(unsigned*)p = ((unsigned)w & 0xffffu) | ((unsigned)w2 << 16);
; }
;     __device__ __forceinline__ void operator()(f32x16 (&o)[4], const float (&rli)[16], int wid, int lane, int r32, int hi) const {
;     ...
;             for (int r = 0; r < 16; ++r) { float s = 0.f;
; #pragma unroll
;                 for (int d0 = 0; d0 < 4; ++d0) { const float v = o[d0][r] * rli[r]; o[d0][r] = v; s += v * v; }
;                 s = half_sum(s); rn[r] = rsqrtf(s * (1.0f / 128.0f) + 1e-5f); }
;             float g[4];
; #pragma unroll
;             for (int d0 = 0; d0 < 4; ++d0) g[d0] = gain[d0 * 32 + r32];
; #pragma unroll
;             for (int r = 0; r < 16; ++r)
; #pragma unroll
;                 for (int d0 = 0; d0 < 4; ++d0) store_quad8(base + (size_t)crow(r, hi) * 4096 + d0 * 32 + r32, o[d0][r] * rn[r] * g[d0], r32);
.LBB0_1130:
	s_or_b64 exec, exec, s[4:5]
	v_mul_f32_e32 v48, v51, v43
	v_mul_f32_e32 v48, v48, v61
	v_max_f32_e32 v48, 0xc3e00000, v48
	v_min_f32_e32 v49, 0x43e00000, v48
	s_nop 1
	v_mov_b32_dpp v51, v49 quad_perm:[1,0,3,2] row_mask:0xf bank_mask:0xf
	v_cvt_pk_fp8_f32 v48, v49, v51
	s_nop 1
	v_mov_b32_dpp v49, v48 quad_perm:[2,3,0,1] row_mask:0xf bank_mask:0xf
	s_and_saveexec_b64 s[4:5], vcc
	v_and_b32_e32 v48, 0xffff, v48
	v_lshl_or_b32 v48, v49, 16, v48
	global_store_dword v[46:47], v48, off offset:64
.LBB0_1132:
	s_or_b64 exec, exec, s[4:5]
	v_mul_f32_e32 v43, v50, v43
	v_mul_f32_e32 v43, v43, v2
	v_max_f32_e32 v43, 0xc3e00000, v43
	v_min_f32_e32 v48, 0x43e00000, v43
	s_nop 1
	v_mov_b32_dpp v49, v48 quad_perm:[1,0,3,2] row_mask:0xf bank_mask:0xf
	v_cvt_pk_fp8_f32 v43, v48, v49
	s_nop 1
	v_mov_b32_dpp v48, v43 quad_perm:[2,3,0,1] row_mask:0xf bank_mask:0xf
	s_and_saveexec_b64 s[4:5], vcc
	v_and_b32_e32 v43, 0xffff, v43
	v_lshl_or_b32 v43, v48, 16, v43
	global_store_dword v[46:47], v43, off offset:96
.LBB0_1134:
	s_or_b64 exec, exec, s[4:5]
	v_pk_add_f32 v[46:47], v[72:73], v[74:75]
	s_nop 0
	v_pk_fma_f32 v[46:47], v[46:47], s[10:11], v[198:199] op_sel_hi:[1,0,0]
	s_nop 0
	v_mul_f32_e32 v43, 0x4b800000, v47
	v_cmp_gt_f32_e64 s[4:5], s53, v47
	s_nop 1
	v_cndmask_b32_e64 v43, v47, v43, s[4:5]
	v_rsq_f32_e32 v43, v43
	s_nop 0
	v_mul_f32_e32 v47, 0x45800000, v43
	v_cndmask_b32_e64 v43, v43, v47, s[4:5]
	v_mul_f32_e32 v47, v56, v43
	v_mul_f32_e32 v47, v47, v60
	v_max_f32_e32 v47, 0xc3e00000, v47
	v_min_f32_e32 v48, 0x43e00000, v47
	s_nop 1
	v_mov_b32_dpp v49, v48 quad_perm:[1,0,3,2] row_mask:0xf bank_mask:0xf
	v_cmp_gt_f32_e64 s[4:5], s53, v46
	v_cvt_pk_fp8_f32 v47, v48, v49
	v_add_u32_e32 v48, 16, v42
	v_ashrrev_i32_e32 v49, 31, v48
	v_lshlrev_b64 v[48:49], 12, v[48:49]
	s_nop 1
	v_mov_b32_dpp v50, v47 quad_perm:[2,3,0,1] row_mask:0xf bank_mask:0xf
	v_lshl_add_u64 v[48:49], v[32:33], 0, v[48:49]
	s_and_saveexec_b64 s[6:7], vcc
	v_and_b32_e32 v47, 0xffff, v47
	v_lshl_or_b32 v47, v50, 16, v47
	global_store_dword v[48:49], v47, off
.LBB0_1136:
	s_or_b64 exec, exec, s[6:7]
	v_mul_f32_e32 v47, v57, v43
	v_mul_f32_e32 v47, v47, v62
	v_max_f32_e32 v47, 0xc3e00000, v47
	v_min_f32_e32 v50, 0x43e00000, v47
	s_nop 1
	v_mov_b32_dpp v51, v50 quad_perm:[1,0,3,2] row_mask:0xf bank_mask:0xf
	v_cvt_pk_fp8_f32 v47, v50, v51
	s_nop 1
	v_mov_b32_dpp v50, v47 quad_perm:[2,3,0,1] row_mask:0xf bank_mask:0xf
	s_and_saveexec_b64 s[6:7], vcc
	v_and_b32_e32 v47, 0xffff, v47
	v_lshl_or_b32 v47, v50, 16, v47
	global_store_dword v[48:49], v47, off offset:32
.LBB0_1138:
	s_or_b64 exec, exec, s[6:7]
	v_mul_f32_e32 v47, v53, v43
	v_mul_f32_e32 v47, v47, v61
	v_max_f32_e32 v47, 0xc3e00000, v47
	v_min_f32_e32 v50, 0x43e00000, v47
	s_nop 1
	v_mov_b32_dpp v51, v50 quad_perm:[1,0,3,2] row_mask:0xf bank_mask:0xf
	v_cvt_pk_fp8_f32 v47, v50, v51
	s_nop 1
	v_mov_b32_dpp v50, v47 quad_perm:[2,3,0,1] row_mask:0xf bank_mask:0xf
	s_and_saveexec_b64 s[6:7], vcc
	v_and_b32_e32 v47, 0xffff, v47
	v_lshl_or_b32 v47, v50, 16, v47
	global_store_dword v[48:49], v47, off offset:64
.LBB0_1140:
	s_or_b64 exec, exec, s[6:7]
	v_mul_f32_e32 v43, v52, v43
	v_mul_f32_e32 v43, v43, v2
	v_max_f32_e32 v43, 0xc3e00000, v43
	v_min_f32_e32 v47, 0x43e00000, v43
	s_nop 1
	v_mov_b32_dpp v50, v47 quad_perm:[1,0,3,2] row_mask:0xf bank_mask:0xf
	v_cvt_pk_fp8_f32 v43, v47, v50
	s_nop 1
	v_mov_b32_dpp v47, v43 quad_perm:[2,3,0,1] row_mask:0xf bank_mask:0xf
	s_and_saveexec_b64 s[6:7], vcc
	v_and_b32_e32 v43, 0xffff, v43
	v_lshl_or_b32 v43, v47, 16, v43
	global_store_dword v[48:49], v43, off offset:96
.LBB0_1142:
	s_or_b64 exec, exec, s[6:7]
	v_mul_f32_e32 v43, 0x4b800000, v46
	v_cndmask_b32_e64 v43, v46, v43, s[4:5]
	v_rsq_f32_e32 v43, v43
	s_nop 0
	v_mul_f32_e32 v46, 0x45800000, v43
	v_cndmask_b32_e64 v43, v43, v46, s[4:5]
	v_mul_f32_e32 v38, v38, v43
	v_mul_f32_e32 v38, v38, v60
	v_max_f32_e32 v38, 0xc3e00000, v38
	v_min_f32_e32 v48, 0x43e00000, v38
	s_nop 1
	v_mov_b32_dpp v49, v48 quad_perm:[1,0,3,2] row_mask:0xf bank_mask:0xf
	v_add_u32_e32 v46, 17, v42
	v_ashrrev_i32_e32 v47, 31, v46
	v_lshlrev_b64 v[46:47], 12, v[46:47]
	v_cvt_pk_fp8_f32 v38, v48, v49
	v_lshl_add_u64 v[46:47], v[32:33], 0, v[46:47]
	s_nop 1
	v_mov_b32_dpp v48, v38 quad_perm:[2,3,0,1] row_mask:0xf bank_mask:0xf
	s_and_saveexec_b64 s[4:5], vcc
	v_and_b32_e32 v38, 0xffff, v38
	v_lshl_or_b32 v38, v48, 16, v38
	global_store_dword v[46:47], v38, off
.LBB0_1144:
	s_or_b64 exec, exec, s[4:5]
	v_mul_f32_e32 v38, v39, v43
	v_mul_f32_e32 v38, v38, v62
	v_max_f32_e32 v38, 0xc3e00000, v38
	v_min_f32_e32 v39, 0x43e00000, v38
	s_nop 1
	v_mov_b32_dpp v48, v39 quad_perm:[1,0,3,2] row_mask:0xf bank_mask:0xf
	v_cvt_pk_fp8_f32 v38, v39, v48
	s_nop 1
	v_mov_b32_dpp v39, v38 quad_perm:[2,3,0,1] row_mask:0xf bank_mask:0xf
	s_and_saveexec_b64 s[4:5], vcc
	v_and_b32_e32 v38, 0xffff, v38
	v_lshl_or_b32 v38, v39, 16, v38
	global_store_dword v[46:47], v38, off offset:32
.LBB0_1146:
	s_or_b64 exec, exec, s[4:5]
	v_mul_f32_e32 v35, v35, v43
	v_mul_f32_e32 v35, v35, v61
	v_max_f32_e32 v35, 0xc3e00000, v35
	v_min_f32_e32 v38, 0x43e00000, v35
	s_nop 1
	v_mov_b32_dpp v39, v38 quad_perm:[1,0,3,2] row_mask:0xf bank_mask:0xf
	v_cvt_pk_fp8_f32 v35, v38, v39
	s_nop 1
	v_mov_b32_dpp v38, v35 quad_perm:[2,3,0,1] row_mask:0xf bank_mask:0xf
	s_and_saveexec_b64 s[4:5], vcc
	v_and_b32_e32 v35, 0xffff, v35
	v_lshl_or_b32 v35, v38, 16, v35
	global_store_dword v[46:47], v35, off offset:64
; __device__ __forceinline__ int crow(int r, int hi) { return (r & 3) + 8 * (r >> 2) + 4 * hi; }
; __device__ __forceinline__ void store_quad8(unsigned char* p, float v, int r32) {
;     v = fminf(fmaxf(v, -448.f), 448.f);
;     const float v1 = swz_xor<1>(v);
;     const int w = __builtin_amdgcn_cvt_pk_fp8_f32(v, v1, 0, false);
;     const int w2 = __builtin_amdgcn_ds_swizzle(w, (2 << 10) | 0x1f);
;     if ((r32 & 3) == 0) *(unsigned*)p = ((unsigned)w & 0xffffu) | ((unsigned)w2 << 16);
; }
;     __device__ __forceinline__ void operator()(f32x16 (&o)[4], const float (&rli)[16], int wid, int lane, int r32, int hi) const {
;     ...
;             for (int r = 0; r < 16; ++r) { float s = 0.f;
; #pragma unroll
;                 for (int d0 = 0; d0 < 4; ++d0) { const float v = o[d0][r] * rli[r]; o[d0][r] = v; s += v * v; }
;                 s = half_sum(s); rn[r] = rsqrtf(s * (1.0f / 128.0f) + 1e-5f); }
;             float g[4];
; #pragma unroll
;             for (int d0 = 0; d0 < 4; ++d0) g[d0] = gain[d0 * 32 + r32];
; #pragma unroll
;             for (int r = 0; r < 16; ++r)
; #pragma unroll
;                 for (int d0 = 0; d0 < 4; ++d0) store_quad8(base + (size_t)crow(r, hi) * 4096 + d0 * 32 + r32, o[d0][r] * rn[r] * g[d0], r32);
.LBB0_1148:
	s_or_b64 exec, exec, s[4:5]
	v_mul_f32_e32 v34, v34, v43
	v_mul_f32_e32 v34, v34, v2
	v_max_f32_e32 v34, 0xc3e00000, v34
	v_min_f32_e32 v35, 0x43e00000, v34
	s_nop 1
	v_mov_b32_dpp v38, v35 quad_perm:[1,0,3,2] row_mask:0xf bank_mask:0xf
	v_cvt_pk_fp8_f32 v34, v35, v38
	s_nop 1
	v_mov_b32_dpp v35, v34 quad_perm:[2,3,0,1] row_mask:0xf bank_mask:0xf
	s_and_saveexec_b64 s[4:5], vcc
	v_and_b32_e32 v34, 0xffff, v34
	v_lshl_or_b32 v34, v35, 16, v34
	global_store_dword v[46:47], v34, off offset:96
.LBB0_1150:
	s_or_b64 exec, exec, s[4:5]
	v_pk_add_f32 v[34:35], v[44:45], v[58:59]
	s_nop 0
	v_pk_fma_f32 v[34:35], v[34:35], s[10:11], v[198:199] op_sel_hi:[1,0,0]
	s_nop 0
	v_mul_f32_e32 v38, 0x4b800000, v35
	v_cmp_gt_f32_e64 s[4:5], s53, v35
	s_nop 1
	v_cndmask_b32_e64 v35, v35, v38, s[4:5]
	v_rsq_f32_e32 v35, v35
	s_nop 0
	v_mul_f32_e32 v38, 0x45800000, v35
	v_cndmask_b32_e64 v35, v35, v38, s[4:5]
	v_mul_f32_e32 v38, v40, v35
	v_mul_f32_e32 v38, v38, v60
	v_max_f32_e32 v38, 0xc3e00000, v38
	v_min_f32_e32 v38, 0x43e00000, v38
	s_nop 1
	v_mov_b32_dpp v39, v38 quad_perm:[1,0,3,2] row_mask:0xf bank_mask:0xf
	v_cmp_gt_f32_e64 s[4:5], s53, v34
	v_cvt_pk_fp8_f32 v40, v38, v39
	v_add_u32_e32 v38, 18, v42
	v_ashrrev_i32_e32 v39, 31, v38
	v_lshlrev_b64 v[38:39], 12, v[38:39]
	s_nop 1
	v_mov_b32_dpp v43, v40 quad_perm:[2,3,0,1] row_mask:0xf bank_mask:0xf
	v_lshl_add_u64 v[38:39], v[32:33], 0, v[38:39]
	s_and_saveexec_b64 s[6:7], vcc
	v_and_b32_e32 v40, 0xffff, v40
	v_lshl_or_b32 v40, v43, 16, v40
	global_store_dword v[38:39], v40, off
.LBB0_1152:
	s_or_b64 exec, exec, s[6:7]
	v_mul_f32_e32 v40, v41, v35
	v_mul_f32_e32 v40, v40, v62
	v_max_f32_e32 v40, 0xc3e00000, v40
	v_min_f32_e32 v41, 0x43e00000, v40
	s_nop 1
	v_mov_b32_dpp v43, v41 quad_perm:[1,0,3,2] row_mask:0xf bank_mask:0xf
	v_cvt_pk_fp8_f32 v40, v41, v43
	s_nop 1
	v_mov_b32_dpp v41, v40 quad_perm:[2,3,0,1] row_mask:0xf bank_mask:0xf
	s_and_saveexec_b64 s[6:7], vcc
	v_and_b32_e32 v40, 0xffff, v40
	v_lshl_or_b32 v40, v41, 16, v40
	global_store_dword v[38:39], v40, off offset:32
.LBB0_1154:
	s_or_b64 exec, exec, s[6:7]
	v_mul_f32_e32 v37, v37, v35
	v_mul_f32_e32 v37, v37, v61
	v_max_f32_e32 v37, 0xc3e00000, v37
	v_min_f32_e32 v40, 0x43e00000, v37
	s_nop 1
	v_mov_b32_dpp v41, v40 quad_perm:[1,0,3,2] row_mask:0xf bank_mask:0xf
	v_cvt_pk_fp8_f32 v37, v40, v41
	s_nop 1
	v_mov_b32_dpp v40, v37 quad_perm:[2,3,0,1] row_mask:0xf bank_mask:0xf
	s_and_saveexec_b64 s[6:7], vcc
	v_and_b32_e32 v37, 0xffff, v37
	v_lshl_or_b32 v37, v40, 16, v37
	global_store_dword v[38:39], v37, off offset:64
.LBB0_1156:
	s_or_b64 exec, exec, s[6:7]
	v_mul_f32_e32 v35, v36, v35
	v_mul_f32_e32 v35, v35, v2
	v_max_f32_e32 v35, 0xc3e00000, v35
	v_min_f32_e32 v36, 0x43e00000, v35
	s_nop 1
	v_mov_b32_dpp v37, v36 quad_perm:[1,0,3,2] row_mask:0xf bank_mask:0xf
	v_cvt_pk_fp8_f32 v35, v36, v37
	s_nop 1
	v_mov_b32_dpp v36, v35 quad_perm:[2,3,0,1] row_mask:0xf bank_mask:0xf
	s_and_saveexec_b64 s[6:7], vcc
	v_and_b32_e32 v35, 0xffff, v35
	v_lshl_or_b32 v35, v36, 16, v35
	global_store_dword v[38:39], v35, off offset:96
.LBB0_1158:
	s_or_b64 exec, exec, s[6:7]
	v_mul_f32_e32 v35, 0x4b800000, v34
	v_cndmask_b32_e64 v34, v34, v35, s[4:5]
	v_rsq_f32_e32 v34, v34
	s_nop 0
	v_mul_f32_e32 v35, 0x45800000, v34
	v_cndmask_b32_e64 v36, v34, v35, s[4:5]
	v_mul_f32_e32 v24, v24, v36
	v_mul_f32_e32 v24, v24, v60
	v_max_f32_e32 v24, 0xc3e00000, v24
	v_min_f32_e32 v37, 0x43e00000, v24
	s_nop 1
	v_mov_b32_dpp v38, v37 quad_perm:[1,0,3,2] row_mask:0xf bank_mask:0xf
	v_add_u32_e32 v34, 19, v42
	v_ashrrev_i32_e32 v35, 31, v34
	v_lshlrev_b64 v[34:35], 12, v[34:35]
	v_cvt_pk_fp8_f32 v24, v37, v38
	v_lshl_add_u64 v[34:35], v[32:33], 0, v[34:35]
	s_nop 1
	v_mov_b32_dpp v37, v24 quad_perm:[2,3,0,1] row_mask:0xf bank_mask:0xf
	s_and_saveexec_b64 s[4:5], vcc
	v_and_b32_e32 v24, 0xffff, v24
	v_lshl_or_b32 v24, v37, 16, v24
	global_store_dword v[34:35], v24, off
.LBB0_1160:
	s_or_b64 exec, exec, s[4:5]
	v_mul_f32_e32 v24, v25, v36
	v_mul_f32_e32 v24, v24, v62
	v_max_f32_e32 v24, 0xc3e00000, v24
	v_min_f32_e32 v25, 0x43e00000, v24
	s_nop 1
	v_mov_b32_dpp v37, v25 quad_perm:[1,0,3,2] row_mask:0xf bank_mask:0xf
	v_cvt_pk_fp8_f32 v24, v25, v37
	s_nop 1
	v_mov_b32_dpp v25, v24 quad_perm:[2,3,0,1] row_mask:0xf bank_mask:0xf
	s_and_saveexec_b64 s[4:5], vcc
	v_and_b32_e32 v24, 0xffff, v24
	v_lshl_or_b32 v24, v25, 16, v24
	global_store_dword v[34:35], v24, off offset:32
.LBB0_1162:
	s_or_b64 exec, exec, s[4:5]
	v_mul_f32_e32 v21, v21, v36
	v_mul_f32_e32 v21, v21, v61
	v_max_f32_e32 v21, 0xc3e00000, v21
	v_min_f32_e32 v24, 0x43e00000, v21
	s_nop 1
	v_mov_b32_dpp v25, v24 quad_perm:[1,0,3,2] row_mask:0xf bank_mask:0xf
	v_cvt_pk_fp8_f32 v21, v24, v25
	s_nop 1
	v_mov_b32_dpp v24, v21 quad_perm:[2,3,0,1] row_mask:0xf bank_mask:0xf
	s_and_saveexec_b64 s[4:5], vcc
	v_and_b32_e32 v21, 0xffff, v21
	v_lshl_or_b32 v21, v24, 16, v21
	global_store_dword v[34:35], v21, off offset:64
.LBB0_1164:
	s_or_b64 exec, exec, s[4:5]
	v_mul_f32_e32 v20, v20, v36
	v_mul_f32_e32 v20, v20, v2
	v_max_f32_e32 v20, 0xc3e00000, v20
	v_min_f32_e32 v21, 0x43e00000, v20
	s_nop 1
	v_mov_b32_dpp v24, v21 quad_perm:[1,0,3,2] row_mask:0xf bank_mask:0xf
	v_cvt_pk_fp8_f32 v20, v21, v24
	s_nop 1
	v_mov_b32_dpp v21, v20 quad_perm:[2,3,0,1] row_mask:0xf bank_mask:0xf
	s_and_saveexec_b64 s[4:5], vcc
	v_and_b32_e32 v20, 0xffff, v20
	v_lshl_or_b32 v20, v21, 16, v20
	global_store_dword v[34:35], v20, off offset:96
; __device__ __forceinline__ int crow(int r, int hi) { return (r & 3) + 8 * (r >> 2) + 4 * hi; }
; __device__ __forceinline__ void store_quad8(unsigned char* p, float v, int r32) {
;     v = fminf(fmaxf(v, -448.f), 448.f);
;     const float v1 = swz_xor<1>(v);
;     const int w = __builtin_amdgcn_cvt_pk_fp8_f32(v, v1, 0, false);
;     const int w2 = __builtin_amdgcn_ds_swizzle(w, (2 << 10) | 0x1f);
;     if ((r32 & 3) == 0) *(unsigned*)p = ((unsigned)w & 0xffffu) | ((unsigned)w2 << 16);
; }
;     __device__ __forceinline__ void operator()(f32x16 (&o)[4], const float (&rli)[16], int wid, int lane, int r32, int hi) const {
;     ...
;             for (int r = 0; r < 16; ++r) { float s = 0.f;
; #pragma unroll
;                 for (int d0 = 0; d0 < 4; ++d0) { const float v = o[d0][r] * rli[r]; o[d0][r] = v; s += v * v; }
;                 s = half_sum(s); rn[r] = rsqrtf(s * (1.0f / 128.0f) + 1e-5f); }
;             float g[4];
; #pragma unroll
;             for (int d0 = 0; d0 < 4; ++d0) g[d0] = gain[d0 * 32 + r32];
; #pragma unroll
;             for (int r = 0; r < 16; ++r)
; #pragma unroll
;                 for (int d0 = 0; d0 < 4; ++d0) store_quad8(base + (size_t)crow(r, hi) * 4096 + d0 * 32 + r32, o[d0][r] * rn[r] * g[d0], r32);
.LBB0_1166:
	s_or_b64 exec, exec, s[4:5]
	v_pk_add_f32 v[20:21], v[28:29], v[30:31]
	s_nop 0
	v_pk_fma_f32 v[20:21], v[20:21], s[10:11], v[198:199] op_sel_hi:[1,0,0]
	s_nop 0
	v_mul_f32_e32 v24, 0x4b800000, v21
	v_cmp_gt_f32_e64 s[4:5], s53, v21
	s_nop 1
	v_cndmask_b32_e64 v21, v21, v24, s[4:5]
	v_rsq_f32_e32 v21, v21
	s_nop 0
	v_mul_f32_e32 v24, 0x45800000, v21
	v_cndmask_b32_e64 v21, v21, v24, s[4:5]
	v_mul_f32_e32 v24, v26, v21
	v_mul_f32_e32 v24, v24, v60
	v_max_f32_e32 v24, 0xc3e00000, v24
	v_min_f32_e32 v24, 0x43e00000, v24
	s_nop 1
	v_mov_b32_dpp v25, v24 quad_perm:[1,0,3,2] row_mask:0xf bank_mask:0xf
	v_cmp_gt_f32_e64 s[4:5], s53, v20
	v_cvt_pk_fp8_f32 v26, v24, v25
	v_add_u32_e32 v24, 24, v42
	v_ashrrev_i32_e32 v25, 31, v24
	v_lshlrev_b64 v[24:25], 12, v[24:25]
	s_nop 1
	v_mov_b32_dpp v28, v26 quad_perm:[2,3,0,1] row_mask:0xf bank_mask:0xf
	v_lshl_add_u64 v[24:25], v[32:33], 0, v[24:25]
	s_and_saveexec_b64 s[6:7], vcc
	v_and_b32_e32 v26, 0xffff, v26
	v_lshl_or_b32 v26, v28, 16, v26
	global_store_dword v[24:25], v26, off
.LBB0_1168:
	s_or_b64 exec, exec, s[6:7]
	v_mul_f32_e32 v26, v27, v21
	v_mul_f32_e32 v26, v26, v62
	v_max_f32_e32 v26, 0xc3e00000, v26
	v_min_f32_e32 v27, 0x43e00000, v26
	s_nop 1
	v_mov_b32_dpp v28, v27 quad_perm:[1,0,3,2] row_mask:0xf bank_mask:0xf
	v_cvt_pk_fp8_f32 v26, v27, v28
	s_nop 1
	v_mov_b32_dpp v27, v26 quad_perm:[2,3,0,1] row_mask:0xf bank_mask:0xf
	s_and_saveexec_b64 s[6:7], vcc
	v_and_b32_e32 v26, 0xffff, v26
	v_lshl_or_b32 v26, v27, 16, v26
	global_store_dword v[24:25], v26, off offset:32
.LBB0_1170:
	s_or_b64 exec, exec, s[6:7]
	v_mul_f32_e32 v23, v23, v21
	v_mul_f32_e32 v23, v23, v61
	v_max_f32_e32 v23, 0xc3e00000, v23
	v_min_f32_e32 v26, 0x43e00000, v23
	s_nop 1
	v_mov_b32_dpp v27, v26 quad_perm:[1,0,3,2] row_mask:0xf bank_mask:0xf
	v_cvt_pk_fp8_f32 v23, v26, v27
	s_nop 1
	v_mov_b32_dpp v26, v23 quad_perm:[2,3,0,1] row_mask:0xf bank_mask:0xf
	s_and_saveexec_b64 s[6:7], vcc
	v_and_b32_e32 v23, 0xffff, v23
	v_lshl_or_b32 v23, v26, 16, v23
	global_store_dword v[24:25], v23, off offset:64
.LBB0_1172:
	s_or_b64 exec, exec, s[6:7]
	v_mul_f32_e32 v21, v22, v21
	v_mul_f32_e32 v21, v21, v2
	v_max_f32_e32 v21, 0xc3e00000, v21
	v_min_f32_e32 v22, 0x43e00000, v21
	s_nop 1
	v_mov_b32_dpp v23, v22 quad_perm:[1,0,3,2] row_mask:0xf bank_mask:0xf
	v_cvt_pk_fp8_f32 v21, v22, v23
	s_nop 1
	v_mov_b32_dpp v22, v21 quad_perm:[2,3,0,1] row_mask:0xf bank_mask:0xf
	s_and_saveexec_b64 s[6:7], vcc
	v_and_b32_e32 v21, 0xffff, v21
	v_lshl_or_b32 v21, v22, 16, v21
	global_store_dword v[24:25], v21, off offset:96
.LBB0_1174:
	s_or_b64 exec, exec, s[6:7]
	v_mul_f32_e32 v21, 0x4b800000, v20
	v_cndmask_b32_e64 v20, v20, v21, s[4:5]
	v_rsq_f32_e32 v20, v20
	s_nop 0
	v_mul_f32_e32 v21, 0x45800000, v20
	v_cndmask_b32_e64 v22, v20, v21, s[4:5]
	v_mul_f32_e32 v14, v14, v22
	v_mul_f32_e32 v14, v14, v60
	v_max_f32_e32 v14, 0xc3e00000, v14
	v_min_f32_e32 v23, 0x43e00000, v14
	s_nop 1
	v_mov_b32_dpp v24, v23 quad_perm:[1,0,3,2] row_mask:0xf bank_mask:0xf
	v_add_u32_e32 v20, 25, v42
	v_ashrrev_i32_e32 v21, 31, v20
	v_lshlrev_b64 v[20:21], 12, v[20:21]
	v_cvt_pk_fp8_f32 v14, v23, v24
	v_lshl_add_u64 v[20:21], v[32:33], 0, v[20:21]
	s_nop 1
	v_mov_b32_dpp v23, v14 quad_perm:[2,3,0,1] row_mask:0xf bank_mask:0xf
	s_and_saveexec_b64 s[4:5], vcc
	v_and_b32_e32 v14, 0xffff, v14
	v_lshl_or_b32 v14, v23, 16, v14
	global_store_dword v[20:21], v14, off
.LBB0_1176:
	s_or_b64 exec, exec, s[4:5]
	v_mul_f32_e32 v14, v15, v22
	v_mul_f32_e32 v14, v14, v62
	v_max_f32_e32 v14, 0xc3e00000, v14
	v_min_f32_e32 v15, 0x43e00000, v14
	s_nop 1
	v_mov_b32_dpp v23, v15 quad_perm:[1,0,3,2] row_mask:0xf bank_mask:0xf
	v_cvt_pk_fp8_f32 v14, v15, v23
	s_nop 1
	v_mov_b32_dpp v15, v14 quad_perm:[2,3,0,1] row_mask:0xf bank_mask:0xf
	s_and_saveexec_b64 s[4:5], vcc
	v_and_b32_e32 v14, 0xffff, v14
	v_lshl_or_b32 v14, v15, 16, v14
	global_store_dword v[20:21], v14, off offset:32
.LBB0_1178:
	s_or_b64 exec, exec, s[4:5]
	v_mul_f32_e32 v13, v13, v22
	v_mul_f32_e32 v13, v13, v61
	v_max_f32_e32 v13, 0xc3e00000, v13
	v_min_f32_e32 v14, 0x43e00000, v13
	s_nop 1
	v_mov_b32_dpp v15, v14 quad_perm:[1,0,3,2] row_mask:0xf bank_mask:0xf
	v_cvt_pk_fp8_f32 v13, v14, v15
	s_nop 1
	v_mov_b32_dpp v14, v13 quad_perm:[2,3,0,1] row_mask:0xf bank_mask:0xf
	s_and_saveexec_b64 s[4:5], vcc
	v_and_b32_e32 v13, 0xffff, v13
	v_lshl_or_b32 v13, v14, 16, v13
	global_store_dword v[20:21], v13, off offset:64
.LBB0_1180:
	s_or_b64 exec, exec, s[4:5]
	v_mul_f32_e32 v12, v12, v22
	v_mul_f32_e32 v12, v12, v2
	v_max_f32_e32 v12, 0xc3e00000, v12
	v_min_f32_e32 v13, 0x43e00000, v12
	s_nop 1
	v_mov_b32_dpp v14, v13 quad_perm:[1,0,3,2] row_mask:0xf bank_mask:0xf
	v_cvt_pk_fp8_f32 v12, v13, v14
	s_nop 1
	v_mov_b32_dpp v13, v12 quad_perm:[2,3,0,1] row_mask:0xf bank_mask:0xf
	s_and_saveexec_b64 s[4:5], vcc
	v_and_b32_e32 v12, 0xffff, v12
	v_lshl_or_b32 v12, v13, 16, v12
	global_store_dword v[20:21], v12, off offset:96
; __device__ __forceinline__ int crow(int r, int hi) { return (r & 3) + 8 * (r >> 2) + 4 * hi; }
; __device__ __forceinline__ void store_quad8(unsigned char* p, float v, int r32) {
;     v = fminf(fmaxf(v, -448.f), 448.f);
;     const float v1 = swz_xor<1>(v);
;     const int w = __builtin_amdgcn_cvt_pk_fp8_f32(v, v1, 0, false);
;     const int w2 = __builtin_amdgcn_ds_swizzle(w, (2 << 10) | 0x1f);
;     if ((r32 & 3) == 0) *(unsigned*)p = ((unsigned)w & 0xffffu) | ((unsigned)w2 << 16);
; }
;     __device__ __forceinline__ void operator()(f32x16 (&o)[4], const float (&rli)[16], int wid, int lane, int r32, int hi) const {
;     ...
;             for (int r = 0; r < 16; ++r) { float s = 0.f;
; #pragma unroll
;                 for (int d0 = 0; d0 < 4; ++d0) { const float v = o[d0][r] * rli[r]; o[d0][r] = v; s += v * v; }
;                 s = half_sum(s); rn[r] = rsqrtf(s * (1.0f / 128.0f) + 1e-5f); }
;             float g[4];
; #pragma unroll
;             for (int d0 = 0; d0 < 4; ++d0) g[d0] = gain[d0 * 32 + r32];
; #pragma unroll
;             for (int r = 0; r < 16; ++r)
; #pragma unroll
;                 for (int d0 = 0; d0 < 4; ++d0) store_quad8(base + (size_t)crow(r, hi) * 4096 + d0 * 32 + r32, o[d0][r] * rn[r] * g[d0], r32);
.LBB0_1182:
	s_or_b64 exec, exec, s[4:5]
	v_pk_add_f32 v[12:13], v[16:17], v[18:19]
	s_nop 0
	v_pk_fma_f32 v[12:13], v[12:13], s[10:11], v[198:199] op_sel_hi:[1,0,0]
	s_nop 0
	v_mul_f32_e32 v14, 0x4b800000, v13
	v_cmp_gt_f32_e64 s[4:5], s53, v13
	s_nop 1
	v_cndmask_b32_e64 v13, v13, v14, s[4:5]
	v_rsq_f32_e32 v13, v13
	s_nop 0
	v_mul_f32_e32 v14, 0x45800000, v13
	v_cndmask_b32_e64 v13, v13, v14, s[4:5]
	v_mul_f32_e32 v10, v10, v13
	v_mul_f32_e32 v10, v60, v10
	v_max_f32_e32 v10, 0xc3e00000, v10
	v_min_f32_e32 v14, 0x43e00000, v10
	s_nop 1
	v_mov_b32_dpp v15, v14 quad_perm:[1,0,3,2] row_mask:0xf bank_mask:0xf
	v_cmp_gt_f32_e64 s[4:5], s53, v12
	v_cvt_pk_fp8_f32 v10, v14, v15
	v_add_u32_e32 v14, 26, v42
	v_ashrrev_i32_e32 v15, 31, v14
	v_lshlrev_b64 v[14:15], 12, v[14:15]
	s_nop 1
	v_mov_b32_dpp v16, v10 quad_perm:[2,3,0,1] row_mask:0xf bank_mask:0xf
	v_lshl_add_u64 v[14:15], v[32:33], 0, v[14:15]
	s_and_saveexec_b64 s[6:7], vcc
	v_and_b32_e32 v10, 0xffff, v10
	v_lshl_or_b32 v10, v16, 16, v10
	global_store_dword v[14:15], v10, off
.LBB0_1184:
	s_or_b64 exec, exec, s[6:7]
	v_mul_f32_e32 v10, v11, v13
	v_mul_f32_e32 v10, v62, v10
	v_max_f32_e32 v10, 0xc3e00000, v10
	v_min_f32_e32 v11, 0x43e00000, v10
	s_nop 1
	v_mov_b32_dpp v16, v11 quad_perm:[1,0,3,2] row_mask:0xf bank_mask:0xf
	v_cvt_pk_fp8_f32 v10, v11, v16
	s_nop 1
	v_mov_b32_dpp v11, v10 quad_perm:[2,3,0,1] row_mask:0xf bank_mask:0xf
	s_and_saveexec_b64 s[6:7], vcc
	v_and_b32_e32 v10, 0xffff, v10
	v_lshl_or_b32 v10, v11, 16, v10
	global_store_dword v[14:15], v10, off offset:32
.LBB0_1186:
	s_or_b64 exec, exec, s[6:7]
	v_mul_f32_e32 v9, v9, v13
	v_mul_f32_e32 v9, v61, v9
	v_max_f32_e32 v9, 0xc3e00000, v9
	v_min_f32_e32 v10, 0x43e00000, v9
	s_nop 1
	v_mov_b32_dpp v11, v10 quad_perm:[1,0,3,2] row_mask:0xf bank_mask:0xf
	v_cvt_pk_fp8_f32 v9, v10, v11
	s_nop 1
	v_mov_b32_dpp v10, v9 quad_perm:[2,3,0,1] row_mask:0xf bank_mask:0xf
	s_and_saveexec_b64 s[6:7], vcc
	v_and_b32_e32 v9, 0xffff, v9
	v_lshl_or_b32 v9, v10, 16, v9
	global_store_dword v[14:15], v9, off offset:64
.LBB0_1188:
	s_or_b64 exec, exec, s[6:7]
	v_mul_f32_e32 v8, v8, v13
	v_mul_f32_e32 v8, v2, v8
	v_max_f32_e32 v8, 0xc3e00000, v8
	v_min_f32_e32 v9, 0x43e00000, v8
	s_nop 1
	v_mov_b32_dpp v10, v9 quad_perm:[1,0,3,2] row_mask:0xf bank_mask:0xf
	v_cvt_pk_fp8_f32 v8, v9, v10
	s_nop 1
	v_mov_b32_dpp v9, v8 quad_perm:[2,3,0,1] row_mask:0xf bank_mask:0xf
	s_and_saveexec_b64 s[6:7], vcc
	v_and_b32_e32 v8, 0xffff, v8
	v_lshl_or_b32 v8, v9, 16, v8
	global_store_dword v[14:15], v8, off offset:96
.LBB0_1190:
	s_or_b64 exec, exec, s[6:7]
	v_mul_f32_e32 v8, 0x4b800000, v12
	v_cndmask_b32_e64 v8, v12, v8, s[4:5]
	v_rsq_f32_e32 v8, v8
	v_mul_f32_e32 v9, 0x45800000, v8
	v_cndmask_b32_e64 v10, v8, v9, s[4:5]
	v_mul_f32_e32 v6, v6, v10
	v_mul_f32_e32 v6, v60, v6
	v_max_f32_e32 v6, 0xc3e00000, v6
	v_min_f32_e32 v8, 0x43e00000, v6
	s_nop 1
	v_mov_b32_dpp v9, v8 quad_perm:[1,0,3,2] row_mask:0xf bank_mask:0xf
	v_cvt_pk_fp8_f32 v6, v8, v9
	v_add_u32_e32 v8, 27, v42
	v_ashrrev_i32_e32 v9, 31, v8
	v_lshlrev_b64 v[8:9], 12, v[8:9]
	s_nop 1
	v_mov_b32_dpp v11, v6 quad_perm:[2,3,0,1] row_mask:0xf bank_mask:0xf
	v_lshl_add_u64 v[8:9], v[32:33], 0, v[8:9]
	s_and_saveexec_b64 s[4:5], vcc
	v_and_b32_e32 v6, 0xffff, v6
	v_lshl_or_b32 v6, v11, 16, v6
	global_store_dword v[8:9], v6, off
.LBB0_1192:
	s_or_b64 exec, exec, s[4:5]
	v_mul_f32_e32 v6, v7, v10
	v_mul_f32_e32 v6, v62, v6
	v_max_f32_e32 v6, 0xc3e00000, v6
	v_min_f32_e32 v7, 0x43e00000, v6
	s_nop 1
	v_mov_b32_dpp v11, v7 quad_perm:[1,0,3,2] row_mask:0xf bank_mask:0xf
	v_cvt_pk_fp8_f32 v6, v7, v11
	s_nop 1
	v_mov_b32_dpp v7, v6 quad_perm:[2,3,0,1] row_mask:0xf bank_mask:0xf
	s_and_saveexec_b64 s[4:5], vcc
	v_and_b32_e32 v6, 0xffff, v6
	v_lshl_or_b32 v6, v7, 16, v6
	global_store_dword v[8:9], v6, off offset:32
.LBB0_1194:
	s_or_b64 exec, exec, s[4:5]
	v_mul_f32_e32 v5, v5, v10
	v_mul_f32_e32 v5, v61, v5
	v_max_f32_e32 v5, 0xc3e00000, v5
	v_min_f32_e32 v6, 0x43e00000, v5
	s_nop 1
	v_mov_b32_dpp v7, v6 quad_perm:[1,0,3,2] row_mask:0xf bank_mask:0xf
	v_cvt_pk_fp8_f32 v5, v6, v7
	s_nop 1
	v_mov_b32_dpp v6, v5 quad_perm:[2,3,0,1] row_mask:0xf bank_mask:0xf
	s_and_saveexec_b64 s[4:5], vcc
	v_and_b32_e32 v5, 0xffff, v5
	v_lshl_or_b32 v5, v6, 16, v5
	global_store_dword v[8:9], v5, off offset:64
.LBB0_1196:
	s_or_b64 exec, exec, s[4:5]
	v_mul_f32_e32 v4, v4, v10
	v_mul_f32_e32 v2, v2, v4
	v_max_f32_e32 v2, 0xc3e00000, v2
	v_min_f32_e32 v4, 0x43e00000, v2
	s_nop 1
	v_mov_b32_dpp v5, v4 quad_perm:[1,0,3,2] row_mask:0xf bank_mask:0xf
	v_cvt_pk_fp8_f32 v2, v4, v5
	s_nop 1
	v_mov_b32_dpp v4, v2 quad_perm:[2,3,0,1] row_mask:0xf bank_mask:0xf
	s_and_saveexec_b64 s[4:5], vcc
	v_and_b32_e32 v2, 0xffff, v2
	v_lshl_or_b32 v2, v4, 16, v2
	global_store_dword v[8:9], v2, off offset:96
.LBB0_1198:
	s_or_b64 exec, exec, s[4:5]
	s_mov_b64 s[4:5], 0
	s_barrier

; #define WBAR() do { asm volatile("s_waitcnt vmcnt(0) lgkmcnt(0)" ::: "memory"); __builtin_amdgcn_s_barrier(); asm volatile("" ::: "memory"); } while (0)
; #define WSTEP_L(t, PAR) do { const bool more_ = (t) + 1 < NT; if (more_) WLOADK(((t) + 1) * KVBLK, 1 - PAR); WQKSM(t, PAR); WBARN(more_, 1); if (more_) WLOADV(((t) + 1) * KVBLK, 1 - PAR); WPV(PAR); WBARN(more_, 4); } while (0)
; #define WSTEP_T(t, PAR) do { const bool more_ = (t) + 1 < NT; if (more_) WLOADK(((t) + 1) * KVBLK, 1 - PAR); if ((t) > 0) WPV(1 - PAR); WBARN(more_, 1); if (more_) WLOADV(((t) + 1) * KVBLK, 1 - PAR); WQKSM(t, PAR); WBARN(more_, 4); } while (0)
; #define WBAR() do { asm volatile("s_waitcnt vmcnt(0) lgkmcnt(0)" ::: "memory"); __builtin_amdgcn_s_barrier(); asm volatile("" ::: "memory"); } while (0)
; #define WSTEP_L(t, PAR) do { const bool more_ = (t) + 1 < NT; if (more_) WLOADK((t) + 1, 1 - PAR); WQKSM(t, PAR); WBARN(more_, 1); if (more_) WLOADV((t) + 1, 1 - PAR); WPV(PAR); WBARN(more_, 2); } while (0)
; #define WSTEP_T(t, PAR) do { const bool more_ = (t) + 1 < NT; if (more_) WLOADK((t) + 1, 1 - PAR); if ((t) > 0) WPV(1 - PAR); WBARN(more_, 1); if (more_) WLOADV((t) + 1, 1 - PAR); WQKSM(t, PAR); WBARN(more_, 2); } while (0)
; template <class Epi>
; __device__ __forceinline__ void block_wide8(const BlockRef& cur, const bf16* V2, int skv, char* lds, Seam& S, const Epi& E) {
;     ...
;         for (int t = 0; t < NT; t += 2) { WSTEP_L(t, 0); WSTEP_L(t + 1, 1); }
;         WBAR();
;     ...
;     } else {
;     ...
;         for (int t = 0; t < NT; t += 2) { WSTEP_T(t, 0); WSTEP_T(t + 1, 1); }
.Lw8_last_0:
	s_waitcnt vmcnt(0) lgkmcnt(0)
	s_mov_b64 s[6:7], 0
	s_branch .LBB0_1223
.Lw8_last_1:
	s_waitcnt vmcnt(0) lgkmcnt(0)
	s_mov_b64 s[8:9], 0
	s_branch .LBB0_1229

;     ...
;     constexpr float SCL = SCALE / (float)(1 << SH), C2 = 1.4426950408889634f * SCL;
;     if (__builtin_expect(__all((pmax - m_reg) * SCL <= (float)THRI), 1)) { mn = m_reg; alpha = 1.f; }
;     else { mn = fmaxf(m_reg, pmax); alpha = __builtin_amdgcn_exp2f((m_reg - mn) * C2); m_reg = mn; }
;     const float mnL = dead ? -__builtin_inff() : -mn * C2 + (float)PSH;
;     for (int r = 0; r < 16; ++r) p0[r] = fmaf(p0[r], C2, mnL); for (int r = 0; r < 16; ++r) p1[r] = fmaf(p1[r], C2, mnL);
;     for (int r = 0; r < 16; ++r) p0[r] = __builtin_amdgcn_exp2f(p0[r]);
.LBB0_1219:
	v_cndmask_b32_e64 v241, v242, v241, s[6:7]
	v_fmamk_f32 v194, v241, 0xba0293ee, v1
	v_fmamk_f32 v4, v162, 0x3a0293ee, v194
	v_fmamk_f32 v5, v163, 0x3a0293ee, v194
	v_fmamk_f32 v6, v164, 0x3a0293ee, v194
	v_fmamk_f32 v7, v165, 0x3a0293ee, v194
	v_fmamk_f32 v164, v172, 0x3a0293ee, v194
	v_fmamk_f32 v165, v173, 0x3a0293ee, v194
	v_fmamk_f32 v146, v146, 0x3a0293ee, v194
	v_fmamk_f32 v147, v147, 0x3a0293ee, v194
	v_fmamk_f32 v148, v148, 0x3a0293ee, v194
	v_fmamk_f32 v149, v149, 0x3a0293ee, v194
	v_fmamk_f32 v8, v166, 0x3a0293ee, v194
	v_fmamk_f32 v11, v168, 0x3a0293ee, v194
	v_fmamk_f32 v13, v169, 0x3a0293ee, v194
	v_fmamk_f32 v162, v170, 0x3a0293ee, v194
	v_fmamk_f32 v168, v176, 0x3a0293ee, v194
	v_fmamk_f32 v169, v177, 0x3a0293ee, v194
	v_fmamk_f32 v170, v150, 0x3a0293ee, v194
	v_fmamk_f32 v152, v152, 0x3a0293ee, v194
	v_fmamk_f32 v172, v154, 0x3a0293ee, v194
	v_fmamk_f32 v173, v155, 0x3a0293ee, v194
	v_fmamk_f32 v176, v158, 0x3a0293ee, v194
	v_fmamk_f32 v177, v159, 0x3a0293ee, v194
	v_exp_f32_e32 v154, v4
	v_exp_f32_e32 v155, v5
	v_exp_f32_e32 v10, v6
	v_exp_f32_e32 v12, v7
	v_exp_f32_e32 v4, v164
	v_exp_f32_e32 v5, v165
	v_exp_f32_e32 v164, v146
	v_exp_f32_e32 v165, v147
	v_exp_f32_e32 v158, v148
	v_exp_f32_e32 v159, v149
	v_fmamk_f32 v9, v167, 0x3a0293ee, v194
	v_fmamk_f32 v163, v171, 0x3a0293ee, v194
	v_fmamk_f32 v171, v151, 0x3a0293ee, v194
	v_fmamk_f32 v153, v153, 0x3a0293ee, v194
	v_fmamk_f32 v195, v160, 0x3a0293ee, v194
	v_exp_f32_e32 v150, v8
	v_exp_f32_e32 v14, v11
	v_exp_f32_e32 v11, v162
	v_exp_f32_e32 v162, v170
	v_exp_f32_e32 v160, v152
	v_fmamk_f32 v166, v174, 0x3a0293ee, v194
	v_fmamk_f32 v167, v175, 0x3a0293ee, v194
	v_fmamk_f32 v174, v156, 0x3a0293ee, v194
	v_fmamk_f32 v175, v157, 0x3a0293ee, v194
	v_fmac_f32_e32 v194, 0x3a0293ee, v161
	v_exp_f32_e32 v151, v9
	v_exp_f32_e32 v15, v13
	v_exp_f32_e32 v13, v163
	v_exp_f32_e32 v163, v171
	v_exp_f32_e32 v161, v153
	v_exp_f32_e32 v156, v172
	v_exp_f32_e32 v146, v174
	v_exp_f32_e32 v8, v166
	v_exp_f32_e32 v9, v167
	v_exp_f32_e32 v6, v168
	v_exp_f32_e32 v7, v169
	v_exp_f32_e32 v157, v173
	v_exp_f32_e32 v147, v175
	v_exp_f32_e32 v152, v176
	v_exp_f32_e32 v148, v195
	v_exp_f32_e32 v153, v177
	v_exp_f32_e32 v149, v194
	s_setprio 0
	s_mov_b64 s[6:7], -1
	s_and_b64 vcc, exec, s[70:71]
	s_cbranch_vccnz .Lw8_last_0
	s_waitcnt vmcnt(2) lgkmcnt(0)

; __device__ __forceinline__ void finishSM8(f32x16& p0, f32x16& p1, float alpha, float& l_reg, i32x8& pa) {
;     for (int r = 0; r < 16; ++r) p1[r] = __builtin_amdgcn_exp2f(p1[r]);
;     float ps;
;     { float s0 = p0[0] + p0[1], s1 = p0[2] + p0[3], s2 = p1[0] + p1[1], s3 = p1[2] + p1[3];
; #pragma unroll
;       for (int r = 4; r < 16; r += 4) { s0 += p0[r]; s0 += p0[r + 1]; s1 += p0[r + 2]; s1 += p0[r + 3]; s2 += p1[r]; s2 += p1[r + 1]; s3 += p1[r + 2]; s3 += p1[r + 3]; }
;       ps = (s0 + s1) + (s2 + s3); }
;     { auto rr = __builtin_amdgcn_permlane32_swap(__float_as_uint(ps), __float_as_uint(ps), false, false);
;       ps = __uint_as_float(rr[0]) + __uint_as_float(rr[1]); }
;     l_reg = l_reg * alpha + ps;
; #pragma unroll
;     for (int d = 0; d < 4; ++d) { int w0 = 0, w1 = 0;
;         w0 = __builtin_amdgcn_cvt_pk_fp8_f32(p0[4 * d], p0[4 * d + 1], w0, false); w0 = __builtin_amdgcn_cvt_pk_fp8_f32(p0[4 * d + 2], p0[4 * d + 3], w0, true);
;         w1 = __builtin_amdgcn_cvt_pk_fp8_f32(p1[4 * d], p1[4 * d + 1], w1, false); w1 = __builtin_amdgcn_cvt_pk_fp8_f32(p1[4 * d + 2], p1[4 * d + 3], w1, true);
;         pa[d] = w0; pa[4 + d] = w1; }
; }
.LBB0_1225:
	v_add_f32_e32 v166, v154, v155
	v_add_f32_e32 v167, v10, v12
	v_add_f32_e32 v168, v164, v165
	v_add_f32_e32 v169, v158, v159
	v_add_f32_e32 v166, v150, v166
	v_add_f32_e32 v167, v14, v167
	v_add_f32_e32 v168, v162, v168
	v_add_f32_e32 v169, v160, v169
	v_add_f32_e32 v166, v151, v166
	v_add_f32_e32 v167, v15, v167
	v_add_f32_e32 v168, v163, v168
	v_add_f32_e32 v169, v161, v169
	v_add_f32_e32 v166, v11, v166
	v_add_f32_e32 v167, v4, v167
	v_add_f32_e32 v168, v156, v168
	v_add_f32_e32 v169, v146, v169
	v_add_f32_e32 v166, v13, v166
	v_add_f32_e32 v167, v5, v167
	v_add_f32_e32 v168, v157, v168
	v_add_f32_e32 v169, v147, v169
	v_add_f32_e32 v166, v8, v166
	v_add_f32_e32 v167, v6, v167
	v_add_f32_e32 v168, v152, v168
	v_add_f32_e32 v169, v148, v169
	v_add_f32_e32 v166, v9, v166
	v_add_f32_e32 v167, v7, v167
	v_add_f32_e32 v168, v153, v168
	v_add_f32_e32 v169, v149, v169
	v_add_f32_e32 v166, v167, v166
	v_add_f32_e32 v167, v168, v169
	v_add_f32_e32 v242, v167, v166
	v_mov_b32_e32 v243, v242
	s_nop 1
	v_permlane32_swap_b32_e32 v242, v243
	v_cvt_pk_fp8_f32 v166, v154, v155
	v_cvt_pk_fp8_f32 v170, v164, v165
	v_cvt_pk_fp8_f32 v167, v150, v151
	v_cvt_pk_fp8_f32 v171, v162, v163
	v_cvt_pk_fp8_f32 v168, v11, v13
	v_cvt_pk_fp8_f32 v172, v156, v157
	v_cvt_pk_fp8_f32 v169, v8, v9
	v_cvt_pk_fp8_f32 v173, v152, v153
	v_cvt_pk_fp8_f32 v166, v10, v12 op_sel:[0,0,1]
	v_cvt_pk_fp8_f32 v170, v158, v159 op_sel:[0,0,1]
	v_cvt_pk_fp8_f32 v167, v14, v15 op_sel:[0,0,1]
	v_cvt_pk_fp8_f32 v171, v160, v161 op_sel:[0,0,1]
	v_cvt_pk_fp8_f32 v168, v4, v5 op_sel:[0,0,1]
	v_cvt_pk_fp8_f32 v172, v146, v147 op_sel:[0,0,1]
	v_cvt_pk_fp8_f32 v169, v6, v7 op_sel:[0,0,1]
	v_cvt_pk_fp8_f32 v173, v148, v149 op_sel:[0,0,1]
	ds_read_b128 v[4:7], v203
	ds_read_b128 v[146:149], v203 offset:2048
	ds_read_b128 v[8:11], v214
	ds_read_b128 v[150:153], v214 offset:2048
	s_waitcnt lgkmcnt(0)
	v_mfma_f32_32x32x64_f8f6f4 v[130:145], v[166:173], v[4:11], v[130:145]
	ds_read_b128 v[4:7], v203 offset:4096
	ds_read_b128 v[8:11], v214 offset:4096
	v_mfma_f32_32x32x64_f8f6f4 v[114:129], v[166:173], v[146:153], v[114:129]
	ds_read_b128 v[146:149], v203 offset:6144
	ds_read_b128 v[150:153], v214 offset:6144
	s_waitcnt lgkmcnt(0)
	v_mfma_f32_32x32x64_f8f6f4 v[98:113], v[166:173], v[4:11], v[98:113]
	ds_read_b128 v[4:7], v203 offset:16384
	ds_read_b128 v[8:11], v214 offset:16384
	v_mfma_f32_32x32x64_f8f6f4 v[82:97], v[166:173], v[146:153], v[82:97]
	ds_read_b128 v[146:149], v203 offset:18432
	ds_read_b128 v[150:153], v214 offset:18432
	s_waitcnt lgkmcnt(0)
	v_mfma_f32_32x32x64_f8f6f4 v[66:81], v[166:173], v[4:11], v[66:81]
	ds_read_b128 v[4:7], v203 offset:20480
	ds_read_b128 v[8:11], v214 offset:20480
	v_mfma_f32_32x32x64_f8f6f4 v[50:65], v[166:173], v[146:153], v[50:65]
	ds_read_b128 v[146:149], v203 offset:22528
	ds_read_b128 v[150:153], v214 offset:22528
	s_waitcnt lgkmcnt(0)
	v_mfma_f32_32x32x64_f8f6f4 v[34:49], v[166:173], v[4:11], v[34:49]
	v_mfma_f32_32x32x64_f8f6f4 v[18:33], v[166:173], v[146:153], v[18:33]
	s_nop 15
	s_nop 15
	s_mov_b64 s[8:9], -1
	s_and_b64 vcc, exec, s[70:71]
	s_cbranch_vccnz .Lw8_last_1
	s_waitcnt vmcnt(1) lgkmcnt(0)

;     ...
;     constexpr float SCL = SCALE / (float)(1 << SH), C2 = 1.4426950408889634f * SCL;
;     if (__builtin_expect(__all((pmax - m_reg) * SCL <= (float)THRI), 1)) { mn = m_reg; alpha = 1.f; }
;     else { mn = fmaxf(m_reg, pmax); alpha = __builtin_amdgcn_exp2f((m_reg - mn) * C2); m_reg = mn; }
;     const float mnL = dead ? -__builtin_inff() : -mn * C2 + (float)PSH;
;     for (int r = 0; r < 16; ++r) p0[r] = fmaf(p0[r], C2, mnL); for (int r = 0; r < 16; ++r) p1[r] = fmaf(p1[r], C2, mnL);
;     for (int r = 0; r < 16; ++r) p0[r] = __builtin_amdgcn_exp2f(p0[r]);
.LBB0_1259:
	v_cndmask_b32_e64 v219, v16, v219, s[6:7]
	v_fmamk_f32 v16, v219, 0xba0293ee, v1
	v_fmamk_f32 v4, v162, 0x3a0293ee, v16
	v_fmamk_f32 v5, v163, 0x3a0293ee, v16
	v_fmamk_f32 v6, v164, 0x3a0293ee, v16
	v_fmamk_f32 v7, v165, 0x3a0293ee, v16
	v_fmamk_f32 v8, v166, 0x3a0293ee, v16
	v_fmamk_f32 v164, v173, 0x3a0293ee, v16
	v_fmamk_f32 v165, v174, 0x3a0293ee, v16
	v_fmamk_f32 v146, v146, 0x3a0293ee, v16
	v_fmamk_f32 v147, v147, 0x3a0293ee, v16
	v_fmamk_f32 v148, v148, 0x3a0293ee, v16
	v_fmamk_f32 v149, v149, 0x3a0293ee, v16
	v_fmamk_f32 v9, v167, 0x3a0293ee, v16
	v_fmamk_f32 v11, v168, 0x3a0293ee, v16
	v_fmamk_f32 v13, v169, 0x3a0293ee, v16
	v_fmamk_f32 v162, v171, 0x3a0293ee, v16
	v_fmamk_f32 v163, v172, 0x3a0293ee, v16
	v_fmamk_f32 v166, v175, 0x3a0293ee, v16
	v_fmamk_f32 v167, v176, 0x3a0293ee, v16
	v_fmamk_f32 v169, v150, 0x3a0293ee, v16
	v_fmamk_f32 v152, v152, 0x3a0293ee, v16
	v_fmamk_f32 v171, v154, 0x3a0293ee, v16
	v_fmamk_f32 v172, v155, 0x3a0293ee, v16
	v_fmamk_f32 v175, v158, 0x3a0293ee, v16
	v_fmamk_f32 v176, v159, 0x3a0293ee, v16
	v_exp_f32_e32 v154, v4
	v_exp_f32_e32 v155, v5
	v_exp_f32_e32 v10, v6
	v_exp_f32_e32 v12, v7
	v_exp_f32_e32 v150, v8
	v_exp_f32_e32 v5, v164
	v_exp_f32_e32 v8, v165
	v_exp_f32_e32 v164, v146
	v_exp_f32_e32 v165, v147
	v_exp_f32_e32 v158, v148
	v_exp_f32_e32 v159, v149
	v_fmamk_f32 v17, v170, 0x3a0293ee, v16
	v_fmamk_f32 v168, v177, 0x3a0293ee, v16
	v_fmamk_f32 v170, v151, 0x3a0293ee, v16
	v_fmamk_f32 v153, v153, 0x3a0293ee, v16
	v_fmamk_f32 v177, v160, 0x3a0293ee, v16
	v_exp_f32_e32 v14, v11
	v_exp_f32_e32 v15, v13
	v_exp_f32_e32 v13, v162
	v_exp_f32_e32 v162, v169
	v_exp_f32_e32 v160, v152
	v_fmamk_f32 v173, v156, 0x3a0293ee, v16
	v_fmamk_f32 v174, v157, 0x3a0293ee, v16
	v_fmac_f32_e32 v16, 0x3a0293ee, v161
	v_exp_f32_e32 v151, v9
	v_exp_f32_e32 v4, v163
	v_exp_f32_e32 v163, v170
	v_exp_f32_e32 v161, v153
	v_exp_f32_e32 v11, v17
	v_exp_f32_e32 v156, v171
	v_exp_f32_e32 v146, v173
	v_exp_f32_e32 v9, v166
	v_exp_f32_e32 v6, v167
	v_exp_f32_e32 v157, v172
	v_exp_f32_e32 v147, v174
	v_exp_f32_e32 v149, v16
	v_exp_f32_e32 v152, v175
	v_exp_f32_e32 v148, v177
	v_exp_f32_e32 v7, v168
	v_exp_f32_e32 v153, v176
	s_setprio 0
	s_mov_b64 s[6:7], -1
	s_and_b64 vcc, exec, s[70:71]
	s_cbranch_vccnz .Lw8_last_2
	s_waitcnt vmcnt(1) lgkmcnt(0)

; __device__ __forceinline__ void finishSM8(f32x16& p0, f32x16& p1, float alpha, float& l_reg, i32x8& pa) {
;     for (int r = 0; r < 16; ++r) p1[r] = __builtin_amdgcn_exp2f(p1[r]);
;     float ps;
;     { float s0 = p0[0] + p0[1], s1 = p0[2] + p0[3], s2 = p1[0] + p1[1], s3 = p1[2] + p1[3];
; #pragma unroll
;       for (int r = 4; r < 16; r += 4) { s0 += p0[r]; s0 += p0[r + 1]; s1 += p0[r + 2]; s1 += p0[r + 3]; s2 += p1[r]; s2 += p1[r + 1]; s3 += p1[r + 2]; s3 += p1[r + 3]; }
;       ps = (s0 + s1) + (s2 + s3); }
;     { auto rr = __builtin_amdgcn_permlane32_swap(__float_as_uint(ps), __float_as_uint(ps), false, false);
;       ps = __uint_as_float(rr[0]) + __uint_as_float(rr[1]); }
;     l_reg = l_reg * alpha + ps;
; #pragma unroll
;     for (int d = 0; d < 4; ++d) { int w0 = 0, w1 = 0;
;         w0 = __builtin_amdgcn_cvt_pk_fp8_f32(p0[4 * d], p0[4 * d + 1], w0, false); w0 = __builtin_amdgcn_cvt_pk_fp8_f32(p0[4 * d + 2], p0[4 * d + 3], w0, true);
;         w1 = __builtin_amdgcn_cvt_pk_fp8_f32(p1[4 * d], p1[4 * d + 1], w1, false); w1 = __builtin_amdgcn_cvt_pk_fp8_f32(p1[4 * d + 2], p1[4 * d + 3], w1, true);
;         pa[d] = w0; pa[4 + d] = w1; }
; }
.LBB0_1265:
	ds_read_b128 v[232:235], v203
	ds_read_b128 v[236:239], v214
	ds_read_b128 v[240:243], v203 offset:2048
	ds_read_b128 v[244:247], v214 offset:2048
	v_add_f32_e32 v254, v154, v155
	v_add_f32_e32 v255, v10, v12
	v_add_f32_e32 v166, v164, v165
	v_add_f32_e32 v167, v158, v159
	v_add_f32_e32 v254, v150, v254
	v_add_f32_e32 v255, v14, v255
	v_add_f32_e32 v166, v162, v166
	v_add_f32_e32 v167, v160, v167
	v_add_f32_e32 v254, v151, v254
	v_add_f32_e32 v255, v15, v255
	v_add_f32_e32 v166, v163, v166
	v_add_f32_e32 v167, v161, v167
	v_add_f32_e32 v254, v11, v254
	v_add_f32_e32 v255, v4, v255
	v_add_f32_e32 v166, v156, v166
	v_add_f32_e32 v167, v146, v167
	v_add_f32_e32 v254, v13, v254
	v_add_f32_e32 v255, v5, v255
	v_add_f32_e32 v166, v157, v166
	v_add_f32_e32 v167, v147, v167
	v_add_f32_e32 v254, v8, v254
	v_add_f32_e32 v255, v6, v255
	v_add_f32_e32 v166, v152, v166
	v_add_f32_e32 v167, v148, v167
	v_add_f32_e32 v254, v9, v254
	v_add_f32_e32 v255, v7, v255
	v_add_f32_e32 v166, v153, v166
	v_add_f32_e32 v167, v149, v167
	v_add_f32_e32 v254, v255, v254
	v_add_f32_e32 v255, v166, v167
	v_add_f32_e32 v217, v255, v254
	v_mov_b32_e32 v218, v217
	s_nop 1
	v_permlane32_swap_b32_e32 v217, v218
	v_cvt_pk_fp8_f32 v166, v154, v155
	v_cvt_pk_fp8_f32 v170, v164, v165
	v_cvt_pk_fp8_f32 v167, v150, v151
	v_cvt_pk_fp8_f32 v171, v162, v163
	v_cvt_pk_fp8_f32 v168, v11, v13
	v_cvt_pk_fp8_f32 v172, v156, v157
	v_cvt_pk_fp8_f32 v169, v8, v9
	v_cvt_pk_fp8_f32 v173, v152, v153
	v_cvt_pk_fp8_f32 v166, v10, v12 op_sel:[0,0,1]
	v_cvt_pk_fp8_f32 v170, v158, v159 op_sel:[0,0,1]
	v_cvt_pk_fp8_f32 v167, v14, v15 op_sel:[0,0,1]
	v_cvt_pk_fp8_f32 v171, v160, v161 op_sel:[0,0,1]
	v_cvt_pk_fp8_f32 v168, v4, v5 op_sel:[0,0,1]
	v_cvt_pk_fp8_f32 v172, v146, v147 op_sel:[0,0,1]
	v_cvt_pk_fp8_f32 v169, v6, v7 op_sel:[0,0,1]
	v_cvt_pk_fp8_f32 v173, v148, v149 op_sel:[0,0,1]
	ds_read_b128 v[4:7], v203 offset:4096
	ds_read_b128 v[8:11], v214 offset:4096
	ds_read_b128 v[146:149], v203 offset:6144
	ds_read_b128 v[150:153], v214 offset:6144
	s_waitcnt lgkmcnt(4)
	v_mfma_f32_32x32x64_f8f6f4 v[130:145], v[166:173], v[232:239], v[130:145]
	ds_read_b128 v[232:235], v203 offset:16384
	ds_read_b128 v[236:239], v214 offset:16384
	v_mfma_f32_32x32x64_f8f6f4 v[114:129], v[166:173], v[240:247], v[114:129]
	ds_read_b128 v[240:243], v203 offset:18432
	ds_read_b128 v[244:247], v214 offset:18432
	s_waitcnt lgkmcnt(4)
	v_mfma_f32_32x32x64_f8f6f4 v[98:113], v[166:173], v[4:11], v[98:113]
	ds_read_b128 v[4:7], v203 offset:20480
	ds_read_b128 v[8:11], v214 offset:20480
	v_mfma_f32_32x32x64_f8f6f4 v[82:97], v[166:173], v[146:153], v[82:97]
	ds_read_b128 v[146:149], v203 offset:22528
	ds_read_b128 v[150:153], v214 offset:22528
	s_waitcnt lgkmcnt(4)
	v_mfma_f32_32x32x64_f8f6f4 v[66:81], v[166:173], v[232:239], v[66:81]
	v_mfma_f32_32x32x64_f8f6f4 v[50:65], v[166:173], v[240:247], v[50:65]
	s_waitcnt lgkmcnt(0)
	v_mfma_f32_32x32x64_f8f6f4 v[34:49], v[166:173], v[4:11], v[34:49]
	v_mfma_f32_32x32x64_f8f6f4 v[18:33], v[166:173], v[146:153], v[18:33]
	s_nop 15
	s_nop 15
	s_mov_b64 s[6:7], -1
	s_and_b64 vcc, exec, s[70:71]
	s_cbranch_vccnz .Lw8_last_3
	s_waitcnt vmcnt(2) lgkmcnt(0)

;     ...
;     constexpr float SCL = SCALE / (float)(1 << SH), C2 = 1.4426950408889634f * SCL;
;     if (__builtin_expect(__all((pmax - m_reg) * SCL <= (float)THRI), 1)) { mn = m_reg; alpha = 1.f; }
;     else { mn = fmaxf(m_reg, pmax); alpha = __builtin_amdgcn_exp2f((m_reg - mn) * C2); m_reg = mn; }
;     const float mnL = dead ? -__builtin_inff() : -mn * C2 + (float)PSH;
;     for (int r = 0; r < 16; ++r) p0[r] = fmaf(p0[r], C2, mnL); for (int r = 0; r < 16; ++r) p1[r] = fmaf(p1[r], C2, mnL);
;     for (int r = 0; r < 16; ++r) p0[r] = __builtin_amdgcn_exp2f(p0[r]);
.LBB0_1277:
	v_cndmask_b32_e64 v219, v209, v219, s[6:7]
	v_fmamk_f32 v4, v219, 0xba0293ee, v1
	v_fmamk_f32 v5, v162, 0x3a0293ee, v4
	v_fmamk_f32 v6, v163, 0x3a0293ee, v4
	v_fmamk_f32 v7, v164, 0x3a0293ee, v4
	v_fmamk_f32 v8, v165, 0x3a0293ee, v4
	v_fmamk_f32 v9, v166, 0x3a0293ee, v4
	v_fmamk_f32 v10, v167, 0x3a0293ee, v4
	v_fmamk_f32 v11, v168, 0x3a0293ee, v4
	v_fmamk_f32 v13, v169, 0x3a0293ee, v4
	v_fmamk_f32 v15, v170, 0x3a0293ee, v4
	v_fmamk_f32 v166, v175, 0x3a0293ee, v4
	v_fmamk_f32 v167, v176, 0x3a0293ee, v4
	v_fmamk_f32 v169, v146, 0x3a0293ee, v4
	v_fmamk_f32 v170, v147, 0x3a0293ee, v4
	v_fmamk_f32 v148, v148, 0x3a0293ee, v4
	v_fmamk_f32 v149, v149, 0x3a0293ee, v4
	v_fmamk_f32 v162, v171, 0x3a0293ee, v4
	v_fmamk_f32 v163, v172, 0x3a0293ee, v4
	v_fmamk_f32 v164, v173, 0x3a0293ee, v4
	v_fmamk_f32 v165, v174, 0x3a0293ee, v4
	v_fmamk_f32 v168, v177, 0x3a0293ee, v4
	v_fmamk_f32 v150, v150, 0x3a0293ee, v4
	v_fmamk_f32 v151, v151, 0x3a0293ee, v4
	v_fmamk_f32 v171, v152, 0x3a0293ee, v4
	v_fmamk_f32 v172, v153, 0x3a0293ee, v4
	v_fmamk_f32 v154, v154, 0x3a0293ee, v4
	v_fmamk_f32 v155, v155, 0x3a0293ee, v4
	v_fmamk_f32 v173, v156, 0x3a0293ee, v4
	v_fmamk_f32 v174, v157, 0x3a0293ee, v4
	v_fmamk_f32 v175, v158, 0x3a0293ee, v4
	v_fmamk_f32 v176, v159, 0x3a0293ee, v4
	v_fmamk_f32 v177, v160, 0x3a0293ee, v4
	v_fmac_f32_e32 v4, 0x3a0293ee, v161
	v_exp_f32_e32 v156, v5
	v_exp_f32_e32 v157, v6
	v_exp_f32_e32 v12, v7
	v_exp_f32_e32 v14, v8
	v_exp_f32_e32 v146, v11
	v_exp_f32_e32 v11, v166
	v_exp_f32_e32 v8, v167
	v_exp_f32_e32 v166, v169
	v_exp_f32_e32 v167, v170
	v_exp_f32_e32 v160, v148
	v_exp_f32_e32 v161, v149
	v_exp_f32_e32 v152, v9
	v_exp_f32_e32 v147, v13
	v_exp_f32_e32 v13, v15
	v_exp_f32_e32 v15, v162
	v_exp_f32_e32 v7, v164
	v_exp_f32_e32 v164, v150
	v_exp_f32_e32 v162, v171
	v_exp_f32_e32 v153, v10
	v_exp_f32_e32 v6, v163
	v_exp_f32_e32 v10, v165
	v_exp_f32_e32 v165, v151
	v_exp_f32_e32 v163, v172
	v_exp_f32_e32 v158, v154
	v_exp_f32_e32 v148, v173
	v_exp_f32_e32 v9, v168
	v_exp_f32_e32 v159, v155
	v_exp_f32_e32 v149, v174
	v_exp_f32_e32 v151, v4
	v_exp_f32_e32 v154, v175
	v_exp_f32_e32 v150, v177
	v_exp_f32_e32 v155, v176
	s_setprio 0
	s_mov_b64 s[6:7], -1
	s_and_b64 vcc, exec, s[70:71]
	s_cbranch_vccnz .Lw8_last_4
	s_waitcnt vmcnt(1) lgkmcnt(0)

; #define SBAR() __builtin_amdgcn_sched_barrier(0)
; __device__ __forceinline__ int crow(int r, int hi) { return (r & 3) + 8 * (r >> 2) + 4 * hi; }
; __device__ __forceinline__ float mul_ns(float a, float b) { float r; asm("v_mul_f32 %0, %1, %2" : "=v"(r) : "v"(a), "v"(b)); return r; }
; __device__ __forceinline__ float fma_ns(float a, float b, float c) { float r; asm("v_fma_f32 %0, %1, %2, %3" : "=v"(r) : "v"(a), "v"(b), "v"(c)); return r; }
; template <class Epi>
; __device__ __forceinline__ void block_wide8(const BlockRef& cur, const bf16* V2, int skv, char* lds, Seam& S, const Epi& E) {
;     ...
;     if (hi == 0) li_l[r32] = l_reg; asm volatile("s_waitcnt lgkmcnt(0)" ::: "memory");
;     float rli[16];
; #pragma unroll
;     for (int r = 0; r < 16; ++r) rli[r] = __builtin_amdgcn_rcpf(li_l[crow(r, hi)]) * (1.0f / 16.0f);
;     __device__ __forceinline__ void operator()(f32x16 (&o)[8], const float (&rli)[16], int wid, int lane, int r32, int hi) const {
;     ...
;             unsigned char* base = out + (size_t)(wid * QBLK) * 4096; const unsigned uo = (unsigned)(hi * 4 * 4096 + r32);
;             const float nlam = -lam;
;             float rn[16];
; #pragma unroll
;             for (int rb = 0; rb < 16; rb += 4) { unsigned tw[4][4];
; #pragma unroll
;                 for (int q = 0; q < 4; ++q)
; #pragma unroll
;                     for (int k = 0; k < 4; ++k) tw[q][k] = (scw + ((rb + q) * 4 + k) * 64)[ul];
;                 asm volatile("" ::: "memory"); SBAR();
; #pragma unroll
;                 for (int q = 0; q < 4; ++q) { const int r = rb + q; float s = 0.f;
; #pragma unroll
;                     for (int d0 = 0; d0 < 8; ++d0) { const float t = __uint_as_float((d0 & 1) ? (tw[q][d0 >> 1] & 0xffff0000u) : (tw[q][d0 >> 1] << 16));
;                         const float dd = fma_ns(nlam, mul_ns(o[d0][r], rli[r]), t); s = fma_ns(dd, dd, s); }
;                     s = half_sum(s); rn[r] = rsqrtf(s * (1.0f / 256.0f) + 1e-5f) * 0.8f; }
.LBB0_1290:
	v_cmp_gt_u32_e32 vcc, 32, v200
	s_and_saveexec_b64 s[4:5], vcc
	v_readlane_b32 s88, v252, 34
	v_readlane_b32 s89, v252, 35
	s_mov_b32 s54, 0x3b800000
	s_mov_b32 s29, s77
	v_lshl_add_u32 v2, v202, 2, s93
	ds_write_b32 v2, v215
	s_or_b64 exec, exec, s[4:5]
	s_waitcnt lgkmcnt(0)
	v_lshl_add_u32 v2, v213, 4, s93
	ds_read_b128 v[4:7], v2
	ds_read_b128 v[8:11], v2 offset:32
	v_readlane_b32 s76, v252, 36
	s_cmp_lg_u32 s30, 0
	v_readlane_b32 s77, v252, 37
	s_waitcnt lgkmcnt(0)
	v_rcp_f32_e32 v4, v4
	v_rcp_f32_e32 v5, v5
	v_rcp_f32_e32 v6, v6
	v_rcp_f32_e32 v7, v7
	v_rcp_f32_e32 v8, v8
	v_mul_f32_e32 v183, 0x3d800000, v4
	v_mul_f32_e32 v182, 0x3d800000, v5
	v_mul_f32_e32 v181, 0x3d800000, v6
	v_mul_f32_e32 v180, 0x3d800000, v7
	v_mul_f32_e32 v179, 0x3d800000, v8
	v_rcp_f32_e32 v8, v9
	v_rcp_f32_e32 v9, v10
	v_rcp_f32_e32 v10, v11
	ds_read_b128 v[4:7], v2 offset:64
	v_mul_f32_e32 v178, 0x3d800000, v8
	v_mul_f32_e32 v177, 0x3d800000, v9
	v_mul_f32_e32 v176, 0x3d800000, v10
	ds_read_b128 v[8:11], v2 offset:96
	s_waitcnt lgkmcnt(0)
	v_rcp_f32_e32 v2, v4
	v_rcp_f32_e32 v4, v5
	v_rcp_f32_e32 v5, v6
	v_rcp_f32_e32 v6, v7
	v_mul_f32_e32 v175, 0x3d800000, v2
	v_mul_f32_e32 v174, 0x3d800000, v4
	v_mul_f32_e32 v173, 0x3d800000, v5
	v_mul_f32_e32 v172, 0x3d800000, v6
	v_rcp_f32_e32 v2, v8
	v_rcp_f32_e32 v4, v9
	v_rcp_f32_e32 v5, v10
	v_rcp_f32_e32 v6, v11
	v_mul_f32_e32 v171, 0x3d800000, v2
	v_mul_f32_e32 v170, 0x3d800000, v4
	v_mul_f32_e32 v169, 0x3d800000, v5
	v_mul_f32_e32 v168, 0x3d800000, v6
	s_cbranch_scc0 .LBB0_1550
	v_readlane_b32 s4, v252, 4
	v_mov_b32_e32 v201, v3
	v_readlane_b32 s5, v252, 5
	s_nop 1
	v_lshl_add_u64 v[4:5], v[200:201], 2, s[4:5]
	global_load_dword v2, v[4:5], off
	global_load_dword v6, v[4:5], off offset:256
	global_load_dword v7, v[4:5], off offset:512
	global_load_dword v8, v[4:5], off offset:768
	global_load_dword v10, v[4:5], off offset:1024
	global_load_dword v11, v[4:5], off offset:1280
	global_load_dword v12, v[4:5], off offset:1536
	global_load_dword v13, v[4:5], off offset:1792
	global_load_dword v14, v[4:5], off offset:2048
	global_load_dword v15, v[4:5], off offset:2304
	global_load_dword v16, v[4:5], off offset:2560
	global_load_dword v17, v[4:5], off offset:2816
	global_load_dword v146, v[4:5], off offset:3072
	global_load_dword v147, v[4:5], off offset:3328
	global_load_dword v148, v[4:5], off offset:3584
	global_load_dword v149, v[4:5], off offset:3840
	s_lshl_b32 s4, s16, 12
	s_add_i32 s86, s4, s86
	s_lshl_b64 s[4:5], s[86:87], 12
	s_add_u32 s4, s88, s4
	s_addc_u32 s5, s89, s5
	s_lshl_b32 s6, s15, 8
	s_add_u32 s8, s4, s6
	s_addc_u32 s9, s5, 0
	v_readlane_b32 s4, v252, 38
	v_readlane_b32 s5, v252, 39
	s_ashr_i32 s5, s4, 31
	s_lshl_b64 s[6:7], s[4:5], 12
	s_waitcnt vmcnt(0)
	v_lshlrev_b32_e32 v9, 16, v2
	v_mul_f32 v192, v130, v183
	v_and_b32_e32 v2, 0xffff0000, v2
	v_fma_f32 v9, v212, v192, v9
	v_mul_f32 v150, v114, v183
	s_nop 0
	v_fma_f32 v9, v9, v9, v3
	v_fma_f32 v2, v212, v150, v2
	v_mul_f32 v150, v98, v183
	s_nop 0
	v_fma_f32 v2, v2, v2, v9
	v_lshlrev_b32_e32 v9, 16, v6
	v_fma_f32 v9, v212, v150, v9
	v_and_b32_e32 v6, 0xffff0000, v6
	v_fma_f32 v2, v9, v9, v2
	v_mul_f32 v9, v82, v183
	s_nop 0
	v_fma_f32 v6, v212, v9, v6
	v_mul_f32 v9, v66, v183
	s_nop 0
	v_fma_f32 v2, v6, v6, v2
	v_lshlrev_b32_e32 v6, 16, v7
	v_fma_f32 v6, v212, v9, v6
	s_nop 0
	v_fma_f32 v2, v6, v6, v2
	v_and_b32_e32 v6, 0xffff0000, v7
	v_mul_f32 v7, v50, v183
	s_nop 0
	v_fma_f32 v6, v212, v7, v6
	v_mul_f32 v7, v34, v183
	s_nop 0
	v_fma_f32 v2, v6, v6, v2
	v_lshlrev_b32_e32 v6, 16, v8
	v_fma_f32 v6, v212, v7, v6
	v_mul_f32 v7, v18, v183
	s_nop 0
	v_fma_f32 v2, v6, v6, v2
	v_and_b32_e32 v6, 0xffff0000, v8
	v_fma_f32 v6, v212, v7, v6
	v_mul_f32 v8, v115, v182
	s_nop 0
	v_fma_f32 v7, v6, v6, v2
	v_lshlrev_b32_e32 v2, 16, v10
	v_mul_f32 v6, v131, v182
	s_nop 1
	v_mov_b32_dpp v9, v7 quad_perm:[1,0,3,2] row_mask:0xf bank_mask:0xf
	v_fma_f32 v2, v212, v6, v2
	v_and_b32_e32 v6, 0xffff0000, v10
	v_fma_f32 v2, v2, v2, v3
	v_fma_f32 v6, v212, v8, v6
	v_mul_f32 v8, v99, v182
	s_nop 0
	v_fma_f32 v2, v6, v6, v2
	v_lshlrev_b32_e32 v6, 16, v11
	v_fma_f32 v6, v212, v8, v6
	v_mul_f32 v8, v83, v182
	s_nop 0
	v_fma_f32 v2, v6, v6, v2
	v_and_b32_e32 v6, 0xffff0000, v11
	v_fma_f32 v6, v212, v8, v6
	v_mul_f32 v8, v67, v182
	s_nop 0
	v_fma_f32 v2, v6, v6, v2
	v_lshlrev_b32_e32 v6, 16, v12
	v_fma_f32 v6, v212, v8, v6
	v_mul_f32 v8, v51, v182
	s_nop 0
	v_fma_f32 v2, v6, v6, v2
	v_and_b32_e32 v6, 0xffff0000, v12
	v_fma_f32 v6, v212, v8, v6
	v_mul_f32 v8, v35, v182
	s_nop 0
	v_fma_f32 v2, v6, v6, v2
	v_lshlrev_b32_e32 v6, 16, v13
	v_fma_f32 v6, v212, v8, v6
	v_mul_f32 v8, v19, v182
	s_nop 0
	v_fma_f32 v2, v6, v6, v2
	v_and_b32_e32 v6, 0xffff0000, v13
	v_fma_f32 v6, v212, v8, v6
	s_nop 0
	v_fma_f32 v6, v6, v6, v2
	s_nop 1
	v_mov_b32_dpp v8, v6 quad_perm:[1,0,3,2] row_mask:0xf bank_mask:0xf
	s_waitcnt lgkmcnt(0)
	v_pk_add_f32 v[6:7], v[6:7], v[8:9]
	s_nop 1
	v_mov_b32_dpp v9, v7 quad_perm:[2,3,0,1] row_mask:0xf bank_mask:0xf
	s_nop 1
	v_mov_b32_dpp v8, v6 quad_perm:[2,3,0,1] row_mask:0xf bank_mask:0xf
	v_pk_add_f32 v[6:7], v[6:7], v[8:9]
	ds_swizzle_b32 v9, v7 offset:swizzle(SWAP,4)
	ds_swizzle_b32 v8, v6 offset:swizzle(SWAP,4)
	s_waitcnt lgkmcnt(0)
	v_pk_add_f32 v[6:7], v[6:7], v[8:9]
	ds_swizzle_b32 v9, v7 offset:swizzle(SWAP,8)
	ds_swizzle_b32 v8, v6 offset:swizzle(SWAP,8)
	s_waitcnt lgkmcnt(0)
	v_pk_add_f32 v[6:7], v[6:7], v[8:9]
	ds_swizzle_b32 v9, v7 offset:swizzle(SWAP,16)
	ds_swizzle_b32 v8, v6 offset:swizzle(SWAP,16)
	s_waitcnt lgkmcnt(0)
; #define SBAR() __builtin_amdgcn_sched_barrier(0)
; __device__ __forceinline__ float mul_ns(float a, float b) { float r; asm("v_mul_f32 %0, %1, %2" : "=v"(r) : "v"(a), "v"(b)); return r; }
; __device__ __forceinline__ float fma_ns(float a, float b, float c) { float r; asm("v_fma_f32 %0, %1, %2, %3" : "=v"(r) : "v"(a), "v"(b), "v"(c)); return r; }
;     __device__ __forceinline__ void operator()(f32x16 (&o)[8], const float (&rli)[16], int wid, int lane, int r32, int hi) const {
;     ...
;             for (int rb = 0; rb < 16; rb += 4) { unsigned tw[4][4];
; #pragma unroll
;                 for (int q = 0; q < 4; ++q)
; #pragma unroll
;                     for (int k = 0; k < 4; ++k) tw[q][k] = (scw + ((rb + q) * 4 + k) * 64)[ul];
;                 asm volatile("" ::: "memory"); SBAR();
; #pragma unroll
;                 for (int q = 0; q < 4; ++q) { const int r = rb + q; float s = 0.f;
; #pragma unroll
;                     for (int d0 = 0; d0 < 8; ++d0) { const float t = __uint_as_float((d0 & 1) ? (tw[q][d0 >> 1] & 0xffff0000u) : (tw[q][d0 >> 1] << 16));
;                         const float dd = fma_ns(nlam, mul_ns(o[d0][r], rli[r]), t); s = fma_ns(dd, dd, s); }
;                     s = half_sum(s); rn[r] = rsqrtf(s * (1.0f / 256.0f) + 1e-5f) * 0.8f; }
;                 asm volatile("" ::: "memory"); SBAR(); }
	v_pk_add_f32 v[6:7], v[6:7], v[8:9]
	s_nop 0
	v_pk_fma_f32 v[164:165], v[6:7], s[54:55], v[198:199] op_sel_hi:[1,0,0]
	v_mul_f32 v7, v116, v181
	v_mul_f32 v8, v117, v180
	s_nop 0
	v_mul_f32_e32 v2, 0x4b800000, v165
	v_cmp_gt_f32_e64 s[4:5], s53, v165
	v_cmp_gt_f32_e32 vcc, s53, v164
	s_nop 0
	v_cndmask_b32_e64 v2, v165, v2, s[4:5]
	v_rsq_f32_e32 v2, v2
	s_nop 0
	v_mul_f32_e32 v6, 0x45800000, v2
	v_cndmask_b32_e64 v2, v2, v6, s[4:5]
	v_mul_f32_e32 v191, 0x3f4ccccd, v2
	v_lshlrev_b32_e32 v2, 16, v14
	v_mul_f32 v6, v132, v181
	s_nop 0
	v_fma_f32 v2, v212, v6, v2
	v_and_b32_e32 v6, 0xffff0000, v14
	v_fma_f32 v2, v2, v2, v3
	v_fma_f32 v6, v212, v7, v6
	v_mul_f32 v7, v100, v181
	s_nop 0
	v_fma_f32 v2, v6, v6, v2
	v_lshlrev_b32_e32 v6, 16, v15
	v_fma_f32 v6, v212, v7, v6
	v_mul_f32 v7, v84, v181
	s_nop 0
	v_fma_f32 v2, v6, v6, v2
	v_and_b32_e32 v6, 0xffff0000, v15
	v_fma_f32 v6, v212, v7, v6
	v_mul_f32 v7, v68, v181
	s_nop 0
	v_fma_f32 v2, v6, v6, v2
	v_lshlrev_b32_e32 v6, 16, v16
	v_fma_f32 v6, v212, v7, v6
	v_mul_f32 v7, v52, v181
	s_nop 0
	v_fma_f32 v2, v6, v6, v2
	v_and_b32_e32 v6, 0xffff0000, v16
	v_fma_f32 v6, v212, v7, v6
	v_mul_f32 v7, v36, v181
	s_nop 0
	v_fma_f32 v2, v6, v6, v2
	v_lshlrev_b32_e32 v6, 16, v17
	v_fma_f32 v6, v212, v7, v6
	v_mul_f32 v7, v20, v181
	s_nop 0
	v_fma_f32 v2, v6, v6, v2
	v_and_b32_e32 v6, 0xffff0000, v17
	v_fma_f32 v6, v212, v7, v6
	s_nop 0
	v_fma_f32 v7, v6, v6, v2
	v_lshlrev_b32_e32 v2, 16, v146
	v_mul_f32 v6, v133, v180
	s_nop 1
	v_mov_b32_dpp v9, v7 quad_perm:[1,0,3,2] row_mask:0xf bank_mask:0xf
	v_fma_f32 v2, v212, v6, v2
	v_and_b32_e32 v6, 0xffff0000, v146
	v_fma_f32 v2, v2, v2, v3
	v_fma_f32 v6, v212, v8, v6
	v_mul_f32 v8, v101, v180
	s_nop 0
	v_fma_f32 v2, v6, v6, v2
	v_lshlrev_b32_e32 v6, 16, v147
	v_fma_f32 v6, v212, v8, v6
	v_mul_f32 v8, v85, v180
	s_nop 0
	v_fma_f32 v2, v6, v6, v2
	v_and_b32_e32 v6, 0xffff0000, v147
	v_fma_f32 v6, v212, v8, v6
	v_mul_f32 v8, v69, v180
	s_nop 0
	v_fma_f32 v2, v6, v6, v2
	v_lshlrev_b32_e32 v6, 16, v148
	v_fma_f32 v6, v212, v8, v6
	v_mul_f32 v8, v53, v180
	s_nop 0
	v_fma_f32 v2, v6, v6, v2
	v_and_b32_e32 v6, 0xffff0000, v148
	v_fma_f32 v6, v212, v8, v6
	v_mul_f32 v8, v37, v180
	s_nop 0
	v_fma_f32 v2, v6, v6, v2
	v_lshlrev_b32_e32 v6, 16, v149
	v_fma_f32 v6, v212, v8, v6
	v_mul_f32 v8, v21, v180
	s_nop 0
	v_fma_f32 v2, v6, v6, v2
	v_and_b32_e32 v6, 0xffff0000, v149
	v_fma_f32 v6, v212, v8, v6
	s_nop 0
	v_fma_f32 v6, v6, v6, v2
	s_nop 1
	v_mov_b32_dpp v8, v6 quad_perm:[1,0,3,2] row_mask:0xf bank_mask:0xf
	v_pk_add_f32 v[6:7], v[6:7], v[8:9]
	s_nop 1
	v_mov_b32_dpp v9, v7 quad_perm:[2,3,0,1] row_mask:0xf bank_mask:0xf
	s_nop 1
	v_mov_b32_dpp v8, v6 quad_perm:[2,3,0,1] row_mask:0xf bank_mask:0xf
	v_pk_add_f32 v[6:7], v[6:7], v[8:9]
	ds_swizzle_b32 v9, v7 offset:swizzle(SWAP,4)
	ds_swizzle_b32 v8, v6 offset:swizzle(SWAP,4)
	s_waitcnt lgkmcnt(0)
	v_pk_add_f32 v[6:7], v[6:7], v[8:9]
	ds_swizzle_b32 v9, v7 offset:swizzle(SWAP,8)
	ds_swizzle_b32 v8, v6 offset:swizzle(SWAP,8)
	s_waitcnt lgkmcnt(0)
	v_pk_add_f32 v[160:161], v[6:7], v[8:9]
	ds_swizzle_b32 v163, v161 offset:swizzle(SWAP,16)
	ds_swizzle_b32 v162, v160 offset:swizzle(SWAP,16)
	s_movk_i32 s4, 0x1000
	v_add_co_u32_e64 v8, s[4:5], s4, v4
	s_nop 1
	v_addc_co_u32_e64 v9, s[4:5], 0, v5, s[4:5]
	s_movk_i32 s4, 0x2000
	s_nop 0
	v_add_co_u32_e64 v6, s[4:5], s4, v4
	s_nop 1
	v_addc_co_u32_e64 v7, s[4:5], 0, v5, s[4:5]
	global_load_dword v2, v[8:9], off offset:256
	global_load_dword v10, v[8:9], off offset:512
	global_load_dword v11, v[8:9], off offset:768
	global_load_dword v12, v[8:9], off offset:1024
	global_load_dword v13, v[8:9], off offset:1280
	global_load_dword v14, v[8:9], off offset:1536
	global_load_dword v15, v[8:9], off offset:1792
	global_load_dword v16, v[8:9], off offset:2048
	global_load_dword v17, v[6:7], off offset:-4096
	global_load_dword v146, v[8:9], off offset:2304
	global_load_dword v147, v[8:9], off offset:2560
	global_load_dword v148, v[8:9], off offset:2816
	global_load_dword v149, v[8:9], off offset:3072
	global_load_dword v150, v[8:9], off offset:3328
	global_load_dword v151, v[8:9], off offset:3584
	global_load_dword v152, v[8:9], off offset:3840
	s_waitcnt vmcnt(7)
	v_lshlrev_b32_e32 v8, 16, v17
	v_mul_f32 v9, v134, v179
	s_nop 0
	v_fma_f32 v8, v212, v9, v8
	v_and_b32_e32 v9, 0xffff0000, v17
	v_fma_f32 v8, v8, v8, v3
	v_mul_f32 v17, v118, v179
	s_nop 0
	v_fma_f32 v9, v212, v17, v9
	v_mul_f32 v17, v102, v179
	s_nop 0
	v_fma_f32 v8, v9, v9, v8
	v_lshlrev_b32_e32 v9, 16, v2
	v_fma_f32 v9, v212, v17, v9
	v_and_b32_e32 v2, 0xffff0000, v2
	v_fma_f32 v8, v9, v9, v8
	v_mul_f32 v9, v86, v179
	s_nop 0
	v_fma_f32 v2, v212, v9, v2
	v_mul_f32 v9, v70, v179
	s_nop 0
	v_fma_f32 v2, v2, v2, v8
	v_lshlrev_b32_e32 v8, 16, v10
	v_fma_f32 v8, v212, v9, v8
	v_mul_f32 v9, v54, v179
	s_nop 0
	v_fma_f32 v2, v8, v8, v2
	v_and_b32_e32 v8, 0xffff0000, v10
	v_fma_f32 v8, v212, v9, v8
	v_mul_f32 v9, v38, v179
	v_mul_f32 v10, v119, v178
	s_nop 0
	v_fma_f32 v2, v8, v8, v2
	v_lshlrev_b32_e32 v8, 16, v11
	v_fma_f32 v8, v212, v9, v8
	v_mul_f32 v9, v22, v179
	s_nop 0
	v_fma_f32 v2, v8, v8, v2
	v_and_b32_e32 v8, 0xffff0000, v11
	v_fma_f32 v8, v212, v9, v8
	s_nop 0
	v_fma_f32 v9, v8, v8, v2
	v_lshlrev_b32_e32 v2, 16, v12
	v_mul_f32 v8, v135, v178
	s_nop 1
	v_mov_b32_dpp v11, v9 quad_perm:[1,0,3,2] row_mask:0xf bank_mask:0xf
	v_fma_f32 v2, v212, v8, v2
	v_and_b32_e32 v8, 0xffff0000, v12
	v_fma_f32 v2, v2, v2, v3
	v_fma_f32 v8, v212, v10, v8
	v_mul_f32 v10, v103, v178
	v_mul_f32 v12, v136, v177
	s_nop 0
	v_fma_f32 v2, v8, v8, v2
	v_lshlrev_b32_e32 v8, 16, v13
	v_fma_f32 v8, v212, v10, v8
	v_mul_f32 v10, v87, v178
	s_nop 0
	v_fma_f32 v2, v8, v8, v2
	v_and_b32_e32 v8, 0xffff0000, v13
	v_fma_f32 v8, v212, v10, v8
	v_mul_f32 v10, v71, v178
	v_mul_f32 v13, v120, v177
	s_nop 0
	v_fma_f32 v2, v8, v8, v2
	v_lshlrev_b32_e32 v8, 16, v14
	v_fma_f32 v8, v212, v10, v8
	v_mul_f32 v10, v55, v178
	s_nop 0
	v_fma_f32 v2, v8, v8, v2
	v_and_b32_e32 v8, 0xffff0000, v14
	v_fma_f32 v8, v212, v10, v8
	v_mul_f32 v10, v39, v178
	v_mul_f32 v14, v121, v176
	s_nop 0
	v_fma_f32 v2, v8, v8, v2
	v_lshlrev_b32_e32 v8, 16, v15
	v_fma_f32 v8, v212, v10, v8
	v_mul_f32 v10, v23, v178
	s_nop 0
	v_fma_f32 v2, v8, v8, v2
	v_and_b32_e32 v8, 0xffff0000, v15
	v_fma_f32 v8, v212, v10, v8
	s_nop 0
	v_fma_f32 v8, v8, v8, v2
	v_lshlrev_b32_e32 v2, 16, v16
	v_fma_f32 v2, v212, v12, v2
	v_and_b32_e32 v12, 0xffff0000, v16
	v_fma_f32 v2, v2, v2, v3
	v_fma_f32 v12, v212, v13, v12
	v_mul_f32 v13, v104, v177
	s_nop 1
	v_mov_b32_dpp v10, v8 quad_perm:[1,0,3,2] row_mask:0xf bank_mask:0xf
	v_fma_f32 v2, v12, v12, v2
	s_waitcnt vmcnt(6)
; #define SBAR() __builtin_amdgcn_sched_barrier(0)
; __device__ __forceinline__ float mul_ns(float a, float b) { float r; asm("v_mul_f32 %0, %1, %2" : "=v"(r) : "v"(a), "v"(b)); return r; }
; __device__ __forceinline__ float fma_ns(float a, float b, float c) { float r; asm("v_fma_f32 %0, %1, %2, %3" : "=v"(r) : "v"(a), "v"(b), "v"(c)); return r; }
;     __device__ __forceinline__ void operator()(f32x16 (&o)[8], const float (&rli)[16], int wid, int lane, int r32, int hi) const {
;     ...
;             for (int rb = 0; rb < 16; rb += 4) { unsigned tw[4][4];
; #pragma unroll
;                 for (int q = 0; q < 4; ++q)
; #pragma unroll
;                     for (int k = 0; k < 4; ++k) tw[q][k] = (scw + ((rb + q) * 4 + k) * 64)[ul];
;                 asm volatile("" ::: "memory"); SBAR();
; #pragma unroll
;                 for (int q = 0; q < 4; ++q) { const int r = rb + q; float s = 0.f;
; #pragma unroll
;                     for (int d0 = 0; d0 < 8; ++d0) { const float t = __uint_as_float((d0 & 1) ? (tw[q][d0 >> 1] & 0xffff0000u) : (tw[q][d0 >> 1] << 16));
;                         const float dd = fma_ns(nlam, mul_ns(o[d0][r], rli[r]), t); s = fma_ns(dd, dd, s); }
;                     s = half_sum(s); rn[r] = rsqrtf(s * (1.0f / 256.0f) + 1e-5f) * 0.8f; }
;                 asm volatile("" ::: "memory"); SBAR(); }
	v_lshlrev_b32_e32 v12, 16, v146
	v_fma_f32 v12, v212, v13, v12
	v_mul_f32 v13, v88, v177
	s_waitcnt lgkmcnt(0)
	v_pk_add_f32 v[8:9], v[8:9], v[10:11]
	v_fma_f32 v2, v12, v12, v2
	v_and_b32_e32 v12, 0xffff0000, v146
	v_fma_f32 v12, v212, v13, v12
	v_mul_f32 v13, v72, v177
	s_nop 1
	v_mov_b32_dpp v11, v9 quad_perm:[2,3,0,1] row_mask:0xf bank_mask:0xf
	v_fma_f32 v2, v12, v12, v2
	s_waitcnt vmcnt(5)
	v_lshlrev_b32_e32 v12, 16, v147
	v_fma_f32 v12, v212, v13, v12
	v_mul_f32 v13, v56, v177
	s_nop 1
	v_mov_b32_dpp v10, v8 quad_perm:[2,3,0,1] row_mask:0xf bank_mask:0xf
	v_fma_f32 v2, v12, v12, v2
	v_and_b32_e32 v12, 0xffff0000, v147
	v_fma_f32 v12, v212, v13, v12
	v_mul_f32 v13, v40, v177
	v_pk_add_f32 v[8:9], v[8:9], v[10:11]
	v_fma_f32 v2, v12, v12, v2
	s_waitcnt vmcnt(4)
	v_lshlrev_b32_e32 v12, 16, v148
	v_fma_f32 v12, v212, v13, v12
	v_mul_f32 v13, v24, v177
	ds_swizzle_b32 v11, v9 offset:swizzle(SWAP,4)
	v_fma_f32 v2, v12, v12, v2
	v_and_b32_e32 v12, 0xffff0000, v148
	v_fma_f32 v12, v212, v13, v12
	ds_swizzle_b32 v10, v8 offset:swizzle(SWAP,4)
	v_fma_f32 v13, v12, v12, v2
	s_waitcnt vmcnt(3)
	v_lshlrev_b32_e32 v2, 16, v149
	v_mul_f32 v12, v137, v176
	s_nop 1
	v_mov_b32_dpp v15, v13 quad_perm:[1,0,3,2] row_mask:0xf bank_mask:0xf
	v_fma_f32 v2, v212, v12, v2
	v_and_b32_e32 v12, 0xffff0000, v149
	v_fma_f32 v2, v2, v2, v3
	v_fma_f32 v12, v212, v14, v12
	v_mul_f32 v14, v105, v176
	s_waitcnt lgkmcnt(0)
	v_pk_add_f32 v[8:9], v[8:9], v[10:11]
	v_fma_f32 v2, v12, v12, v2
	s_waitcnt vmcnt(2)
	v_lshlrev_b32_e32 v12, 16, v150
	v_fma_f32 v12, v212, v14, v12
	v_mul_f32 v14, v89, v176
	ds_swizzle_b32 v11, v9 offset:swizzle(SWAP,8)
	v_fma_f32 v2, v12, v12, v2
	v_and_b32_e32 v12, 0xffff0000, v150
	v_fma_f32 v12, v212, v14, v12
	v_mul_f32 v14, v73, v176
	ds_swizzle_b32 v10, v8 offset:swizzle(SWAP,8)
	v_fma_f32 v2, v12, v12, v2
	s_waitcnt vmcnt(1)
	v_lshlrev_b32_e32 v12, 16, v151
	v_fma_f32 v12, v212, v14, v12
	v_mul_f32 v14, v57, v176
	s_waitcnt lgkmcnt(0)
	v_pk_add_f32 v[156:157], v[8:9], v[10:11]
	v_fma_f32 v2, v12, v12, v2
	v_and_b32_e32 v12, 0xffff0000, v151
	v_fma_f32 v12, v212, v14, v12
	v_mul_f32 v14, v41, v176
	ds_swizzle_b32 v159, v157 offset:swizzle(SWAP,16)
	v_fma_f32 v2, v12, v12, v2
	s_waitcnt vmcnt(0)
	v_lshlrev_b32_e32 v12, 16, v152
	v_fma_f32 v12, v212, v14, v12
	v_mul_f32 v14, v25, v176
	ds_swizzle_b32 v158, v156 offset:swizzle(SWAP,16)
	v_fma_f32 v2, v12, v12, v2
	v_and_b32_e32 v12, 0xffff0000, v152
	v_fma_f32 v12, v212, v14, v12
	s_nop 0
	v_fma_f32 v12, v12, v12, v2
	s_nop 1
	v_mov_b32_dpp v14, v12 quad_perm:[1,0,3,2] row_mask:0xf bank_mask:0xf
	s_waitcnt lgkmcnt(0)
	v_pk_add_f32 v[12:13], v[12:13], v[14:15]
	s_nop 1
	v_mov_b32_dpp v15, v13 quad_perm:[2,3,0,1] row_mask:0xf bank_mask:0xf
	s_nop 1
	v_mov_b32_dpp v14, v12 quad_perm:[2,3,0,1] row_mask:0xf bank_mask:0xf
	v_pk_add_f32 v[12:13], v[12:13], v[14:15]
	ds_swizzle_b32 v15, v13 offset:swizzle(SWAP,4)
	ds_swizzle_b32 v14, v12 offset:swizzle(SWAP,4)
	s_waitcnt lgkmcnt(0)
	v_pk_add_f32 v[12:13], v[12:13], v[14:15]
	ds_swizzle_b32 v15, v13 offset:swizzle(SWAP,8)
	ds_swizzle_b32 v14, v12 offset:swizzle(SWAP,8)
	s_waitcnt lgkmcnt(0)
	v_pk_add_f32 v[152:153], v[12:13], v[14:15]
	ds_swizzle_b32 v155, v153 offset:swizzle(SWAP,16)
	ds_swizzle_b32 v154, v152 offset:swizzle(SWAP,16)
	global_load_dword v2, v[6:7], off
	global_load_dword v8, v[6:7], off offset:256
	global_load_dword v9, v[6:7], off offset:512
	global_load_dword v10, v[6:7], off offset:768
	global_load_dword v11, v[6:7], off offset:1024
	global_load_dword v12, v[6:7], off offset:1280
	global_load_dword v13, v[6:7], off offset:1536
	global_load_dword v14, v[6:7], off offset:1792
	global_load_dword v15, v[6:7], off offset:2048
	global_load_dword v16, v[6:7], off offset:2304
	global_load_dword v17, v[6:7], off offset:2560
	global_load_dword v146, v[6:7], off offset:2816
	global_load_dword v147, v[6:7], off offset:3072
	global_load_dword v148, v[6:7], off offset:3328
	global_load_dword v149, v[6:7], off offset:3584
	global_load_dword v150, v[6:7], off offset:3840
	s_waitcnt vmcnt(15)
	v_lshlrev_b32_e32 v6, 16, v2
	v_mul_f32 v7, v138, v175
	v_and_b32_e32 v2, 0xffff0000, v2
	v_fma_f32 v6, v212, v7, v6
	v_mul_f32 v7, v122, v175
	s_nop 0
	v_fma_f32 v6, v6, v6, v3
	v_fma_f32 v2, v212, v7, v2
	v_mul_f32 v7, v106, v175
	s_nop 0
	v_fma_f32 v2, v2, v2, v6
	s_waitcnt vmcnt(14)
	v_lshlrev_b32_e32 v6, 16, v8
	v_fma_f32 v6, v212, v7, v6
	v_mul_f32 v7, v90, v175
	s_nop 0
	v_fma_f32 v2, v6, v6, v2
	v_and_b32_e32 v6, 0xffff0000, v8
	v_fma_f32 v6, v212, v7, v6
	v_mul_f32 v7, v74, v175
	v_mul_f32 v8, v123, v174
	s_nop 0
	v_fma_f32 v2, v6, v6, v2
	s_waitcnt vmcnt(13)
	v_lshlrev_b32_e32 v6, 16, v9
	v_fma_f32 v6, v212, v7, v6
	v_mul_f32 v7, v58, v175
	s_nop 0
	v_fma_f32 v2, v6, v6, v2
	v_and_b32_e32 v6, 0xffff0000, v9
	v_fma_f32 v6, v212, v7, v6
	v_mul_f32 v7, v42, v175
	s_nop 0
	v_fma_f32 v2, v6, v6, v2
	s_waitcnt vmcnt(12)
	v_lshlrev_b32_e32 v6, 16, v10
	v_fma_f32 v6, v212, v7, v6
	v_mul_f32 v7, v26, v175
	s_nop 0
	v_fma_f32 v2, v6, v6, v2
	v_and_b32_e32 v6, 0xffff0000, v10
	v_fma_f32 v6, v212, v7, v6
	v_mul_f32 v10, v140, v173
	s_nop 0
	v_fma_f32 v7, v6, v6, v2
	s_waitcnt vmcnt(11)
	v_lshlrev_b32_e32 v2, 16, v11
	v_mul_f32 v6, v139, v174
	s_nop 1
	v_mov_b32_dpp v9, v7 quad_perm:[1,0,3,2] row_mask:0xf bank_mask:0xf
	v_fma_f32 v2, v212, v6, v2
	v_and_b32_e32 v6, 0xffff0000, v11
	v_fma_f32 v2, v2, v2, v3
	v_fma_f32 v6, v212, v8, v6
	v_mul_f32 v8, v107, v174
	v_mul_f32 v11, v124, v173
	s_nop 0
	v_fma_f32 v2, v6, v6, v2
	s_waitcnt vmcnt(10)
; #define SBAR() __builtin_amdgcn_sched_barrier(0)
; __device__ __forceinline__ float mul_ns(float a, float b) { float r; asm("v_mul_f32 %0, %1, %2" : "=v"(r) : "v"(a), "v"(b)); return r; }
; __device__ __forceinline__ float fma_ns(float a, float b, float c) { float r; asm("v_fma_f32 %0, %1, %2, %3" : "=v"(r) : "v"(a), "v"(b), "v"(c)); return r; }
;     __device__ __forceinline__ void operator()(f32x16 (&o)[8], const float (&rli)[16], int wid, int lane, int r32, int hi) const {
;     ...
;             for (int rb = 0; rb < 16; rb += 4) { unsigned tw[4][4];
; #pragma unroll
;                 for (int q = 0; q < 4; ++q)
; #pragma unroll
;                     for (int k = 0; k < 4; ++k) tw[q][k] = (scw + ((rb + q) * 4 + k) * 64)[ul];
;                 asm volatile("" ::: "memory"); SBAR();
; #pragma unroll
;                 for (int q = 0; q < 4; ++q) { const int r = rb + q; float s = 0.f;
; #pragma unroll
;                     for (int d0 = 0; d0 < 8; ++d0) { const float t = __uint_as_float((d0 & 1) ? (tw[q][d0 >> 1] & 0xffff0000u) : (tw[q][d0 >> 1] << 16));
;                         const float dd = fma_ns(nlam, mul_ns(o[d0][r], rli[r]), t); s = fma_ns(dd, dd, s); }
;                     s = half_sum(s); rn[r] = rsqrtf(s * (1.0f / 256.0f) + 1e-5f) * 0.8f; }
;                 asm volatile("" ::: "memory"); SBAR(); }
	v_lshlrev_b32_e32 v6, 16, v12
	v_fma_f32 v6, v212, v8, v6
	v_mul_f32 v8, v91, v174
	s_nop 0
	v_fma_f32 v2, v6, v6, v2
	v_and_b32_e32 v6, 0xffff0000, v12
	v_fma_f32 v6, v212, v8, v6
	v_mul_f32 v8, v75, v174
	v_mul_f32 v12, v125, v172
	s_nop 0
	v_fma_f32 v2, v6, v6, v2
	s_waitcnt vmcnt(9)
	v_lshlrev_b32_e32 v6, 16, v13
	v_fma_f32 v6, v212, v8, v6
	v_mul_f32 v8, v59, v174
	s_nop 0
	v_fma_f32 v2, v6, v6, v2
	v_and_b32_e32 v6, 0xffff0000, v13
	v_fma_f32 v6, v212, v8, v6
	v_mul_f32 v8, v43, v174
	s_nop 0
	v_fma_f32 v2, v6, v6, v2
	s_waitcnt vmcnt(8)
	v_lshlrev_b32_e32 v6, 16, v14
	v_fma_f32 v6, v212, v8, v6
	v_mul_f32 v8, v27, v174
	s_nop 0
	v_fma_f32 v2, v6, v6, v2
	v_and_b32_e32 v6, 0xffff0000, v14
	v_fma_f32 v6, v212, v8, v6
	s_nop 0
	v_fma_f32 v6, v6, v6, v2
	s_waitcnt vmcnt(7)
	v_lshlrev_b32_e32 v2, 16, v15
	v_fma_f32 v2, v212, v10, v2
	v_and_b32_e32 v10, 0xffff0000, v15
	v_fma_f32 v2, v2, v2, v3
	v_fma_f32 v10, v212, v11, v10
	v_mul_f32 v11, v108, v173
	s_nop 1
	v_mov_b32_dpp v8, v6 quad_perm:[1,0,3,2] row_mask:0xf bank_mask:0xf
	v_fma_f32 v2, v10, v10, v2
	s_waitcnt vmcnt(6)
	v_lshlrev_b32_e32 v10, 16, v16
	v_fma_f32 v10, v212, v11, v10
	v_mul_f32 v11, v92, v173
	s_waitcnt lgkmcnt(0)
	v_pk_add_f32 v[6:7], v[6:7], v[8:9]
	v_fma_f32 v2, v10, v10, v2
	v_and_b32_e32 v10, 0xffff0000, v16
	v_fma_f32 v10, v212, v11, v10
	v_mul_f32 v11, v76, v173
	s_nop 1
	v_mov_b32_dpp v9, v7 quad_perm:[2,3,0,1] row_mask:0xf bank_mask:0xf
	v_fma_f32 v2, v10, v10, v2
	s_waitcnt vmcnt(5)
	v_lshlrev_b32_e32 v10, 16, v17
	v_fma_f32 v10, v212, v11, v10
	v_mul_f32 v11, v60, v173
	s_nop 1
	v_mov_b32_dpp v8, v6 quad_perm:[2,3,0,1] row_mask:0xf bank_mask:0xf
	v_fma_f32 v2, v10, v10, v2
	v_and_b32_e32 v10, 0xffff0000, v17
	v_fma_f32 v10, v212, v11, v10
	v_mul_f32 v11, v44, v173
	v_pk_add_f32 v[6:7], v[6:7], v[8:9]
	v_fma_f32 v2, v10, v10, v2
	s_waitcnt vmcnt(4)
	v_lshlrev_b32_e32 v10, 16, v146
	v_fma_f32 v10, v212, v11, v10
	v_mul_f32 v11, v28, v173
	ds_swizzle_b32 v9, v7 offset:swizzle(SWAP,4)
	v_fma_f32 v2, v10, v10, v2
	v_and_b32_e32 v10, 0xffff0000, v146
	v_fma_f32 v10, v212, v11, v10
	ds_swizzle_b32 v8, v6 offset:swizzle(SWAP,4)
	v_fma_f32 v11, v10, v10, v2
	s_waitcnt vmcnt(3)
	v_lshlrev_b32_e32 v2, 16, v147
	v_mul_f32 v10, v141, v172
	s_nop 1
	v_mov_b32_dpp v13, v11 quad_perm:[1,0,3,2] row_mask:0xf bank_mask:0xf
	v_fma_f32 v2, v212, v10, v2
	v_and_b32_e32 v10, 0xffff0000, v147
	v_fma_f32 v2, v2, v2, v3
	v_fma_f32 v10, v212, v12, v10
	v_mul_f32 v12, v109, v172
	s_waitcnt lgkmcnt(0)
	v_pk_add_f32 v[6:7], v[6:7], v[8:9]
	v_fma_f32 v2, v10, v10, v2
	s_waitcnt vmcnt(2)
	v_lshlrev_b32_e32 v10, 16, v148
	v_fma_f32 v10, v212, v12, v10
	v_mul_f32 v12, v93, v172
	ds_swizzle_b32 v9, v7 offset:swizzle(SWAP,8)
	v_fma_f32 v2, v10, v10, v2
	v_and_b32_e32 v10, 0xffff0000, v148
	v_fma_f32 v10, v212, v12, v10
	v_mul_f32 v12, v77, v172
	ds_swizzle_b32 v8, v6 offset:swizzle(SWAP,8)
	v_fma_f32 v2, v10, v10, v2
	s_waitcnt vmcnt(1)
	v_lshlrev_b32_e32 v10, 16, v149
	v_fma_f32 v10, v212, v12, v10
	v_mul_f32 v12, v61, v172
	s_nop 0
	v_fma_f32 v2, v10, v10, v2
	v_and_b32_e32 v10, 0xffff0000, v149
	v_fma_f32 v10, v212, v12, v10
	v_mul_f32 v12, v45, v172
	s_waitcnt lgkmcnt(0)
	v_pk_add_f32 v[148:149], v[6:7], v[8:9]
	v_fma_f32 v2, v10, v10, v2
	s_waitcnt vmcnt(0)
	v_lshlrev_b32_e32 v10, 16, v150
	v_fma_f32 v10, v212, v12, v10
	v_mul_f32 v12, v29, v172
	ds_swizzle_b32 v151, v149 offset:swizzle(SWAP,16)
	v_fma_f32 v2, v10, v10, v2
	v_and_b32_e32 v10, 0xffff0000, v150
	v_fma_f32 v10, v212, v12, v10
	ds_swizzle_b32 v150, v148 offset:swizzle(SWAP,16)
	v_fma_f32 v10, v10, v10, v2
	s_nop 1
	v_mov_b32_dpp v12, v10 quad_perm:[1,0,3,2] row_mask:0xf bank_mask:0xf
	s_waitcnt lgkmcnt(0)
	v_pk_add_f32 v[10:11], v[10:11], v[12:13]
	s_nop 1
	v_mov_b32_dpp v13, v11 quad_perm:[2,3,0,1] row_mask:0xf bank_mask:0xf
	s_nop 1
	v_mov_b32_dpp v12, v10 quad_perm:[2,3,0,1] row_mask:0xf bank_mask:0xf
	v_pk_add_f32 v[10:11], v[10:11], v[12:13]
	ds_swizzle_b32 v13, v11 offset:swizzle(SWAP,4)
	ds_swizzle_b32 v12, v10 offset:swizzle(SWAP,4)
	s_waitcnt lgkmcnt(0)
	v_pk_add_f32 v[10:11], v[10:11], v[12:13]
	ds_swizzle_b32 v13, v11 offset:swizzle(SWAP,8)
	ds_swizzle_b32 v12, v10 offset:swizzle(SWAP,8)
	s_waitcnt lgkmcnt(0)
	v_pk_add_f32 v[16:17], v[10:11], v[12:13]
	ds_swizzle_b32 v147, v17 offset:swizzle(SWAP,16)
	ds_swizzle_b32 v146, v16 offset:swizzle(SWAP,16)
	s_movk_i32 s4, 0x3000
	v_add_co_u32_e64 v6, s[4:5], s4, v4
	s_nop 1
	v_addc_co_u32_e64 v7, s[4:5], 0, v5, s[4:5]
	global_load_dword v2, v[6:7], off
	global_load_dword v8, v[6:7], off offset:256
	global_load_dword v9, v[6:7], off offset:512
	global_load_dword v10, v[6:7], off offset:768
	global_load_dword v11, v[6:7], off offset:1024
	global_load_dword v12, v[6:7], off offset:1280
	global_load_dword v13, v[6:7], off offset:1536
	global_load_dword v14, v[6:7], off offset:1792
	global_load_dword v15, v[6:7], off offset:2048
	global_load_dword v165, v[6:7], off offset:2304
	global_load_dword v166, v[6:7], off offset:2560
	global_load_dword v167, v[6:7], off offset:2816
	global_load_dword v184, v[6:7], off offset:3072
	global_load_dword v185, v[6:7], off offset:3328
	global_load_dword v186, v[6:7], off offset:3584
	global_load_dword v187, v[6:7], off offset:3840
	s_waitcnt vmcnt(15)
	v_lshlrev_b32_e32 v6, 16, v2
	v_mul_f32 v7, v142, v171
	v_and_b32_e32 v2, 0xffff0000, v2
	v_fma_f32 v6, v212, v7, v6
	v_mul_f32 v7, v126, v171
	s_nop 0
	v_fma_f32 v6, v6, v6, v3
	v_fma_f32 v2, v212, v7, v2
	v_mul_f32 v7, v110, v171
	s_nop 0
	v_fma_f32 v2, v2, v2, v6
	s_waitcnt vmcnt(14)
; #define SBAR() __builtin_amdgcn_sched_barrier(0)
; __device__ __forceinline__ float mul_ns(float a, float b) { float r; asm("v_mul_f32 %0, %1, %2" : "=v"(r) : "v"(a), "v"(b)); return r; }
; __device__ __forceinline__ float fma_ns(float a, float b, float c) { float r; asm("v_fma_f32 %0, %1, %2, %3" : "=v"(r) : "v"(a), "v"(b), "v"(c)); return r; }
;     __device__ __forceinline__ void operator()(f32x16 (&o)[8], const float (&rli)[16], int wid, int lane, int r32, int hi) const {
;     ...
;             for (int rb = 0; rb < 16; rb += 4) { unsigned tw[4][4];
; #pragma unroll
;                 for (int q = 0; q < 4; ++q)
; #pragma unroll
;                     for (int k = 0; k < 4; ++k) tw[q][k] = (scw + ((rb + q) * 4 + k) * 64)[ul];
;                 asm volatile("" ::: "memory"); SBAR();
; #pragma unroll
;                 for (int q = 0; q < 4; ++q) { const int r = rb + q; float s = 0.f;
; #pragma unroll
;                     for (int d0 = 0; d0 < 8; ++d0) { const float t = __uint_as_float((d0 & 1) ? (tw[q][d0 >> 1] & 0xffff0000u) : (tw[q][d0 >> 1] << 16));
;                         const float dd = fma_ns(nlam, mul_ns(o[d0][r], rli[r]), t); s = fma_ns(dd, dd, s); }
;                     s = half_sum(s); rn[r] = rsqrtf(s * (1.0f / 256.0f) + 1e-5f) * 0.8f; }
;                 asm volatile("" ::: "memory"); SBAR(); }
	v_lshlrev_b32_e32 v6, 16, v8
	v_fma_f32 v6, v212, v7, v6
	v_mul_f32 v7, v94, v171
	s_nop 0
	v_fma_f32 v2, v6, v6, v2
	v_and_b32_e32 v6, 0xffff0000, v8
	v_fma_f32 v6, v212, v7, v6
	v_mul_f32 v7, v78, v171
	v_mul_f32 v8, v127, v170
	s_nop 0
	v_fma_f32 v2, v6, v6, v2
	s_waitcnt vmcnt(13)
	v_lshlrev_b32_e32 v6, 16, v9
	v_fma_f32 v6, v212, v7, v6
	v_mul_f32 v7, v62, v171
	s_nop 0
	v_fma_f32 v2, v6, v6, v2
	v_and_b32_e32 v6, 0xffff0000, v9
	v_fma_f32 v6, v212, v7, v6
	v_mul_f32 v7, v46, v171
	s_nop 0
	v_fma_f32 v2, v6, v6, v2
	s_waitcnt vmcnt(12)
	v_lshlrev_b32_e32 v6, 16, v10
	v_fma_f32 v6, v212, v7, v6
	v_mul_f32 v7, v30, v171
	s_nop 0
	v_fma_f32 v2, v6, v6, v2
	v_and_b32_e32 v6, 0xffff0000, v10
	v_fma_f32 v6, v212, v7, v6
	v_mul_f32 v10, v144, v169
	s_nop 0
	v_fma_f32 v7, v6, v6, v2
	s_waitcnt vmcnt(11)
	v_lshlrev_b32_e32 v2, 16, v11
	v_mul_f32 v6, v143, v170
	s_nop 1
	v_mov_b32_dpp v9, v7 quad_perm:[1,0,3,2] row_mask:0xf bank_mask:0xf
	v_fma_f32 v2, v212, v6, v2
	v_and_b32_e32 v6, 0xffff0000, v11
	v_fma_f32 v2, v2, v2, v3
	v_fma_f32 v6, v212, v8, v6
	v_mul_f32 v8, v111, v170
	v_mul_f32 v11, v128, v169
	s_nop 0
	v_fma_f32 v2, v6, v6, v2
	s_waitcnt vmcnt(10)
	v_lshlrev_b32_e32 v6, 16, v12
	v_fma_f32 v6, v212, v8, v6
	v_mul_f32 v8, v95, v170
	s_nop 0
	v_fma_f32 v2, v6, v6, v2
	v_and_b32_e32 v6, 0xffff0000, v12
	v_fma_f32 v6, v212, v8, v6
	v_mul_f32 v8, v79, v170
	v_mul_f32 v12, v129, v168
	s_nop 0
	v_fma_f32 v2, v6, v6, v2
	s_waitcnt vmcnt(9)
	v_lshlrev_b32_e32 v6, 16, v13
	v_fma_f32 v6, v212, v8, v6
	v_mul_f32 v8, v63, v170
	s_nop 0
	v_fma_f32 v2, v6, v6, v2
	v_and_b32_e32 v6, 0xffff0000, v13
	v_fma_f32 v6, v212, v8, v6
	v_mul_f32 v8, v47, v170
	s_nop 0
	v_fma_f32 v2, v6, v6, v2
	s_waitcnt vmcnt(8)
	v_lshlrev_b32_e32 v6, 16, v14
	v_fma_f32 v6, v212, v8, v6
	v_mul_f32 v8, v31, v170
	s_nop 0
	v_fma_f32 v2, v6, v6, v2
	v_and_b32_e32 v6, 0xffff0000, v14
	v_fma_f32 v6, v212, v8, v6
	s_nop 0
	v_fma_f32 v6, v6, v6, v2
	s_waitcnt vmcnt(7)
	v_lshlrev_b32_e32 v2, 16, v15
	v_fma_f32 v2, v212, v10, v2
	v_and_b32_e32 v10, 0xffff0000, v15
	v_fma_f32 v2, v2, v2, v3
	v_fma_f32 v10, v212, v11, v10
	v_mul_f32 v11, v112, v169
	s_nop 1
	v_mov_b32_dpp v8, v6 quad_perm:[1,0,3,2] row_mask:0xf bank_mask:0xf
	v_fma_f32 v2, v10, v10, v2
	s_waitcnt vmcnt(6)
	v_lshlrev_b32_e32 v10, 16, v165
	v_fma_f32 v10, v212, v11, v10
	v_mul_f32 v11, v96, v169
	s_waitcnt lgkmcnt(0)
	v_pk_add_f32 v[6:7], v[6:7], v[8:9]
	v_fma_f32 v2, v10, v10, v2
	v_and_b32_e32 v10, 0xffff0000, v165
	v_fma_f32 v10, v212, v11, v10
	v_mul_f32 v11, v80, v169
	s_nop 1
	v_mov_b32_dpp v9, v7 quad_perm:[2,3,0,1] row_mask:0xf bank_mask:0xf
	v_fma_f32 v2, v10, v10, v2
	s_waitcnt vmcnt(5)
	v_lshlrev_b32_e32 v10, 16, v166
	v_fma_f32 v10, v212, v11, v10
	v_mul_f32 v11, v64, v169
	s_nop 1
	v_mov_b32_dpp v8, v6 quad_perm:[2,3,0,1] row_mask:0xf bank_mask:0xf
	v_fma_f32 v2, v10, v10, v2
	v_and_b32_e32 v10, 0xffff0000, v166
	v_fma_f32 v10, v212, v11, v10
	v_mul_f32 v11, v48, v169
	v_pk_add_f32 v[6:7], v[6:7], v[8:9]
	v_fma_f32 v2, v10, v10, v2
	s_waitcnt vmcnt(4)
	v_lshlrev_b32_e32 v10, 16, v167
	v_fma_f32 v10, v212, v11, v10
	v_mul_f32 v11, v32, v169
	ds_swizzle_b32 v9, v7 offset:swizzle(SWAP,4)
	v_fma_f32 v2, v10, v10, v2
	v_and_b32_e32 v10, 0xffff0000, v167
	v_fma_f32 v10, v212, v11, v10
	ds_swizzle_b32 v8, v6 offset:swizzle(SWAP,4)
	v_fma_f32 v11, v10, v10, v2
	s_waitcnt vmcnt(3)
	v_lshlrev_b32_e32 v2, 16, v184
	v_mul_f32 v10, v145, v168
	s_nop 1
	v_mov_b32_dpp v13, v11 quad_perm:[1,0,3,2] row_mask:0xf bank_mask:0xf
	v_fma_f32 v2, v212, v10, v2
	v_and_b32_e32 v10, 0xffff0000, v184
	v_fma_f32 v2, v2, v2, v3
	v_fma_f32 v10, v212, v12, v10
	v_mul_f32 v12, v113, v168
	s_waitcnt lgkmcnt(0)
	v_pk_add_f32 v[6:7], v[6:7], v[8:9]
	v_fma_f32 v2, v10, v10, v2
	s_waitcnt vmcnt(2)
	v_lshlrev_b32_e32 v10, 16, v185
	v_fma_f32 v10, v212, v12, v10
	v_mul_f32 v12, v97, v168
	ds_swizzle_b32 v9, v7 offset:swizzle(SWAP,8)
	v_fma_f32 v2, v10, v10, v2
	v_and_b32_e32 v10, 0xffff0000, v185
	v_fma_f32 v10, v212, v12, v10
	v_mul_f32 v12, v81, v168
	ds_swizzle_b32 v8, v6 offset:swizzle(SWAP,8)
	v_fma_f32 v2, v10, v10, v2
	s_waitcnt vmcnt(1)
	v_lshlrev_b32_e32 v10, 16, v186
	v_fma_f32 v10, v212, v12, v10
	v_mul_f32 v12, v65, v168
	s_nop 0
	v_fma_f32 v2, v10, v10, v2
	v_and_b32_e32 v10, 0xffff0000, v186
	v_fma_f32 v10, v212, v12, v10
	v_mul_f32 v12, v49, v168
	s_nop 0
	v_fma_f32 v2, v10, v10, v2
	s_waitcnt vmcnt(0)
	v_lshlrev_b32_e32 v10, 16, v187
	v_fma_f32 v10, v212, v12, v10
	v_mul_f32 v12, v33, v168
	s_nop 0
	v_fma_f32 v2, v10, v10, v2
	v_and_b32_e32 v10, 0xffff0000, v187
	v_fma_f32 v10, v212, v12, v10
	s_nop 0
	v_fma_f32 v10, v10, v10, v2
	s_nop 1
	v_mov_b32_dpp v12, v10 quad_perm:[1,0,3,2] row_mask:0xf bank_mask:0xf
	s_waitcnt lgkmcnt(0)
	v_pk_add_f32 v[10:11], v[10:11], v[12:13]
	s_nop 1
	v_mov_b32_dpp v13, v11 quad_perm:[2,3,0,1] row_mask:0xf bank_mask:0xf
	s_nop 1
	v_mov_b32_dpp v12, v10 quad_perm:[2,3,0,1] row_mask:0xf bank_mask:0xf
	v_pk_add_f32 v[10:11], v[10:11], v[12:13]
	ds_swizzle_b32 v13, v11 offset:swizzle(SWAP,4)
	ds_swizzle_b32 v12, v10 offset:swizzle(SWAP,4)
	s_waitcnt lgkmcnt(0)
	v_pk_add_f32 v[10:11], v[10:11], v[12:13]
	ds_swizzle_b32 v167, v11 offset:swizzle(SWAP,8)
	ds_swizzle_b32 v166, v10 offset:swizzle(SWAP,8)
	v_pk_add_f32 v[12:13], v[6:7], v[8:9]
	ds_swizzle_b32 v15, v13 offset:swizzle(SWAP,16)
	ds_swizzle_b32 v14, v12 offset:swizzle(SWAP,16)
	s_waitcnt lgkmcnt(0)
; #define SBAR() __builtin_amdgcn_sched_barrier(0)
; __device__ __forceinline__ int crow(int r, int hi) { return (r & 3) + 8 * (r >> 2) + 4 * hi; }
; __device__ __forceinline__ float mul_ns(float a, float b) { float r; asm("v_mul_f32 %0, %1, %2" : "=v"(r) : "v"(a), "v"(b)); return r; }
; __device__ __forceinline__ float fma_ns(float a, float b, float c) { float r; asm("v_fma_f32 %0, %1, %2, %3" : "=v"(r) : "v"(a), "v"(b), "v"(c)); return r; }
; __device__ __forceinline__ void store_quad8(unsigned char* p, float v, int r32) {
;     v = fminf(fmaxf(v, -448.f), 448.f);
;     const float v1 = swz_xor<1>(v);
;     const int w = __builtin_amdgcn_cvt_pk_fp8_f32(v, v1, 0, false);
;     const int w2 = __builtin_amdgcn_ds_swizzle(w, (2 << 10) | 0x1f);
;     if ((r32 & 3) == 0) *(unsigned*)p = ((unsigned)w & 0xffffu) | ((unsigned)w2 << 16);
; }
;     __device__ __forceinline__ void operator()(f32x16 (&o)[8], const float (&rli)[16], int wid, int lane, int r32, int hi) const {
;     ...
;             float g[8];
; #pragma unroll
;             for (int d0 = 0; d0 < 8; ++d0) g[d0] = gain[d0 * 32 + r32];
; #pragma unroll
;             for (int rb = 0; rb < 16; rb += 4) { unsigned tw[4][4];
; #pragma unroll
;                 for (int q = 0; q < 4; ++q)
; #pragma unroll
;                     for (int k = 0; k < 4; ++k) tw[q][k] = (scw + ((rb + q) * 4 + k) * 64)[ul];
;                 asm volatile("" ::: "memory"); SBAR();
; #pragma unroll
;                 for (int q = 0; q < 4; ++q) { const int r = rb + q;
; #pragma unroll
;                     for (int d0 = 0; d0 < 8; ++d0) { const float t = __uint_as_float((d0 & 1) ? (tw[q][d0 >> 1] & 0xffff0000u) : (tw[q][d0 >> 1] << 16));
;                         const float dd = fma_ns(nlam, mul_ns(o[d0][r], rli[r]), t);
;                         store_quad8(base + (crow(r, 0) * 4096 + d0 * 32) + uo, mul_ns(mul_ns(dd, rn[r]), g[d0]), r32); } }
;                 asm volatile("" ::: "memory"); SBAR(); }
	v_pk_add_f32 v[8:9], v[10:11], v[166:167]
	ds_swizzle_b32 v11, v9 offset:swizzle(SWAP,16)
	ds_swizzle_b32 v10, v8 offset:swizzle(SWAP,16)
	v_readlane_b32 s12, v253, 10
	v_ashrrev_i32_e32 v203, 31, v202
	v_readlane_b32 s14, v253, 12
	v_readlane_b32 s15, v253, 13
	s_add_u32 s6, s8, s6
	s_addc_u32 s7, s9, s7
	v_lshl_add_u64 v[6:7], v[202:203], 2, s[14:15]
	global_load_dword v190, v[6:7], off
	global_load_dword v189, v[6:7], off offset:128
	global_load_dword v188, v[6:7], off offset:256
	global_load_dword v187, v[6:7], off offset:384
	global_load_dword v186, v[6:7], off offset:512
	global_load_dword v185, v[6:7], off offset:640
	global_load_dword v184, v[6:7], off offset:768
	global_load_dword v165, v[6:7], off offset:896
	global_load_dword v217, v[4:5], off
	global_load_dword v215, v[4:5], off offset:256
	global_load_dword v214, v[4:5], off offset:512
	global_load_dword v209, v[4:5], off offset:768
	global_load_dword v208, v[4:5], off offset:1024
	global_load_dword v207, v[4:5], off offset:1280
	global_load_dword v206, v[4:5], off offset:1536
	global_load_dword v205, v[4:5], off offset:1792
	global_load_dword v204, v[4:5], off offset:2048
	global_load_dword v203, v[4:5], off offset:2304
	global_load_dword v201, v[4:5], off offset:2560
	global_load_dword v197, v[4:5], off offset:2816
	global_load_dword v196, v[4:5], off offset:3072
	global_load_dword v195, v[4:5], off offset:3328
	global_load_dword v194, v[4:5], off offset:3584
	global_load_dword v193, v[4:5], off offset:3840
	v_lshl_add_u32 v2, v213, 14, v202
	v_and_b32_e32 v6, 3, v202
	v_lshl_add_u64 v[166:167], s[6:7], 0, v[2:3]
	s_mov_b64 s[6:7], 0x800
	v_cmp_eq_u32_e64 s[4:5], 0, v6
	v_lshl_add_u64 v[6:7], v[166:167], 0, s[6:7]
	v_readlane_b32 s13, v253, 11
	v_readlane_b32 s16, v253, 14
	v_readlane_b32 s17, v253, 15
	v_readlane_b32 s18, v253, 16
	v_readlane_b32 s19, v253, 17
	v_readlane_b32 s20, v253, 18
	v_readlane_b32 s21, v253, 19
	v_readlane_b32 s22, v253, 20
	v_readlane_b32 s23, v253, 21
	v_readlane_b32 s24, v253, 22
	v_readlane_b32 s25, v253, 23
	v_readlane_b32 s26, v253, 24
	v_readlane_b32 s27, v253, 25
	s_waitcnt vmcnt(15)
	v_lshlrev_b32_e32 v2, 16, v217
	v_fma_f32 v2, v212, v192, v2
	s_nop 0
	v_mul_f32 v2, v2, v191
	s_nop 0
	v_mul_f32 v2, v2, v190
	s_nop 0
	v_max_f32_e32 v2, 0xc3e00000, v2
	v_min_f32_e32 v192, 0x43e00000, v2
	s_nop 1
	v_mov_b32_dpp v202, v192 quad_perm:[1,0,3,2] row_mask:0xf bank_mask:0xf
	s_waitcnt lgkmcnt(0)
	v_cvt_pk_fp8_f32 v2, v192, v202
	s_nop 1
	v_mov_b32_dpp v192, v2 quad_perm:[2,3,0,1] row_mask:0xf bank_mask:0xf
	s_and_saveexec_b64 s[6:7], s[4:5]
	v_and_b32_e32 v2, 0xffff, v2
	v_lshl_or_b32 v2, v192, 16, v2
	global_store_dword v[6:7], v2, off
.LBB0_1295:
	s_or_b64 exec, exec, s[6:7]
	v_and_b32_e32 v2, 0xffff0000, v217
	v_mul_f32 v192, v114, v183
	s_nop 0
	v_fma_f32 v2, v212, v192, v2
	s_nop 0
	v_mul_f32 v2, v2, v191
	s_nop 0
	v_mul_f32 v2, v2, v189
	s_nop 0
	v_max_f32_e32 v2, 0xc3e00000, v2
	v_min_f32_e32 v192, 0x43e00000, v2
	s_nop 1
	v_mov_b32_dpp v202, v192 quad_perm:[1,0,3,2] row_mask:0xf bank_mask:0xf
	v_cvt_pk_fp8_f32 v2, v192, v202
	s_nop 1
	v_mov_b32_dpp v192, v2 quad_perm:[2,3,0,1] row_mask:0xf bank_mask:0xf
	s_and_saveexec_b64 s[6:7], s[4:5]
	v_and_b32_e32 v2, 0xffff, v2
	v_lshl_or_b32 v2, v192, 16, v2
	global_store_dword v[166:167], v2, off offset:2080
.LBB0_1297:
	s_or_b64 exec, exec, s[6:7]
	s_waitcnt vmcnt(14)
	v_lshlrev_b32_e32 v2, 16, v215
	v_mul_f32 v192, v98, v183
	s_nop 0
	v_fma_f32 v2, v212, v192, v2
	s_nop 0
	v_mul_f32 v2, v2, v191
	s_nop 0
	v_mul_f32 v2, v2, v188
	s_nop 0
	v_max_f32_e32 v2, 0xc3e00000, v2
	v_min_f32_e32 v192, 0x43e00000, v2
	s_nop 1
	v_mov_b32_dpp v202, v192 quad_perm:[1,0,3,2] row_mask:0xf bank_mask:0xf
	v_cvt_pk_fp8_f32 v2, v192, v202
	s_nop 1
	v_mov_b32_dpp v192, v2 quad_perm:[2,3,0,1] row_mask:0xf bank_mask:0xf
	s_and_saveexec_b64 s[6:7], s[4:5]
	v_and_b32_e32 v2, 0xffff, v2
	v_lshl_or_b32 v2, v192, 16, v2
	global_store_dword v[166:167], v2, off offset:2112
.LBB0_1299:
	s_or_b64 exec, exec, s[6:7]
	v_and_b32_e32 v2, 0xffff0000, v215
	v_mul_f32 v192, v82, v183
	s_nop 0
	v_fma_f32 v2, v212, v192, v2
	s_nop 0
	v_mul_f32 v2, v2, v191
	s_nop 0
	v_mul_f32 v2, v2, v187
	s_nop 0
	v_max_f32_e32 v2, 0xc3e00000, v2
	v_min_f32_e32 v192, 0x43e00000, v2
	s_nop 1
	v_mov_b32_dpp v202, v192 quad_perm:[1,0,3,2] row_mask:0xf bank_mask:0xf
	v_cvt_pk_fp8_f32 v2, v192, v202
	s_nop 1
	v_mov_b32_dpp v192, v2 quad_perm:[2,3,0,1] row_mask:0xf bank_mask:0xf
	s_and_saveexec_b64 s[6:7], s[4:5]
	v_and_b32_e32 v2, 0xffff, v2
	v_lshl_or_b32 v2, v192, 16, v2
	global_store_dword v[166:167], v2, off offset:2144
.LBB0_1301:
	s_or_b64 exec, exec, s[6:7]
	s_waitcnt vmcnt(13)
	v_lshlrev_b32_e32 v2, 16, v214
	v_mul_f32 v192, v66, v183
	s_nop 0
	v_fma_f32 v2, v212, v192, v2
	s_nop 0
	v_mul_f32 v2, v2, v191
	s_nop 0
	v_mul_f32 v2, v2, v186
	s_nop 0
	v_max_f32_e32 v2, 0xc3e00000, v2
	v_min_f32_e32 v192, 0x43e00000, v2
	s_nop 1
	v_mov_b32_dpp v202, v192 quad_perm:[1,0,3,2] row_mask:0xf bank_mask:0xf
	v_cvt_pk_fp8_f32 v2, v192, v202
	s_nop 1
	v_mov_b32_dpp v192, v2 quad_perm:[2,3,0,1] row_mask:0xf bank_mask:0xf
	s_and_saveexec_b64 s[6:7], s[4:5]
	v_and_b32_e32 v2, 0xffff, v2
	v_lshl_or_b32 v2, v192, 16, v2
	global_store_dword v[166:167], v2, off offset:2176
.LBB0_1303:
	s_or_b64 exec, exec, s[6:7]
	v_and_b32_e32 v2, 0xffff0000, v214
	v_mul_f32 v192, v50, v183
	s_nop 0
	v_fma_f32 v2, v212, v192, v2
	s_nop 0
	v_mul_f32 v2, v2, v191
	s_nop 0
	v_mul_f32 v2, v2, v185
	s_nop 0
	v_max_f32_e32 v2, 0xc3e00000, v2
	v_min_f32_e32 v192, 0x43e00000, v2
	s_nop 1
	v_mov_b32_dpp v202, v192 quad_perm:[1,0,3,2] row_mask:0xf bank_mask:0xf
	v_cvt_pk_fp8_f32 v2, v192, v202
	s_nop 1
	v_mov_b32_dpp v192, v2 quad_perm:[2,3,0,1] row_mask:0xf bank_mask:0xf
	s_and_saveexec_b64 s[6:7], s[4:5]
	v_and_b32_e32 v2, 0xffff, v2
	v_lshl_or_b32 v2, v192, 16, v2
	global_store_dword v[166:167], v2, off offset:2208
; #define SBAR() __builtin_amdgcn_sched_barrier(0)
; __device__ __forceinline__ int crow(int r, int hi) { return (r & 3) + 8 * (r >> 2) + 4 * hi; }
; __device__ __forceinline__ float mul_ns(float a, float b) { float r; asm("v_mul_f32 %0, %1, %2" : "=v"(r) : "v"(a), "v"(b)); return r; }
; __device__ __forceinline__ float fma_ns(float a, float b, float c) { float r; asm("v_fma_f32 %0, %1, %2, %3" : "=v"(r) : "v"(a), "v"(b), "v"(c)); return r; }
; __device__ __forceinline__ void store_quad8(unsigned char* p, float v, int r32) {
;     v = fminf(fmaxf(v, -448.f), 448.f);
;     const float v1 = swz_xor<1>(v);
;     const int w = __builtin_amdgcn_cvt_pk_fp8_f32(v, v1, 0, false);
;     const int w2 = __builtin_amdgcn_ds_swizzle(w, (2 << 10) | 0x1f);
;     if ((r32 & 3) == 0) *(unsigned*)p = ((unsigned)w & 0xffffu) | ((unsigned)w2 << 16);
; }
;     __device__ __forceinline__ void operator()(f32x16 (&o)[8], const float (&rli)[16], int wid, int lane, int r32, int hi) const {
;     ...
;             for (int rb = 0; rb < 16; rb += 4) { unsigned tw[4][4];
; #pragma unroll
;                 for (int q = 0; q < 4; ++q)
; #pragma unroll
;                     for (int k = 0; k < 4; ++k) tw[q][k] = (scw + ((rb + q) * 4 + k) * 64)[ul];
;                 asm volatile("" ::: "memory"); SBAR();
; #pragma unroll
;                 for (int q = 0; q < 4; ++q) { const int r = rb + q;
; #pragma unroll
;                     for (int d0 = 0; d0 < 8; ++d0) { const float t = __uint_as_float((d0 & 1) ? (tw[q][d0 >> 1] & 0xffff0000u) : (tw[q][d0 >> 1] << 16));
;                         const float dd = fma_ns(nlam, mul_ns(o[d0][r], rli[r]), t);
;                         store_quad8(base + (crow(r, 0) * 4096 + d0 * 32) + uo, mul_ns(mul_ns(dd, rn[r]), g[d0]), r32); } }
;                 asm volatile("" ::: "memory"); SBAR(); }
.LBB0_1305:
	s_or_b64 exec, exec, s[6:7]
	s_waitcnt vmcnt(12)
	v_lshlrev_b32_e32 v2, 16, v209
	v_mul_f32 v192, v34, v183
	s_nop 0
	v_fma_f32 v2, v212, v192, v2
	s_nop 0
	v_mul_f32 v2, v2, v191
	s_nop 0
	v_mul_f32 v2, v2, v184
	s_nop 0
	v_max_f32_e32 v2, 0xc3e00000, v2
	v_min_f32_e32 v192, 0x43e00000, v2
	s_nop 1
	v_mov_b32_dpp v202, v192 quad_perm:[1,0,3,2] row_mask:0xf bank_mask:0xf
	v_cvt_pk_fp8_f32 v2, v192, v202
	s_nop 1
	v_mov_b32_dpp v192, v2 quad_perm:[2,3,0,1] row_mask:0xf bank_mask:0xf
	s_and_saveexec_b64 s[6:7], s[4:5]
	v_and_b32_e32 v2, 0xffff, v2
	v_lshl_or_b32 v2, v192, 16, v2
	global_store_dword v[166:167], v2, off offset:2240
.LBB0_1307:
	s_or_b64 exec, exec, s[6:7]
	v_and_b32_e32 v2, 0xffff0000, v209
	v_mul_f32 v192, v18, v183
	s_nop 0
	v_fma_f32 v2, v212, v192, v2
	s_nop 0
	v_mul_f32 v2, v2, v191
	s_nop 0
	v_mul_f32 v2, v2, v165
	s_nop 0
	v_max_f32_e32 v2, 0xc3e00000, v2
	v_min_f32_e32 v191, 0x43e00000, v2
	s_nop 1
	v_mov_b32_dpp v192, v191 quad_perm:[1,0,3,2] row_mask:0xf bank_mask:0xf
	v_cvt_pk_fp8_f32 v2, v191, v192
	s_nop 1
	v_mov_b32_dpp v191, v2 quad_perm:[2,3,0,1] row_mask:0xf bank_mask:0xf
	s_and_saveexec_b64 s[6:7], s[4:5]
	v_and_b32_e32 v2, 0xffff, v2
	v_lshl_or_b32 v2, v191, 16, v2
	global_store_dword v[166:167], v2, off offset:2272
.LBB0_1309:
	s_or_b64 exec, exec, s[6:7]
	v_mul_f32_e32 v2, 0x4b800000, v164
	v_cndmask_b32_e32 v2, v164, v2, vcc
	v_rsq_f32_e32 v2, v2
	v_mul_f32 v166, v131, v182
	s_nop 0
	v_mul_f32_e32 v164, 0x45800000, v2
	v_cndmask_b32_e32 v2, v2, v164, vcc
	s_waitcnt vmcnt(11)
	v_lshlrev_b32_e32 v164, 16, v208
	v_fma_f32 v164, v212, v166, v164
	v_mul_f32_e32 v2, 0x3f4ccccd, v2
	v_mul_f32 v164, v164, v2
	s_nop 0
	v_mul_f32 v164, v164, v190
	s_nop 0
	v_max_f32_e32 v164, 0xc3e00000, v164
	v_min_f32_e32 v166, 0x43e00000, v164
	s_nop 1
	v_mov_b32_dpp v167, v166 quad_perm:[1,0,3,2] row_mask:0xf bank_mask:0xf
	v_cvt_pk_fp8_f32 v164, v166, v167
	s_nop 1
	v_mov_b32_dpp v166, v164 quad_perm:[2,3,0,1] row_mask:0xf bank_mask:0xf
	s_and_saveexec_b64 s[6:7], s[4:5]
	s_cbranch_execz .LBB0_1311
	v_and_b32_e32 v164, 0xffff, v164
	s_waitcnt lgkmcnt(0)
	v_lshl_or_b32 v164, v166, 16, v164
	v_add_co_u32_e32 v166, vcc, 0x1000, v6
	s_nop 1
	v_addc_co_u32_e32 v167, vcc, 0, v7, vcc
	global_store_dword v[166:167], v164, off
.LBB0_1311:
	s_or_b64 exec, exec, s[6:7]
	v_and_b32_e32 v164, 0xffff0000, v208
	s_waitcnt lgkmcnt(0)
	v_mul_f32 v166, v115, v182
	s_nop 0
	v_fma_f32 v164, v212, v166, v164
	s_nop 0
	v_mul_f32 v164, v164, v2
	s_nop 0
	v_mul_f32 v164, v164, v189
	s_nop 0
	v_max_f32_e32 v164, 0xc3e00000, v164
	v_min_f32_e32 v166, 0x43e00000, v164
	s_nop 1
	v_mov_b32_dpp v167, v166 quad_perm:[1,0,3,2] row_mask:0xf bank_mask:0xf
	v_cvt_pk_fp8_f32 v164, v166, v167
	s_nop 1
	v_mov_b32_dpp v166, v164 quad_perm:[2,3,0,1] row_mask:0xf bank_mask:0xf
	s_and_saveexec_b64 s[6:7], s[4:5]
	s_cbranch_execz .LBB0_1313
	v_and_b32_e32 v164, 0xffff, v164
	s_waitcnt lgkmcnt(0)
	v_lshl_or_b32 v164, v166, 16, v164
	v_add_co_u32_e32 v166, vcc, 0x1000, v6
	s_nop 1
	v_addc_co_u32_e32 v167, vcc, 0, v7, vcc
	global_store_dword v[166:167], v164, off offset:32
.LBB0_1313:
	s_or_b64 exec, exec, s[6:7]
	s_waitcnt vmcnt(10)
	v_lshlrev_b32_e32 v164, 16, v207
	s_waitcnt lgkmcnt(0)
	v_mul_f32 v166, v99, v182
	s_nop 0
	v_fma_f32 v164, v212, v166, v164
	s_nop 0
	v_mul_f32 v164, v164, v2
	s_nop 0
	v_mul_f32 v164, v164, v188
	s_nop 0
	v_max_f32_e32 v164, 0xc3e00000, v164
	v_min_f32_e32 v166, 0x43e00000, v164
	s_nop 1
	v_mov_b32_dpp v167, v166 quad_perm:[1,0,3,2] row_mask:0xf bank_mask:0xf
	v_cvt_pk_fp8_f32 v164, v166, v167
	s_nop 1
	v_mov_b32_dpp v166, v164 quad_perm:[2,3,0,1] row_mask:0xf bank_mask:0xf
	s_and_saveexec_b64 s[6:7], s[4:5]
	s_cbranch_execz .LBB0_1315
	v_and_b32_e32 v164, 0xffff, v164
	s_waitcnt lgkmcnt(0)
	v_lshl_or_b32 v164, v166, 16, v164
	v_add_co_u32_e32 v166, vcc, 0x1000, v6
	s_nop 1
	v_addc_co_u32_e32 v167, vcc, 0, v7, vcc
	global_store_dword v[166:167], v164, off offset:64
.LBB0_1315:
	s_or_b64 exec, exec, s[6:7]
	v_and_b32_e32 v164, 0xffff0000, v207
	s_waitcnt lgkmcnt(0)
	v_mul_f32 v166, v83, v182
	s_nop 0
	v_fma_f32 v164, v212, v166, v164
	s_nop 0
	v_mul_f32 v164, v164, v2
	s_nop 0
	v_mul_f32 v164, v164, v187
	s_nop 0
	v_max_f32_e32 v164, 0xc3e00000, v164
	v_min_f32_e32 v166, 0x43e00000, v164
	s_nop 1
	v_mov_b32_dpp v167, v166 quad_perm:[1,0,3,2] row_mask:0xf bank_mask:0xf
	v_cvt_pk_fp8_f32 v164, v166, v167
	s_nop 1
	v_mov_b32_dpp v166, v164 quad_perm:[2,3,0,1] row_mask:0xf bank_mask:0xf
	s_and_saveexec_b64 s[6:7], s[4:5]
	s_cbranch_execz .LBB0_1317
	v_and_b32_e32 v164, 0xffff, v164
	s_waitcnt lgkmcnt(0)
	v_lshl_or_b32 v164, v166, 16, v164
	v_add_co_u32_e32 v166, vcc, 0x1000, v6
	s_nop 1
	v_addc_co_u32_e32 v167, vcc, 0, v7, vcc
	global_store_dword v[166:167], v164, off offset:96
.LBB0_1317:
	s_or_b64 exec, exec, s[6:7]
	s_waitcnt vmcnt(9)
	v_lshlrev_b32_e32 v164, 16, v206
	s_waitcnt lgkmcnt(0)
	v_mul_f32 v166, v67, v182
	s_nop 0
	v_fma_f32 v164, v212, v166, v164
	s_nop 0
	v_mul_f32 v164, v164, v2
	s_nop 0
	v_mul_f32 v164, v164, v186
	s_nop 0
	v_max_f32_e32 v164, 0xc3e00000, v164
	v_min_f32_e32 v166, 0x43e00000, v164
	s_nop 1
	v_mov_b32_dpp v167, v166 quad_perm:[1,0,3,2] row_mask:0xf bank_mask:0xf
	v_cvt_pk_fp8_f32 v164, v166, v167
	s_nop 1
	v_mov_b32_dpp v166, v164 quad_perm:[2,3,0,1] row_mask:0xf bank_mask:0xf
	s_and_saveexec_b64 s[6:7], s[4:5]
	s_cbranch_execz .LBB0_1319
	v_and_b32_e32 v164, 0xffff, v164
	s_waitcnt lgkmcnt(0)
	v_lshl_or_b32 v164, v166, 16, v164
	v_add_co_u32_e32 v166, vcc, 0x1000, v6
	s_nop 1
	v_addc_co_u32_e32 v167, vcc, 0, v7, vcc
	global_store_dword v[166:167], v164, off offset:128
; #define SBAR() __builtin_amdgcn_sched_barrier(0)
; __device__ __forceinline__ int crow(int r, int hi) { return (r & 3) + 8 * (r >> 2) + 4 * hi; }
; __device__ __forceinline__ float mul_ns(float a, float b) { float r; asm("v_mul_f32 %0, %1, %2" : "=v"(r) : "v"(a), "v"(b)); return r; }
; __device__ __forceinline__ float fma_ns(float a, float b, float c) { float r; asm("v_fma_f32 %0, %1, %2, %3" : "=v"(r) : "v"(a), "v"(b), "v"(c)); return r; }
; __device__ __forceinline__ void store_quad8(unsigned char* p, float v, int r32) {
;     v = fminf(fmaxf(v, -448.f), 448.f);
;     const float v1 = swz_xor<1>(v);
;     const int w = __builtin_amdgcn_cvt_pk_fp8_f32(v, v1, 0, false);
;     const int w2 = __builtin_amdgcn_ds_swizzle(w, (2 << 10) | 0x1f);
;     if ((r32 & 3) == 0) *(unsigned*)p = ((unsigned)w & 0xffffu) | ((unsigned)w2 << 16);
; }
;     __device__ __forceinline__ void operator()(f32x16 (&o)[8], const float (&rli)[16], int wid, int lane, int r32, int hi) const {
;     ...
;             for (int rb = 0; rb < 16; rb += 4) { unsigned tw[4][4];
; #pragma unroll
;                 for (int q = 0; q < 4; ++q)
; #pragma unroll
;                     for (int k = 0; k < 4; ++k) tw[q][k] = (scw + ((rb + q) * 4 + k) * 64)[ul];
;                 asm volatile("" ::: "memory"); SBAR();
; #pragma unroll
;                 for (int q = 0; q < 4; ++q) { const int r = rb + q;
; #pragma unroll
;                     for (int d0 = 0; d0 < 8; ++d0) { const float t = __uint_as_float((d0 & 1) ? (tw[q][d0 >> 1] & 0xffff0000u) : (tw[q][d0 >> 1] << 16));
;                         const float dd = fma_ns(nlam, mul_ns(o[d0][r], rli[r]), t);
;                         store_quad8(base + (crow(r, 0) * 4096 + d0 * 32) + uo, mul_ns(mul_ns(dd, rn[r]), g[d0]), r32); } }
;                 asm volatile("" ::: "memory"); SBAR(); }
.LBB0_1319:
	s_or_b64 exec, exec, s[6:7]
	v_and_b32_e32 v164, 0xffff0000, v206
	s_waitcnt lgkmcnt(0)
	v_mul_f32 v166, v51, v182
	s_nop 0
	v_fma_f32 v164, v212, v166, v164
	s_nop 0
	v_mul_f32 v164, v164, v2
	s_nop 0
	v_mul_f32 v164, v164, v185
	s_nop 0
	v_max_f32_e32 v164, 0xc3e00000, v164
	v_min_f32_e32 v166, 0x43e00000, v164
	s_nop 1
	v_mov_b32_dpp v167, v166 quad_perm:[1,0,3,2] row_mask:0xf bank_mask:0xf
	v_cvt_pk_fp8_f32 v164, v166, v167
	s_nop 1
	v_mov_b32_dpp v166, v164 quad_perm:[2,3,0,1] row_mask:0xf bank_mask:0xf
	s_and_saveexec_b64 s[6:7], s[4:5]
	s_cbranch_execz .LBB0_1321
	v_and_b32_e32 v164, 0xffff, v164
	s_waitcnt lgkmcnt(0)
	v_lshl_or_b32 v164, v166, 16, v164
	v_add_co_u32_e32 v166, vcc, 0x1000, v6
	s_nop 1
	v_addc_co_u32_e32 v167, vcc, 0, v7, vcc
	global_store_dword v[166:167], v164, off offset:160
.LBB0_1321:
	s_or_b64 exec, exec, s[6:7]
	s_waitcnt vmcnt(8)
	v_lshlrev_b32_e32 v164, 16, v205
	s_waitcnt lgkmcnt(0)
	v_mul_f32 v166, v35, v182
	s_nop 0
	v_fma_f32 v164, v212, v166, v164
	s_nop 0
	v_mul_f32 v164, v164, v2
	s_nop 0
	v_mul_f32 v164, v164, v184
	s_nop 0
	v_max_f32_e32 v164, 0xc3e00000, v164
	v_min_f32_e32 v166, 0x43e00000, v164
	s_nop 1
	v_mov_b32_dpp v167, v166 quad_perm:[1,0,3,2] row_mask:0xf bank_mask:0xf
	v_cvt_pk_fp8_f32 v164, v166, v167
	s_nop 1
	v_mov_b32_dpp v166, v164 quad_perm:[2,3,0,1] row_mask:0xf bank_mask:0xf
	s_and_saveexec_b64 s[6:7], s[4:5]
	s_cbranch_execz .LBB0_1323
	v_and_b32_e32 v164, 0xffff, v164
	s_waitcnt lgkmcnt(0)
	v_lshl_or_b32 v164, v166, 16, v164
	v_add_co_u32_e32 v166, vcc, 0x1000, v6
	s_nop 1
	v_addc_co_u32_e32 v167, vcc, 0, v7, vcc
	global_store_dword v[166:167], v164, off offset:192
.LBB0_1323:
	s_or_b64 exec, exec, s[6:7]
	v_and_b32_e32 v164, 0xffff0000, v205
	s_waitcnt lgkmcnt(0)
	v_mul_f32 v166, v19, v182
	s_nop 0
	v_fma_f32 v164, v212, v166, v164
	s_nop 0
	v_mul_f32 v2, v164, v2
	s_nop 0
	v_mul_f32 v2, v2, v165
	s_nop 0
	v_max_f32_e32 v2, 0xc3e00000, v2
	v_min_f32_e32 v164, 0x43e00000, v2
	s_nop 1
	v_mov_b32_dpp v166, v164 quad_perm:[1,0,3,2] row_mask:0xf bank_mask:0xf
	v_cvt_pk_fp8_f32 v2, v164, v166
	s_nop 1
	v_mov_b32_dpp v164, v2 quad_perm:[2,3,0,1] row_mask:0xf bank_mask:0xf
	s_and_saveexec_b64 s[6:7], s[4:5]
	v_and_b32_e32 v2, 0xffff, v2
	v_add_co_u32_e32 v166, vcc, 0x1000, v6
	v_lshl_or_b32 v2, v164, 16, v2
	v_addc_co_u32_e32 v167, vcc, 0, v7, vcc
	global_store_dword v[166:167], v2, off offset:224
.LBB0_1325:
	s_or_b64 exec, exec, s[6:7]
	v_pk_add_f32 v[160:161], v[160:161], v[162:163]
	v_mul_f32 v162, v132, v181
	s_nop 0
	v_pk_fma_f32 v[160:161], v[160:161], s[54:55], v[198:199] op_sel_hi:[1,0,0]
	s_nop 0
	v_mul_f32_e32 v2, 0x4b800000, v161
	v_cmp_gt_f32_e32 vcc, s53, v161
	v_cmp_gt_f32_e64 s[6:7], s53, v160
	s_nop 0
	v_cndmask_b32_e32 v2, v161, v2, vcc
	v_rsq_f32_e32 v2, v2
	s_waitcnt vmcnt(7)
	v_lshlrev_b32_e32 v161, 16, v204
	v_fma_f32 v161, v212, v162, v161
	v_mul_f32_e32 v163, 0x45800000, v2
	v_cndmask_b32_e32 v2, v2, v163, vcc
	v_mul_f32_e32 v2, 0x3f4ccccd, v2
	v_mul_f32 v161, v161, v2
	s_nop 0
	v_mul_f32 v161, v161, v190
	s_nop 0
	v_max_f32_e32 v161, 0xc3e00000, v161
	v_min_f32_e32 v162, 0x43e00000, v161
	s_nop 1
	v_mov_b32_dpp v163, v162 quad_perm:[1,0,3,2] row_mask:0xf bank_mask:0xf
	v_cvt_pk_fp8_f32 v161, v162, v163
	s_nop 1
	v_mov_b32_dpp v162, v161 quad_perm:[2,3,0,1] row_mask:0xf bank_mask:0xf
	s_and_saveexec_b64 s[8:9], s[4:5]
	s_cbranch_execz .LBB0_1327
	v_and_b32_e32 v161, 0xffff, v161
	s_waitcnt lgkmcnt(0)
	v_lshl_or_b32 v161, v162, 16, v161
	v_add_co_u32_e32 v162, vcc, 0x2000, v6
	s_nop 1
	v_addc_co_u32_e32 v163, vcc, 0, v7, vcc
	global_store_dword v[162:163], v161, off
.LBB0_1327:
	s_or_b64 exec, exec, s[8:9]
	v_and_b32_e32 v161, 0xffff0000, v204
	s_waitcnt lgkmcnt(0)
	v_mul_f32 v162, v116, v181
	s_nop 0
	v_fma_f32 v161, v212, v162, v161
	s_nop 0
	v_mul_f32 v161, v161, v2
	s_nop 0
	v_mul_f32 v161, v161, v189
	s_nop 0
	v_max_f32_e32 v161, 0xc3e00000, v161
	v_min_f32_e32 v162, 0x43e00000, v161
	s_nop 1
	v_mov_b32_dpp v163, v162 quad_perm:[1,0,3,2] row_mask:0xf bank_mask:0xf
	v_cvt_pk_fp8_f32 v161, v162, v163
	s_nop 1
	v_mov_b32_dpp v162, v161 quad_perm:[2,3,0,1] row_mask:0xf bank_mask:0xf
	s_and_saveexec_b64 s[8:9], s[4:5]
	s_cbranch_execz .LBB0_1329
	v_and_b32_e32 v161, 0xffff, v161
	s_waitcnt lgkmcnt(0)
	v_lshl_or_b32 v161, v162, 16, v161
	v_add_co_u32_e32 v162, vcc, 0x2000, v6
	s_nop 1
	v_addc_co_u32_e32 v163, vcc, 0, v7, vcc
	global_store_dword v[162:163], v161, off offset:32
.LBB0_1329:
	s_or_b64 exec, exec, s[8:9]
	s_waitcnt vmcnt(6)
	v_lshlrev_b32_e32 v161, 16, v203
	s_waitcnt lgkmcnt(0)
	v_mul_f32 v162, v100, v181
	s_nop 0
	v_fma_f32 v161, v212, v162, v161
	s_nop 0
	v_mul_f32 v161, v161, v2
	s_nop 0
	v_mul_f32 v161, v161, v188
	s_nop 0
	v_max_f32_e32 v161, 0xc3e00000, v161
	v_min_f32_e32 v162, 0x43e00000, v161
	s_nop 1
	v_mov_b32_dpp v163, v162 quad_perm:[1,0,3,2] row_mask:0xf bank_mask:0xf
	v_cvt_pk_fp8_f32 v161, v162, v163
	s_nop 1
	v_mov_b32_dpp v162, v161 quad_perm:[2,3,0,1] row_mask:0xf bank_mask:0xf
	s_and_saveexec_b64 s[8:9], s[4:5]
	s_cbranch_execz .LBB0_1331
	v_and_b32_e32 v161, 0xffff, v161
	s_waitcnt lgkmcnt(0)
	v_lshl_or_b32 v161, v162, 16, v161
	v_add_co_u32_e32 v162, vcc, 0x2000, v6
	s_nop 1
	v_addc_co_u32_e32 v163, vcc, 0, v7, vcc
	global_store_dword v[162:163], v161, off offset:64
; #define SBAR() __builtin_amdgcn_sched_barrier(0)
; __device__ __forceinline__ int crow(int r, int hi) { return (r & 3) + 8 * (r >> 2) + 4 * hi; }
; __device__ __forceinline__ float mul_ns(float a, float b) { float r; asm("v_mul_f32 %0, %1, %2" : "=v"(r) : "v"(a), "v"(b)); return r; }
; __device__ __forceinline__ float fma_ns(float a, float b, float c) { float r; asm("v_fma_f32 %0, %1, %2, %3" : "=v"(r) : "v"(a), "v"(b), "v"(c)); return r; }
; __device__ __forceinline__ void store_quad8(unsigned char* p, float v, int r32) {
;     v = fminf(fmaxf(v, -448.f), 448.f);
;     const float v1 = swz_xor<1>(v);
;     const int w = __builtin_amdgcn_cvt_pk_fp8_f32(v, v1, 0, false);
;     const int w2 = __builtin_amdgcn_ds_swizzle(w, (2 << 10) | 0x1f);
;     if ((r32 & 3) == 0) *(unsigned*)p = ((unsigned)w & 0xffffu) | ((unsigned)w2 << 16);
; }
;     __device__ __forceinline__ void operator()(f32x16 (&o)[8], const float (&rli)[16], int wid, int lane, int r32, int hi) const {
;     ...
;             for (int rb = 0; rb < 16; rb += 4) { unsigned tw[4][4];
; #pragma unroll
;                 for (int q = 0; q < 4; ++q)
; #pragma unroll
;                     for (int k = 0; k < 4; ++k) tw[q][k] = (scw + ((rb + q) * 4 + k) * 64)[ul];
;                 asm volatile("" ::: "memory"); SBAR();
; #pragma unroll
;                 for (int q = 0; q < 4; ++q) { const int r = rb + q;
; #pragma unroll
;                     for (int d0 = 0; d0 < 8; ++d0) { const float t = __uint_as_float((d0 & 1) ? (tw[q][d0 >> 1] & 0xffff0000u) : (tw[q][d0 >> 1] << 16));
;                         const float dd = fma_ns(nlam, mul_ns(o[d0][r], rli[r]), t);
;                         store_quad8(base + (crow(r, 0) * 4096 + d0 * 32) + uo, mul_ns(mul_ns(dd, rn[r]), g[d0]), r32); } }
;                 asm volatile("" ::: "memory"); SBAR(); }
.LBB0_1331:
	s_or_b64 exec, exec, s[8:9]
	v_and_b32_e32 v161, 0xffff0000, v203
	s_waitcnt lgkmcnt(0)
	v_mul_f32 v162, v84, v181
	s_nop 0
	v_fma_f32 v161, v212, v162, v161
	s_nop 0
	v_mul_f32 v161, v161, v2
	s_nop 0
	v_mul_f32 v161, v161, v187
	s_nop 0
	v_max_f32_e32 v161, 0xc3e00000, v161
	v_min_f32_e32 v162, 0x43e00000, v161
	s_nop 1
	v_mov_b32_dpp v163, v162 quad_perm:[1,0,3,2] row_mask:0xf bank_mask:0xf
	v_cvt_pk_fp8_f32 v161, v162, v163
	s_nop 1
	v_mov_b32_dpp v162, v161 quad_perm:[2,3,0,1] row_mask:0xf bank_mask:0xf
	s_and_saveexec_b64 s[8:9], s[4:5]
	s_cbranch_execz .LBB0_1333
	v_and_b32_e32 v161, 0xffff, v161
	s_waitcnt lgkmcnt(0)
	v_lshl_or_b32 v161, v162, 16, v161
	v_add_co_u32_e32 v162, vcc, 0x2000, v6
	s_nop 1
	v_addc_co_u32_e32 v163, vcc, 0, v7, vcc
	global_store_dword v[162:163], v161, off offset:96
.LBB0_1333:
	s_or_b64 exec, exec, s[8:9]
	s_waitcnt vmcnt(5)
	v_lshlrev_b32_e32 v161, 16, v201
	s_waitcnt lgkmcnt(0)
	v_mul_f32 v162, v68, v181
	s_nop 0
	v_fma_f32 v161, v212, v162, v161
	s_nop 0
	v_mul_f32 v161, v161, v2
	s_nop 0
	v_mul_f32 v161, v161, v186
	s_nop 0
	v_max_f32_e32 v161, 0xc3e00000, v161
	v_min_f32_e32 v162, 0x43e00000, v161
	s_nop 1
	v_mov_b32_dpp v163, v162 quad_perm:[1,0,3,2] row_mask:0xf bank_mask:0xf
	v_cvt_pk_fp8_f32 v161, v162, v163
	s_nop 1
	v_mov_b32_dpp v162, v161 quad_perm:[2,3,0,1] row_mask:0xf bank_mask:0xf
	s_and_saveexec_b64 s[8:9], s[4:5]
	s_cbranch_execz .LBB0_1335
	v_and_b32_e32 v161, 0xffff, v161
	s_waitcnt lgkmcnt(0)
	v_lshl_or_b32 v161, v162, 16, v161
	v_add_co_u32_e32 v162, vcc, 0x2000, v6
	s_nop 1
	v_addc_co_u32_e32 v163, vcc, 0, v7, vcc
	global_store_dword v[162:163], v161, off offset:128
.LBB0_1335:
	s_or_b64 exec, exec, s[8:9]
	v_and_b32_e32 v161, 0xffff0000, v201
	s_waitcnt lgkmcnt(0)
	v_mul_f32 v162, v52, v181
	s_nop 0
	v_fma_f32 v161, v212, v162, v161
	s_nop 0
	v_mul_f32 v161, v161, v2
	s_nop 0
	v_mul_f32 v161, v161, v185
	s_nop 0
	v_max_f32_e32 v161, 0xc3e00000, v161
	v_min_f32_e32 v162, 0x43e00000, v161
	s_nop 1
	v_mov_b32_dpp v163, v162 quad_perm:[1,0,3,2] row_mask:0xf bank_mask:0xf
	v_cvt_pk_fp8_f32 v161, v162, v163
	s_nop 1
	v_mov_b32_dpp v162, v161 quad_perm:[2,3,0,1] row_mask:0xf bank_mask:0xf
	s_and_saveexec_b64 s[8:9], s[4:5]
	s_cbranch_execz .LBB0_1337
	v_and_b32_e32 v161, 0xffff, v161
	s_waitcnt lgkmcnt(0)
	v_lshl_or_b32 v161, v162, 16, v161
	v_add_co_u32_e32 v162, vcc, 0x2000, v6
	s_nop 1
	v_addc_co_u32_e32 v163, vcc, 0, v7, vcc
	global_store_dword v[162:163], v161, off offset:160
.LBB0_1337:
	s_or_b64 exec, exec, s[8:9]
	s_waitcnt vmcnt(4)
	v_lshlrev_b32_e32 v161, 16, v197
	s_waitcnt lgkmcnt(0)
	v_mul_f32 v162, v36, v181
	s_nop 0
	v_fma_f32 v161, v212, v162, v161
	s_nop 0
	v_mul_f32 v161, v161, v2
	s_nop 0
	v_mul_f32 v161, v161, v184
	s_nop 0
	v_max_f32_e32 v161, 0xc3e00000, v161
	v_min_f32_e32 v162, 0x43e00000, v161
	s_nop 1
	v_mov_b32_dpp v163, v162 quad_perm:[1,0,3,2] row_mask:0xf bank_mask:0xf
	v_cvt_pk_fp8_f32 v161, v162, v163
	s_nop 1
	v_mov_b32_dpp v162, v161 quad_perm:[2,3,0,1] row_mask:0xf bank_mask:0xf
	s_and_saveexec_b64 s[8:9], s[4:5]
	s_cbranch_execz .LBB0_1339
	v_and_b32_e32 v161, 0xffff, v161
	s_waitcnt lgkmcnt(0)
	v_lshl_or_b32 v161, v162, 16, v161
	v_add_co_u32_e32 v162, vcc, 0x2000, v6
	s_nop 1
	v_addc_co_u32_e32 v163, vcc, 0, v7, vcc
	global_store_dword v[162:163], v161, off offset:192
.LBB0_1339:
	s_or_b64 exec, exec, s[8:9]
	v_and_b32_e32 v161, 0xffff0000, v197
	s_waitcnt lgkmcnt(0)
	v_mul_f32 v162, v20, v181
	s_nop 0
	v_fma_f32 v161, v212, v162, v161
	s_nop 0
	v_mul_f32 v2, v161, v2
	s_nop 0
	v_mul_f32 v2, v2, v165
	s_nop 0
	v_max_f32_e32 v2, 0xc3e00000, v2
	v_min_f32_e32 v161, 0x43e00000, v2
	s_nop 1
	v_mov_b32_dpp v162, v161 quad_perm:[1,0,3,2] row_mask:0xf bank_mask:0xf
	v_cvt_pk_fp8_f32 v2, v161, v162
	s_nop 1
	v_mov_b32_dpp v161, v2 quad_perm:[2,3,0,1] row_mask:0xf bank_mask:0xf
	s_and_saveexec_b64 s[8:9], s[4:5]
	v_and_b32_e32 v2, 0xffff, v2
	v_add_co_u32_e32 v162, vcc, 0x2000, v6
	v_lshl_or_b32 v2, v161, 16, v2
	v_addc_co_u32_e32 v163, vcc, 0, v7, vcc
	global_store_dword v[162:163], v2, off offset:224
.LBB0_1341:
	s_or_b64 exec, exec, s[8:9]
	v_mul_f32_e32 v2, 0x4b800000, v160
	v_cndmask_b32_e64 v2, v160, v2, s[6:7]
	v_rsq_f32_e32 v2, v2
	v_mul_f32 v161, v133, v180
	v_mul_f32_e32 v160, 0x45800000, v2
	v_cndmask_b32_e64 v2, v2, v160, s[6:7]
	s_waitcnt vmcnt(3)
	v_lshlrev_b32_e32 v160, 16, v196
	v_fma_f32 v160, v212, v161, v160
	v_mul_f32_e32 v2, 0x3f4ccccd, v2
	v_mul_f32 v160, v160, v2
	s_nop 0
	v_mul_f32 v160, v160, v190
	s_nop 0
	v_max_f32_e32 v160, 0xc3e00000, v160
	v_min_f32_e32 v161, 0x43e00000, v160
	s_nop 1
	v_mov_b32_dpp v162, v161 quad_perm:[1,0,3,2] row_mask:0xf bank_mask:0xf
	v_cvt_pk_fp8_f32 v160, v161, v162
	s_nop 1
	v_mov_b32_dpp v161, v160 quad_perm:[2,3,0,1] row_mask:0xf bank_mask:0xf
	s_and_saveexec_b64 s[6:7], s[4:5]
	s_cbranch_execz .LBB0_1343
	v_and_b32_e32 v160, 0xffff, v160
	s_waitcnt lgkmcnt(0)
	v_lshl_or_b32 v162, v161, 16, v160
	v_add_co_u32_e32 v160, vcc, 0x3000, v6
	s_nop 1
	v_addc_co_u32_e32 v161, vcc, 0, v7, vcc
	global_store_dword v[160:161], v162, off
.LBB0_1343:
	s_or_b64 exec, exec, s[6:7]
	v_and_b32_e32 v160, 0xffff0000, v196
	s_waitcnt lgkmcnt(0)
	v_mul_f32 v161, v117, v180
	s_nop 0
	v_fma_f32 v160, v212, v161, v160
	s_nop 0
	v_mul_f32 v160, v160, v2
	s_nop 0
	v_mul_f32 v160, v160, v189
	s_nop 0
	v_max_f32_e32 v160, 0xc3e00000, v160
	v_min_f32_e32 v161, 0x43e00000, v160
	s_nop 1
	v_mov_b32_dpp v162, v161 quad_perm:[1,0,3,2] row_mask:0xf bank_mask:0xf
	v_cvt_pk_fp8_f32 v160, v161, v162
	s_nop 1
	v_mov_b32_dpp v161, v160 quad_perm:[2,3,0,1] row_mask:0xf bank_mask:0xf
	s_and_saveexec_b64 s[6:7], s[4:5]
	s_cbranch_execz .LBB0_1345
	v_and_b32_e32 v160, 0xffff, v160
	s_waitcnt lgkmcnt(0)
	v_lshl_or_b32 v162, v161, 16, v160
	v_add_co_u32_e32 v160, vcc, 0x3000, v6
	s_nop 1
	v_addc_co_u32_e32 v161, vcc, 0, v7, vcc
	global_store_dword v[160:161], v162, off offset:32
; #define SBAR() __builtin_amdgcn_sched_barrier(0)
; __device__ __forceinline__ int crow(int r, int hi) { return (r & 3) + 8 * (r >> 2) + 4 * hi; }
; __device__ __forceinline__ float mul_ns(float a, float b) { float r; asm("v_mul_f32 %0, %1, %2" : "=v"(r) : "v"(a), "v"(b)); return r; }
; __device__ __forceinline__ float fma_ns(float a, float b, float c) { float r; asm("v_fma_f32 %0, %1, %2, %3" : "=v"(r) : "v"(a), "v"(b), "v"(c)); return r; }
; __device__ __forceinline__ void store_quad8(unsigned char* p, float v, int r32) {
;     v = fminf(fmaxf(v, -448.f), 448.f);
;     const float v1 = swz_xor<1>(v);
;     const int w = __builtin_amdgcn_cvt_pk_fp8_f32(v, v1, 0, false);
;     const int w2 = __builtin_amdgcn_ds_swizzle(w, (2 << 10) | 0x1f);
;     if ((r32 & 3) == 0) *(unsigned*)p = ((unsigned)w & 0xffffu) | ((unsigned)w2 << 16);
; }
;     __device__ __forceinline__ void operator()(f32x16 (&o)[8], const float (&rli)[16], int wid, int lane, int r32, int hi) const {
;     ...
;             for (int rb = 0; rb < 16; rb += 4) { unsigned tw[4][4];
; #pragma unroll
;                 for (int q = 0; q < 4; ++q)
; #pragma unroll
;                     for (int k = 0; k < 4; ++k) tw[q][k] = (scw + ((rb + q) * 4 + k) * 64)[ul];
;                 asm volatile("" ::: "memory"); SBAR();
; #pragma unroll
;                 for (int q = 0; q < 4; ++q) { const int r = rb + q;
; #pragma unroll
;                     for (int d0 = 0; d0 < 8; ++d0) { const float t = __uint_as_float((d0 & 1) ? (tw[q][d0 >> 1] & 0xffff0000u) : (tw[q][d0 >> 1] << 16));
;                         const float dd = fma_ns(nlam, mul_ns(o[d0][r], rli[r]), t);
;                         store_quad8(base + (crow(r, 0) * 4096 + d0 * 32) + uo, mul_ns(mul_ns(dd, rn[r]), g[d0]), r32); } }
;                 asm volatile("" ::: "memory"); SBAR(); }
.LBB0_1345:
	s_or_b64 exec, exec, s[6:7]
	s_waitcnt vmcnt(2)
	v_lshlrev_b32_e32 v160, 16, v195
	s_waitcnt lgkmcnt(0)
	v_mul_f32 v161, v101, v180
	s_nop 0
	v_fma_f32 v160, v212, v161, v160
	s_nop 0
	v_mul_f32 v160, v160, v2
	s_nop 0
	v_mul_f32 v160, v160, v188
	s_nop 0
	v_max_f32_e32 v160, 0xc3e00000, v160
	v_min_f32_e32 v161, 0x43e00000, v160
	s_nop 1
	v_mov_b32_dpp v162, v161 quad_perm:[1,0,3,2] row_mask:0xf bank_mask:0xf
	v_cvt_pk_fp8_f32 v160, v161, v162
	s_nop 1
	v_mov_b32_dpp v161, v160 quad_perm:[2,3,0,1] row_mask:0xf bank_mask:0xf
	s_and_saveexec_b64 s[6:7], s[4:5]
	s_cbranch_execz .LBB0_1347
	v_and_b32_e32 v160, 0xffff, v160
	s_waitcnt lgkmcnt(0)
	v_lshl_or_b32 v162, v161, 16, v160
	v_add_co_u32_e32 v160, vcc, 0x3000, v6
	s_nop 1
	v_addc_co_u32_e32 v161, vcc, 0, v7, vcc
	global_store_dword v[160:161], v162, off offset:64
.LBB0_1347:
	s_or_b64 exec, exec, s[6:7]
	v_and_b32_e32 v160, 0xffff0000, v195
	s_waitcnt lgkmcnt(0)
	v_mul_f32 v161, v85, v180
	s_nop 0
	v_fma_f32 v160, v212, v161, v160
	s_nop 0
	v_mul_f32 v160, v160, v2
	s_nop 0
	v_mul_f32 v160, v160, v187
	s_nop 0
	v_max_f32_e32 v160, 0xc3e00000, v160
	v_min_f32_e32 v161, 0x43e00000, v160
	s_nop 1
	v_mov_b32_dpp v162, v161 quad_perm:[1,0,3,2] row_mask:0xf bank_mask:0xf
	v_cvt_pk_fp8_f32 v160, v161, v162
	s_nop 1
	v_mov_b32_dpp v161, v160 quad_perm:[2,3,0,1] row_mask:0xf bank_mask:0xf
	s_and_saveexec_b64 s[6:7], s[4:5]
	s_cbranch_execz .LBB0_1349
	v_and_b32_e32 v160, 0xffff, v160
	s_waitcnt lgkmcnt(0)
	v_lshl_or_b32 v162, v161, 16, v160
	v_add_co_u32_e32 v160, vcc, 0x3000, v6
	s_nop 1
	v_addc_co_u32_e32 v161, vcc, 0, v7, vcc
	global_store_dword v[160:161], v162, off offset:96
.LBB0_1349:
	s_or_b64 exec, exec, s[6:7]
	s_waitcnt vmcnt(1)
	v_lshlrev_b32_e32 v160, 16, v194
	s_waitcnt lgkmcnt(0)
	v_mul_f32 v161, v69, v180
	s_nop 0
	v_fma_f32 v160, v212, v161, v160
	s_nop 0
	v_mul_f32 v160, v160, v2
	s_nop 0
	v_mul_f32 v160, v160, v186
	s_nop 0
	v_max_f32_e32 v160, 0xc3e00000, v160
	v_min_f32_e32 v161, 0x43e00000, v160
	s_nop 1
	v_mov_b32_dpp v162, v161 quad_perm:[1,0,3,2] row_mask:0xf bank_mask:0xf
	v_cvt_pk_fp8_f32 v160, v161, v162
	s_nop 1
	v_mov_b32_dpp v161, v160 quad_perm:[2,3,0,1] row_mask:0xf bank_mask:0xf
	s_and_saveexec_b64 s[6:7], s[4:5]
	s_cbranch_execz .LBB0_1351
	v_and_b32_e32 v160, 0xffff, v160
	s_waitcnt lgkmcnt(0)
	v_lshl_or_b32 v162, v161, 16, v160
	v_add_co_u32_e32 v160, vcc, 0x3000, v6
	s_nop 1
	v_addc_co_u32_e32 v161, vcc, 0, v7, vcc
	global_store_dword v[160:161], v162, off offset:128
.LBB0_1351:
	s_or_b64 exec, exec, s[6:7]
	v_and_b32_e32 v160, 0xffff0000, v194
	s_waitcnt lgkmcnt(0)
	v_mul_f32 v161, v53, v180
	s_nop 0
	v_fma_f32 v160, v212, v161, v160
	s_nop 0
	v_mul_f32 v160, v160, v2
	s_nop 0
	v_mul_f32 v160, v160, v185
	s_nop 0
	v_max_f32_e32 v160, 0xc3e00000, v160
	v_min_f32_e32 v161, 0x43e00000, v160
	s_nop 1
	v_mov_b32_dpp v162, v161 quad_perm:[1,0,3,2] row_mask:0xf bank_mask:0xf
	v_cvt_pk_fp8_f32 v160, v161, v162
	s_nop 1
	v_mov_b32_dpp v161, v160 quad_perm:[2,3,0,1] row_mask:0xf bank_mask:0xf
	s_and_saveexec_b64 s[6:7], s[4:5]
	s_cbranch_execz .LBB0_1353
	v_and_b32_e32 v160, 0xffff, v160
	s_waitcnt lgkmcnt(0)
	v_lshl_or_b32 v162, v161, 16, v160
	v_add_co_u32_e32 v160, vcc, 0x3000, v6
	s_nop 1
	v_addc_co_u32_e32 v161, vcc, 0, v7, vcc
	global_store_dword v[160:161], v162, off offset:160
.LBB0_1353:
	s_or_b64 exec, exec, s[6:7]
	s_waitcnt vmcnt(0)
	v_lshlrev_b32_e32 v160, 16, v193
	s_waitcnt lgkmcnt(0)
	v_mul_f32 v161, v37, v180
	s_nop 0
	v_fma_f32 v160, v212, v161, v160
	s_nop 0
	v_mul_f32 v160, v160, v2
	s_nop 0
	v_mul_f32 v160, v160, v184
	s_nop 0
	v_max_f32_e32 v160, 0xc3e00000, v160
	v_min_f32_e32 v161, 0x43e00000, v160
	s_nop 1
	v_mov_b32_dpp v162, v161 quad_perm:[1,0,3,2] row_mask:0xf bank_mask:0xf
	v_cvt_pk_fp8_f32 v160, v161, v162
	s_nop 1
	v_mov_b32_dpp v161, v160 quad_perm:[2,3,0,1] row_mask:0xf bank_mask:0xf
	s_and_saveexec_b64 s[6:7], s[4:5]
	s_cbranch_execz .LBB0_1355
	v_and_b32_e32 v160, 0xffff, v160
	s_waitcnt lgkmcnt(0)
	v_lshl_or_b32 v162, v161, 16, v160
	v_add_co_u32_e32 v160, vcc, 0x3000, v6
	s_nop 1
	v_addc_co_u32_e32 v161, vcc, 0, v7, vcc
	global_store_dword v[160:161], v162, off offset:192
.LBB0_1355:
	s_or_b64 exec, exec, s[6:7]
	v_and_b32_e32 v160, 0xffff0000, v193
	s_waitcnt lgkmcnt(0)
	v_mul_f32 v161, v21, v180
	s_nop 0
	v_fma_f32 v160, v212, v161, v160
	s_nop 0
	v_mul_f32 v2, v160, v2
	s_nop 0
	v_mul_f32 v2, v2, v165
	s_nop 0
	v_max_f32_e32 v2, 0xc3e00000, v2
	v_min_f32_e32 v160, 0x43e00000, v2
	s_nop 1
	v_mov_b32_dpp v161, v160 quad_perm:[1,0,3,2] row_mask:0xf bank_mask:0xf
	v_cvt_pk_fp8_f32 v2, v160, v161
	s_nop 1
	v_mov_b32_dpp v160, v2 quad_perm:[2,3,0,1] row_mask:0xf bank_mask:0xf
	s_and_saveexec_b64 s[6:7], s[4:5]
	s_cbranch_execz .LBB0_1357
	v_and_b32_e32 v2, 0xffff, v2
	s_waitcnt lgkmcnt(0)
	v_lshl_or_b32 v2, v160, 16, v2
	v_add_co_u32_e32 v160, vcc, 0x3000, v6
	s_nop 1
	v_addc_co_u32_e32 v161, vcc, 0, v7, vcc
	global_store_dword v[160:161], v2, off offset:224
; #define SBAR() __builtin_amdgcn_sched_barrier(0)
; __device__ __forceinline__ int crow(int r, int hi) { return (r & 3) + 8 * (r >> 2) + 4 * hi; }
; __device__ __forceinline__ float mul_ns(float a, float b) { float r; asm("v_mul_f32 %0, %1, %2" : "=v"(r) : "v"(a), "v"(b)); return r; }
; __device__ __forceinline__ float fma_ns(float a, float b, float c) { float r; asm("v_fma_f32 %0, %1, %2, %3" : "=v"(r) : "v"(a), "v"(b), "v"(c)); return r; }
; __device__ __forceinline__ void store_quad8(unsigned char* p, float v, int r32) {
;     v = fminf(fmaxf(v, -448.f), 448.f);
;     const float v1 = swz_xor<1>(v);
;     const int w = __builtin_amdgcn_cvt_pk_fp8_f32(v, v1, 0, false);
;     const int w2 = __builtin_amdgcn_ds_swizzle(w, (2 << 10) | 0x1f);
;     if ((r32 & 3) == 0) *(unsigned*)p = ((unsigned)w & 0xffffu) | ((unsigned)w2 << 16);
; }
;     __device__ __forceinline__ void operator()(f32x16 (&o)[8], const float (&rli)[16], int wid, int lane, int r32, int hi) const {
;     ...
;             for (int rb = 0; rb < 16; rb += 4) { unsigned tw[4][4];
; #pragma unroll
;                 for (int q = 0; q < 4; ++q)
; #pragma unroll
;                     for (int k = 0; k < 4; ++k) tw[q][k] = (scw + ((rb + q) * 4 + k) * 64)[ul];
;                 asm volatile("" ::: "memory"); SBAR();
; #pragma unroll
;                 for (int q = 0; q < 4; ++q) { const int r = rb + q;
; #pragma unroll
;                     for (int d0 = 0; d0 < 8; ++d0) { const float t = __uint_as_float((d0 & 1) ? (tw[q][d0 >> 1] & 0xffff0000u) : (tw[q][d0 >> 1] << 16));
;                         const float dd = fma_ns(nlam, mul_ns(o[d0][r], rli[r]), t);
;                         store_quad8(base + (crow(r, 0) * 4096 + d0 * 32) + uo, mul_ns(mul_ns(dd, rn[r]), g[d0]), r32); } }
;                 asm volatile("" ::: "memory"); SBAR(); }
.LBB0_1357:
	s_or_b64 exec, exec, s[6:7]
	s_mov_b64 s[6:7], 0x1000
	s_waitcnt lgkmcnt(0)
	v_lshl_add_u64 v[160:161], v[4:5], 0, s[6:7]
	s_mov_b64 s[6:7], 0x1100
	v_lshl_add_u64 v[162:163], v[4:5], 0, s[6:7]
	s_mov_b64 s[6:7], 0x1200
	v_lshl_add_u64 v[166:167], v[4:5], 0, s[6:7]
	s_mov_b64 s[6:7], 0x1300
	v_lshl_add_u64 v[202:203], v[4:5], 0, s[6:7]
	s_mov_b64 s[6:7], 0x1400
	v_lshl_add_u64 v[204:205], v[4:5], 0, s[6:7]
	s_mov_b64 s[6:7], 0x1500
	v_lshl_add_u64 v[206:207], v[4:5], 0, s[6:7]
	s_mov_b64 s[6:7], 0x1600
	v_pk_add_f32 v[156:157], v[156:157], v[158:159]
	v_lshl_add_u64 v[208:209], v[4:5], 0, s[6:7]
	s_mov_b64 s[6:7], 0x1700
	v_pk_fma_f32 v[156:157], v[156:157], s[54:55], v[198:199] op_sel_hi:[1,0,0]
	v_lshl_add_u64 v[214:215], v[4:5], 0, s[6:7]
	s_mov_b64 s[6:7], 0x1800
	v_mul_f32_e32 v2, 0x4b800000, v157
	v_cmp_gt_f32_e32 vcc, s53, v157
	v_lshl_add_u64 v[218:219], v[4:5], 0, s[6:7]
	s_mov_b64 s[6:7], 0x1900
	v_cndmask_b32_e32 v2, v157, v2, vcc
	v_lshl_add_u64 v[220:221], v[4:5], 0, s[6:7]
	s_mov_b64 s[6:7], 0x1a00
	v_rsq_f32_e32 v2, v2
	v_lshl_add_u64 v[222:223], v[4:5], 0, s[6:7]
	s_mov_b64 s[6:7], 0x1b00
	v_lshl_add_u64 v[224:225], v[4:5], 0, s[6:7]
	s_mov_b64 s[6:7], 0x1c00
	v_lshl_add_u64 v[226:227], v[4:5], 0, s[6:7]
	s_mov_b64 s[6:7], 0x1d00
	v_lshl_add_u64 v[228:229], v[4:5], 0, s[6:7]
	s_mov_b64 s[6:7], 0x1e00
	v_mul_f32_e32 v157, 0x45800000, v2
	v_lshl_add_u64 v[230:231], v[4:5], 0, s[6:7]
	s_mov_b64 s[6:7], 0x1f00
	v_cndmask_b32_e32 v2, v2, v157, vcc
	v_lshl_add_u64 v[232:233], v[4:5], 0, s[6:7]
	v_cmp_gt_f32_e64 s[6:7], s53, v156
	v_mul_f32_e32 v192, 0x3f4ccccd, v2
	global_load_dword v196, v[160:161], off
	global_load_dword v195, v[162:163], off
	global_load_dword v194, v[166:167], off
	global_load_dword v193, v[202:203], off
	global_load_dword v191, v[204:205], off
	s_nop 0
	global_load_dword v167, v[206:207], off
	global_load_dword v166, v[208:209], off
	global_load_dword v164, v[214:215], off
	global_load_dword v163, v[218:219], off
	global_load_dword v162, v[220:221], off
	global_load_dword v161, v[222:223], off
	global_load_dword v160, v[224:225], off
	global_load_dword v159, v[226:227], off
	global_load_dword v158, v[228:229], off
	global_load_dword v157, v[230:231], off
	global_load_dword v2, v[232:233], off
	s_waitcnt vmcnt(15)
	v_lshlrev_b32_e32 v197, 16, v196
	v_mul_f32 v201, v134, v179
	s_nop 0
	v_fma_f32 v197, v212, v201, v197
	s_nop 0
	v_mul_f32 v197, v197, v192
	s_nop 0
	v_mul_f32 v197, v197, v190
	s_nop 0
	v_max_f32_e32 v197, 0xc3e00000, v197
	v_min_f32_e32 v201, 0x43e00000, v197
	s_nop 1
	v_mov_b32_dpp v202, v201 quad_perm:[1,0,3,2] row_mask:0xf bank_mask:0xf
	v_cvt_pk_fp8_f32 v197, v201, v202
	s_nop 1
	v_mov_b32_dpp v201, v197 quad_perm:[2,3,0,1] row_mask:0xf bank_mask:0xf
	s_and_saveexec_b64 s[8:9], s[4:5]
	v_and_b32_e32 v197, 0xffff, v197
	v_add_co_u32_e32 v202, vcc, 0x8000, v6
	v_lshl_or_b32 v197, v201, 16, v197
	v_addc_co_u32_e32 v203, vcc, 0, v7, vcc
	global_store_dword v[202:203], v197, off
.LBB0_1359:
	s_or_b64 exec, exec, s[8:9]
	v_and_b32_e32 v196, 0xffff0000, v196
	v_mul_f32 v197, v118, v179
	s_nop 0
	v_fma_f32 v196, v212, v197, v196
	s_nop 0
	v_mul_f32 v196, v196, v192
	s_nop 0
	v_mul_f32 v196, v196, v189
	s_nop 0
	v_max_f32_e32 v196, 0xc3e00000, v196
	v_min_f32_e32 v197, 0x43e00000, v196
	s_nop 1
	v_mov_b32_dpp v201, v197 quad_perm:[1,0,3,2] row_mask:0xf bank_mask:0xf
	v_cvt_pk_fp8_f32 v196, v197, v201
	s_nop 1
	v_mov_b32_dpp v197, v196 quad_perm:[2,3,0,1] row_mask:0xf bank_mask:0xf
	s_and_saveexec_b64 s[8:9], s[4:5]
	s_cbranch_execz .LBB0_1361
	v_and_b32_e32 v196, 0xffff, v196
	s_waitcnt lgkmcnt(0)
	v_lshl_or_b32 v201, v197, 16, v196
	v_add_co_u32_e32 v196, vcc, 0x8000, v6
	s_nop 1
	v_addc_co_u32_e32 v197, vcc, 0, v7, vcc
	global_store_dword v[196:197], v201, off offset:32
.LBB0_1361:
	s_or_b64 exec, exec, s[8:9]
	s_waitcnt vmcnt(14)
	v_lshlrev_b32_e32 v196, 16, v195
	s_waitcnt lgkmcnt(0)
	v_mul_f32 v197, v102, v179
	s_nop 0
	v_fma_f32 v196, v212, v197, v196
	s_nop 0
	v_mul_f32 v196, v196, v192
	s_nop 0
	v_mul_f32 v196, v196, v188
	s_nop 0
	v_max_f32_e32 v196, 0xc3e00000, v196
	v_min_f32_e32 v197, 0x43e00000, v196
	s_nop 1
	v_mov_b32_dpp v201, v197 quad_perm:[1,0,3,2] row_mask:0xf bank_mask:0xf
	v_cvt_pk_fp8_f32 v196, v197, v201
	s_nop 1
	v_mov_b32_dpp v197, v196 quad_perm:[2,3,0,1] row_mask:0xf bank_mask:0xf
	s_and_saveexec_b64 s[8:9], s[4:5]
	s_cbranch_execz .LBB0_1363
	v_and_b32_e32 v196, 0xffff, v196
	s_waitcnt lgkmcnt(0)
	v_lshl_or_b32 v201, v197, 16, v196
	v_add_co_u32_e32 v196, vcc, 0x8000, v6
	s_nop 1
	v_addc_co_u32_e32 v197, vcc, 0, v7, vcc
	global_store_dword v[196:197], v201, off offset:64
.LBB0_1363:
	s_or_b64 exec, exec, s[8:9]
	v_and_b32_e32 v195, 0xffff0000, v195
	v_mul_f32 v196, v86, v179
	s_nop 0
	v_fma_f32 v195, v212, v196, v195
	s_nop 0
	v_mul_f32 v195, v195, v192
	s_nop 0
	v_mul_f32 v195, v195, v187
	s_nop 0
	v_max_f32_e32 v195, 0xc3e00000, v195
	v_min_f32_e32 v196, 0x43e00000, v195
	s_waitcnt lgkmcnt(0)
	s_nop 1
	v_mov_b32_dpp v197, v196 quad_perm:[1,0,3,2] row_mask:0xf bank_mask:0xf
	v_cvt_pk_fp8_f32 v195, v196, v197
	s_nop 1
	v_mov_b32_dpp v196, v195 quad_perm:[2,3,0,1] row_mask:0xf bank_mask:0xf
	s_and_saveexec_b64 s[8:9], s[4:5]
	s_cbranch_execz .LBB0_1365
	v_and_b32_e32 v195, 0xffff, v195
	s_waitcnt lgkmcnt(0)
	v_lshl_or_b32 v195, v196, 16, v195
	v_add_co_u32_e32 v196, vcc, 0x8000, v6
	s_nop 1
	v_addc_co_u32_e32 v197, vcc, 0, v7, vcc
	global_store_dword v[196:197], v195, off offset:96
; #define SBAR() __builtin_amdgcn_sched_barrier(0)
; __device__ __forceinline__ int crow(int r, int hi) { return (r & 3) + 8 * (r >> 2) + 4 * hi; }
; __device__ __forceinline__ float mul_ns(float a, float b) { float r; asm("v_mul_f32 %0, %1, %2" : "=v"(r) : "v"(a), "v"(b)); return r; }
; __device__ __forceinline__ float fma_ns(float a, float b, float c) { float r; asm("v_fma_f32 %0, %1, %2, %3" : "=v"(r) : "v"(a), "v"(b), "v"(c)); return r; }
; __device__ __forceinline__ void store_quad8(unsigned char* p, float v, int r32) {
;     v = fminf(fmaxf(v, -448.f), 448.f);
;     const float v1 = swz_xor<1>(v);
;     const int w = __builtin_amdgcn_cvt_pk_fp8_f32(v, v1, 0, false);
;     const int w2 = __builtin_amdgcn_ds_swizzle(w, (2 << 10) | 0x1f);
;     if ((r32 & 3) == 0) *(unsigned*)p = ((unsigned)w & 0xffffu) | ((unsigned)w2 << 16);
; }
;     __device__ __forceinline__ void operator()(f32x16 (&o)[8], const float (&rli)[16], int wid, int lane, int r32, int hi) const {
;     ...
;             for (int rb = 0; rb < 16; rb += 4) { unsigned tw[4][4];
; #pragma unroll
;                 for (int q = 0; q < 4; ++q)
; #pragma unroll
;                     for (int k = 0; k < 4; ++k) tw[q][k] = (scw + ((rb + q) * 4 + k) * 64)[ul];
;                 asm volatile("" ::: "memory"); SBAR();
; #pragma unroll
;                 for (int q = 0; q < 4; ++q) { const int r = rb + q;
; #pragma unroll
;                     for (int d0 = 0; d0 < 8; ++d0) { const float t = __uint_as_float((d0 & 1) ? (tw[q][d0 >> 1] & 0xffff0000u) : (tw[q][d0 >> 1] << 16));
;                         const float dd = fma_ns(nlam, mul_ns(o[d0][r], rli[r]), t);
;                         store_quad8(base + (crow(r, 0) * 4096 + d0 * 32) + uo, mul_ns(mul_ns(dd, rn[r]), g[d0]), r32); } }
;                 asm volatile("" ::: "memory"); SBAR(); }
.LBB0_1365:
	s_or_b64 exec, exec, s[8:9]
	s_waitcnt vmcnt(13)
	v_lshlrev_b32_e32 v195, 16, v194
	s_waitcnt lgkmcnt(0)
	v_mul_f32 v196, v70, v179
	s_nop 0
	v_fma_f32 v195, v212, v196, v195
	s_nop 0
	v_mul_f32 v195, v195, v192
	s_nop 0
	v_mul_f32 v195, v195, v186
	s_nop 0
	v_max_f32_e32 v195, 0xc3e00000, v195
	v_min_f32_e32 v196, 0x43e00000, v195
	s_nop 1
	v_mov_b32_dpp v197, v196 quad_perm:[1,0,3,2] row_mask:0xf bank_mask:0xf
	v_cvt_pk_fp8_f32 v195, v196, v197
	s_nop 1
	v_mov_b32_dpp v196, v195 quad_perm:[2,3,0,1] row_mask:0xf bank_mask:0xf
	s_and_saveexec_b64 s[8:9], s[4:5]
	s_cbranch_execz .LBB0_1367
	v_and_b32_e32 v195, 0xffff, v195
	s_waitcnt lgkmcnt(0)
	v_lshl_or_b32 v195, v196, 16, v195
	v_add_co_u32_e32 v196, vcc, 0x8000, v6
	s_nop 1
	v_addc_co_u32_e32 v197, vcc, 0, v7, vcc
	global_store_dword v[196:197], v195, off offset:128
.LBB0_1367:
	s_or_b64 exec, exec, s[8:9]
	v_and_b32_e32 v194, 0xffff0000, v194
	v_mul_f32 v195, v54, v179
	s_nop 0
	v_fma_f32 v194, v212, v195, v194
	s_nop 0
	v_mul_f32 v194, v194, v192
	s_nop 0
	v_mul_f32 v194, v194, v185
	s_nop 0
	v_max_f32_e32 v194, 0xc3e00000, v194
	v_min_f32_e32 v195, 0x43e00000, v194
	s_waitcnt lgkmcnt(0)
	s_nop 1
	v_mov_b32_dpp v196, v195 quad_perm:[1,0,3,2] row_mask:0xf bank_mask:0xf
	v_cvt_pk_fp8_f32 v194, v195, v196
	s_nop 1
	v_mov_b32_dpp v195, v194 quad_perm:[2,3,0,1] row_mask:0xf bank_mask:0xf
	s_and_saveexec_b64 s[8:9], s[4:5]
	s_cbranch_execz .LBB0_1369
	v_and_b32_e32 v194, 0xffff, v194
	s_waitcnt lgkmcnt(0)
	v_lshl_or_b32 v196, v195, 16, v194
	v_add_co_u32_e32 v194, vcc, 0x8000, v6
	s_nop 1
	v_addc_co_u32_e32 v195, vcc, 0, v7, vcc
	global_store_dword v[194:195], v196, off offset:160
.LBB0_1369:
	s_or_b64 exec, exec, s[8:9]
	s_waitcnt vmcnt(12)
	v_lshlrev_b32_e32 v194, 16, v193
	s_waitcnt lgkmcnt(0)
	v_mul_f32 v195, v38, v179
	s_nop 0
	v_fma_f32 v194, v212, v195, v194
	s_nop 0
	v_mul_f32 v194, v194, v192
	s_nop 0
	v_mul_f32 v194, v194, v184
	s_nop 0
	v_max_f32_e32 v194, 0xc3e00000, v194
	v_min_f32_e32 v195, 0x43e00000, v194
	s_nop 1
	v_mov_b32_dpp v196, v195 quad_perm:[1,0,3,2] row_mask:0xf bank_mask:0xf
	v_cvt_pk_fp8_f32 v194, v195, v196
	s_nop 1
	v_mov_b32_dpp v195, v194 quad_perm:[2,3,0,1] row_mask:0xf bank_mask:0xf
	s_and_saveexec_b64 s[8:9], s[4:5]
	s_cbranch_execz .LBB0_1371
	v_and_b32_e32 v194, 0xffff, v194
	s_waitcnt lgkmcnt(0)
	v_lshl_or_b32 v196, v195, 16, v194
	v_add_co_u32_e32 v194, vcc, 0x8000, v6
	s_nop 1
	v_addc_co_u32_e32 v195, vcc, 0, v7, vcc
	global_store_dword v[194:195], v196, off offset:192
.LBB0_1371:
	s_or_b64 exec, exec, s[8:9]
	v_and_b32_e32 v193, 0xffff0000, v193
	v_mul_f32 v194, v22, v179
	s_nop 0
	v_fma_f32 v193, v212, v194, v193
	s_nop 0
	v_mul_f32 v192, v193, v192
	s_nop 0
	v_mul_f32 v192, v192, v165
	s_nop 0
	v_max_f32_e32 v192, 0xc3e00000, v192
	v_min_f32_e32 v193, 0x43e00000, v192
	s_nop 1
	v_mov_b32_dpp v194, v193 quad_perm:[1,0,3,2] row_mask:0xf bank_mask:0xf
	s_waitcnt lgkmcnt(0)
	v_cvt_pk_fp8_f32 v192, v193, v194
	s_nop 1
	v_mov_b32_dpp v193, v192 quad_perm:[2,3,0,1] row_mask:0xf bank_mask:0xf
	s_and_saveexec_b64 s[8:9], s[4:5]
	s_cbranch_execz .LBB0_1373
	v_and_b32_e32 v192, 0xffff, v192
	s_waitcnt lgkmcnt(0)
	v_lshl_or_b32 v194, v193, 16, v192
	v_add_co_u32_e32 v192, vcc, 0x8000, v6
	s_nop 1
	v_addc_co_u32_e32 v193, vcc, 0, v7, vcc
	global_store_dword v[192:193], v194, off offset:224
.LBB0_1373:
	s_or_b64 exec, exec, s[8:9]
	v_mul_f32_e32 v192, 0x4b800000, v156
	v_cndmask_b32_e64 v156, v156, v192, s[6:7]
	v_rsq_f32_e32 v156, v156
	s_waitcnt lgkmcnt(0)
	v_mul_f32 v193, v135, v178
	v_mul_f32_e32 v192, 0x45800000, v156
	v_cndmask_b32_e64 v156, v156, v192, s[6:7]
	s_waitcnt vmcnt(11)
	v_lshlrev_b32_e32 v192, 16, v191
	v_fma_f32 v192, v212, v193, v192
	v_mul_f32_e32 v156, 0x3f4ccccd, v156
	v_mul_f32 v192, v192, v156
	s_nop 0
	v_mul_f32 v192, v192, v190
	s_nop 0
	v_max_f32_e32 v192, 0xc3e00000, v192
	v_min_f32_e32 v193, 0x43e00000, v192
	s_nop 1
	v_mov_b32_dpp v194, v193 quad_perm:[1,0,3,2] row_mask:0xf bank_mask:0xf
	v_cvt_pk_fp8_f32 v192, v193, v194
	s_nop 1
	v_mov_b32_dpp v193, v192 quad_perm:[2,3,0,1] row_mask:0xf bank_mask:0xf
	s_and_saveexec_b64 s[6:7], s[4:5]
	s_cbranch_execz .LBB0_1375
	v_and_b32_e32 v192, 0xffff, v192
	s_waitcnt lgkmcnt(0)
	v_lshl_or_b32 v194, v193, 16, v192
	v_add_co_u32_e32 v192, vcc, 0x9000, v6
	s_nop 1
	v_addc_co_u32_e32 v193, vcc, 0, v7, vcc
	global_store_dword v[192:193], v194, off
.LBB0_1375:
	s_or_b64 exec, exec, s[6:7]
	v_and_b32_e32 v191, 0xffff0000, v191
	v_mul_f32 v192, v119, v178
	s_nop 0
	v_fma_f32 v191, v212, v192, v191
	s_nop 0
	v_mul_f32 v191, v191, v156
	s_nop 0
	v_mul_f32 v191, v191, v189
	s_nop 0
	v_max_f32_e32 v191, 0xc3e00000, v191
	v_min_f32_e32 v192, 0x43e00000, v191
	s_waitcnt lgkmcnt(0)
	s_nop 1
	v_mov_b32_dpp v193, v192 quad_perm:[1,0,3,2] row_mask:0xf bank_mask:0xf
	v_cvt_pk_fp8_f32 v191, v192, v193
	s_nop 1
	v_mov_b32_dpp v192, v191 quad_perm:[2,3,0,1] row_mask:0xf bank_mask:0xf
	s_and_saveexec_b64 s[6:7], s[4:5]
	s_cbranch_execz .LBB0_1377
	v_and_b32_e32 v191, 0xffff, v191
	s_waitcnt lgkmcnt(0)
	v_lshl_or_b32 v191, v192, 16, v191
	v_add_co_u32_e32 v192, vcc, 0x9000, v6
	s_nop 1
	v_addc_co_u32_e32 v193, vcc, 0, v7, vcc
	global_store_dword v[192:193], v191, off offset:32
.LBB0_1377:
	s_or_b64 exec, exec, s[6:7]
	s_waitcnt vmcnt(10)
	v_lshlrev_b32_e32 v191, 16, v167
	s_waitcnt lgkmcnt(0)
	v_mul_f32 v192, v103, v178
	s_nop 0
	v_fma_f32 v191, v212, v192, v191
	s_nop 0
	v_mul_f32 v191, v191, v156
	s_nop 0
	v_mul_f32 v191, v191, v188
	s_nop 0
	v_max_f32_e32 v191, 0xc3e00000, v191
	v_min_f32_e32 v192, 0x43e00000, v191
	s_nop 1
	v_mov_b32_dpp v193, v192 quad_perm:[1,0,3,2] row_mask:0xf bank_mask:0xf
	v_cvt_pk_fp8_f32 v191, v192, v193
	s_nop 1
	v_mov_b32_dpp v192, v191 quad_perm:[2,3,0,1] row_mask:0xf bank_mask:0xf
	s_and_saveexec_b64 s[6:7], s[4:5]
	s_cbranch_execz .LBB0_1379
	v_and_b32_e32 v191, 0xffff, v191
	s_waitcnt lgkmcnt(0)
	v_lshl_or_b32 v191, v192, 16, v191
	v_add_co_u32_e32 v192, vcc, 0x9000, v6
	s_nop 1
	v_addc_co_u32_e32 v193, vcc, 0, v7, vcc
	global_store_dword v[192:193], v191, off offset:64
; #define SBAR() __builtin_amdgcn_sched_barrier(0)
; __device__ __forceinline__ int crow(int r, int hi) { return (r & 3) + 8 * (r >> 2) + 4 * hi; }
; __device__ __forceinline__ float mul_ns(float a, float b) { float r; asm("v_mul_f32 %0, %1, %2" : "=v"(r) : "v"(a), "v"(b)); return r; }
; __device__ __forceinline__ float fma_ns(float a, float b, float c) { float r; asm("v_fma_f32 %0, %1, %2, %3" : "=v"(r) : "v"(a), "v"(b), "v"(c)); return r; }
; __device__ __forceinline__ void store_quad8(unsigned char* p, float v, int r32) {
;     v = fminf(fmaxf(v, -448.f), 448.f);
;     const float v1 = swz_xor<1>(v);
;     const int w = __builtin_amdgcn_cvt_pk_fp8_f32(v, v1, 0, false);
;     const int w2 = __builtin_amdgcn_ds_swizzle(w, (2 << 10) | 0x1f);
;     if ((r32 & 3) == 0) *(unsigned*)p = ((unsigned)w & 0xffffu) | ((unsigned)w2 << 16);
; }
;     __device__ __forceinline__ void operator()(f32x16 (&o)[8], const float (&rli)[16], int wid, int lane, int r32, int hi) const {
;     ...
;             for (int rb = 0; rb < 16; rb += 4) { unsigned tw[4][4];
; #pragma unroll
;                 for (int q = 0; q < 4; ++q)
; #pragma unroll
;                     for (int k = 0; k < 4; ++k) tw[q][k] = (scw + ((rb + q) * 4 + k) * 64)[ul];
;                 asm volatile("" ::: "memory"); SBAR();
; #pragma unroll
;                 for (int q = 0; q < 4; ++q) { const int r = rb + q;
; #pragma unroll
;                     for (int d0 = 0; d0 < 8; ++d0) { const float t = __uint_as_float((d0 & 1) ? (tw[q][d0 >> 1] & 0xffff0000u) : (tw[q][d0 >> 1] << 16));
;                         const float dd = fma_ns(nlam, mul_ns(o[d0][r], rli[r]), t);
;                         store_quad8(base + (crow(r, 0) * 4096 + d0 * 32) + uo, mul_ns(mul_ns(dd, rn[r]), g[d0]), r32); } }
;                 asm volatile("" ::: "memory"); SBAR(); }
.LBB0_1379:
	s_or_b64 exec, exec, s[6:7]
	v_and_b32_e32 v167, 0xffff0000, v167
	v_mul_f32 v191, v87, v178
	s_nop 0
	v_fma_f32 v167, v212, v191, v167
	s_nop 0
	v_mul_f32 v167, v167, v156
	s_nop 0
	v_mul_f32 v167, v167, v187
	s_nop 0
	v_max_f32_e32 v167, 0xc3e00000, v167
	v_min_f32_e32 v191, 0x43e00000, v167
	s_waitcnt lgkmcnt(0)
	s_nop 1
	v_mov_b32_dpp v192, v191 quad_perm:[1,0,3,2] row_mask:0xf bank_mask:0xf
	v_cvt_pk_fp8_f32 v167, v191, v192
	s_nop 1
	v_mov_b32_dpp v191, v167 quad_perm:[2,3,0,1] row_mask:0xf bank_mask:0xf
	s_and_saveexec_b64 s[6:7], s[4:5]
	v_and_b32_e32 v167, 0xffff, v167
	v_add_co_u32_e32 v192, vcc, 0x9000, v6
	v_lshl_or_b32 v167, v191, 16, v167
	v_addc_co_u32_e32 v193, vcc, 0, v7, vcc
	global_store_dword v[192:193], v167, off offset:96
.LBB0_1381:
	s_or_b64 exec, exec, s[6:7]
	s_waitcnt vmcnt(9)
	v_lshlrev_b32_e32 v167, 16, v166
	v_mul_f32 v191, v71, v178
	s_nop 0
	v_fma_f32 v167, v212, v191, v167
	s_nop 0
	v_mul_f32 v167, v167, v156
	s_nop 0
	v_mul_f32 v167, v167, v186
	s_nop 0
	v_max_f32_e32 v167, 0xc3e00000, v167
	v_min_f32_e32 v191, 0x43e00000, v167
	s_nop 1
	v_mov_b32_dpp v192, v191 quad_perm:[1,0,3,2] row_mask:0xf bank_mask:0xf
	v_cvt_pk_fp8_f32 v167, v191, v192
	s_nop 1
	v_mov_b32_dpp v191, v167 quad_perm:[2,3,0,1] row_mask:0xf bank_mask:0xf
	s_and_saveexec_b64 s[6:7], s[4:5]
	v_and_b32_e32 v167, 0xffff, v167
	v_add_co_u32_e32 v192, vcc, 0x9000, v6
	v_lshl_or_b32 v167, v191, 16, v167
	v_addc_co_u32_e32 v193, vcc, 0, v7, vcc
	global_store_dword v[192:193], v167, off offset:128
.LBB0_1383:
	s_or_b64 exec, exec, s[6:7]
	v_and_b32_e32 v166, 0xffff0000, v166
	v_mul_f32 v167, v55, v178
	s_nop 0
	v_fma_f32 v166, v212, v167, v166
	s_nop 0
	v_mul_f32 v166, v166, v156
	s_nop 0
	v_mul_f32 v166, v166, v185
	s_nop 0
	v_max_f32_e32 v166, 0xc3e00000, v166
	v_min_f32_e32 v167, 0x43e00000, v166
	s_nop 1
	v_mov_b32_dpp v191, v167 quad_perm:[1,0,3,2] row_mask:0xf bank_mask:0xf
	v_cvt_pk_fp8_f32 v166, v167, v191
	s_nop 1
	v_mov_b32_dpp v167, v166 quad_perm:[2,3,0,1] row_mask:0xf bank_mask:0xf
	s_and_saveexec_b64 s[6:7], s[4:5]
	s_cbranch_execz .LBB0_1385
	v_and_b32_e32 v166, 0xffff, v166
	s_waitcnt lgkmcnt(0)
	v_lshl_or_b32 v191, v167, 16, v166
	v_add_co_u32_e32 v166, vcc, 0x9000, v6
	s_nop 1
	v_addc_co_u32_e32 v167, vcc, 0, v7, vcc
	global_store_dword v[166:167], v191, off offset:160
.LBB0_1385:
	s_or_b64 exec, exec, s[6:7]
	s_waitcnt vmcnt(8)
	v_lshlrev_b32_e32 v166, 16, v164
	s_waitcnt lgkmcnt(0)
	v_mul_f32 v167, v39, v178
	s_nop 0
	v_fma_f32 v166, v212, v167, v166
	s_nop 0
	v_mul_f32 v166, v166, v156
	s_nop 0
	v_mul_f32 v166, v166, v184
	s_nop 0
	v_max_f32_e32 v166, 0xc3e00000, v166
	v_min_f32_e32 v167, 0x43e00000, v166
	s_nop 1
	v_mov_b32_dpp v191, v167 quad_perm:[1,0,3,2] row_mask:0xf bank_mask:0xf
	v_cvt_pk_fp8_f32 v166, v167, v191
	s_nop 1
	v_mov_b32_dpp v167, v166 quad_perm:[2,3,0,1] row_mask:0xf bank_mask:0xf
	s_and_saveexec_b64 s[6:7], s[4:5]
	s_cbranch_execz .LBB0_1387
	v_and_b32_e32 v166, 0xffff, v166
	s_waitcnt lgkmcnt(0)
	v_lshl_or_b32 v191, v167, 16, v166
	v_add_co_u32_e32 v166, vcc, 0x9000, v6
	s_nop 1
	v_addc_co_u32_e32 v167, vcc, 0, v7, vcc
	global_store_dword v[166:167], v191, off offset:192
.LBB0_1387:
	s_or_b64 exec, exec, s[6:7]
	v_and_b32_e32 v164, 0xffff0000, v164
	v_mul_f32 v166, v23, v178
	s_nop 0
	v_fma_f32 v164, v212, v166, v164
	s_nop 0
	v_mul_f32 v156, v164, v156
	s_nop 0
	v_mul_f32 v156, v156, v165
	s_nop 0
	v_max_f32_e32 v156, 0xc3e00000, v156
	v_min_f32_e32 v164, 0x43e00000, v156
	s_nop 1
	v_mov_b32_dpp v166, v164 quad_perm:[1,0,3,2] row_mask:0xf bank_mask:0xf
	s_waitcnt lgkmcnt(0)
	v_cvt_pk_fp8_f32 v156, v164, v166
	s_nop 1
	v_mov_b32_dpp v164, v156 quad_perm:[2,3,0,1] row_mask:0xf bank_mask:0xf
	s_and_saveexec_b64 s[6:7], s[4:5]
	v_and_b32_e32 v156, 0xffff, v156
	v_add_co_u32_e32 v166, vcc, 0x9000, v6
	v_lshl_or_b32 v156, v164, 16, v156
	v_addc_co_u32_e32 v167, vcc, 0, v7, vcc
	global_store_dword v[166:167], v156, off offset:224
.LBB0_1389:
	s_or_b64 exec, exec, s[6:7]
	v_pk_add_f32 v[152:153], v[152:153], v[154:155]
	v_mul_f32 v155, v136, v177
	s_nop 0
	v_pk_fma_f32 v[152:153], v[152:153], s[54:55], v[198:199] op_sel_hi:[1,0,0]
	s_nop 0
	v_mul_f32_e32 v154, 0x4b800000, v153
	v_cmp_gt_f32_e32 vcc, s53, v153
	v_cmp_gt_f32_e64 s[6:7], s53, v152
	s_nop 0
	v_cndmask_b32_e32 v153, v153, v154, vcc
	v_rsq_f32_e32 v153, v153
	s_waitcnt vmcnt(7)
	v_lshlrev_b32_e32 v154, 16, v163
	v_fma_f32 v154, v212, v155, v154
	v_mul_f32_e32 v156, 0x45800000, v153
	v_cndmask_b32_e32 v153, v153, v156, vcc
	v_mul_f32_e32 v153, 0x3f4ccccd, v153
	v_mul_f32 v154, v154, v153
	s_nop 0
	v_mul_f32 v154, v154, v190
	s_nop 0
	v_max_f32_e32 v154, 0xc3e00000, v154
	v_min_f32_e32 v155, 0x43e00000, v154
	s_nop 1
	v_mov_b32_dpp v156, v155 quad_perm:[1,0,3,2] row_mask:0xf bank_mask:0xf
	v_cvt_pk_fp8_f32 v154, v155, v156
	s_nop 1
	v_mov_b32_dpp v155, v154 quad_perm:[2,3,0,1] row_mask:0xf bank_mask:0xf
	s_and_saveexec_b64 s[8:9], s[4:5]
	s_cbranch_execz .LBB0_1391
	v_and_b32_e32 v154, 0xffff, v154
	s_waitcnt lgkmcnt(0)
	v_lshl_or_b32 v156, v155, 16, v154
	v_add_co_u32_e32 v154, vcc, 0xa000, v6
	s_nop 1
	v_addc_co_u32_e32 v155, vcc, 0, v7, vcc
	global_store_dword v[154:155], v156, off
.LBB0_1391:
	s_or_b64 exec, exec, s[8:9]
	v_and_b32_e32 v154, 0xffff0000, v163
	s_waitcnt lgkmcnt(0)
	v_mul_f32 v155, v120, v177
	s_nop 0
	v_fma_f32 v154, v212, v155, v154
	s_nop 0
	v_mul_f32 v154, v154, v153
	s_nop 0
	v_mul_f32 v154, v154, v189
	s_nop 0
	v_max_f32_e32 v154, 0xc3e00000, v154
	v_min_f32_e32 v155, 0x43e00000, v154
	s_nop 1
	v_mov_b32_dpp v156, v155 quad_perm:[1,0,3,2] row_mask:0xf bank_mask:0xf
	v_cvt_pk_fp8_f32 v154, v155, v156
	s_nop 1
	v_mov_b32_dpp v155, v154 quad_perm:[2,3,0,1] row_mask:0xf bank_mask:0xf
	s_and_saveexec_b64 s[8:9], s[4:5]
	s_cbranch_execz .LBB0_1393
	v_and_b32_e32 v154, 0xffff, v154
	s_waitcnt lgkmcnt(0)
	v_lshl_or_b32 v156, v155, 16, v154
	v_add_co_u32_e32 v154, vcc, 0xa000, v6
	s_nop 1
	v_addc_co_u32_e32 v155, vcc, 0, v7, vcc
	global_store_dword v[154:155], v156, off offset:32
; #define SBAR() __builtin_amdgcn_sched_barrier(0)
; __device__ __forceinline__ int crow(int r, int hi) { return (r & 3) + 8 * (r >> 2) + 4 * hi; }
; __device__ __forceinline__ float mul_ns(float a, float b) { float r; asm("v_mul_f32 %0, %1, %2" : "=v"(r) : "v"(a), "v"(b)); return r; }
; __device__ __forceinline__ float fma_ns(float a, float b, float c) { float r; asm("v_fma_f32 %0, %1, %2, %3" : "=v"(r) : "v"(a), "v"(b), "v"(c)); return r; }
; __device__ __forceinline__ void store_quad8(unsigned char* p, float v, int r32) {
;     v = fminf(fmaxf(v, -448.f), 448.f);
;     const float v1 = swz_xor<1>(v);
;     const int w = __builtin_amdgcn_cvt_pk_fp8_f32(v, v1, 0, false);
;     const int w2 = __builtin_amdgcn_ds_swizzle(w, (2 << 10) | 0x1f);
;     if ((r32 & 3) == 0) *(unsigned*)p = ((unsigned)w & 0xffffu) | ((unsigned)w2 << 16);
; }
;     __device__ __forceinline__ void operator()(f32x16 (&o)[8], const float (&rli)[16], int wid, int lane, int r32, int hi) const {
;     ...
;             for (int rb = 0; rb < 16; rb += 4) { unsigned tw[4][4];
; #pragma unroll
;                 for (int q = 0; q < 4; ++q)
; #pragma unroll
;                     for (int k = 0; k < 4; ++k) tw[q][k] = (scw + ((rb + q) * 4 + k) * 64)[ul];
;                 asm volatile("" ::: "memory"); SBAR();
; #pragma unroll
;                 for (int q = 0; q < 4; ++q) { const int r = rb + q;
; #pragma unroll
;                     for (int d0 = 0; d0 < 8; ++d0) { const float t = __uint_as_float((d0 & 1) ? (tw[q][d0 >> 1] & 0xffff0000u) : (tw[q][d0 >> 1] << 16));
;                         const float dd = fma_ns(nlam, mul_ns(o[d0][r], rli[r]), t);
;                         store_quad8(base + (crow(r, 0) * 4096 + d0 * 32) + uo, mul_ns(mul_ns(dd, rn[r]), g[d0]), r32); } }
;                 asm volatile("" ::: "memory"); SBAR(); }
.LBB0_1393:
	s_or_b64 exec, exec, s[8:9]
	s_waitcnt vmcnt(6)
	v_lshlrev_b32_e32 v154, 16, v162
	s_waitcnt lgkmcnt(0)
	v_mul_f32 v155, v104, v177
	s_nop 0
	v_fma_f32 v154, v212, v155, v154
	s_nop 0
	v_mul_f32 v154, v154, v153
	s_nop 0
	v_mul_f32 v154, v154, v188
	s_nop 0
	v_max_f32_e32 v154, 0xc3e00000, v154
	v_min_f32_e32 v155, 0x43e00000, v154
	s_nop 1
	v_mov_b32_dpp v156, v155 quad_perm:[1,0,3,2] row_mask:0xf bank_mask:0xf
	v_cvt_pk_fp8_f32 v154, v155, v156
	s_nop 1
	v_mov_b32_dpp v155, v154 quad_perm:[2,3,0,1] row_mask:0xf bank_mask:0xf
	s_and_saveexec_b64 s[8:9], s[4:5]
	s_cbranch_execz .LBB0_1395
	v_and_b32_e32 v154, 0xffff, v154
	s_waitcnt lgkmcnt(0)
	v_lshl_or_b32 v156, v155, 16, v154
	v_add_co_u32_e32 v154, vcc, 0xa000, v6
	s_nop 1
	v_addc_co_u32_e32 v155, vcc, 0, v7, vcc
	global_store_dword v[154:155], v156, off offset:64
.LBB0_1395:
	s_or_b64 exec, exec, s[8:9]
	v_and_b32_e32 v154, 0xffff0000, v162
	s_waitcnt lgkmcnt(0)
	v_mul_f32 v155, v88, v177
	s_nop 0
	v_fma_f32 v154, v212, v155, v154
	s_nop 0
	v_mul_f32 v154, v154, v153
	s_nop 0
	v_mul_f32 v154, v154, v187
	s_nop 0
	v_max_f32_e32 v154, 0xc3e00000, v154
	v_min_f32_e32 v155, 0x43e00000, v154
	s_nop 1
	v_mov_b32_dpp v156, v155 quad_perm:[1,0,3,2] row_mask:0xf bank_mask:0xf
	v_cvt_pk_fp8_f32 v154, v155, v156
	s_nop 1
	v_mov_b32_dpp v155, v154 quad_perm:[2,3,0,1] row_mask:0xf bank_mask:0xf
	s_and_saveexec_b64 s[8:9], s[4:5]
	s_cbranch_execz .LBB0_1397
	v_and_b32_e32 v154, 0xffff, v154
	s_waitcnt lgkmcnt(0)
	v_lshl_or_b32 v156, v155, 16, v154
	v_add_co_u32_e32 v154, vcc, 0xa000, v6
	s_nop 1
	v_addc_co_u32_e32 v155, vcc, 0, v7, vcc
	global_store_dword v[154:155], v156, off offset:96
.LBB0_1397:
	s_or_b64 exec, exec, s[8:9]
	s_waitcnt vmcnt(5)
	v_lshlrev_b32_e32 v154, 16, v161
	s_waitcnt lgkmcnt(0)
	v_mul_f32 v155, v72, v177
	s_nop 0
	v_fma_f32 v154, v212, v155, v154
	s_nop 0
	v_mul_f32 v154, v154, v153
	s_nop 0
	v_mul_f32 v154, v154, v186
	s_nop 0
	v_max_f32_e32 v154, 0xc3e00000, v154
	v_min_f32_e32 v155, 0x43e00000, v154
	s_nop 1
	v_mov_b32_dpp v156, v155 quad_perm:[1,0,3,2] row_mask:0xf bank_mask:0xf
	v_cvt_pk_fp8_f32 v154, v155, v156
	s_nop 1
	v_mov_b32_dpp v155, v154 quad_perm:[2,3,0,1] row_mask:0xf bank_mask:0xf
	s_and_saveexec_b64 s[8:9], s[4:5]
	s_cbranch_execz .LBB0_1399
	v_and_b32_e32 v154, 0xffff, v154
	s_waitcnt lgkmcnt(0)
	v_lshl_or_b32 v156, v155, 16, v154
	v_add_co_u32_e32 v154, vcc, 0xa000, v6
	s_nop 1
	v_addc_co_u32_e32 v155, vcc, 0, v7, vcc
	global_store_dword v[154:155], v156, off offset:128
.LBB0_1399:
	s_or_b64 exec, exec, s[8:9]
	v_and_b32_e32 v154, 0xffff0000, v161
	s_waitcnt lgkmcnt(0)
	v_mul_f32 v155, v56, v177
	s_nop 0
	v_fma_f32 v154, v212, v155, v154
	s_nop 0
	v_mul_f32 v154, v154, v153
	s_nop 0
	v_mul_f32 v154, v154, v185
	s_nop 0
	v_max_f32_e32 v154, 0xc3e00000, v154
	v_min_f32_e32 v155, 0x43e00000, v154
	s_nop 1
	v_mov_b32_dpp v156, v155 quad_perm:[1,0,3,2] row_mask:0xf bank_mask:0xf
	v_cvt_pk_fp8_f32 v154, v155, v156
	s_nop 1
	v_mov_b32_dpp v155, v154 quad_perm:[2,3,0,1] row_mask:0xf bank_mask:0xf
	s_and_saveexec_b64 s[8:9], s[4:5]
	s_cbranch_execz .LBB0_1401
	v_and_b32_e32 v154, 0xffff, v154
	s_waitcnt lgkmcnt(0)
	v_lshl_or_b32 v156, v155, 16, v154
	v_add_co_u32_e32 v154, vcc, 0xa000, v6
	s_nop 1
	v_addc_co_u32_e32 v155, vcc, 0, v7, vcc
	global_store_dword v[154:155], v156, off offset:160
.LBB0_1401:
	s_or_b64 exec, exec, s[8:9]
	s_waitcnt vmcnt(4)
	v_lshlrev_b32_e32 v154, 16, v160
	s_waitcnt lgkmcnt(0)
	v_mul_f32 v155, v40, v177
	s_nop 0
	v_fma_f32 v154, v212, v155, v154
	s_nop 0
	v_mul_f32 v154, v154, v153
	s_nop 0
	v_mul_f32 v154, v154, v184
	s_nop 0
	v_max_f32_e32 v154, 0xc3e00000, v154
	v_min_f32_e32 v155, 0x43e00000, v154
	s_nop 1
	v_mov_b32_dpp v156, v155 quad_perm:[1,0,3,2] row_mask:0xf bank_mask:0xf
	v_cvt_pk_fp8_f32 v154, v155, v156
	s_nop 1
	v_mov_b32_dpp v155, v154 quad_perm:[2,3,0,1] row_mask:0xf bank_mask:0xf
	s_and_saveexec_b64 s[8:9], s[4:5]
	s_cbranch_execz .LBB0_1403
	v_and_b32_e32 v154, 0xffff, v154
	s_waitcnt lgkmcnt(0)
	v_lshl_or_b32 v156, v155, 16, v154
	v_add_co_u32_e32 v154, vcc, 0xa000, v6
	s_nop 1
	v_addc_co_u32_e32 v155, vcc, 0, v7, vcc
	global_store_dword v[154:155], v156, off offset:192
.LBB0_1403:
	s_or_b64 exec, exec, s[8:9]
	v_and_b32_e32 v154, 0xffff0000, v160
	s_waitcnt lgkmcnt(0)
	v_mul_f32 v155, v24, v177
	s_nop 0
	v_fma_f32 v154, v212, v155, v154
	s_nop 0
	v_mul_f32 v153, v154, v153
	s_nop 0
	v_mul_f32 v153, v153, v165
	s_nop 0
	v_max_f32_e32 v153, 0xc3e00000, v153
	v_min_f32_e32 v154, 0x43e00000, v153
	s_nop 1
	v_mov_b32_dpp v155, v154 quad_perm:[1,0,3,2] row_mask:0xf bank_mask:0xf
	v_cvt_pk_fp8_f32 v153, v154, v155
	s_nop 1
	v_mov_b32_dpp v154, v153 quad_perm:[2,3,0,1] row_mask:0xf bank_mask:0xf
	s_and_saveexec_b64 s[8:9], s[4:5]
	s_cbranch_execz .LBB0_1405
	v_and_b32_e32 v153, 0xffff, v153
	s_waitcnt lgkmcnt(0)
	v_lshl_or_b32 v153, v154, 16, v153
	v_add_co_u32_e32 v154, vcc, 0xa000, v6
	s_nop 1
	v_addc_co_u32_e32 v155, vcc, 0, v7, vcc
	global_store_dword v[154:155], v153, off offset:224
.LBB0_1405:
	s_or_b64 exec, exec, s[8:9]
	v_mul_f32_e32 v153, 0x4b800000, v152
	v_cndmask_b32_e64 v152, v152, v153, s[6:7]
	v_rsq_f32_e32 v152, v152
	s_waitcnt lgkmcnt(0)
	v_mul_f32 v154, v137, v176
	v_mul_f32_e32 v153, 0x45800000, v152
	v_cndmask_b32_e64 v152, v152, v153, s[6:7]
	s_waitcnt vmcnt(3)
	v_lshlrev_b32_e32 v153, 16, v159
	v_fma_f32 v153, v212, v154, v153
	v_mul_f32_e32 v152, 0x3f4ccccd, v152
	v_mul_f32 v153, v153, v152
	s_nop 0
	v_mul_f32 v153, v153, v190
	s_nop 0
	v_max_f32_e32 v153, 0xc3e00000, v153
	v_min_f32_e32 v154, 0x43e00000, v153
	s_nop 1
	v_mov_b32_dpp v155, v154 quad_perm:[1,0,3,2] row_mask:0xf bank_mask:0xf
	v_cvt_pk_fp8_f32 v153, v154, v155
	s_nop 1
	v_mov_b32_dpp v154, v153 quad_perm:[2,3,0,1] row_mask:0xf bank_mask:0xf
	s_and_saveexec_b64 s[6:7], s[4:5]
	s_cbranch_execz .LBB0_1407
	v_and_b32_e32 v153, 0xffff, v153
	s_waitcnt lgkmcnt(0)
	v_lshl_or_b32 v153, v154, 16, v153
	v_add_co_u32_e32 v154, vcc, 0xb000, v6
	s_nop 1
	v_addc_co_u32_e32 v155, vcc, 0, v7, vcc
	global_store_dword v[154:155], v153, off
; #define SBAR() __builtin_amdgcn_sched_barrier(0)
; __device__ __forceinline__ int crow(int r, int hi) { return (r & 3) + 8 * (r >> 2) + 4 * hi; }
; __device__ __forceinline__ float mul_ns(float a, float b) { float r; asm("v_mul_f32 %0, %1, %2" : "=v"(r) : "v"(a), "v"(b)); return r; }
; __device__ __forceinline__ float fma_ns(float a, float b, float c) { float r; asm("v_fma_f32 %0, %1, %2, %3" : "=v"(r) : "v"(a), "v"(b), "v"(c)); return r; }
; __device__ __forceinline__ void store_quad8(unsigned char* p, float v, int r32) {
;     v = fminf(fmaxf(v, -448.f), 448.f);
;     const float v1 = swz_xor<1>(v);
;     const int w = __builtin_amdgcn_cvt_pk_fp8_f32(v, v1, 0, false);
;     const int w2 = __builtin_amdgcn_ds_swizzle(w, (2 << 10) | 0x1f);
;     if ((r32 & 3) == 0) *(unsigned*)p = ((unsigned)w & 0xffffu) | ((unsigned)w2 << 16);
; }
;     __device__ __forceinline__ void operator()(f32x16 (&o)[8], const float (&rli)[16], int wid, int lane, int r32, int hi) const {
;     ...
;             for (int rb = 0; rb < 16; rb += 4) { unsigned tw[4][4];
; #pragma unroll
;                 for (int q = 0; q < 4; ++q)
; #pragma unroll
;                     for (int k = 0; k < 4; ++k) tw[q][k] = (scw + ((rb + q) * 4 + k) * 64)[ul];
;                 asm volatile("" ::: "memory"); SBAR();
; #pragma unroll
;                 for (int q = 0; q < 4; ++q) { const int r = rb + q;
; #pragma unroll
;                     for (int d0 = 0; d0 < 8; ++d0) { const float t = __uint_as_float((d0 & 1) ? (tw[q][d0 >> 1] & 0xffff0000u) : (tw[q][d0 >> 1] << 16));
;                         const float dd = fma_ns(nlam, mul_ns(o[d0][r], rli[r]), t);
;                         store_quad8(base + (crow(r, 0) * 4096 + d0 * 32) + uo, mul_ns(mul_ns(dd, rn[r]), g[d0]), r32); } }
;                 asm volatile("" ::: "memory"); SBAR(); }
.LBB0_1407:
	s_or_b64 exec, exec, s[6:7]
	v_and_b32_e32 v153, 0xffff0000, v159
	s_waitcnt lgkmcnt(0)
	v_mul_f32 v154, v121, v176
	s_nop 0
	v_fma_f32 v153, v212, v154, v153
	s_nop 0
	v_mul_f32 v153, v153, v152
	s_nop 0
	v_mul_f32 v153, v153, v189
	s_nop 0
	v_max_f32_e32 v153, 0xc3e00000, v153
	v_min_f32_e32 v154, 0x43e00000, v153
	s_nop 1
	v_mov_b32_dpp v155, v154 quad_perm:[1,0,3,2] row_mask:0xf bank_mask:0xf
	v_cvt_pk_fp8_f32 v153, v154, v155
	s_nop 1
	v_mov_b32_dpp v154, v153 quad_perm:[2,3,0,1] row_mask:0xf bank_mask:0xf
	s_and_saveexec_b64 s[6:7], s[4:5]
	s_cbranch_execz .LBB0_1409
	v_and_b32_e32 v153, 0xffff, v153
	s_waitcnt lgkmcnt(0)
	v_lshl_or_b32 v153, v154, 16, v153
	v_add_co_u32_e32 v154, vcc, 0xb000, v6
	s_nop 1
	v_addc_co_u32_e32 v155, vcc, 0, v7, vcc
	global_store_dword v[154:155], v153, off offset:32
.LBB0_1409:
	s_or_b64 exec, exec, s[6:7]
	s_waitcnt vmcnt(2)
	v_lshlrev_b32_e32 v153, 16, v158
	s_waitcnt lgkmcnt(0)
	v_mul_f32 v154, v105, v176
	s_nop 0
	v_fma_f32 v153, v212, v154, v153
	s_nop 0
	v_mul_f32 v153, v153, v152
	s_nop 0
	v_mul_f32 v153, v153, v188
	s_nop 0
	v_max_f32_e32 v153, 0xc3e00000, v153
	v_min_f32_e32 v154, 0x43e00000, v153
	s_nop 1
	v_mov_b32_dpp v155, v154 quad_perm:[1,0,3,2] row_mask:0xf bank_mask:0xf
	v_cvt_pk_fp8_f32 v153, v154, v155
	s_nop 1
	v_mov_b32_dpp v154, v153 quad_perm:[2,3,0,1] row_mask:0xf bank_mask:0xf
	s_and_saveexec_b64 s[6:7], s[4:5]
	s_cbranch_execz .LBB0_1411
	v_and_b32_e32 v153, 0xffff, v153
	s_waitcnt lgkmcnt(0)
	v_lshl_or_b32 v153, v154, 16, v153
	v_add_co_u32_e32 v154, vcc, 0xb000, v6
	s_nop 1
	v_addc_co_u32_e32 v155, vcc, 0, v7, vcc
	global_store_dword v[154:155], v153, off offset:64
.LBB0_1411:
	s_or_b64 exec, exec, s[6:7]
	v_and_b32_e32 v153, 0xffff0000, v158
	s_waitcnt lgkmcnt(0)
	v_mul_f32 v154, v89, v176
	s_nop 0
	v_fma_f32 v153, v212, v154, v153
	s_nop 0
	v_mul_f32 v153, v153, v152
	s_nop 0
	v_mul_f32 v153, v153, v187
	s_nop 0
	v_max_f32_e32 v153, 0xc3e00000, v153
	v_min_f32_e32 v154, 0x43e00000, v153
	s_nop 1
	v_mov_b32_dpp v155, v154 quad_perm:[1,0,3,2] row_mask:0xf bank_mask:0xf
	v_cvt_pk_fp8_f32 v153, v154, v155
	s_nop 1
	v_mov_b32_dpp v154, v153 quad_perm:[2,3,0,1] row_mask:0xf bank_mask:0xf
	s_and_saveexec_b64 s[6:7], s[4:5]
	s_cbranch_execz .LBB0_1413
	v_and_b32_e32 v153, 0xffff, v153
	s_waitcnt lgkmcnt(0)
	v_lshl_or_b32 v153, v154, 16, v153
	v_add_co_u32_e32 v154, vcc, 0xb000, v6
	s_nop 1
	v_addc_co_u32_e32 v155, vcc, 0, v7, vcc
	global_store_dword v[154:155], v153, off offset:96
.LBB0_1413:
	s_or_b64 exec, exec, s[6:7]
	s_waitcnt vmcnt(1)
	v_lshlrev_b32_e32 v153, 16, v157
	s_waitcnt lgkmcnt(0)
	v_mul_f32 v154, v73, v176
	s_nop 0
	v_fma_f32 v153, v212, v154, v153
	s_nop 0
	v_mul_f32 v153, v153, v152
	s_nop 0
	v_mul_f32 v153, v153, v186
	s_nop 0
	v_max_f32_e32 v153, 0xc3e00000, v153
	v_min_f32_e32 v154, 0x43e00000, v153
	s_nop 1
	v_mov_b32_dpp v155, v154 quad_perm:[1,0,3,2] row_mask:0xf bank_mask:0xf
	v_cvt_pk_fp8_f32 v153, v154, v155
	s_nop 1
	v_mov_b32_dpp v154, v153 quad_perm:[2,3,0,1] row_mask:0xf bank_mask:0xf
	s_and_saveexec_b64 s[6:7], s[4:5]
	s_cbranch_execz .LBB0_1415
	v_and_b32_e32 v153, 0xffff, v153
	s_waitcnt lgkmcnt(0)
	v_lshl_or_b32 v153, v154, 16, v153
	v_add_co_u32_e32 v154, vcc, 0xb000, v6
	s_nop 1
	v_addc_co_u32_e32 v155, vcc, 0, v7, vcc
	global_store_dword v[154:155], v153, off offset:128
.LBB0_1415:
	s_or_b64 exec, exec, s[6:7]
	v_and_b32_e32 v153, 0xffff0000, v157
	s_waitcnt lgkmcnt(0)
	v_mul_f32 v154, v57, v176
	s_nop 0
	v_fma_f32 v153, v212, v154, v153
	s_nop 0
	v_mul_f32 v153, v153, v152
	s_nop 0
	v_mul_f32 v153, v153, v185
	s_nop 0
	v_max_f32_e32 v153, 0xc3e00000, v153
	v_min_f32_e32 v154, 0x43e00000, v153
	s_nop 1
	v_mov_b32_dpp v155, v154 quad_perm:[1,0,3,2] row_mask:0xf bank_mask:0xf
	v_cvt_pk_fp8_f32 v153, v154, v155
	s_nop 1
	v_mov_b32_dpp v154, v153 quad_perm:[2,3,0,1] row_mask:0xf bank_mask:0xf
	s_and_saveexec_b64 s[6:7], s[4:5]
	s_cbranch_execz .LBB0_1417
	v_and_b32_e32 v153, 0xffff, v153
	s_waitcnt lgkmcnt(0)
	v_lshl_or_b32 v153, v154, 16, v153
	v_add_co_u32_e32 v154, vcc, 0xb000, v6
	s_nop 1
	v_addc_co_u32_e32 v155, vcc, 0, v7, vcc
	global_store_dword v[154:155], v153, off offset:160
.LBB0_1417:
	s_or_b64 exec, exec, s[6:7]
	s_waitcnt vmcnt(0)
	v_lshlrev_b32_e32 v153, 16, v2
	s_waitcnt lgkmcnt(0)
	v_mul_f32 v154, v41, v176
	s_nop 0
	v_fma_f32 v153, v212, v154, v153
	s_nop 0
	v_mul_f32 v153, v153, v152
	s_nop 0
	v_mul_f32 v153, v153, v184
	s_nop 0
	v_max_f32_e32 v153, 0xc3e00000, v153
	v_min_f32_e32 v154, 0x43e00000, v153
	s_nop 1
	v_mov_b32_dpp v155, v154 quad_perm:[1,0,3,2] row_mask:0xf bank_mask:0xf
	v_cvt_pk_fp8_f32 v153, v154, v155
	s_nop 1
	v_mov_b32_dpp v154, v153 quad_perm:[2,3,0,1] row_mask:0xf bank_mask:0xf
	s_and_saveexec_b64 s[6:7], s[4:5]
	s_cbranch_execz .LBB0_1419
	v_and_b32_e32 v153, 0xffff, v153
	s_waitcnt lgkmcnt(0)
	v_lshl_or_b32 v153, v154, 16, v153
	v_add_co_u32_e32 v154, vcc, 0xb000, v6
	s_nop 1
	v_addc_co_u32_e32 v155, vcc, 0, v7, vcc
	global_store_dword v[154:155], v153, off offset:192
.LBB0_1419:
	s_or_b64 exec, exec, s[6:7]
	v_and_b32_e32 v2, 0xffff0000, v2
	v_mul_f32 v153, v25, v176
	s_nop 0
	v_fma_f32 v2, v212, v153, v2
	s_nop 0
	v_mul_f32 v2, v2, v152
	s_nop 0
	v_mul_f32 v2, v2, v165
	s_nop 0
	v_max_f32_e32 v2, 0xc3e00000, v2
	v_min_f32_e32 v152, 0x43e00000, v2
	s_nop 1
	v_mov_b32_dpp v153, v152 quad_perm:[1,0,3,2] row_mask:0xf bank_mask:0xf
	s_waitcnt lgkmcnt(0)
	v_cvt_pk_fp8_f32 v2, v152, v153
	s_nop 1
	v_mov_b32_dpp v152, v2 quad_perm:[2,3,0,1] row_mask:0xf bank_mask:0xf
	s_and_saveexec_b64 s[6:7], s[4:5]
	s_cbranch_execz .LBB0_1421
	v_and_b32_e32 v2, 0xffff, v2
	s_waitcnt lgkmcnt(0)
	v_lshl_or_b32 v2, v152, 16, v2
	v_add_co_u32_e32 v152, vcc, 0xb000, v6
	s_nop 1
	v_addc_co_u32_e32 v153, vcc, 0, v7, vcc
	global_store_dword v[152:153], v2, off offset:224
; #define SBAR() __builtin_amdgcn_sched_barrier(0)
; __device__ __forceinline__ int crow(int r, int hi) { return (r & 3) + 8 * (r >> 2) + 4 * hi; }
; __device__ __forceinline__ float mul_ns(float a, float b) { float r; asm("v_mul_f32 %0, %1, %2" : "=v"(r) : "v"(a), "v"(b)); return r; }
; __device__ __forceinline__ float fma_ns(float a, float b, float c) { float r; asm("v_fma_f32 %0, %1, %2, %3" : "=v"(r) : "v"(a), "v"(b), "v"(c)); return r; }
; __device__ __forceinline__ void store_quad8(unsigned char* p, float v, int r32) {
;     v = fminf(fmaxf(v, -448.f), 448.f);
;     const float v1 = swz_xor<1>(v);
;     const int w = __builtin_amdgcn_cvt_pk_fp8_f32(v, v1, 0, false);
;     const int w2 = __builtin_amdgcn_ds_swizzle(w, (2 << 10) | 0x1f);
;     if ((r32 & 3) == 0) *(unsigned*)p = ((unsigned)w & 0xffffu) | ((unsigned)w2 << 16);
; }
;     __device__ __forceinline__ void operator()(f32x16 (&o)[8], const float (&rli)[16], int wid, int lane, int r32, int hi) const {
;     ...
;                 for (int q = 0; q < 4; ++q) { const int r = rb + q; float s = 0.f;
; #pragma unroll
;                     for (int d0 = 0; d0 < 8; ++d0) { const float t = __uint_as_float((d0 & 1) ? (tw[q][d0 >> 1] & 0xffff0000u) : (tw[q][d0 >> 1] << 16));
;                         const float dd = fma_ns(nlam, mul_ns(o[d0][r], rli[r]), t); s = fma_ns(dd, dd, s); }
;                     s = half_sum(s); rn[r] = rsqrtf(s * (1.0f / 256.0f) + 1e-5f) * 0.8f; }
;     ...
;             for (int rb = 0; rb < 16; rb += 4) { unsigned tw[4][4];
; #pragma unroll
;                 for (int q = 0; q < 4; ++q)
; #pragma unroll
;                     for (int k = 0; k < 4; ++k) tw[q][k] = (scw + ((rb + q) * 4 + k) * 64)[ul];
;                 asm volatile("" ::: "memory"); SBAR();
; #pragma unroll
;                 for (int q = 0; q < 4; ++q) { const int r = rb + q;
; #pragma unroll
;                     for (int d0 = 0; d0 < 8; ++d0) { const float t = __uint_as_float((d0 & 1) ? (tw[q][d0 >> 1] & 0xffff0000u) : (tw[q][d0 >> 1] << 16));
;                         const float dd = fma_ns(nlam, mul_ns(o[d0][r], rli[r]), t);
;                         store_quad8(base + (crow(r, 0) * 4096 + d0 * 32) + uo, mul_ns(mul_ns(dd, rn[r]), g[d0]), r32); } }
;                 asm volatile("" ::: "memory"); SBAR(); }
.LBB0_1421:
	s_or_b64 exec, exec, s[6:7]
	s_mov_b64 s[6:7], 0x2000
	s_waitcnt lgkmcnt(0)
	v_lshl_add_u64 v[152:153], v[4:5], 0, s[6:7]
	s_mov_b64 s[6:7], 0x2100
	v_lshl_add_u64 v[154:155], v[4:5], 0, s[6:7]
	s_mov_b64 s[6:7], 0x2200
	v_lshl_add_u64 v[156:157], v[4:5], 0, s[6:7]
	s_mov_b64 s[6:7], 0x2300
	v_lshl_add_u64 v[158:159], v[4:5], 0, s[6:7]
	s_mov_b64 s[6:7], 0x2400
	v_lshl_add_u64 v[166:167], v[4:5], 0, s[6:7]
	s_mov_b64 s[6:7], 0x2500
	v_lshl_add_u64 v[192:193], v[4:5], 0, s[6:7]
	s_mov_b64 s[6:7], 0x2600
	v_pk_add_f32 v[148:149], v[148:149], v[150:151]
	v_lshl_add_u64 v[194:195], v[4:5], 0, s[6:7]
	s_mov_b64 s[6:7], 0x2700
	v_pk_fma_f32 v[148:149], v[148:149], s[54:55], v[198:199] op_sel_hi:[1,0,0]
	v_lshl_add_u64 v[196:197], v[4:5], 0, s[6:7]
	s_mov_b64 s[6:7], 0x2800
	v_mul_f32_e32 v2, 0x4b800000, v149
	v_cmp_gt_f32_e32 vcc, s53, v149
	v_lshl_add_u64 v[202:203], v[4:5], 0, s[6:7]
	s_mov_b64 s[6:7], 0x2900
	v_cndmask_b32_e32 v2, v149, v2, vcc
	v_lshl_add_u64 v[204:205], v[4:5], 0, s[6:7]
	s_mov_b64 s[6:7], 0x2a00
	v_rsq_f32_e32 v2, v2
	v_lshl_add_u64 v[206:207], v[4:5], 0, s[6:7]
	s_mov_b64 s[6:7], 0x2b00
	v_lshl_add_u64 v[208:209], v[4:5], 0, s[6:7]
	s_mov_b64 s[6:7], 0x2c00
	v_lshl_add_u64 v[214:215], v[4:5], 0, s[6:7]
	s_mov_b64 s[6:7], 0x2d00
	v_lshl_add_u64 v[218:219], v[4:5], 0, s[6:7]
	s_mov_b64 s[6:7], 0x2e00
	v_mul_f32_e32 v149, 0x45800000, v2
	v_lshl_add_u64 v[220:221], v[4:5], 0, s[6:7]
	s_mov_b64 s[6:7], 0x2f00
	v_cndmask_b32_e32 v2, v2, v149, vcc
	v_lshl_add_u64 v[222:223], v[4:5], 0, s[6:7]
	v_cmp_gt_f32_e64 s[6:7], s53, v148
	v_mul_f32_e32 v160, 0x3f4ccccd, v2
	global_load_dword v164, v[152:153], off
	global_load_dword v163, v[154:155], off
	global_load_dword v162, v[156:157], off
	global_load_dword v161, v[158:159], off
	s_nop 0
	global_load_dword v159, v[166:167], off
	global_load_dword v158, v[192:193], off
	global_load_dword v157, v[194:195], off
	global_load_dword v156, v[196:197], off
	global_load_dword v155, v[202:203], off
	global_load_dword v154, v[204:205], off
	global_load_dword v153, v[206:207], off
	global_load_dword v152, v[208:209], off
	global_load_dword v151, v[214:215], off
	global_load_dword v150, v[218:219], off
	global_load_dword v149, v[220:221], off
	global_load_dword v2, v[222:223], off
	s_waitcnt vmcnt(15)
	v_lshlrev_b32_e32 v166, 16, v164
	v_mul_f32 v167, v138, v175
	s_nop 0
	v_fma_f32 v166, v212, v167, v166
	s_nop 0
	v_mul_f32 v166, v166, v160
	s_nop 0
	v_mul_f32 v166, v166, v190
	s_nop 0
	v_max_f32_e32 v166, 0xc3e00000, v166
	v_min_f32_e32 v167, 0x43e00000, v166
	s_nop 1
	v_mov_b32_dpp v191, v167 quad_perm:[1,0,3,2] row_mask:0xf bank_mask:0xf
	v_cvt_pk_fp8_f32 v166, v167, v191
	s_nop 1
	v_mov_b32_dpp v167, v166 quad_perm:[2,3,0,1] row_mask:0xf bank_mask:0xf
	s_and_saveexec_b64 s[8:9], s[4:5]
	s_cbranch_execz .LBB0_1423
	v_and_b32_e32 v166, 0xffff, v166
	s_waitcnt lgkmcnt(0)
	v_lshl_or_b32 v191, v167, 16, v166
	v_add_co_u32_e32 v166, vcc, 0x10000, v6
	s_nop 1
	v_addc_co_u32_e32 v167, vcc, 0, v7, vcc
	global_store_dword v[166:167], v191, off
.LBB0_1423:
	s_or_b64 exec, exec, s[8:9]
	v_and_b32_e32 v164, 0xffff0000, v164
	v_mul_f32 v166, v122, v175
	s_nop 0
	v_fma_f32 v164, v212, v166, v164
	s_nop 0
	v_mul_f32 v164, v164, v160
	s_nop 0
	v_mul_f32 v164, v164, v189
	s_nop 0
	v_max_f32_e32 v164, 0xc3e00000, v164
	v_min_f32_e32 v166, 0x43e00000, v164
	s_waitcnt lgkmcnt(0)
	s_nop 1
	v_mov_b32_dpp v167, v166 quad_perm:[1,0,3,2] row_mask:0xf bank_mask:0xf
	v_cvt_pk_fp8_f32 v164, v166, v167
	s_nop 1
	v_mov_b32_dpp v166, v164 quad_perm:[2,3,0,1] row_mask:0xf bank_mask:0xf
	s_and_saveexec_b64 s[8:9], s[4:5]
	s_cbranch_execz .LBB0_1425
	v_and_b32_e32 v164, 0xffff, v164
	s_waitcnt lgkmcnt(0)
	v_lshl_or_b32 v164, v166, 16, v164
	v_add_co_u32_e32 v166, vcc, 0x10000, v6
	s_nop 1
	v_addc_co_u32_e32 v167, vcc, 0, v7, vcc
	global_store_dword v[166:167], v164, off offset:32
.LBB0_1425:
	s_or_b64 exec, exec, s[8:9]
	s_waitcnt vmcnt(14)
	v_lshlrev_b32_e32 v164, 16, v163
	s_waitcnt lgkmcnt(0)
	v_mul_f32 v166, v106, v175
	s_nop 0
	v_fma_f32 v164, v212, v166, v164
	s_nop 0
	v_mul_f32 v164, v164, v160
	s_nop 0
	v_mul_f32 v164, v164, v188
	s_nop 0
	v_max_f32_e32 v164, 0xc3e00000, v164
	v_min_f32_e32 v166, 0x43e00000, v164
	s_nop 1
	v_mov_b32_dpp v167, v166 quad_perm:[1,0,3,2] row_mask:0xf bank_mask:0xf
	v_cvt_pk_fp8_f32 v164, v166, v167
	s_nop 1
	v_mov_b32_dpp v166, v164 quad_perm:[2,3,0,1] row_mask:0xf bank_mask:0xf
	s_and_saveexec_b64 s[8:9], s[4:5]
	s_cbranch_execz .LBB0_1427
	v_and_b32_e32 v164, 0xffff, v164
	s_waitcnt lgkmcnt(0)
	v_lshl_or_b32 v164, v166, 16, v164
	v_add_co_u32_e32 v166, vcc, 0x10000, v6
	s_nop 1
	v_addc_co_u32_e32 v167, vcc, 0, v7, vcc
	global_store_dword v[166:167], v164, off offset:64
.LBB0_1427:
	s_or_b64 exec, exec, s[8:9]
	v_and_b32_e32 v163, 0xffff0000, v163
	v_mul_f32 v164, v90, v175
	s_nop 0
	v_fma_f32 v163, v212, v164, v163
	s_nop 0
	v_mul_f32 v163, v163, v160
	s_nop 0
	v_mul_f32 v163, v163, v187
	s_nop 0
	v_max_f32_e32 v163, 0xc3e00000, v163
	v_min_f32_e32 v164, 0x43e00000, v163
	s_waitcnt lgkmcnt(0)
	s_nop 1
	v_mov_b32_dpp v166, v164 quad_perm:[1,0,3,2] row_mask:0xf bank_mask:0xf
	v_cvt_pk_fp8_f32 v163, v164, v166
	s_nop 1
	v_mov_b32_dpp v164, v163 quad_perm:[2,3,0,1] row_mask:0xf bank_mask:0xf
	s_and_saveexec_b64 s[8:9], s[4:5]
	v_and_b32_e32 v163, 0xffff, v163
	v_add_co_u32_e32 v166, vcc, 0x10000, v6
	v_lshl_or_b32 v163, v164, 16, v163
	v_addc_co_u32_e32 v167, vcc, 0, v7, vcc
	global_store_dword v[166:167], v163, off offset:96
; #define SBAR() __builtin_amdgcn_sched_barrier(0)
; __device__ __forceinline__ int crow(int r, int hi) { return (r & 3) + 8 * (r >> 2) + 4 * hi; }
; __device__ __forceinline__ float mul_ns(float a, float b) { float r; asm("v_mul_f32 %0, %1, %2" : "=v"(r) : "v"(a), "v"(b)); return r; }
; __device__ __forceinline__ float fma_ns(float a, float b, float c) { float r; asm("v_fma_f32 %0, %1, %2, %3" : "=v"(r) : "v"(a), "v"(b), "v"(c)); return r; }
; __device__ __forceinline__ void store_quad8(unsigned char* p, float v, int r32) {
;     v = fminf(fmaxf(v, -448.f), 448.f);
;     const float v1 = swz_xor<1>(v);
;     const int w = __builtin_amdgcn_cvt_pk_fp8_f32(v, v1, 0, false);
;     const int w2 = __builtin_amdgcn_ds_swizzle(w, (2 << 10) | 0x1f);
;     if ((r32 & 3) == 0) *(unsigned*)p = ((unsigned)w & 0xffffu) | ((unsigned)w2 << 16);
; }
;     __device__ __forceinline__ void operator()(f32x16 (&o)[8], const float (&rli)[16], int wid, int lane, int r32, int hi) const {
;     ...
;             for (int rb = 0; rb < 16; rb += 4) { unsigned tw[4][4];
; #pragma unroll
;                 for (int q = 0; q < 4; ++q)
; #pragma unroll
;                     for (int k = 0; k < 4; ++k) tw[q][k] = (scw + ((rb + q) * 4 + k) * 64)[ul];
;                 asm volatile("" ::: "memory"); SBAR();
; #pragma unroll
;                 for (int q = 0; q < 4; ++q) { const int r = rb + q;
; #pragma unroll
;                     for (int d0 = 0; d0 < 8; ++d0) { const float t = __uint_as_float((d0 & 1) ? (tw[q][d0 >> 1] & 0xffff0000u) : (tw[q][d0 >> 1] << 16));
;                         const float dd = fma_ns(nlam, mul_ns(o[d0][r], rli[r]), t);
;                         store_quad8(base + (crow(r, 0) * 4096 + d0 * 32) + uo, mul_ns(mul_ns(dd, rn[r]), g[d0]), r32); } }
;                 asm volatile("" ::: "memory"); SBAR(); }
.LBB0_1429:
	s_or_b64 exec, exec, s[8:9]
	s_waitcnt vmcnt(13)
	v_lshlrev_b32_e32 v163, 16, v162
	v_mul_f32 v164, v74, v175
	s_nop 0
	v_fma_f32 v163, v212, v164, v163
	s_nop 0
	v_mul_f32 v163, v163, v160
	s_nop 0
	v_mul_f32 v163, v163, v186
	s_nop 0
	v_max_f32_e32 v163, 0xc3e00000, v163
	v_min_f32_e32 v164, 0x43e00000, v163
	s_nop 1
	v_mov_b32_dpp v166, v164 quad_perm:[1,0,3,2] row_mask:0xf bank_mask:0xf
	v_cvt_pk_fp8_f32 v163, v164, v166
	s_nop 1
	v_mov_b32_dpp v164, v163 quad_perm:[2,3,0,1] row_mask:0xf bank_mask:0xf
	s_and_saveexec_b64 s[8:9], s[4:5]
	v_and_b32_e32 v163, 0xffff, v163
	v_add_co_u32_e32 v166, vcc, 0x10000, v6
	v_lshl_or_b32 v163, v164, 16, v163
	v_addc_co_u32_e32 v167, vcc, 0, v7, vcc
	global_store_dword v[166:167], v163, off offset:128
.LBB0_1431:
	s_or_b64 exec, exec, s[8:9]
	v_and_b32_e32 v162, 0xffff0000, v162
	v_mul_f32 v163, v58, v175
	s_nop 0
	v_fma_f32 v162, v212, v163, v162
	s_nop 0
	v_mul_f32 v162, v162, v160
	s_nop 0
	v_mul_f32 v162, v162, v185
	s_nop 0
	v_max_f32_e32 v162, 0xc3e00000, v162
	v_min_f32_e32 v163, 0x43e00000, v162
	s_nop 1
	v_mov_b32_dpp v164, v163 quad_perm:[1,0,3,2] row_mask:0xf bank_mask:0xf
	v_cvt_pk_fp8_f32 v162, v163, v164
	s_nop 1
	v_mov_b32_dpp v163, v162 quad_perm:[2,3,0,1] row_mask:0xf bank_mask:0xf
	s_and_saveexec_b64 s[8:9], s[4:5]
	s_cbranch_execz .LBB0_1433
	v_and_b32_e32 v162, 0xffff, v162
	s_waitcnt lgkmcnt(0)
	v_lshl_or_b32 v164, v163, 16, v162
	v_add_co_u32_e32 v162, vcc, 0x10000, v6
	s_nop 1
	v_addc_co_u32_e32 v163, vcc, 0, v7, vcc
	global_store_dword v[162:163], v164, off offset:160
.LBB0_1433:
	s_or_b64 exec, exec, s[8:9]
	s_waitcnt vmcnt(12)
	v_lshlrev_b32_e32 v162, 16, v161
	s_waitcnt lgkmcnt(0)
	v_mul_f32 v163, v42, v175
	s_nop 0
	v_fma_f32 v162, v212, v163, v162
	s_nop 0
	v_mul_f32 v162, v162, v160
	s_nop 0
	v_mul_f32 v162, v162, v184
	s_nop 0
	v_max_f32_e32 v162, 0xc3e00000, v162
	v_min_f32_e32 v163, 0x43e00000, v162
	s_nop 1
	v_mov_b32_dpp v164, v163 quad_perm:[1,0,3,2] row_mask:0xf bank_mask:0xf
	v_cvt_pk_fp8_f32 v162, v163, v164
	s_nop 1
	v_mov_b32_dpp v163, v162 quad_perm:[2,3,0,1] row_mask:0xf bank_mask:0xf
	s_and_saveexec_b64 s[8:9], s[4:5]
	s_cbranch_execz .LBB0_1435
	v_and_b32_e32 v162, 0xffff, v162
	s_waitcnt lgkmcnt(0)
	v_lshl_or_b32 v164, v163, 16, v162
	v_add_co_u32_e32 v162, vcc, 0x10000, v6
	s_nop 1
	v_addc_co_u32_e32 v163, vcc, 0, v7, vcc
	global_store_dword v[162:163], v164, off offset:192
.LBB0_1435:
	s_or_b64 exec, exec, s[8:9]
	v_and_b32_e32 v161, 0xffff0000, v161
	v_mul_f32 v162, v26, v175
	s_nop 0
	v_fma_f32 v161, v212, v162, v161
	s_nop 0
	v_mul_f32 v160, v161, v160
	s_nop 0
	v_mul_f32 v160, v160, v165
	s_nop 0
	v_max_f32_e32 v160, 0xc3e00000, v160
	v_min_f32_e32 v161, 0x43e00000, v160
	s_nop 1
	v_mov_b32_dpp v162, v161 quad_perm:[1,0,3,2] row_mask:0xf bank_mask:0xf
	s_waitcnt lgkmcnt(0)
	v_cvt_pk_fp8_f32 v160, v161, v162
	s_nop 1
	v_mov_b32_dpp v161, v160 quad_perm:[2,3,0,1] row_mask:0xf bank_mask:0xf
	s_and_saveexec_b64 s[8:9], s[4:5]
	s_cbranch_execz .LBB0_1437
	v_and_b32_e32 v160, 0xffff, v160
	s_waitcnt lgkmcnt(0)
	v_lshl_or_b32 v162, v161, 16, v160
	v_add_co_u32_e32 v160, vcc, 0x10000, v6
	s_nop 1
	v_addc_co_u32_e32 v161, vcc, 0, v7, vcc
	global_store_dword v[160:161], v162, off offset:224
.LBB0_1437:
	s_or_b64 exec, exec, s[8:9]
	v_mul_f32_e32 v160, 0x4b800000, v148
	v_cndmask_b32_e64 v148, v148, v160, s[6:7]
	v_rsq_f32_e32 v148, v148
	s_waitcnt lgkmcnt(0)
	v_mul_f32 v161, v139, v174
	v_mul_f32_e32 v160, 0x45800000, v148
	v_cndmask_b32_e64 v148, v148, v160, s[6:7]
	s_waitcnt vmcnt(11)
	v_lshlrev_b32_e32 v160, 16, v159
	v_fma_f32 v160, v212, v161, v160
	v_mul_f32_e32 v148, 0x3f4ccccd, v148
	v_mul_f32 v160, v160, v148
	s_nop 0
	v_mul_f32 v160, v160, v190
	s_nop 0
	v_max_f32_e32 v160, 0xc3e00000, v160
	v_min_f32_e32 v161, 0x43e00000, v160
	s_nop 1
	v_mov_b32_dpp v162, v161 quad_perm:[1,0,3,2] row_mask:0xf bank_mask:0xf
	v_cvt_pk_fp8_f32 v160, v161, v162
	s_nop 1
	v_mov_b32_dpp v161, v160 quad_perm:[2,3,0,1] row_mask:0xf bank_mask:0xf
	s_and_saveexec_b64 s[6:7], s[4:5]
	s_cbranch_execz .LBB0_1439
	v_and_b32_e32 v160, 0xffff, v160
	s_waitcnt lgkmcnt(0)
	v_lshl_or_b32 v162, v161, 16, v160
	v_add_co_u32_e32 v160, vcc, 0x11000, v6
	s_nop 1
	v_addc_co_u32_e32 v161, vcc, 0, v7, vcc
	global_store_dword v[160:161], v162, off
.LBB0_1439:
	s_or_b64 exec, exec, s[6:7]
	v_and_b32_e32 v159, 0xffff0000, v159
	v_mul_f32 v160, v123, v174
	s_nop 0
	v_fma_f32 v159, v212, v160, v159
	s_nop 0
	v_mul_f32 v159, v159, v148
	s_nop 0
	v_mul_f32 v159, v159, v189
	s_nop 0
	v_max_f32_e32 v159, 0xc3e00000, v159
	v_min_f32_e32 v160, 0x43e00000, v159
	s_waitcnt lgkmcnt(0)
	s_nop 1
	v_mov_b32_dpp v161, v160 quad_perm:[1,0,3,2] row_mask:0xf bank_mask:0xf
	v_cvt_pk_fp8_f32 v159, v160, v161
	s_nop 1
	v_mov_b32_dpp v160, v159 quad_perm:[2,3,0,1] row_mask:0xf bank_mask:0xf
	s_and_saveexec_b64 s[6:7], s[4:5]
	s_cbranch_execz .LBB0_1441
	v_and_b32_e32 v159, 0xffff, v159
	s_waitcnt lgkmcnt(0)
	v_lshl_or_b32 v159, v160, 16, v159
	v_add_co_u32_e32 v160, vcc, 0x11000, v6
	s_nop 1
	v_addc_co_u32_e32 v161, vcc, 0, v7, vcc
	global_store_dword v[160:161], v159, off offset:32
.LBB0_1441:
	s_or_b64 exec, exec, s[6:7]
	s_waitcnt vmcnt(10)
	v_lshlrev_b32_e32 v159, 16, v158
	s_waitcnt lgkmcnt(0)
	v_mul_f32 v160, v107, v174
	s_nop 0
	v_fma_f32 v159, v212, v160, v159
	s_nop 0
	v_mul_f32 v159, v159, v148
	s_nop 0
	v_mul_f32 v159, v159, v188
	s_nop 0
	v_max_f32_e32 v159, 0xc3e00000, v159
	v_min_f32_e32 v160, 0x43e00000, v159
	s_nop 1
	v_mov_b32_dpp v161, v160 quad_perm:[1,0,3,2] row_mask:0xf bank_mask:0xf
	v_cvt_pk_fp8_f32 v159, v160, v161
	s_nop 1
	v_mov_b32_dpp v160, v159 quad_perm:[2,3,0,1] row_mask:0xf bank_mask:0xf
	s_and_saveexec_b64 s[6:7], s[4:5]
	s_cbranch_execz .LBB0_1443
	v_and_b32_e32 v159, 0xffff, v159
	s_waitcnt lgkmcnt(0)
	v_lshl_or_b32 v159, v160, 16, v159
	v_add_co_u32_e32 v160, vcc, 0x11000, v6
	s_nop 1
	v_addc_co_u32_e32 v161, vcc, 0, v7, vcc
	global_store_dword v[160:161], v159, off offset:64
; #define SBAR() __builtin_amdgcn_sched_barrier(0)
; __device__ __forceinline__ int crow(int r, int hi) { return (r & 3) + 8 * (r >> 2) + 4 * hi; }
; __device__ __forceinline__ float mul_ns(float a, float b) { float r; asm("v_mul_f32 %0, %1, %2" : "=v"(r) : "v"(a), "v"(b)); return r; }
; __device__ __forceinline__ float fma_ns(float a, float b, float c) { float r; asm("v_fma_f32 %0, %1, %2, %3" : "=v"(r) : "v"(a), "v"(b), "v"(c)); return r; }
; __device__ __forceinline__ void store_quad8(unsigned char* p, float v, int r32) {
;     v = fminf(fmaxf(v, -448.f), 448.f);
;     const float v1 = swz_xor<1>(v);
;     const int w = __builtin_amdgcn_cvt_pk_fp8_f32(v, v1, 0, false);
;     const int w2 = __builtin_amdgcn_ds_swizzle(w, (2 << 10) | 0x1f);
;     if ((r32 & 3) == 0) *(unsigned*)p = ((unsigned)w & 0xffffu) | ((unsigned)w2 << 16);
; }
;     __device__ __forceinline__ void operator()(f32x16 (&o)[8], const float (&rli)[16], int wid, int lane, int r32, int hi) const {
;     ...
;                 for (int q = 0; q < 4; ++q) { const int r = rb + q; float s = 0.f;
; #pragma unroll
;                     for (int d0 = 0; d0 < 8; ++d0) { const float t = __uint_as_float((d0 & 1) ? (tw[q][d0 >> 1] & 0xffff0000u) : (tw[q][d0 >> 1] << 16));
;                         const float dd = fma_ns(nlam, mul_ns(o[d0][r], rli[r]), t); s = fma_ns(dd, dd, s); }
;                     s = half_sum(s); rn[r] = rsqrtf(s * (1.0f / 256.0f) + 1e-5f) * 0.8f; }
;     ...
;             for (int rb = 0; rb < 16; rb += 4) { unsigned tw[4][4];
; #pragma unroll
;                 for (int q = 0; q < 4; ++q)
; #pragma unroll
;                     for (int k = 0; k < 4; ++k) tw[q][k] = (scw + ((rb + q) * 4 + k) * 64)[ul];
;                 asm volatile("" ::: "memory"); SBAR();
; #pragma unroll
;                 for (int q = 0; q < 4; ++q) { const int r = rb + q;
; #pragma unroll
;                     for (int d0 = 0; d0 < 8; ++d0) { const float t = __uint_as_float((d0 & 1) ? (tw[q][d0 >> 1] & 0xffff0000u) : (tw[q][d0 >> 1] << 16));
;                         const float dd = fma_ns(nlam, mul_ns(o[d0][r], rli[r]), t);
;                         store_quad8(base + (crow(r, 0) * 4096 + d0 * 32) + uo, mul_ns(mul_ns(dd, rn[r]), g[d0]), r32); } }
;                 asm volatile("" ::: "memory"); SBAR(); }
.LBB0_1443:
	s_or_b64 exec, exec, s[6:7]
	v_and_b32_e32 v158, 0xffff0000, v158
	v_mul_f32 v159, v91, v174
	s_nop 0
	v_fma_f32 v158, v212, v159, v158
	s_nop 0
	v_mul_f32 v158, v158, v148
	s_nop 0
	v_mul_f32 v158, v158, v187
	s_nop 0
	v_max_f32_e32 v158, 0xc3e00000, v158
	v_min_f32_e32 v159, 0x43e00000, v158
	s_waitcnt lgkmcnt(0)
	s_nop 1
	v_mov_b32_dpp v160, v159 quad_perm:[1,0,3,2] row_mask:0xf bank_mask:0xf
	v_cvt_pk_fp8_f32 v158, v159, v160
	s_nop 1
	v_mov_b32_dpp v159, v158 quad_perm:[2,3,0,1] row_mask:0xf bank_mask:0xf
	s_and_saveexec_b64 s[6:7], s[4:5]
	s_cbranch_execz .LBB0_1445
	v_and_b32_e32 v158, 0xffff, v158
	s_waitcnt lgkmcnt(0)
	v_lshl_or_b32 v160, v159, 16, v158
	v_add_co_u32_e32 v158, vcc, 0x11000, v6
	s_nop 1
	v_addc_co_u32_e32 v159, vcc, 0, v7, vcc
	global_store_dword v[158:159], v160, off offset:96
.LBB0_1445:
	s_or_b64 exec, exec, s[6:7]
	s_waitcnt vmcnt(9)
	v_lshlrev_b32_e32 v158, 16, v157
	s_waitcnt lgkmcnt(0)
	v_mul_f32 v159, v75, v174
	s_nop 0
	v_fma_f32 v158, v212, v159, v158
	s_nop 0
	v_mul_f32 v158, v158, v148
	s_nop 0
	v_mul_f32 v158, v158, v186
	s_nop 0
	v_max_f32_e32 v158, 0xc3e00000, v158
	v_min_f32_e32 v159, 0x43e00000, v158
	s_nop 1
	v_mov_b32_dpp v160, v159 quad_perm:[1,0,3,2] row_mask:0xf bank_mask:0xf
	v_cvt_pk_fp8_f32 v158, v159, v160
	s_nop 1
	v_mov_b32_dpp v159, v158 quad_perm:[2,3,0,1] row_mask:0xf bank_mask:0xf
	s_and_saveexec_b64 s[6:7], s[4:5]
	s_cbranch_execz .LBB0_1447
	v_and_b32_e32 v158, 0xffff, v158
	s_waitcnt lgkmcnt(0)
	v_lshl_or_b32 v160, v159, 16, v158
	v_add_co_u32_e32 v158, vcc, 0x11000, v6
	s_nop 1
	v_addc_co_u32_e32 v159, vcc, 0, v7, vcc
	global_store_dword v[158:159], v160, off offset:128
.LBB0_1447:
	s_or_b64 exec, exec, s[6:7]
	v_and_b32_e32 v157, 0xffff0000, v157
	v_mul_f32 v158, v59, v174
	s_nop 0
	v_fma_f32 v157, v212, v158, v157
	s_nop 0
	v_mul_f32 v157, v157, v148
	s_nop 0
	v_mul_f32 v157, v157, v185
	s_nop 0
	v_max_f32_e32 v157, 0xc3e00000, v157
	v_min_f32_e32 v158, 0x43e00000, v157
	s_waitcnt lgkmcnt(0)
	s_nop 1
	v_mov_b32_dpp v159, v158 quad_perm:[1,0,3,2] row_mask:0xf bank_mask:0xf
	v_cvt_pk_fp8_f32 v157, v158, v159
	s_nop 1
	v_mov_b32_dpp v158, v157 quad_perm:[2,3,0,1] row_mask:0xf bank_mask:0xf
	s_and_saveexec_b64 s[6:7], s[4:5]
	s_cbranch_execz .LBB0_1449
	v_and_b32_e32 v157, 0xffff, v157
	s_waitcnt lgkmcnt(0)
	v_lshl_or_b32 v157, v158, 16, v157
	v_add_co_u32_e32 v158, vcc, 0x11000, v6
	s_nop 1
	v_addc_co_u32_e32 v159, vcc, 0, v7, vcc
	global_store_dword v[158:159], v157, off offset:160
.LBB0_1449:
	s_or_b64 exec, exec, s[6:7]
	s_waitcnt vmcnt(8)
	v_lshlrev_b32_e32 v157, 16, v156
	s_waitcnt lgkmcnt(0)
	v_mul_f32 v158, v43, v174
	s_nop 0
	v_fma_f32 v157, v212, v158, v157
	s_nop 0
	v_mul_f32 v157, v157, v148
	s_nop 0
	v_mul_f32 v157, v157, v184
	s_nop 0
	v_max_f32_e32 v157, 0xc3e00000, v157
	v_min_f32_e32 v158, 0x43e00000, v157
	s_nop 1
	v_mov_b32_dpp v159, v158 quad_perm:[1,0,3,2] row_mask:0xf bank_mask:0xf
	v_cvt_pk_fp8_f32 v157, v158, v159
	s_nop 1
	v_mov_b32_dpp v158, v157 quad_perm:[2,3,0,1] row_mask:0xf bank_mask:0xf
	s_and_saveexec_b64 s[6:7], s[4:5]
	s_cbranch_execz .LBB0_1451
	v_and_b32_e32 v157, 0xffff, v157
	s_waitcnt lgkmcnt(0)
	v_lshl_or_b32 v157, v158, 16, v157
	v_add_co_u32_e32 v158, vcc, 0x11000, v6
	s_nop 1
	v_addc_co_u32_e32 v159, vcc, 0, v7, vcc
	global_store_dword v[158:159], v157, off offset:192
.LBB0_1451:
	s_or_b64 exec, exec, s[6:7]
	v_and_b32_e32 v156, 0xffff0000, v156
	v_mul_f32 v157, v27, v174
	s_nop 0
	v_fma_f32 v156, v212, v157, v156
	s_nop 0
	v_mul_f32 v148, v156, v148
	s_nop 0
	v_mul_f32 v148, v148, v165
	s_nop 0
	v_max_f32_e32 v148, 0xc3e00000, v148
	v_min_f32_e32 v156, 0x43e00000, v148
	s_nop 1
	v_mov_b32_dpp v157, v156 quad_perm:[1,0,3,2] row_mask:0xf bank_mask:0xf
	s_waitcnt lgkmcnt(0)
	v_cvt_pk_fp8_f32 v148, v156, v157
	s_nop 1
	v_mov_b32_dpp v156, v148 quad_perm:[2,3,0,1] row_mask:0xf bank_mask:0xf
	s_and_saveexec_b64 s[6:7], s[4:5]
	s_cbranch_execz .LBB0_1453
	v_and_b32_e32 v148, 0xffff, v148
	s_waitcnt lgkmcnt(0)
	v_lshl_or_b32 v148, v156, 16, v148
	v_add_co_u32_e32 v156, vcc, 0x11000, v6
	s_nop 1
	v_addc_co_u32_e32 v157, vcc, 0, v7, vcc
	global_store_dword v[156:157], v148, off offset:224
.LBB0_1453:
	s_or_b64 exec, exec, s[6:7]
	v_pk_add_f32 v[16:17], v[16:17], v[146:147]
	v_mul_f32 v147, v140, v173
	s_nop 0
	v_pk_fma_f32 v[16:17], v[16:17], s[54:55], v[198:199] op_sel_hi:[1,0,0]
	s_nop 0
	v_mul_f32_e32 v146, 0x4b800000, v17
	v_cmp_gt_f32_e32 vcc, s53, v17
	v_cmp_gt_f32_e64 s[6:7], s53, v16
	s_nop 0
	v_cndmask_b32_e32 v17, v17, v146, vcc
	v_rsq_f32_e32 v17, v17
	s_waitcnt vmcnt(7)
	v_lshlrev_b32_e32 v146, 16, v155
	v_fma_f32 v146, v212, v147, v146
	v_mul_f32_e32 v148, 0x45800000, v17
	v_cndmask_b32_e32 v17, v17, v148, vcc
	v_mul_f32_e32 v17, 0x3f4ccccd, v17
	v_mul_f32 v146, v146, v17
	s_nop 0
	v_mul_f32 v146, v146, v190
	s_nop 0
	v_max_f32_e32 v146, 0xc3e00000, v146
	v_min_f32_e32 v147, 0x43e00000, v146
	s_nop 1
	v_mov_b32_dpp v148, v147 quad_perm:[1,0,3,2] row_mask:0xf bank_mask:0xf
	s_waitcnt lgkmcnt(0)
	v_cvt_pk_fp8_f32 v146, v147, v148
	s_nop 1
	v_mov_b32_dpp v147, v146 quad_perm:[2,3,0,1] row_mask:0xf bank_mask:0xf
	s_and_saveexec_b64 s[8:9], s[4:5]
	s_cbranch_execz .LBB0_1455
	v_and_b32_e32 v146, 0xffff, v146
	s_waitcnt lgkmcnt(0)
	v_lshl_or_b32 v148, v147, 16, v146
	v_add_co_u32_e32 v146, vcc, 0x12000, v6
	s_nop 1
	v_addc_co_u32_e32 v147, vcc, 0, v7, vcc
	global_store_dword v[146:147], v148, off
; #define SBAR() __builtin_amdgcn_sched_barrier(0)
; __device__ __forceinline__ int crow(int r, int hi) { return (r & 3) + 8 * (r >> 2) + 4 * hi; }
; __device__ __forceinline__ float mul_ns(float a, float b) { float r; asm("v_mul_f32 %0, %1, %2" : "=v"(r) : "v"(a), "v"(b)); return r; }
; __device__ __forceinline__ float fma_ns(float a, float b, float c) { float r; asm("v_fma_f32 %0, %1, %2, %3" : "=v"(r) : "v"(a), "v"(b), "v"(c)); return r; }
; __device__ __forceinline__ void store_quad8(unsigned char* p, float v, int r32) {
;     v = fminf(fmaxf(v, -448.f), 448.f);
;     const float v1 = swz_xor<1>(v);
;     const int w = __builtin_amdgcn_cvt_pk_fp8_f32(v, v1, 0, false);
;     const int w2 = __builtin_amdgcn_ds_swizzle(w, (2 << 10) | 0x1f);
;     if ((r32 & 3) == 0) *(unsigned*)p = ((unsigned)w & 0xffffu) | ((unsigned)w2 << 16);
; }
;     __device__ __forceinline__ void operator()(f32x16 (&o)[8], const float (&rli)[16], int wid, int lane, int r32, int hi) const {
;     ...
;             for (int rb = 0; rb < 16; rb += 4) { unsigned tw[4][4];
; #pragma unroll
;                 for (int q = 0; q < 4; ++q)
; #pragma unroll
;                     for (int k = 0; k < 4; ++k) tw[q][k] = (scw + ((rb + q) * 4 + k) * 64)[ul];
;                 asm volatile("" ::: "memory"); SBAR();
; #pragma unroll
;                 for (int q = 0; q < 4; ++q) { const int r = rb + q;
; #pragma unroll
;                     for (int d0 = 0; d0 < 8; ++d0) { const float t = __uint_as_float((d0 & 1) ? (tw[q][d0 >> 1] & 0xffff0000u) : (tw[q][d0 >> 1] << 16));
;                         const float dd = fma_ns(nlam, mul_ns(o[d0][r], rli[r]), t);
;                         store_quad8(base + (crow(r, 0) * 4096 + d0 * 32) + uo, mul_ns(mul_ns(dd, rn[r]), g[d0]), r32); } }
;                 asm volatile("" ::: "memory"); SBAR(); }
.LBB0_1455:
	s_or_b64 exec, exec, s[8:9]
	v_and_b32_e32 v146, 0xffff0000, v155
	s_waitcnt lgkmcnt(0)
	v_mul_f32 v147, v124, v173
	s_nop 0
	v_fma_f32 v146, v212, v147, v146
	s_nop 0
	v_mul_f32 v146, v146, v17
	s_nop 0
	v_mul_f32 v146, v146, v189
	s_nop 0
	v_max_f32_e32 v146, 0xc3e00000, v146
	v_min_f32_e32 v147, 0x43e00000, v146
	s_nop 1
	v_mov_b32_dpp v148, v147 quad_perm:[1,0,3,2] row_mask:0xf bank_mask:0xf
	v_cvt_pk_fp8_f32 v146, v147, v148
	s_nop 1
	v_mov_b32_dpp v147, v146 quad_perm:[2,3,0,1] row_mask:0xf bank_mask:0xf
	s_and_saveexec_b64 s[8:9], s[4:5]
	s_cbranch_execz .LBB0_1457
	v_and_b32_e32 v146, 0xffff, v146
	s_waitcnt lgkmcnt(0)
	v_lshl_or_b32 v148, v147, 16, v146
	v_add_co_u32_e32 v146, vcc, 0x12000, v6
	s_nop 1
	v_addc_co_u32_e32 v147, vcc, 0, v7, vcc
	global_store_dword v[146:147], v148, off offset:32
.LBB0_1457:
	s_or_b64 exec, exec, s[8:9]
	s_waitcnt vmcnt(6)
	v_lshlrev_b32_e32 v146, 16, v154
	s_waitcnt lgkmcnt(0)
	v_mul_f32 v147, v108, v173
	s_nop 0
	v_fma_f32 v146, v212, v147, v146
	s_nop 0
	v_mul_f32 v146, v146, v17
	s_nop 0
	v_mul_f32 v146, v146, v188
	s_nop 0
	v_max_f32_e32 v146, 0xc3e00000, v146
	v_min_f32_e32 v147, 0x43e00000, v146
	s_nop 1
	v_mov_b32_dpp v148, v147 quad_perm:[1,0,3,2] row_mask:0xf bank_mask:0xf
	v_cvt_pk_fp8_f32 v146, v147, v148
	s_nop 1
	v_mov_b32_dpp v147, v146 quad_perm:[2,3,0,1] row_mask:0xf bank_mask:0xf
	s_and_saveexec_b64 s[8:9], s[4:5]
	s_cbranch_execz .LBB0_1459
	v_and_b32_e32 v146, 0xffff, v146
	s_waitcnt lgkmcnt(0)
	v_lshl_or_b32 v148, v147, 16, v146
	v_add_co_u32_e32 v146, vcc, 0x12000, v6
	s_nop 1
	v_addc_co_u32_e32 v147, vcc, 0, v7, vcc
	global_store_dword v[146:147], v148, off offset:64
.LBB0_1459:
	s_or_b64 exec, exec, s[8:9]
	v_and_b32_e32 v146, 0xffff0000, v154
	s_waitcnt lgkmcnt(0)
	v_mul_f32 v147, v92, v173
	s_nop 0
	v_fma_f32 v146, v212, v147, v146
	s_nop 0
	v_mul_f32 v146, v146, v17
	s_nop 0
	v_mul_f32 v146, v146, v187
	s_nop 0
	v_max_f32_e32 v146, 0xc3e00000, v146
	v_min_f32_e32 v147, 0x43e00000, v146
	s_nop 1
	v_mov_b32_dpp v148, v147 quad_perm:[1,0,3,2] row_mask:0xf bank_mask:0xf
	v_cvt_pk_fp8_f32 v146, v147, v148
	s_nop 1
	v_mov_b32_dpp v147, v146 quad_perm:[2,3,0,1] row_mask:0xf bank_mask:0xf
	s_and_saveexec_b64 s[8:9], s[4:5]
	s_cbranch_execz .LBB0_1461
	v_and_b32_e32 v146, 0xffff, v146
	s_waitcnt lgkmcnt(0)
	v_lshl_or_b32 v148, v147, 16, v146
	v_add_co_u32_e32 v146, vcc, 0x12000, v6
	s_nop 1
	v_addc_co_u32_e32 v147, vcc, 0, v7, vcc
	global_store_dword v[146:147], v148, off offset:96
.LBB0_1461:
	s_or_b64 exec, exec, s[8:9]
	s_waitcnt vmcnt(5)
	v_lshlrev_b32_e32 v146, 16, v153
	s_waitcnt lgkmcnt(0)
	v_mul_f32 v147, v76, v173
	s_nop 0
	v_fma_f32 v146, v212, v147, v146
	s_nop 0
	v_mul_f32 v146, v146, v17
	s_nop 0
	v_mul_f32 v146, v146, v186
	s_nop 0
	v_max_f32_e32 v146, 0xc3e00000, v146
	v_min_f32_e32 v147, 0x43e00000, v146
	s_nop 1
	v_mov_b32_dpp v148, v147 quad_perm:[1,0,3,2] row_mask:0xf bank_mask:0xf
	v_cvt_pk_fp8_f32 v146, v147, v148
	s_nop 1
	v_mov_b32_dpp v147, v146 quad_perm:[2,3,0,1] row_mask:0xf bank_mask:0xf
	s_and_saveexec_b64 s[8:9], s[4:5]
	s_cbranch_execz .LBB0_1463
	v_and_b32_e32 v146, 0xffff, v146
	s_waitcnt lgkmcnt(0)
	v_lshl_or_b32 v148, v147, 16, v146
	v_add_co_u32_e32 v146, vcc, 0x12000, v6
	s_nop 1
	v_addc_co_u32_e32 v147, vcc, 0, v7, vcc
	global_store_dword v[146:147], v148, off offset:128
.LBB0_1463:
	s_or_b64 exec, exec, s[8:9]
	v_and_b32_e32 v146, 0xffff0000, v153
	s_waitcnt lgkmcnt(0)
	v_mul_f32 v147, v60, v173
	s_nop 0
	v_fma_f32 v146, v212, v147, v146
	s_nop 0
	v_mul_f32 v146, v146, v17
	s_nop 0
	v_mul_f32 v146, v146, v185
	s_nop 0
	v_max_f32_e32 v146, 0xc3e00000, v146
	v_min_f32_e32 v147, 0x43e00000, v146
	s_nop 1
	v_mov_b32_dpp v148, v147 quad_perm:[1,0,3,2] row_mask:0xf bank_mask:0xf
	v_cvt_pk_fp8_f32 v146, v147, v148
	s_nop 1
	v_mov_b32_dpp v147, v146 quad_perm:[2,3,0,1] row_mask:0xf bank_mask:0xf
	s_and_saveexec_b64 s[8:9], s[4:5]
	s_cbranch_execz .LBB0_1465
	v_and_b32_e32 v146, 0xffff, v146
	s_waitcnt lgkmcnt(0)
	v_lshl_or_b32 v148, v147, 16, v146
	v_add_co_u32_e32 v146, vcc, 0x12000, v6
	s_nop 1
	v_addc_co_u32_e32 v147, vcc, 0, v7, vcc
	global_store_dword v[146:147], v148, off offset:160
.LBB0_1465:
	s_or_b64 exec, exec, s[8:9]
	s_waitcnt vmcnt(4)
	v_lshlrev_b32_e32 v146, 16, v152
	s_waitcnt lgkmcnt(0)
	v_mul_f32 v147, v44, v173
	s_nop 0
	v_fma_f32 v146, v212, v147, v146
	s_nop 0
	v_mul_f32 v146, v146, v17
	s_nop 0
	v_mul_f32 v146, v146, v184
	s_nop 0
	v_max_f32_e32 v146, 0xc3e00000, v146
	v_min_f32_e32 v147, 0x43e00000, v146
	s_nop 1
	v_mov_b32_dpp v148, v147 quad_perm:[1,0,3,2] row_mask:0xf bank_mask:0xf
	v_cvt_pk_fp8_f32 v146, v147, v148
	s_nop 1
	v_mov_b32_dpp v147, v146 quad_perm:[2,3,0,1] row_mask:0xf bank_mask:0xf
	s_and_saveexec_b64 s[8:9], s[4:5]
	s_cbranch_execz .LBB0_1467
	v_and_b32_e32 v146, 0xffff, v146
	s_waitcnt lgkmcnt(0)
	v_lshl_or_b32 v148, v147, 16, v146
	v_add_co_u32_e32 v146, vcc, 0x12000, v6
	s_nop 1
	v_addc_co_u32_e32 v147, vcc, 0, v7, vcc
	global_store_dword v[146:147], v148, off offset:192
.LBB0_1467:
	s_or_b64 exec, exec, s[8:9]
	v_and_b32_e32 v146, 0xffff0000, v152
	s_waitcnt lgkmcnt(0)
	v_mul_f32 v147, v28, v173
	s_nop 0
	v_fma_f32 v146, v212, v147, v146
	s_nop 0
	v_mul_f32 v17, v146, v17
	s_nop 0
	v_mul_f32 v17, v17, v165
	s_nop 0
	v_max_f32_e32 v17, 0xc3e00000, v17
	v_min_f32_e32 v146, 0x43e00000, v17
	s_nop 1
	v_mov_b32_dpp v147, v146 quad_perm:[1,0,3,2] row_mask:0xf bank_mask:0xf
	v_cvt_pk_fp8_f32 v17, v146, v147
	s_nop 1
	v_mov_b32_dpp v146, v17 quad_perm:[2,3,0,1] row_mask:0xf bank_mask:0xf
	s_and_saveexec_b64 s[8:9], s[4:5]
	s_cbranch_execz .LBB0_1469
	v_and_b32_e32 v17, 0xffff, v17
	s_waitcnt lgkmcnt(0)
	v_lshl_or_b32 v17, v146, 16, v17
	v_add_co_u32_e32 v146, vcc, 0x12000, v6
	s_nop 1
	v_addc_co_u32_e32 v147, vcc, 0, v7, vcc
	global_store_dword v[146:147], v17, off offset:224
; #define SBAR() __builtin_amdgcn_sched_barrier(0)
; __device__ __forceinline__ int crow(int r, int hi) { return (r & 3) + 8 * (r >> 2) + 4 * hi; }
; __device__ __forceinline__ float mul_ns(float a, float b) { float r; asm("v_mul_f32 %0, %1, %2" : "=v"(r) : "v"(a), "v"(b)); return r; }
; __device__ __forceinline__ float fma_ns(float a, float b, float c) { float r; asm("v_fma_f32 %0, %1, %2, %3" : "=v"(r) : "v"(a), "v"(b), "v"(c)); return r; }
; __device__ __forceinline__ void store_quad8(unsigned char* p, float v, int r32) {
;     v = fminf(fmaxf(v, -448.f), 448.f);
;     const float v1 = swz_xor<1>(v);
;     const int w = __builtin_amdgcn_cvt_pk_fp8_f32(v, v1, 0, false);
;     const int w2 = __builtin_amdgcn_ds_swizzle(w, (2 << 10) | 0x1f);
;     if ((r32 & 3) == 0) *(unsigned*)p = ((unsigned)w & 0xffffu) | ((unsigned)w2 << 16);
; }
;     __device__ __forceinline__ void operator()(f32x16 (&o)[8], const float (&rli)[16], int wid, int lane, int r32, int hi) const {
;     ...
;             for (int rb = 0; rb < 16; rb += 4) { unsigned tw[4][4];
; #pragma unroll
;                 for (int q = 0; q < 4; ++q)
; #pragma unroll
;                     for (int k = 0; k < 4; ++k) tw[q][k] = (scw + ((rb + q) * 4 + k) * 64)[ul];
;                 asm volatile("" ::: "memory"); SBAR();
; #pragma unroll
;                 for (int q = 0; q < 4; ++q) { const int r = rb + q;
; #pragma unroll
;                     for (int d0 = 0; d0 < 8; ++d0) { const float t = __uint_as_float((d0 & 1) ? (tw[q][d0 >> 1] & 0xffff0000u) : (tw[q][d0 >> 1] << 16));
;                         const float dd = fma_ns(nlam, mul_ns(o[d0][r], rli[r]), t);
;                         store_quad8(base + (crow(r, 0) * 4096 + d0 * 32) + uo, mul_ns(mul_ns(dd, rn[r]), g[d0]), r32); } }
;                 asm volatile("" ::: "memory"); SBAR(); }
.LBB0_1469:
	s_or_b64 exec, exec, s[8:9]
	v_mul_f32_e32 v17, 0x4b800000, v16
	v_cndmask_b32_e64 v16, v16, v17, s[6:7]
	v_rsq_f32_e32 v16, v16
	s_waitcnt lgkmcnt(0)
	v_mul_f32 v146, v141, v172
	v_mul_f32_e32 v17, 0x45800000, v16
	v_cndmask_b32_e64 v16, v16, v17, s[6:7]
	s_waitcnt vmcnt(3)
	v_lshlrev_b32_e32 v17, 16, v151
	v_fma_f32 v17, v212, v146, v17
	v_mul_f32_e32 v16, 0x3f4ccccd, v16
	v_mul_f32 v17, v17, v16
	s_nop 0
	v_mul_f32 v17, v17, v190
	s_nop 0
	v_max_f32_e32 v17, 0xc3e00000, v17
	v_min_f32_e32 v146, 0x43e00000, v17
	s_nop 1
	v_mov_b32_dpp v147, v146 quad_perm:[1,0,3,2] row_mask:0xf bank_mask:0xf
	v_cvt_pk_fp8_f32 v17, v146, v147
	s_nop 1
	v_mov_b32_dpp v146, v17 quad_perm:[2,3,0,1] row_mask:0xf bank_mask:0xf
	s_and_saveexec_b64 s[6:7], s[4:5]
	s_cbranch_execz .LBB0_1471
	v_and_b32_e32 v17, 0xffff, v17
	s_waitcnt lgkmcnt(0)
	v_lshl_or_b32 v17, v146, 16, v17
	v_add_co_u32_e32 v146, vcc, 0x13000, v6
	s_nop 1
	v_addc_co_u32_e32 v147, vcc, 0, v7, vcc
	global_store_dword v[146:147], v17, off
.LBB0_1471:
	s_or_b64 exec, exec, s[6:7]
	v_and_b32_e32 v17, 0xffff0000, v151
	s_waitcnt lgkmcnt(0)
	v_mul_f32 v146, v125, v172
	s_nop 0
	v_fma_f32 v17, v212, v146, v17
	s_nop 0
	v_mul_f32 v17, v17, v16
	s_nop 0
	v_mul_f32 v17, v17, v189
	s_nop 0
	v_max_f32_e32 v17, 0xc3e00000, v17
	v_min_f32_e32 v146, 0x43e00000, v17
	s_nop 1
	v_mov_b32_dpp v147, v146 quad_perm:[1,0,3,2] row_mask:0xf bank_mask:0xf
	v_cvt_pk_fp8_f32 v17, v146, v147
	s_nop 1
	v_mov_b32_dpp v146, v17 quad_perm:[2,3,0,1] row_mask:0xf bank_mask:0xf
	s_and_saveexec_b64 s[6:7], s[4:5]
	s_cbranch_execz .LBB0_1473
	v_and_b32_e32 v17, 0xffff, v17
	s_waitcnt lgkmcnt(0)
	v_lshl_or_b32 v17, v146, 16, v17
	v_add_co_u32_e32 v146, vcc, 0x13000, v6
	s_nop 1
	v_addc_co_u32_e32 v147, vcc, 0, v7, vcc
	global_store_dword v[146:147], v17, off offset:32
.LBB0_1473:
	s_or_b64 exec, exec, s[6:7]
	s_waitcnt vmcnt(2)
	v_lshlrev_b32_e32 v17, 16, v150
	s_waitcnt lgkmcnt(0)
	v_mul_f32 v146, v109, v172
	s_nop 0
	v_fma_f32 v17, v212, v146, v17
	s_nop 0
	v_mul_f32 v17, v17, v16
	s_nop 0
	v_mul_f32 v17, v17, v188
	s_nop 0
	v_max_f32_e32 v17, 0xc3e00000, v17
	v_min_f32_e32 v146, 0x43e00000, v17
	s_nop 1
	v_mov_b32_dpp v147, v146 quad_perm:[1,0,3,2] row_mask:0xf bank_mask:0xf
	v_cvt_pk_fp8_f32 v17, v146, v147
	s_nop 1
	v_mov_b32_dpp v146, v17 quad_perm:[2,3,0,1] row_mask:0xf bank_mask:0xf
	s_and_saveexec_b64 s[6:7], s[4:5]
	s_cbranch_execz .LBB0_1475
	v_and_b32_e32 v17, 0xffff, v17
	s_waitcnt lgkmcnt(0)
	v_lshl_or_b32 v17, v146, 16, v17
	v_add_co_u32_e32 v146, vcc, 0x13000, v6
	s_nop 1
	v_addc_co_u32_e32 v147, vcc, 0, v7, vcc
	global_store_dword v[146:147], v17, off offset:64
.LBB0_1475:
	s_or_b64 exec, exec, s[6:7]
	v_and_b32_e32 v17, 0xffff0000, v150
	s_waitcnt lgkmcnt(0)
	v_mul_f32 v146, v93, v172
	s_nop 0
	v_fma_f32 v17, v212, v146, v17
	s_nop 0
	v_mul_f32 v17, v17, v16
	s_nop 0
	v_mul_f32 v17, v17, v187
	s_nop 0
	v_max_f32_e32 v17, 0xc3e00000, v17
	v_min_f32_e32 v146, 0x43e00000, v17
	s_nop 1
	v_mov_b32_dpp v147, v146 quad_perm:[1,0,3,2] row_mask:0xf bank_mask:0xf
	v_cvt_pk_fp8_f32 v17, v146, v147
	s_nop 1
	v_mov_b32_dpp v146, v17 quad_perm:[2,3,0,1] row_mask:0xf bank_mask:0xf
	s_and_saveexec_b64 s[6:7], s[4:5]
	s_cbranch_execz .LBB0_1477
	v_and_b32_e32 v17, 0xffff, v17
	s_waitcnt lgkmcnt(0)
	v_lshl_or_b32 v17, v146, 16, v17
	v_add_co_u32_e32 v146, vcc, 0x13000, v6
	s_nop 1
	v_addc_co_u32_e32 v147, vcc, 0, v7, vcc
	global_store_dword v[146:147], v17, off offset:96
.LBB0_1477:
	s_or_b64 exec, exec, s[6:7]
	s_waitcnt vmcnt(1)
	v_lshlrev_b32_e32 v17, 16, v149
	s_waitcnt lgkmcnt(0)
	v_mul_f32 v146, v77, v172
	s_nop 0
	v_fma_f32 v17, v212, v146, v17
	s_nop 0
	v_mul_f32 v17, v17, v16
	s_nop 0
	v_mul_f32 v17, v17, v186
	s_nop 0
	v_max_f32_e32 v17, 0xc3e00000, v17
	v_min_f32_e32 v146, 0x43e00000, v17
	s_nop 1
	v_mov_b32_dpp v147, v146 quad_perm:[1,0,3,2] row_mask:0xf bank_mask:0xf
	v_cvt_pk_fp8_f32 v17, v146, v147
	s_nop 1
	v_mov_b32_dpp v146, v17 quad_perm:[2,3,0,1] row_mask:0xf bank_mask:0xf
	s_and_saveexec_b64 s[6:7], s[4:5]
	s_cbranch_execz .LBB0_1479
	v_and_b32_e32 v17, 0xffff, v17
	s_waitcnt lgkmcnt(0)
	v_lshl_or_b32 v17, v146, 16, v17
	v_add_co_u32_e32 v146, vcc, 0x13000, v6
	s_nop 1
	v_addc_co_u32_e32 v147, vcc, 0, v7, vcc
	global_store_dword v[146:147], v17, off offset:128
.LBB0_1479:
	s_or_b64 exec, exec, s[6:7]
	v_and_b32_e32 v17, 0xffff0000, v149
	s_waitcnt lgkmcnt(0)
	v_mul_f32 v146, v61, v172
	s_nop 0
	v_fma_f32 v17, v212, v146, v17
	s_nop 0
	v_mul_f32 v17, v17, v16
	s_nop 0
	v_mul_f32 v17, v17, v185
	s_nop 0
	v_max_f32_e32 v17, 0xc3e00000, v17
	v_min_f32_e32 v146, 0x43e00000, v17
	s_nop 1
	v_mov_b32_dpp v147, v146 quad_perm:[1,0,3,2] row_mask:0xf bank_mask:0xf
	v_cvt_pk_fp8_f32 v17, v146, v147
	s_nop 1
	v_mov_b32_dpp v146, v17 quad_perm:[2,3,0,1] row_mask:0xf bank_mask:0xf
	s_and_saveexec_b64 s[6:7], s[4:5]
	s_cbranch_execz .LBB0_1481
	v_and_b32_e32 v17, 0xffff, v17
	s_waitcnt lgkmcnt(0)
	v_lshl_or_b32 v17, v146, 16, v17
	v_add_co_u32_e32 v146, vcc, 0x13000, v6
	s_nop 1
	v_addc_co_u32_e32 v147, vcc, 0, v7, vcc
	global_store_dword v[146:147], v17, off offset:160
.LBB0_1481:
	s_or_b64 exec, exec, s[6:7]
	s_waitcnt vmcnt(0)
	v_lshlrev_b32_e32 v17, 16, v2
	s_waitcnt lgkmcnt(0)
	v_mul_f32 v146, v45, v172
	s_nop 0
	v_fma_f32 v17, v212, v146, v17
	s_nop 0
	v_mul_f32 v17, v17, v16
	s_nop 0
	v_mul_f32 v17, v17, v184
	s_nop 0
	v_max_f32_e32 v17, 0xc3e00000, v17
	v_min_f32_e32 v146, 0x43e00000, v17
	s_nop 1
	v_mov_b32_dpp v147, v146 quad_perm:[1,0,3,2] row_mask:0xf bank_mask:0xf
	v_cvt_pk_fp8_f32 v17, v146, v147
	s_nop 1
	v_mov_b32_dpp v146, v17 quad_perm:[2,3,0,1] row_mask:0xf bank_mask:0xf
	s_and_saveexec_b64 s[6:7], s[4:5]
	s_cbranch_execz .LBB0_1483
	v_and_b32_e32 v17, 0xffff, v17
	s_waitcnt lgkmcnt(0)
	v_lshl_or_b32 v17, v146, 16, v17
	v_add_co_u32_e32 v146, vcc, 0x13000, v6
	s_nop 1
	v_addc_co_u32_e32 v147, vcc, 0, v7, vcc
	global_store_dword v[146:147], v17, off offset:192
; #define SBAR() __builtin_amdgcn_sched_barrier(0)
; __device__ __forceinline__ int crow(int r, int hi) { return (r & 3) + 8 * (r >> 2) + 4 * hi; }
; __device__ __forceinline__ float mul_ns(float a, float b) { float r; asm("v_mul_f32 %0, %1, %2" : "=v"(r) : "v"(a), "v"(b)); return r; }
; __device__ __forceinline__ float fma_ns(float a, float b, float c) { float r; asm("v_fma_f32 %0, %1, %2, %3" : "=v"(r) : "v"(a), "v"(b), "v"(c)); return r; }
; __device__ __forceinline__ void store_quad8(unsigned char* p, float v, int r32) {
;     v = fminf(fmaxf(v, -448.f), 448.f);
;     const float v1 = swz_xor<1>(v);
;     const int w = __builtin_amdgcn_cvt_pk_fp8_f32(v, v1, 0, false);
;     const int w2 = __builtin_amdgcn_ds_swizzle(w, (2 << 10) | 0x1f);
;     if ((r32 & 3) == 0) *(unsigned*)p = ((unsigned)w & 0xffffu) | ((unsigned)w2 << 16);
; }
;     __device__ __forceinline__ void operator()(f32x16 (&o)[8], const float (&rli)[16], int wid, int lane, int r32, int hi) const {
;     ...
;                 for (int q = 0; q < 4; ++q) { const int r = rb + q; float s = 0.f;
; #pragma unroll
;                     for (int d0 = 0; d0 < 8; ++d0) { const float t = __uint_as_float((d0 & 1) ? (tw[q][d0 >> 1] & 0xffff0000u) : (tw[q][d0 >> 1] << 16));
;                         const float dd = fma_ns(nlam, mul_ns(o[d0][r], rli[r]), t); s = fma_ns(dd, dd, s); }
;                     s = half_sum(s); rn[r] = rsqrtf(s * (1.0f / 256.0f) + 1e-5f) * 0.8f; }
;     ...
;             for (int rb = 0; rb < 16; rb += 4) { unsigned tw[4][4];
; #pragma unroll
;                 for (int q = 0; q < 4; ++q)
; #pragma unroll
;                     for (int k = 0; k < 4; ++k) tw[q][k] = (scw + ((rb + q) * 4 + k) * 64)[ul];
;                 asm volatile("" ::: "memory"); SBAR();
; #pragma unroll
;                 for (int q = 0; q < 4; ++q) { const int r = rb + q;
; #pragma unroll
;                     for (int d0 = 0; d0 < 8; ++d0) { const float t = __uint_as_float((d0 & 1) ? (tw[q][d0 >> 1] & 0xffff0000u) : (tw[q][d0 >> 1] << 16));
;                         const float dd = fma_ns(nlam, mul_ns(o[d0][r], rli[r]), t);
;                         store_quad8(base + (crow(r, 0) * 4096 + d0 * 32) + uo, mul_ns(mul_ns(dd, rn[r]), g[d0]), r32); } }
;                 asm volatile("" ::: "memory"); SBAR(); }
.LBB0_1483:
	s_or_b64 exec, exec, s[6:7]
	v_and_b32_e32 v2, 0xffff0000, v2
	v_mul_f32 v17, v29, v172
	s_nop 0
	v_fma_f32 v2, v212, v17, v2
	s_nop 0
	v_mul_f32 v2, v2, v16
	s_nop 0
	v_mul_f32 v2, v2, v165
	s_nop 0
	v_max_f32_e32 v2, 0xc3e00000, v2
	v_min_f32_e32 v16, 0x43e00000, v2
	s_nop 1
	v_mov_b32_dpp v17, v16 quad_perm:[1,0,3,2] row_mask:0xf bank_mask:0xf
	s_waitcnt lgkmcnt(0)
	v_cvt_pk_fp8_f32 v2, v16, v17
	s_nop 1
	v_mov_b32_dpp v16, v2 quad_perm:[2,3,0,1] row_mask:0xf bank_mask:0xf
	s_and_saveexec_b64 s[6:7], s[4:5]
	s_cbranch_execz .LBB0_1485
	v_and_b32_e32 v2, 0xffff, v2
	s_waitcnt lgkmcnt(0)
	v_lshl_or_b32 v2, v16, 16, v2
	v_add_co_u32_e32 v16, vcc, 0x13000, v6
	s_nop 1
	v_addc_co_u32_e32 v17, vcc, 0, v7, vcc
	global_store_dword v[16:17], v2, off offset:224
.LBB0_1485:
	s_or_b64 exec, exec, s[6:7]
	s_mov_b64 s[6:7], 0x3000
	s_waitcnt lgkmcnt(0)
	v_lshl_add_u64 v[16:17], v[4:5], 0, s[6:7]
	s_mov_b64 s[6:7], 0x3100
	v_lshl_add_u64 v[146:147], v[4:5], 0, s[6:7]
	s_mov_b64 s[6:7], 0x3200
	v_lshl_add_u64 v[148:149], v[4:5], 0, s[6:7]
	s_mov_b64 s[6:7], 0x3300
	v_lshl_add_u64 v[156:157], v[4:5], 0, s[6:7]
	s_mov_b64 s[6:7], 0x3400
	v_lshl_add_u64 v[158:159], v[4:5], 0, s[6:7]
	s_mov_b64 s[6:7], 0x3500
	v_lshl_add_u64 v[160:161], v[4:5], 0, s[6:7]
	s_mov_b64 s[6:7], 0x3600
	v_lshl_add_u64 v[162:163], v[4:5], 0, s[6:7]
	s_mov_b64 s[6:7], 0x3700
	v_lshl_add_u64 v[166:167], v[4:5], 0, s[6:7]
	s_mov_b64 s[6:7], 0x3800
	v_pk_add_f32 v[12:13], v[12:13], v[14:15]
	v_lshl_add_u64 v[192:193], v[4:5], 0, s[6:7]
	s_mov_b64 s[6:7], 0x3900
	v_pk_fma_f32 v[12:13], v[12:13], s[54:55], v[198:199] op_sel_hi:[1,0,0]
	v_lshl_add_u64 v[194:195], v[4:5], 0, s[6:7]
	s_mov_b64 s[6:7], 0x3a00
	v_mul_f32_e32 v2, 0x4b800000, v13
	v_cmp_gt_f32_e32 vcc, s53, v13
	v_lshl_add_u64 v[196:197], v[4:5], 0, s[6:7]
	s_mov_b64 s[6:7], 0x3b00
	v_cndmask_b32_e32 v2, v13, v2, vcc
	v_lshl_add_u64 v[202:203], v[4:5], 0, s[6:7]
	s_mov_b64 s[6:7], 0x3c00
	v_rsq_f32_e32 v2, v2
	v_lshl_add_u64 v[204:205], v[4:5], 0, s[6:7]
	s_mov_b64 s[6:7], 0x3d00
	v_lshl_add_u64 v[206:207], v[4:5], 0, s[6:7]
	s_mov_b64 s[6:7], 0x3e00
	v_lshl_add_u64 v[208:209], v[4:5], 0, s[6:7]
	s_mov_b64 s[6:7], 0x3f00
	v_lshl_add_u64 v[214:215], v[4:5], 0, s[6:7]
	v_mul_f32_e32 v4, 0x45800000, v2
	v_cndmask_b32_e32 v2, v2, v4, vcc
	v_cmp_gt_f32_e64 s[6:7], s53, v12
	v_mul_f32_e32 v150, 0x3f4ccccd, v2
	global_load_dword v154, v[16:17], off
	global_load_dword v153, v[146:147], off
	global_load_dword v152, v[148:149], off
	global_load_dword v151, v[156:157], off
	s_nop 0
	global_load_dword v149, v[158:159], off
	global_load_dword v148, v[160:161], off
	global_load_dword v5, v[162:163], off
	global_load_dword v4, v[166:167], off
	global_load_dword v147, v[192:193], off
	global_load_dword v146, v[194:195], off
	global_load_dword v17, v[196:197], off
	global_load_dword v16, v[202:203], off
	global_load_dword v15, v[204:205], off
	global_load_dword v14, v[206:207], off
	global_load_dword v13, v[208:209], off
	global_load_dword v2, v[214:215], off
	s_waitcnt vmcnt(15)
	v_lshlrev_b32_e32 v155, 16, v154
	v_mul_f32 v156, v142, v171
	s_nop 0
	v_fma_f32 v155, v212, v156, v155
	s_nop 0
	v_mul_f32 v155, v155, v150
	s_nop 0
	v_mul_f32 v155, v155, v190
	s_nop 0
	v_max_f32_e32 v155, 0xc3e00000, v155
	v_min_f32_e32 v156, 0x43e00000, v155
	s_nop 1
	v_mov_b32_dpp v157, v156 quad_perm:[1,0,3,2] row_mask:0xf bank_mask:0xf
	v_cvt_pk_fp8_f32 v155, v156, v157
	s_nop 1
	v_mov_b32_dpp v156, v155 quad_perm:[2,3,0,1] row_mask:0xf bank_mask:0xf
	s_and_saveexec_b64 s[8:9], s[4:5]
	s_cbranch_execz .LBB0_1487
	v_and_b32_e32 v155, 0xffff, v155
	s_waitcnt lgkmcnt(0)
	v_lshl_or_b32 v155, v156, 16, v155
	v_add_co_u32_e32 v156, vcc, 0x18000, v6
	s_nop 1
	v_addc_co_u32_e32 v157, vcc, 0, v7, vcc
	global_store_dword v[156:157], v155, off
.LBB0_1487:
	s_or_b64 exec, exec, s[8:9]
	v_and_b32_e32 v154, 0xffff0000, v154
	v_mul_f32 v155, v126, v171
	s_nop 0
	v_fma_f32 v154, v212, v155, v154
	s_nop 0
	v_mul_f32 v154, v154, v150
	s_nop 0
	v_mul_f32 v154, v154, v189
	s_nop 0
	v_max_f32_e32 v154, 0xc3e00000, v154
	v_min_f32_e32 v155, 0x43e00000, v154
	s_waitcnt lgkmcnt(0)
	s_nop 1
	v_mov_b32_dpp v156, v155 quad_perm:[1,0,3,2] row_mask:0xf bank_mask:0xf
	v_cvt_pk_fp8_f32 v154, v155, v156
	s_nop 1
	v_mov_b32_dpp v155, v154 quad_perm:[2,3,0,1] row_mask:0xf bank_mask:0xf
	s_and_saveexec_b64 s[8:9], s[4:5]
	s_cbranch_execz .LBB0_1489
	v_and_b32_e32 v154, 0xffff, v154
	s_waitcnt lgkmcnt(0)
	v_lshl_or_b32 v156, v155, 16, v154
	v_add_co_u32_e32 v154, vcc, 0x18000, v6
	s_nop 1
	v_addc_co_u32_e32 v155, vcc, 0, v7, vcc
	global_store_dword v[154:155], v156, off offset:32
.LBB0_1489:
	s_or_b64 exec, exec, s[8:9]
	s_waitcnt vmcnt(14)
	v_lshlrev_b32_e32 v154, 16, v153
	s_waitcnt lgkmcnt(0)
	v_mul_f32 v155, v110, v171
	s_nop 0
	v_fma_f32 v154, v212, v155, v154
	s_nop 0
	v_mul_f32 v154, v154, v150
	s_nop 0
	v_mul_f32 v154, v154, v188
	s_nop 0
	v_max_f32_e32 v154, 0xc3e00000, v154
	v_min_f32_e32 v155, 0x43e00000, v154
	s_nop 1
	v_mov_b32_dpp v156, v155 quad_perm:[1,0,3,2] row_mask:0xf bank_mask:0xf
	v_cvt_pk_fp8_f32 v154, v155, v156
	s_nop 1
	v_mov_b32_dpp v155, v154 quad_perm:[2,3,0,1] row_mask:0xf bank_mask:0xf
	s_and_saveexec_b64 s[8:9], s[4:5]
	s_cbranch_execz .LBB0_1491
	v_and_b32_e32 v154, 0xffff, v154
	s_waitcnt lgkmcnt(0)
	v_lshl_or_b32 v156, v155, 16, v154
	v_add_co_u32_e32 v154, vcc, 0x18000, v6
	s_nop 1
	v_addc_co_u32_e32 v155, vcc, 0, v7, vcc
	global_store_dword v[154:155], v156, off offset:64
; #define SBAR() __builtin_amdgcn_sched_barrier(0)
; __device__ __forceinline__ int crow(int r, int hi) { return (r & 3) + 8 * (r >> 2) + 4 * hi; }
; __device__ __forceinline__ float mul_ns(float a, float b) { float r; asm("v_mul_f32 %0, %1, %2" : "=v"(r) : "v"(a), "v"(b)); return r; }
; __device__ __forceinline__ float fma_ns(float a, float b, float c) { float r; asm("v_fma_f32 %0, %1, %2, %3" : "=v"(r) : "v"(a), "v"(b), "v"(c)); return r; }
; __device__ __forceinline__ void store_quad8(unsigned char* p, float v, int r32) {
;     v = fminf(fmaxf(v, -448.f), 448.f);
;     const float v1 = swz_xor<1>(v);
;     const int w = __builtin_amdgcn_cvt_pk_fp8_f32(v, v1, 0, false);
;     const int w2 = __builtin_amdgcn_ds_swizzle(w, (2 << 10) | 0x1f);
;     if ((r32 & 3) == 0) *(unsigned*)p = ((unsigned)w & 0xffffu) | ((unsigned)w2 << 16);
; }
;     __device__ __forceinline__ void operator()(f32x16 (&o)[8], const float (&rli)[16], int wid, int lane, int r32, int hi) const {
;     ...
;             for (int rb = 0; rb < 16; rb += 4) { unsigned tw[4][4];
; #pragma unroll
;                 for (int q = 0; q < 4; ++q)
; #pragma unroll
;                     for (int k = 0; k < 4; ++k) tw[q][k] = (scw + ((rb + q) * 4 + k) * 64)[ul];
;                 asm volatile("" ::: "memory"); SBAR();
; #pragma unroll
;                 for (int q = 0; q < 4; ++q) { const int r = rb + q;
; #pragma unroll
;                     for (int d0 = 0; d0 < 8; ++d0) { const float t = __uint_as_float((d0 & 1) ? (tw[q][d0 >> 1] & 0xffff0000u) : (tw[q][d0 >> 1] << 16));
;                         const float dd = fma_ns(nlam, mul_ns(o[d0][r], rli[r]), t);
;                         store_quad8(base + (crow(r, 0) * 4096 + d0 * 32) + uo, mul_ns(mul_ns(dd, rn[r]), g[d0]), r32); } }
;                 asm volatile("" ::: "memory"); SBAR(); }
.LBB0_1491:
	s_or_b64 exec, exec, s[8:9]
	v_and_b32_e32 v153, 0xffff0000, v153
	v_mul_f32 v154, v94, v171
	s_nop 0
	v_fma_f32 v153, v212, v154, v153
	s_nop 0
	v_mul_f32 v153, v153, v150
	s_nop 0
	v_mul_f32 v153, v153, v187
	s_nop 0
	v_max_f32_e32 v153, 0xc3e00000, v153
	v_min_f32_e32 v154, 0x43e00000, v153
	s_waitcnt lgkmcnt(0)
	s_nop 1
	v_mov_b32_dpp v155, v154 quad_perm:[1,0,3,2] row_mask:0xf bank_mask:0xf
	v_cvt_pk_fp8_f32 v153, v154, v155
	s_nop 1
	v_mov_b32_dpp v154, v153 quad_perm:[2,3,0,1] row_mask:0xf bank_mask:0xf
	s_and_saveexec_b64 s[8:9], s[4:5]
	s_cbranch_execz .LBB0_1493
	v_and_b32_e32 v153, 0xffff, v153
	s_waitcnt lgkmcnt(0)
	v_lshl_or_b32 v153, v154, 16, v153
	v_add_co_u32_e32 v154, vcc, 0x18000, v6
	s_nop 1
	v_addc_co_u32_e32 v155, vcc, 0, v7, vcc
	global_store_dword v[154:155], v153, off offset:96
.LBB0_1493:
	s_or_b64 exec, exec, s[8:9]
	s_waitcnt vmcnt(13)
	v_lshlrev_b32_e32 v153, 16, v152
	s_waitcnt lgkmcnt(0)
	v_mul_f32 v154, v78, v171
	s_nop 0
	v_fma_f32 v153, v212, v154, v153
	s_nop 0
	v_mul_f32 v153, v153, v150
	s_nop 0
	v_mul_f32 v153, v153, v186
	s_nop 0
	v_max_f32_e32 v153, 0xc3e00000, v153
	v_min_f32_e32 v154, 0x43e00000, v153
	s_nop 1
	v_mov_b32_dpp v155, v154 quad_perm:[1,0,3,2] row_mask:0xf bank_mask:0xf
	v_cvt_pk_fp8_f32 v153, v154, v155
	s_nop 1
	v_mov_b32_dpp v154, v153 quad_perm:[2,3,0,1] row_mask:0xf bank_mask:0xf
	s_and_saveexec_b64 s[8:9], s[4:5]
	s_cbranch_execz .LBB0_1495
	v_and_b32_e32 v153, 0xffff, v153
	s_waitcnt lgkmcnt(0)
	v_lshl_or_b32 v153, v154, 16, v153
	v_add_co_u32_e32 v154, vcc, 0x18000, v6
	s_nop 1
	v_addc_co_u32_e32 v155, vcc, 0, v7, vcc
	global_store_dword v[154:155], v153, off offset:128
.LBB0_1495:
	s_or_b64 exec, exec, s[8:9]
	v_and_b32_e32 v152, 0xffff0000, v152
	v_mul_f32 v153, v62, v171
	s_nop 0
	v_fma_f32 v152, v212, v153, v152
	s_nop 0
	v_mul_f32 v152, v152, v150
	s_nop 0
	v_mul_f32 v152, v152, v185
	s_nop 0
	v_max_f32_e32 v152, 0xc3e00000, v152
	v_min_f32_e32 v153, 0x43e00000, v152
	s_waitcnt lgkmcnt(0)
	s_nop 1
	v_mov_b32_dpp v154, v153 quad_perm:[1,0,3,2] row_mask:0xf bank_mask:0xf
	v_cvt_pk_fp8_f32 v152, v153, v154
	s_nop 1
	v_mov_b32_dpp v153, v152 quad_perm:[2,3,0,1] row_mask:0xf bank_mask:0xf
	s_and_saveexec_b64 s[8:9], s[4:5]
	s_cbranch_execz .LBB0_1497
	v_and_b32_e32 v152, 0xffff, v152
	s_waitcnt lgkmcnt(0)
	v_lshl_or_b32 v154, v153, 16, v152
	v_add_co_u32_e32 v152, vcc, 0x18000, v6
	s_nop 1
	v_addc_co_u32_e32 v153, vcc, 0, v7, vcc
	global_store_dword v[152:153], v154, off offset:160
.LBB0_1497:
	s_or_b64 exec, exec, s[8:9]
	s_waitcnt vmcnt(12)
	v_lshlrev_b32_e32 v152, 16, v151
	s_waitcnt lgkmcnt(0)
	v_mul_f32 v153, v46, v171
	s_nop 0
	v_fma_f32 v152, v212, v153, v152
	s_nop 0
	v_mul_f32 v152, v152, v150
	s_nop 0
	v_mul_f32 v152, v152, v184
	s_nop 0
	v_max_f32_e32 v152, 0xc3e00000, v152
	v_min_f32_e32 v153, 0x43e00000, v152
	s_nop 1
	v_mov_b32_dpp v154, v153 quad_perm:[1,0,3,2] row_mask:0xf bank_mask:0xf
	v_cvt_pk_fp8_f32 v152, v153, v154
	s_nop 1
	v_mov_b32_dpp v153, v152 quad_perm:[2,3,0,1] row_mask:0xf bank_mask:0xf
	s_and_saveexec_b64 s[8:9], s[4:5]
	s_cbranch_execz .LBB0_1499
	v_and_b32_e32 v152, 0xffff, v152
	s_waitcnt lgkmcnt(0)
	v_lshl_or_b32 v154, v153, 16, v152
	v_add_co_u32_e32 v152, vcc, 0x18000, v6
	s_nop 1
	v_addc_co_u32_e32 v153, vcc, 0, v7, vcc
	global_store_dword v[152:153], v154, off offset:192
.LBB0_1499:
	s_or_b64 exec, exec, s[8:9]
	v_and_b32_e32 v151, 0xffff0000, v151
	v_mul_f32 v152, v30, v171
	s_nop 0
	v_fma_f32 v151, v212, v152, v151
	s_nop 0
	v_mul_f32 v150, v151, v150
	s_nop 0
	v_mul_f32 v150, v150, v165
	s_nop 0
	v_max_f32_e32 v150, 0xc3e00000, v150
	v_min_f32_e32 v151, 0x43e00000, v150
	s_nop 1
	v_mov_b32_dpp v152, v151 quad_perm:[1,0,3,2] row_mask:0xf bank_mask:0xf
	s_waitcnt lgkmcnt(0)
	v_cvt_pk_fp8_f32 v150, v151, v152
	s_nop 1
	v_mov_b32_dpp v151, v150 quad_perm:[2,3,0,1] row_mask:0xf bank_mask:0xf
	s_and_saveexec_b64 s[8:9], s[4:5]
	s_cbranch_execz .LBB0_1501
	v_and_b32_e32 v150, 0xffff, v150
	s_waitcnt lgkmcnt(0)
	v_lshl_or_b32 v152, v151, 16, v150
	v_add_co_u32_e32 v150, vcc, 0x18000, v6
	s_nop 1
	v_addc_co_u32_e32 v151, vcc, 0, v7, vcc
	global_store_dword v[150:151], v152, off offset:224
.LBB0_1501:
	s_or_b64 exec, exec, s[8:9]
	v_mul_f32_e32 v150, 0x4b800000, v12
	v_cndmask_b32_e64 v12, v12, v150, s[6:7]
	v_rsq_f32_e32 v12, v12
	s_waitcnt lgkmcnt(0)
	v_mul_f32 v151, v143, v170
	v_mul_f32_e32 v150, 0x45800000, v12
	v_cndmask_b32_e64 v12, v12, v150, s[6:7]
	s_waitcnt vmcnt(11)
	v_lshlrev_b32_e32 v150, 16, v149
	v_fma_f32 v150, v212, v151, v150
	v_mul_f32_e32 v12, 0x3f4ccccd, v12
	v_mul_f32 v150, v150, v12
	s_nop 0
	v_mul_f32 v150, v150, v190
	s_nop 0
	v_max_f32_e32 v150, 0xc3e00000, v150
	v_min_f32_e32 v151, 0x43e00000, v150
	s_nop 1
	v_mov_b32_dpp v152, v151 quad_perm:[1,0,3,2] row_mask:0xf bank_mask:0xf
	v_cvt_pk_fp8_f32 v150, v151, v152
	s_nop 1
	v_mov_b32_dpp v151, v150 quad_perm:[2,3,0,1] row_mask:0xf bank_mask:0xf
	s_and_saveexec_b64 s[6:7], s[4:5]
	s_cbranch_execz .LBB0_1503
	v_and_b32_e32 v150, 0xffff, v150
	s_waitcnt lgkmcnt(0)
	v_lshl_or_b32 v152, v151, 16, v150
	v_add_co_u32_e32 v150, vcc, 0x19000, v6
	s_nop 1
	v_addc_co_u32_e32 v151, vcc, 0, v7, vcc
	global_store_dword v[150:151], v152, off
.LBB0_1503:
	s_or_b64 exec, exec, s[6:7]
	v_and_b32_e32 v149, 0xffff0000, v149
	v_mul_f32 v150, v127, v170
	s_nop 0
	v_fma_f32 v149, v212, v150, v149
	s_nop 0
	v_mul_f32 v149, v149, v12
	s_nop 0
	v_mul_f32 v149, v149, v189
	s_nop 0
	v_max_f32_e32 v149, 0xc3e00000, v149
	v_min_f32_e32 v150, 0x43e00000, v149
	s_waitcnt lgkmcnt(0)
	s_nop 1
	v_mov_b32_dpp v151, v150 quad_perm:[1,0,3,2] row_mask:0xf bank_mask:0xf
	v_cvt_pk_fp8_f32 v149, v150, v151
	s_nop 1
	v_mov_b32_dpp v150, v149 quad_perm:[2,3,0,1] row_mask:0xf bank_mask:0xf
	s_and_saveexec_b64 s[6:7], s[4:5]
	s_cbranch_execz .LBB0_1505
	v_and_b32_e32 v149, 0xffff, v149
	s_waitcnt lgkmcnt(0)
	v_lshl_or_b32 v149, v150, 16, v149
	v_add_co_u32_e32 v150, vcc, 0x19000, v6
	s_nop 1
	v_addc_co_u32_e32 v151, vcc, 0, v7, vcc
	global_store_dword v[150:151], v149, off offset:32
; #define SBAR() __builtin_amdgcn_sched_barrier(0)
; __device__ __forceinline__ int crow(int r, int hi) { return (r & 3) + 8 * (r >> 2) + 4 * hi; }
; __device__ __forceinline__ float mul_ns(float a, float b) { float r; asm("v_mul_f32 %0, %1, %2" : "=v"(r) : "v"(a), "v"(b)); return r; }
; __device__ __forceinline__ float fma_ns(float a, float b, float c) { float r; asm("v_fma_f32 %0, %1, %2, %3" : "=v"(r) : "v"(a), "v"(b), "v"(c)); return r; }
; __device__ __forceinline__ void store_quad8(unsigned char* p, float v, int r32) {
;     v = fminf(fmaxf(v, -448.f), 448.f);
;     const float v1 = swz_xor<1>(v);
;     const int w = __builtin_amdgcn_cvt_pk_fp8_f32(v, v1, 0, false);
;     const int w2 = __builtin_amdgcn_ds_swizzle(w, (2 << 10) | 0x1f);
;     if ((r32 & 3) == 0) *(unsigned*)p = ((unsigned)w & 0xffffu) | ((unsigned)w2 << 16);
; }
;     __device__ __forceinline__ void operator()(f32x16 (&o)[8], const float (&rli)[16], int wid, int lane, int r32, int hi) const {
;     ...
;                 for (int q = 0; q < 4; ++q) { const int r = rb + q; float s = 0.f;
; #pragma unroll
;                     for (int d0 = 0; d0 < 8; ++d0) { const float t = __uint_as_float((d0 & 1) ? (tw[q][d0 >> 1] & 0xffff0000u) : (tw[q][d0 >> 1] << 16));
;                         const float dd = fma_ns(nlam, mul_ns(o[d0][r], rli[r]), t); s = fma_ns(dd, dd, s); }
;                     s = half_sum(s); rn[r] = rsqrtf(s * (1.0f / 256.0f) + 1e-5f) * 0.8f; }
;     ...
;             for (int rb = 0; rb < 16; rb += 4) { unsigned tw[4][4];
; #pragma unroll
;                 for (int q = 0; q < 4; ++q)
; #pragma unroll
;                     for (int k = 0; k < 4; ++k) tw[q][k] = (scw + ((rb + q) * 4 + k) * 64)[ul];
;                 asm volatile("" ::: "memory"); SBAR();
; #pragma unroll
;                 for (int q = 0; q < 4; ++q) { const int r = rb + q;
; #pragma unroll
;                     for (int d0 = 0; d0 < 8; ++d0) { const float t = __uint_as_float((d0 & 1) ? (tw[q][d0 >> 1] & 0xffff0000u) : (tw[q][d0 >> 1] << 16));
;                         const float dd = fma_ns(nlam, mul_ns(o[d0][r], rli[r]), t);
;                         store_quad8(base + (crow(r, 0) * 4096 + d0 * 32) + uo, mul_ns(mul_ns(dd, rn[r]), g[d0]), r32); } }
;                 asm volatile("" ::: "memory"); SBAR(); }
.LBB0_1505:
	s_or_b64 exec, exec, s[6:7]
	s_waitcnt vmcnt(10)
	v_lshlrev_b32_e32 v149, 16, v148
	s_waitcnt lgkmcnt(0)
	v_mul_f32 v150, v111, v170
	s_nop 0
	v_fma_f32 v149, v212, v150, v149
	s_nop 0
	v_mul_f32 v149, v149, v12
	s_nop 0
	v_mul_f32 v149, v149, v188
	s_nop 0
	v_max_f32_e32 v149, 0xc3e00000, v149
	v_min_f32_e32 v150, 0x43e00000, v149
	s_nop 1
	v_mov_b32_dpp v151, v150 quad_perm:[1,0,3,2] row_mask:0xf bank_mask:0xf
	v_cvt_pk_fp8_f32 v149, v150, v151
	s_nop 1
	v_mov_b32_dpp v150, v149 quad_perm:[2,3,0,1] row_mask:0xf bank_mask:0xf
	s_and_saveexec_b64 s[6:7], s[4:5]
	s_cbranch_execz .LBB0_1507
	v_and_b32_e32 v149, 0xffff, v149
	s_waitcnt lgkmcnt(0)
	v_lshl_or_b32 v149, v150, 16, v149
	v_add_co_u32_e32 v150, vcc, 0x19000, v6
	s_nop 1
	v_addc_co_u32_e32 v151, vcc, 0, v7, vcc
	global_store_dword v[150:151], v149, off offset:64
.LBB0_1507:
	s_or_b64 exec, exec, s[6:7]
	v_and_b32_e32 v148, 0xffff0000, v148
	v_mul_f32 v149, v95, v170
	s_nop 0
	v_fma_f32 v148, v212, v149, v148
	s_nop 0
	v_mul_f32 v148, v148, v12
	s_nop 0
	v_mul_f32 v148, v148, v187
	s_nop 0
	v_max_f32_e32 v148, 0xc3e00000, v148
	v_min_f32_e32 v149, 0x43e00000, v148
	s_waitcnt lgkmcnt(0)
	s_nop 1
	v_mov_b32_dpp v150, v149 quad_perm:[1,0,3,2] row_mask:0xf bank_mask:0xf
	v_cvt_pk_fp8_f32 v148, v149, v150
	s_nop 1
	v_mov_b32_dpp v149, v148 quad_perm:[2,3,0,1] row_mask:0xf bank_mask:0xf
	s_and_saveexec_b64 s[6:7], s[4:5]
	s_cbranch_execz .LBB0_1509
	v_and_b32_e32 v148, 0xffff, v148
	s_waitcnt lgkmcnt(0)
	v_lshl_or_b32 v150, v149, 16, v148
	v_add_co_u32_e32 v148, vcc, 0x19000, v6
	s_nop 1
	v_addc_co_u32_e32 v149, vcc, 0, v7, vcc
	global_store_dword v[148:149], v150, off offset:96
.LBB0_1509:
	s_or_b64 exec, exec, s[6:7]
	s_waitcnt vmcnt(9)
	v_lshlrev_b32_e32 v148, 16, v5
	s_waitcnt lgkmcnt(0)
	v_mul_f32 v149, v79, v170
	s_nop 0
	v_fma_f32 v148, v212, v149, v148
	s_nop 0
	v_mul_f32 v148, v148, v12
	s_nop 0
	v_mul_f32 v148, v148, v186
	s_nop 0
	v_max_f32_e32 v148, 0xc3e00000, v148
	v_min_f32_e32 v149, 0x43e00000, v148
	s_nop 1
	v_mov_b32_dpp v150, v149 quad_perm:[1,0,3,2] row_mask:0xf bank_mask:0xf
	v_cvt_pk_fp8_f32 v148, v149, v150
	s_nop 1
	v_mov_b32_dpp v149, v148 quad_perm:[2,3,0,1] row_mask:0xf bank_mask:0xf
	s_and_saveexec_b64 s[6:7], s[4:5]
	s_cbranch_execz .LBB0_1511
	v_and_b32_e32 v148, 0xffff, v148
	s_waitcnt lgkmcnt(0)
	v_lshl_or_b32 v150, v149, 16, v148
	v_add_co_u32_e32 v148, vcc, 0x19000, v6
	s_nop 1
	v_addc_co_u32_e32 v149, vcc, 0, v7, vcc
	global_store_dword v[148:149], v150, off offset:128
.LBB0_1511:
	s_or_b64 exec, exec, s[6:7]
	v_and_b32_e32 v5, 0xffff0000, v5
	v_mul_f32 v148, v63, v170
	s_nop 0
	v_fma_f32 v5, v212, v148, v5
	s_nop 0
	v_mul_f32 v5, v5, v12
	s_nop 0
	v_mul_f32 v5, v5, v185
	s_nop 0
	v_max_f32_e32 v5, 0xc3e00000, v5
	v_min_f32_e32 v148, 0x43e00000, v5
	s_waitcnt lgkmcnt(0)
	s_nop 1
	v_mov_b32_dpp v149, v148 quad_perm:[1,0,3,2] row_mask:0xf bank_mask:0xf
	v_cvt_pk_fp8_f32 v5, v148, v149
	s_nop 1
	v_mov_b32_dpp v148, v5 quad_perm:[2,3,0,1] row_mask:0xf bank_mask:0xf
	s_and_saveexec_b64 s[6:7], s[4:5]
	s_cbranch_execz .LBB0_1513
	v_and_b32_e32 v5, 0xffff, v5
	s_waitcnt lgkmcnt(0)
	v_lshl_or_b32 v5, v148, 16, v5
	v_add_co_u32_e32 v148, vcc, 0x19000, v6
	s_nop 1
	v_addc_co_u32_e32 v149, vcc, 0, v7, vcc
	global_store_dword v[148:149], v5, off offset:160
.LBB0_1513:
	s_or_b64 exec, exec, s[6:7]
	s_waitcnt vmcnt(8)
	v_lshlrev_b32_e32 v5, 16, v4
	s_waitcnt lgkmcnt(0)
	v_mul_f32 v148, v47, v170
	s_nop 0
	v_fma_f32 v5, v212, v148, v5
	s_nop 0
	v_mul_f32 v5, v5, v12
	s_nop 0
	v_mul_f32 v5, v5, v184
	s_nop 0
	v_max_f32_e32 v5, 0xc3e00000, v5
	v_min_f32_e32 v148, 0x43e00000, v5
	s_nop 1
	v_mov_b32_dpp v149, v148 quad_perm:[1,0,3,2] row_mask:0xf bank_mask:0xf
	v_cvt_pk_fp8_f32 v5, v148, v149
	s_nop 1
	v_mov_b32_dpp v148, v5 quad_perm:[2,3,0,1] row_mask:0xf bank_mask:0xf
	s_and_saveexec_b64 s[6:7], s[4:5]
	s_cbranch_execz .LBB0_1515
	v_and_b32_e32 v5, 0xffff, v5
	s_waitcnt lgkmcnt(0)
	v_lshl_or_b32 v5, v148, 16, v5
	v_add_co_u32_e32 v148, vcc, 0x19000, v6
	s_nop 1
	v_addc_co_u32_e32 v149, vcc, 0, v7, vcc
	global_store_dword v[148:149], v5, off offset:192
.LBB0_1515:
	s_or_b64 exec, exec, s[6:7]
	v_and_b32_e32 v4, 0xffff0000, v4
	v_mul_f32 v5, v31, v170
	s_nop 0
	v_fma_f32 v4, v212, v5, v4
	s_nop 0
	v_mul_f32 v4, v4, v12
	s_nop 0
	v_mul_f32 v4, v4, v165
	s_nop 0
	v_max_f32_e32 v4, 0xc3e00000, v4
	v_min_f32_e32 v5, 0x43e00000, v4
	s_nop 1
	v_mov_b32_dpp v12, v5 quad_perm:[1,0,3,2] row_mask:0xf bank_mask:0xf
	s_waitcnt lgkmcnt(0)
	v_cvt_pk_fp8_f32 v4, v5, v12
	s_nop 1
	v_mov_b32_dpp v5, v4 quad_perm:[2,3,0,1] row_mask:0xf bank_mask:0xf
	s_and_saveexec_b64 s[6:7], s[4:5]
	s_cbranch_execz .LBB0_1517
	v_and_b32_e32 v4, 0xffff, v4
	s_waitcnt lgkmcnt(0)
	v_lshl_or_b32 v12, v5, 16, v4
	v_add_co_u32_e32 v4, vcc, 0x19000, v6
	s_nop 1
	v_addc_co_u32_e32 v5, vcc, 0, v7, vcc
	global_store_dword v[4:5], v12, off offset:224
.LBB0_1517:
	s_or_b64 exec, exec, s[6:7]
	s_waitcnt lgkmcnt(0)
	v_pk_add_f32 v[4:5], v[8:9], v[10:11]
	v_mul_f32 v9, v144, v169
	s_nop 0
	v_pk_fma_f32 v[4:5], v[4:5], s[54:55], v[198:199] op_sel_hi:[1,0,0]
	s_nop 0
	v_mul_f32_e32 v8, 0x4b800000, v5
	v_cmp_gt_f32_e32 vcc, s53, v5
	v_cmp_gt_f32_e64 s[6:7], s53, v4
	s_nop 0
	v_cndmask_b32_e32 v5, v5, v8, vcc
	v_rsq_f32_e32 v5, v5
	s_waitcnt vmcnt(7)
	v_lshlrev_b32_e32 v8, 16, v147
	v_fma_f32 v8, v212, v9, v8
	v_mul_f32_e32 v10, 0x45800000, v5
	v_cndmask_b32_e32 v5, v5, v10, vcc
	v_mul_f32_e32 v5, 0x3f4ccccd, v5
	v_mul_f32 v8, v8, v5
	s_nop 0
	v_mul_f32 v8, v8, v190
	s_nop 0
	v_max_f32_e32 v8, 0xc3e00000, v8
	v_min_f32_e32 v9, 0x43e00000, v8
	s_nop 1
	v_mov_b32_dpp v10, v9 quad_perm:[1,0,3,2] row_mask:0xf bank_mask:0xf
	v_cvt_pk_fp8_f32 v8, v9, v10
	s_nop 1
	v_mov_b32_dpp v9, v8 quad_perm:[2,3,0,1] row_mask:0xf bank_mask:0xf
	s_and_saveexec_b64 s[8:9], s[4:5]
	s_cbranch_execz .LBB0_1519
	v_and_b32_e32 v8, 0xffff, v8
	s_waitcnt lgkmcnt(0)
	v_lshl_or_b32 v10, v9, 16, v8
	v_add_co_u32_e32 v8, vcc, 0x1a000, v6
	s_nop 1
	v_addc_co_u32_e32 v9, vcc, 0, v7, vcc
	global_store_dword v[8:9], v10, off
; #define SBAR() __builtin_amdgcn_sched_barrier(0)
; __device__ __forceinline__ int crow(int r, int hi) { return (r & 3) + 8 * (r >> 2) + 4 * hi; }
; __device__ __forceinline__ float mul_ns(float a, float b) { float r; asm("v_mul_f32 %0, %1, %2" : "=v"(r) : "v"(a), "v"(b)); return r; }
; __device__ __forceinline__ float fma_ns(float a, float b, float c) { float r; asm("v_fma_f32 %0, %1, %2, %3" : "=v"(r) : "v"(a), "v"(b), "v"(c)); return r; }
; __device__ __forceinline__ void store_quad8(unsigned char* p, float v, int r32) {
;     v = fminf(fmaxf(v, -448.f), 448.f);
;     const float v1 = swz_xor<1>(v);
;     const int w = __builtin_amdgcn_cvt_pk_fp8_f32(v, v1, 0, false);
;     const int w2 = __builtin_amdgcn_ds_swizzle(w, (2 << 10) | 0x1f);
;     if ((r32 & 3) == 0) *(unsigned*)p = ((unsigned)w & 0xffffu) | ((unsigned)w2 << 16);
; }
;     __device__ __forceinline__ void operator()(f32x16 (&o)[8], const float (&rli)[16], int wid, int lane, int r32, int hi) const {
;     ...
;             for (int rb = 0; rb < 16; rb += 4) { unsigned tw[4][4];
; #pragma unroll
;                 for (int q = 0; q < 4; ++q)
; #pragma unroll
;                     for (int k = 0; k < 4; ++k) tw[q][k] = (scw + ((rb + q) * 4 + k) * 64)[ul];
;                 asm volatile("" ::: "memory"); SBAR();
; #pragma unroll
;                 for (int q = 0; q < 4; ++q) { const int r = rb + q;
; #pragma unroll
;                     for (int d0 = 0; d0 < 8; ++d0) { const float t = __uint_as_float((d0 & 1) ? (tw[q][d0 >> 1] & 0xffff0000u) : (tw[q][d0 >> 1] << 16));
;                         const float dd = fma_ns(nlam, mul_ns(o[d0][r], rli[r]), t);
;                         store_quad8(base + (crow(r, 0) * 4096 + d0 * 32) + uo, mul_ns(mul_ns(dd, rn[r]), g[d0]), r32); } }
;                 asm volatile("" ::: "memory"); SBAR(); }
.LBB0_1519:
	s_or_b64 exec, exec, s[8:9]
	v_and_b32_e32 v8, 0xffff0000, v147
	s_waitcnt lgkmcnt(0)
	v_mul_f32 v9, v128, v169
	s_nop 0
	v_fma_f32 v8, v212, v9, v8
	s_nop 0
	v_mul_f32 v8, v8, v5
	s_nop 0
	v_mul_f32 v8, v8, v189
	s_nop 0
	v_max_f32_e32 v8, 0xc3e00000, v8
	v_min_f32_e32 v9, 0x43e00000, v8
	s_nop 1
	v_mov_b32_dpp v10, v9 quad_perm:[1,0,3,2] row_mask:0xf bank_mask:0xf
	v_cvt_pk_fp8_f32 v8, v9, v10
	s_nop 1
	v_mov_b32_dpp v9, v8 quad_perm:[2,3,0,1] row_mask:0xf bank_mask:0xf
	s_and_saveexec_b64 s[8:9], s[4:5]
	s_cbranch_execz .LBB0_1521
	v_and_b32_e32 v8, 0xffff, v8
	s_waitcnt lgkmcnt(0)
	v_lshl_or_b32 v10, v9, 16, v8
	v_add_co_u32_e32 v8, vcc, 0x1a000, v6
	s_nop 1
	v_addc_co_u32_e32 v9, vcc, 0, v7, vcc
	global_store_dword v[8:9], v10, off offset:32
.LBB0_1521:
	s_or_b64 exec, exec, s[8:9]
	s_waitcnt vmcnt(6)
	v_lshlrev_b32_e32 v8, 16, v146
	s_waitcnt lgkmcnt(0)
	v_mul_f32 v9, v112, v169
	s_nop 0
	v_fma_f32 v8, v212, v9, v8
	s_nop 0
	v_mul_f32 v8, v8, v5
	s_nop 0
	v_mul_f32 v8, v8, v188
	s_nop 0
	v_max_f32_e32 v8, 0xc3e00000, v8
	v_min_f32_e32 v9, 0x43e00000, v8
	s_nop 1
	v_mov_b32_dpp v10, v9 quad_perm:[1,0,3,2] row_mask:0xf bank_mask:0xf
	v_cvt_pk_fp8_f32 v8, v9, v10
	s_nop 1
	v_mov_b32_dpp v9, v8 quad_perm:[2,3,0,1] row_mask:0xf bank_mask:0xf
	s_and_saveexec_b64 s[8:9], s[4:5]
	s_cbranch_execz .LBB0_1523
	v_and_b32_e32 v8, 0xffff, v8
	s_waitcnt lgkmcnt(0)
	v_lshl_or_b32 v10, v9, 16, v8
	v_add_co_u32_e32 v8, vcc, 0x1a000, v6
	s_nop 1
	v_addc_co_u32_e32 v9, vcc, 0, v7, vcc
	global_store_dword v[8:9], v10, off offset:64
.LBB0_1523:
	s_or_b64 exec, exec, s[8:9]
	v_and_b32_e32 v8, 0xffff0000, v146
	s_waitcnt lgkmcnt(0)
	v_mul_f32 v9, v96, v169
	s_nop 0
	v_fma_f32 v8, v212, v9, v8
	s_nop 0
	v_mul_f32 v8, v8, v5
	s_nop 0
	v_mul_f32 v8, v8, v187
	s_nop 0
	v_max_f32_e32 v8, 0xc3e00000, v8
	v_min_f32_e32 v9, 0x43e00000, v8
	s_nop 1
	v_mov_b32_dpp v10, v9 quad_perm:[1,0,3,2] row_mask:0xf bank_mask:0xf
	v_cvt_pk_fp8_f32 v8, v9, v10
	s_nop 1
	v_mov_b32_dpp v9, v8 quad_perm:[2,3,0,1] row_mask:0xf bank_mask:0xf
	s_and_saveexec_b64 s[8:9], s[4:5]
	s_cbranch_execz .LBB0_1525
	v_and_b32_e32 v8, 0xffff, v8
	s_waitcnt lgkmcnt(0)
	v_lshl_or_b32 v10, v9, 16, v8
	v_add_co_u32_e32 v8, vcc, 0x1a000, v6
	s_nop 1
	v_addc_co_u32_e32 v9, vcc, 0, v7, vcc
	global_store_dword v[8:9], v10, off offset:96
.LBB0_1525:
	s_or_b64 exec, exec, s[8:9]
	s_waitcnt vmcnt(5)
	v_lshlrev_b32_e32 v8, 16, v17
	s_waitcnt lgkmcnt(0)
	v_mul_f32 v9, v80, v169
	s_nop 0
	v_fma_f32 v8, v212, v9, v8
	s_nop 0
	v_mul_f32 v8, v8, v5
	s_nop 0
	v_mul_f32 v8, v8, v186
	s_nop 0
	v_max_f32_e32 v8, 0xc3e00000, v8
	v_min_f32_e32 v9, 0x43e00000, v8
	s_nop 1
	v_mov_b32_dpp v10, v9 quad_perm:[1,0,3,2] row_mask:0xf bank_mask:0xf
	v_cvt_pk_fp8_f32 v8, v9, v10
	s_nop 1
	v_mov_b32_dpp v9, v8 quad_perm:[2,3,0,1] row_mask:0xf bank_mask:0xf
	s_and_saveexec_b64 s[8:9], s[4:5]
	s_cbranch_execz .LBB0_1527
	v_and_b32_e32 v8, 0xffff, v8
	s_waitcnt lgkmcnt(0)
	v_lshl_or_b32 v10, v9, 16, v8
	v_add_co_u32_e32 v8, vcc, 0x1a000, v6
	s_nop 1
	v_addc_co_u32_e32 v9, vcc, 0, v7, vcc
	global_store_dword v[8:9], v10, off offset:128
.LBB0_1527:
	s_or_b64 exec, exec, s[8:9]
	v_and_b32_e32 v8, 0xffff0000, v17
	s_waitcnt lgkmcnt(0)
	v_mul_f32 v9, v64, v169
	s_nop 0
	v_fma_f32 v8, v212, v9, v8
	s_nop 0
	v_mul_f32 v8, v8, v5
	s_nop 0
	v_mul_f32 v8, v8, v185
	s_nop 0
	v_max_f32_e32 v8, 0xc3e00000, v8
	v_min_f32_e32 v9, 0x43e00000, v8
	s_nop 1
	v_mov_b32_dpp v10, v9 quad_perm:[1,0,3,2] row_mask:0xf bank_mask:0xf
	v_cvt_pk_fp8_f32 v8, v9, v10
	s_nop 1
	v_mov_b32_dpp v9, v8 quad_perm:[2,3,0,1] row_mask:0xf bank_mask:0xf
	s_and_saveexec_b64 s[8:9], s[4:5]
	s_cbranch_execz .LBB0_1529
	v_and_b32_e32 v8, 0xffff, v8
	s_waitcnt lgkmcnt(0)
	v_lshl_or_b32 v10, v9, 16, v8
	v_add_co_u32_e32 v8, vcc, 0x1a000, v6
	s_nop 1
	v_addc_co_u32_e32 v9, vcc, 0, v7, vcc
	global_store_dword v[8:9], v10, off offset:160
.LBB0_1529:
	s_or_b64 exec, exec, s[8:9]
	s_waitcnt vmcnt(4)
	v_lshlrev_b32_e32 v8, 16, v16
	s_waitcnt lgkmcnt(0)
	v_mul_f32 v9, v48, v169
	s_nop 0
	v_fma_f32 v8, v212, v9, v8
	s_nop 0
	v_mul_f32 v8, v8, v5
	s_nop 0
	v_mul_f32 v8, v8, v184
	s_nop 0
	v_max_f32_e32 v8, 0xc3e00000, v8
	v_min_f32_e32 v9, 0x43e00000, v8
	s_nop 1
	v_mov_b32_dpp v10, v9 quad_perm:[1,0,3,2] row_mask:0xf bank_mask:0xf
	v_cvt_pk_fp8_f32 v8, v9, v10
	s_nop 1
	v_mov_b32_dpp v9, v8 quad_perm:[2,3,0,1] row_mask:0xf bank_mask:0xf
	s_and_saveexec_b64 s[8:9], s[4:5]
	s_cbranch_execz .LBB0_1531
	v_and_b32_e32 v8, 0xffff, v8
	s_waitcnt lgkmcnt(0)
	v_lshl_or_b32 v10, v9, 16, v8
	v_add_co_u32_e32 v8, vcc, 0x1a000, v6
	s_nop 1
	v_addc_co_u32_e32 v9, vcc, 0, v7, vcc
	global_store_dword v[8:9], v10, off offset:192
.LBB0_1531:
	s_or_b64 exec, exec, s[8:9]
	v_and_b32_e32 v8, 0xffff0000, v16
	s_waitcnt lgkmcnt(0)
	v_mul_f32 v9, v32, v169
	s_nop 0
	v_fma_f32 v8, v212, v9, v8
	s_nop 0
	v_mul_f32 v5, v8, v5
	s_nop 0
	v_mul_f32 v5, v5, v165
	s_nop 0
	v_max_f32_e32 v5, 0xc3e00000, v5
	v_min_f32_e32 v8, 0x43e00000, v5
	s_nop 1
	v_mov_b32_dpp v9, v8 quad_perm:[1,0,3,2] row_mask:0xf bank_mask:0xf
	v_cvt_pk_fp8_f32 v5, v8, v9
	s_nop 1
	v_mov_b32_dpp v8, v5 quad_perm:[2,3,0,1] row_mask:0xf bank_mask:0xf
	s_and_saveexec_b64 s[8:9], s[4:5]
	s_cbranch_execz .LBB0_1533
	v_and_b32_e32 v5, 0xffff, v5
	s_waitcnt lgkmcnt(0)
	v_lshl_or_b32 v5, v8, 16, v5
	v_add_co_u32_e32 v8, vcc, 0x1a000, v6
	s_nop 1
	v_addc_co_u32_e32 v9, vcc, 0, v7, vcc
	global_store_dword v[8:9], v5, off offset:224
; #define SBAR() __builtin_amdgcn_sched_barrier(0)
; __device__ __forceinline__ int crow(int r, int hi) { return (r & 3) + 8 * (r >> 2) + 4 * hi; }
; __device__ __forceinline__ float mul_ns(float a, float b) { float r; asm("v_mul_f32 %0, %1, %2" : "=v"(r) : "v"(a), "v"(b)); return r; }
; __device__ __forceinline__ float fma_ns(float a, float b, float c) { float r; asm("v_fma_f32 %0, %1, %2, %3" : "=v"(r) : "v"(a), "v"(b), "v"(c)); return r; }
; __device__ __forceinline__ void store_quad8(unsigned char* p, float v, int r32) {
;     v = fminf(fmaxf(v, -448.f), 448.f);
;     const float v1 = swz_xor<1>(v);
;     const int w = __builtin_amdgcn_cvt_pk_fp8_f32(v, v1, 0, false);
;     const int w2 = __builtin_amdgcn_ds_swizzle(w, (2 << 10) | 0x1f);
;     if ((r32 & 3) == 0) *(unsigned*)p = ((unsigned)w & 0xffffu) | ((unsigned)w2 << 16);
; }
;     __device__ __forceinline__ void operator()(f32x16 (&o)[8], const float (&rli)[16], int wid, int lane, int r32, int hi) const {
;     ...
;             for (int rb = 0; rb < 16; rb += 4) { unsigned tw[4][4];
; #pragma unroll
;                 for (int q = 0; q < 4; ++q)
; #pragma unroll
;                     for (int k = 0; k < 4; ++k) tw[q][k] = (scw + ((rb + q) * 4 + k) * 64)[ul];
;                 asm volatile("" ::: "memory"); SBAR();
; #pragma unroll
;                 for (int q = 0; q < 4; ++q) { const int r = rb + q;
; #pragma unroll
;                     for (int d0 = 0; d0 < 8; ++d0) { const float t = __uint_as_float((d0 & 1) ? (tw[q][d0 >> 1] & 0xffff0000u) : (tw[q][d0 >> 1] << 16));
;                         const float dd = fma_ns(nlam, mul_ns(o[d0][r], rli[r]), t);
;                         store_quad8(base + (crow(r, 0) * 4096 + d0 * 32) + uo, mul_ns(mul_ns(dd, rn[r]), g[d0]), r32); } }
;                 asm volatile("" ::: "memory"); SBAR(); }
.LBB0_1533:
	s_or_b64 exec, exec, s[8:9]
	v_mul_f32_e32 v5, 0x4b800000, v4
	v_cndmask_b32_e64 v4, v4, v5, s[6:7]
	v_rsq_f32_e32 v4, v4
	s_waitcnt lgkmcnt(0)
	v_mul_f32 v8, v145, v168
	v_mul_f32_e32 v5, 0x45800000, v4
	v_cndmask_b32_e64 v4, v4, v5, s[6:7]
	s_waitcnt vmcnt(3)
	v_lshlrev_b32_e32 v5, 16, v15
	v_fma_f32 v5, v212, v8, v5
	v_mul_f32_e32 v4, 0x3f4ccccd, v4
	v_mul_f32 v5, v5, v4
	s_nop 0
	v_mul_f32 v5, v5, v190
	s_nop 0
	v_max_f32_e32 v5, 0xc3e00000, v5
	v_min_f32_e32 v8, 0x43e00000, v5
	s_nop 1
	v_mov_b32_dpp v9, v8 quad_perm:[1,0,3,2] row_mask:0xf bank_mask:0xf
	v_cvt_pk_fp8_f32 v5, v8, v9
	s_nop 1
	v_mov_b32_dpp v8, v5 quad_perm:[2,3,0,1] row_mask:0xf bank_mask:0xf
	s_and_saveexec_b64 s[6:7], s[4:5]
	s_cbranch_execz .LBB0_1535
	v_and_b32_e32 v5, 0xffff, v5
	s_waitcnt lgkmcnt(0)
	v_lshl_or_b32 v5, v8, 16, v5
	v_add_co_u32_e32 v8, vcc, 0x1b000, v6
	s_nop 1
	v_addc_co_u32_e32 v9, vcc, 0, v7, vcc
	global_store_dword v[8:9], v5, off
.LBB0_1535:
	s_or_b64 exec, exec, s[6:7]
	v_and_b32_e32 v5, 0xffff0000, v15
	s_waitcnt lgkmcnt(0)
	v_mul_f32 v8, v129, v168
	s_nop 0
	v_fma_f32 v5, v212, v8, v5
	s_nop 0
	v_mul_f32 v5, v5, v4
	s_nop 0
	v_mul_f32 v5, v5, v189
	s_nop 0
	v_max_f32_e32 v5, 0xc3e00000, v5
	v_min_f32_e32 v8, 0x43e00000, v5
	s_nop 1
	v_mov_b32_dpp v9, v8 quad_perm:[1,0,3,2] row_mask:0xf bank_mask:0xf
	v_cvt_pk_fp8_f32 v5, v8, v9
	s_nop 1
	v_mov_b32_dpp v8, v5 quad_perm:[2,3,0,1] row_mask:0xf bank_mask:0xf
	s_and_saveexec_b64 s[6:7], s[4:5]
	s_cbranch_execz .LBB0_1537
	v_and_b32_e32 v5, 0xffff, v5
	s_waitcnt lgkmcnt(0)
	v_lshl_or_b32 v5, v8, 16, v5
	v_add_co_u32_e32 v8, vcc, 0x1b000, v6
	s_nop 1
	v_addc_co_u32_e32 v9, vcc, 0, v7, vcc
	global_store_dword v[8:9], v5, off offset:32
.LBB0_1537:
	s_or_b64 exec, exec, s[6:7]
	s_waitcnt vmcnt(2)
	v_lshlrev_b32_e32 v5, 16, v14
	s_waitcnt lgkmcnt(0)
	v_mul_f32 v8, v113, v168
	s_nop 0
	v_fma_f32 v5, v212, v8, v5
	s_nop 0
	v_mul_f32 v5, v5, v4
	s_nop 0
	v_mul_f32 v5, v5, v188
	s_nop 0
	v_max_f32_e32 v5, 0xc3e00000, v5
	v_min_f32_e32 v8, 0x43e00000, v5
	s_nop 1
	v_mov_b32_dpp v9, v8 quad_perm:[1,0,3,2] row_mask:0xf bank_mask:0xf
	v_cvt_pk_fp8_f32 v5, v8, v9
	s_nop 1
	v_mov_b32_dpp v8, v5 quad_perm:[2,3,0,1] row_mask:0xf bank_mask:0xf
	s_and_saveexec_b64 s[6:7], s[4:5]
	s_cbranch_execz .LBB0_1539
	v_and_b32_e32 v5, 0xffff, v5
	s_waitcnt lgkmcnt(0)
	v_lshl_or_b32 v5, v8, 16, v5
	v_add_co_u32_e32 v8, vcc, 0x1b000, v6
	s_nop 1
	v_addc_co_u32_e32 v9, vcc, 0, v7, vcc
	global_store_dword v[8:9], v5, off offset:64
.LBB0_1539:
	s_or_b64 exec, exec, s[6:7]
	v_and_b32_e32 v5, 0xffff0000, v14
	s_waitcnt lgkmcnt(0)
	v_mul_f32 v8, v97, v168
	s_nop 0
	v_fma_f32 v5, v212, v8, v5
	s_nop 0
	v_mul_f32 v5, v5, v4
	s_nop 0
	v_mul_f32 v5, v5, v187
	s_nop 0
	v_max_f32_e32 v5, 0xc3e00000, v5
	v_min_f32_e32 v8, 0x43e00000, v5
	s_nop 1
	v_mov_b32_dpp v9, v8 quad_perm:[1,0,3,2] row_mask:0xf bank_mask:0xf
	v_cvt_pk_fp8_f32 v5, v8, v9
	s_nop 1
	v_mov_b32_dpp v8, v5 quad_perm:[2,3,0,1] row_mask:0xf bank_mask:0xf
	s_and_saveexec_b64 s[6:7], s[4:5]
	s_cbranch_execz .LBB0_1541
	v_and_b32_e32 v5, 0xffff, v5
	s_waitcnt lgkmcnt(0)
	v_lshl_or_b32 v5, v8, 16, v5
	v_add_co_u32_e32 v8, vcc, 0x1b000, v6
	s_nop 1
	v_addc_co_u32_e32 v9, vcc, 0, v7, vcc
	global_store_dword v[8:9], v5, off offset:96
.LBB0_1541:
	s_or_b64 exec, exec, s[6:7]
	s_waitcnt vmcnt(1)
	v_lshlrev_b32_e32 v5, 16, v13
	s_waitcnt lgkmcnt(0)
	v_mul_f32 v8, v81, v168
	s_nop 0
	v_fma_f32 v5, v212, v8, v5
	s_nop 0
	v_mul_f32 v5, v5, v4
	s_nop 0
	v_mul_f32 v5, v5, v186
	s_nop 0
	v_max_f32_e32 v5, 0xc3e00000, v5
	v_min_f32_e32 v8, 0x43e00000, v5
	s_nop 1
	v_mov_b32_dpp v9, v8 quad_perm:[1,0,3,2] row_mask:0xf bank_mask:0xf
	v_cvt_pk_fp8_f32 v5, v8, v9
	s_nop 1
	v_mov_b32_dpp v8, v5 quad_perm:[2,3,0,1] row_mask:0xf bank_mask:0xf
	s_and_saveexec_b64 s[6:7], s[4:5]
	s_cbranch_execz .LBB0_1543
	v_and_b32_e32 v5, 0xffff, v5
	s_waitcnt lgkmcnt(0)
	v_lshl_or_b32 v5, v8, 16, v5
	v_add_co_u32_e32 v8, vcc, 0x1b000, v6
	s_nop 1
	v_addc_co_u32_e32 v9, vcc, 0, v7, vcc
	global_store_dword v[8:9], v5, off offset:128
.LBB0_1543:
	s_or_b64 exec, exec, s[6:7]
	v_and_b32_e32 v5, 0xffff0000, v13
	s_waitcnt lgkmcnt(0)
	v_mul_f32 v8, v65, v168
	s_nop 0
	v_fma_f32 v5, v212, v8, v5
	s_nop 0
	v_mul_f32 v5, v5, v4
	s_nop 0
	v_mul_f32 v5, v5, v185
	s_nop 0
	v_max_f32_e32 v5, 0xc3e00000, v5
	v_min_f32_e32 v8, 0x43e00000, v5
	s_nop 1
	v_mov_b32_dpp v9, v8 quad_perm:[1,0,3,2] row_mask:0xf bank_mask:0xf
	v_cvt_pk_fp8_f32 v5, v8, v9
	s_nop 1
	v_mov_b32_dpp v8, v5 quad_perm:[2,3,0,1] row_mask:0xf bank_mask:0xf
	s_and_saveexec_b64 s[6:7], s[4:5]
	s_cbranch_execz .LBB0_1545
	v_and_b32_e32 v5, 0xffff, v5
	s_waitcnt lgkmcnt(0)
	v_lshl_or_b32 v5, v8, 16, v5
	v_add_co_u32_e32 v8, vcc, 0x1b000, v6
	s_nop 1
	v_addc_co_u32_e32 v9, vcc, 0, v7, vcc
	global_store_dword v[8:9], v5, off offset:160
.LBB0_1545:
	s_or_b64 exec, exec, s[6:7]
	s_waitcnt vmcnt(0)
	v_lshlrev_b32_e32 v5, 16, v2
	s_waitcnt lgkmcnt(0)
	v_mul_f32 v8, v49, v168
	s_nop 0
	v_fma_f32 v5, v212, v8, v5
	s_nop 0
	v_mul_f32 v5, v5, v4
	s_nop 0
	v_mul_f32 v5, v5, v184
	s_nop 0
	v_max_f32_e32 v5, 0xc3e00000, v5
	v_min_f32_e32 v8, 0x43e00000, v5
	s_nop 1
	v_mov_b32_dpp v9, v8 quad_perm:[1,0,3,2] row_mask:0xf bank_mask:0xf
	v_cvt_pk_fp8_f32 v5, v8, v9
	s_nop 1
	v_mov_b32_dpp v8, v5 quad_perm:[2,3,0,1] row_mask:0xf bank_mask:0xf
	s_and_saveexec_b64 s[6:7], s[4:5]
	s_cbranch_execz .LBB0_1547
	v_and_b32_e32 v5, 0xffff, v5
	s_waitcnt lgkmcnt(0)
	v_lshl_or_b32 v5, v8, 16, v5
	v_add_co_u32_e32 v8, vcc, 0x1b000, v6
	s_nop 1
	v_addc_co_u32_e32 v9, vcc, 0, v7, vcc
	global_store_dword v[8:9], v5, off offset:192
.LBB0_1547:
	s_or_b64 exec, exec, s[6:7]
	v_and_b32_e32 v2, 0xffff0000, v2
	v_mul_f32 v5, v33, v168
	s_nop 0
	v_fma_f32 v2, v212, v5, v2
	s_nop 0
	v_mul_f32 v2, v2, v4
	s_nop 0
	v_mul_f32 v2, v2, v165
	s_nop 0
	v_max_f32_e32 v2, 0xc3e00000, v2
	v_min_f32_e32 v4, 0x43e00000, v2
	s_nop 1
	v_mov_b32_dpp v5, v4 quad_perm:[1,0,3,2] row_mask:0xf bank_mask:0xf
	s_waitcnt lgkmcnt(0)
	v_cvt_pk_fp8_f32 v2, v4, v5
	s_nop 1
	v_mov_b32_dpp v4, v2 quad_perm:[2,3,0,1] row_mask:0xf bank_mask:0xf
	s_and_saveexec_b64 s[6:7], s[4:5]
	s_cbranch_execz .LBB0_1549
	v_and_b32_e32 v2, 0xffff, v2
	s_waitcnt lgkmcnt(0)
	v_lshl_or_b32 v2, v4, 16, v2
	v_add_co_u32_e32 v4, vcc, 0x1b000, v6
	s_nop 1
	v_addc_co_u32_e32 v5, vcc, 0, v7, vcc
	global_store_dword v[4:5], v2, off offset:224
